# router phase: LDS weight reads software-pipelined 8 deep with counted lgkmcnt waits; 64 LDS address registers replaced by two bases plus immediate offsets
# speedup vs baseline: 1.0086x; 1.0086x over previous
; #define PG8_STAGE(bufoff, soff, voff) do { _Pragma("unroll") for (int _i = 0; _i < 2; ++_i) \
;         __builtin_amdgcn_raw_ptr_buffer_load_lds(rs, (LAS void*)(lds + (bufoff) + ldsw + _i * 8192), 16, (int)(voff)[_i], (int)(soff), 0, 0); } while (0)
; #define PG8_MM(ai, bj, At, Bt) do { if constexpr (F8) PG8_MMA8(ai, bj, At, Bt); else PG8_MMA(ai, bj, At, Bt); } while (0)
; #define PG8_WAIT_V(n) asm volatile("s_waitcnt vmcnt(" #n ")" ::: "memory")
; #define PG8_WAIT_L(n) asm volatile("s_waitcnt lgkmcnt(" #n ")" ::: "memory")
; #define PG8_BAR __builtin_amdgcn_s_barrier()
; #define PG8_SCHED __builtin_amdgcn_sched_barrier(0)
;     ...
;         for (int t = 0; t < nt; t += 2) {
;             const bool last = (t == nt - 2);
;             const unsigned a1 = cA + (unsigned)(t + 1) * kstep;
;             const unsigned a2 = last ? nA : cA + (unsigned)(t + 2) * kstep, b2 = last ? nB : cB + (unsigned)(t + 2) * kstep;
;             const unsigned a3 = a2 + kstep, b3 = b2 + kstep;
;             if (last && has_next) S.a_ready(nxt);
;             const unsigned w0[2] = {last ? nA0[0] : vA0[0], last ? nA0[1] : vA0[1]}, w1[2] = {last ? nA1[0] : vA1[0], last ? nA1[1] : vA1[1]};
;             PG8_LDB(B0, 0, 0); PG8_LDB(B1, 0, 1); PG8_SCHED; PG8_LDA(At, 0, 0); PG8_STAGE(PG8_SA(1, 1), a1, vA1);
;             PG8_WAIT_V(8); PG8_WAIT_L(0); PG8_BAR; PG8_MM(0, 0, At, B0); PG8_MM(0, 1, At, B1); PG8_BAR; PG8_SCHED;
;             PG8_LDA(At, 0, 1); PG8_STAGE(PG8_SB(0, 0), b2, voffB); PG8_STAGE(PG8_SB(0, 1), b2 + hsB, voffB); PG8_STAGE(PG8_SA(0, 0), a2, w0);
;             PG8_WAIT_V(8); PG8_WAIT_L(0); PG8_BAR; PG8_MM(1, 0, At, B0); PG8_MM(1, 1, At, B1); PG8_BAR; PG8_SCHED;
;             PG8_LDB(B0, 1, 0); PG8_LDB(B1, 1, 1); PG8_SCHED; PG8_LDA(At, 1, 0); PG8_STAGE(PG8_SA(0, 1), a2, w1);
;             PG8_WAIT_V(8); PG8_WAIT_L(0); PG8_BAR; PG8_MM(0, 0, At, B0); PG8_MM(0, 1, At, B1); PG8_BAR; PG8_SCHED;
;             PG8_LDA(At, 1, 1); PG8_STAGE(PG8_SB(1, 0), b3, voffB); PG8_STAGE(PG8_SB(1, 1), b3 + hsB, voffB); PG8_STAGE(PG8_SA(1, 0), a3, w0);
;             PG8_WAIT_V(8); PG8_WAIT_L(0); PG8_BAR; PG8_MM(1, 0, At, B0); PG8_MM(1, 1, At, B1); PG8_BAR; PG8_SCHED;
.LBB0_827:
	v_add_u32_e32 v0, s19, v179
	v_add_u32_e32 v12, s22, v179
	ds_read_b128 v[16:19], v0
	ds_read_b128 v[20:23], v0 offset:1024
	ds_read_b128 v[24:27], v0 offset:2048
	ds_read_b128 v[28:31], v0 offset:3072
	ds_read_b128 v[0:3], v12
	ds_read_b128 v[4:7], v12 offset:1024
	ds_read_b128 v[8:11], v12 offset:2048
	ds_read_b128 v[12:15], v12 offset:3072
	s_add_i32 s55, s51, 0x80
	s_cmp_eq_u32 s39, s54
	s_cselect_b32 s64, s49, s55
	s_cselect_b32 s60, s50, s53
	s_add_i32 s55, s64, 0x80
	s_mov_b32 s57, s5
	s_mov_b32 m0, s40
	ds_read_b128 v[160:163], v181
	ds_read_b128 v[164:167], v181 offset:1024
	ds_read_b128 v[182:185], v181 offset:2048
	ds_read_b128 v[186:189], v181 offset:3072
	ds_read_b128 v[198:201], v181 offset:4096
	ds_read_b128 v[202:205], v181 offset:5120
	ds_read_b128 v[216:219], v181 offset:6144
	ds_read_b128 v[220:223], v181 offset:7168
	buffer_load_dwordx4 v173, s[56:59], s51 offen lds
	s_mov_b32 m0, s41
	s_nop 0
	buffer_load_dwordx4 v176, s[56:59], s51 offen lds
	s_waitcnt vmcnt(8)
	s_waitcnt lgkmcnt(0)
	s_barrier
	s_setprio 1
	s_waitcnt lgkmcnt(0)
	v_mfma_f32_16x16x128_f8f6f4 v[156:159], v[16:23], v[160:167], v[156:159]
	v_mfma_f32_16x16x128_f8f6f4 v[152:155], v[24:31], v[160:167], v[152:155]
	v_mfma_f32_16x16x128_f8f6f4 v[148:151], v[16:23], v[182:189], v[148:151]
	v_mfma_f32_16x16x128_f8f6f4 v[144:147], v[24:31], v[182:189], v[144:147]
	v_mfma_f32_16x16x128_f8f6f4 v[136:139], v[16:23], v[198:205], v[136:139]
	v_mfma_f32_16x16x128_f8f6f4 v[128:131], v[24:31], v[198:205], v[128:131]
	v_mfma_f32_16x16x128_f8f6f4 v[120:123], v[16:23], v[216:223], v[120:123]
	v_mfma_f32_16x16x128_f8f6f4 v[112:115], v[24:31], v[216:223], v[112:115]
	s_setprio 0
	s_setprio 1
	v_mfma_f32_16x16x128_f8f6f4 v[140:143], v[0:7], v[160:167], v[140:143]
	v_mfma_f32_16x16x128_f8f6f4 v[132:135], v[8:15], v[160:167], v[132:135]
	v_mfma_f32_16x16x128_f8f6f4 v[124:127], v[0:7], v[182:189], v[124:127]
	v_mfma_f32_16x16x128_f8f6f4 v[116:119], v[8:15], v[182:189], v[116:119]
	v_mfma_f32_16x16x128_f8f6f4 v[108:111], v[0:7], v[198:205], v[108:111]
	v_mfma_f32_16x16x128_f8f6f4 v[104:107], v[8:15], v[198:205], v[104:107]
	v_mfma_f32_16x16x128_f8f6f4 v[100:103], v[0:7], v[216:223], v[100:103]
	v_mfma_f32_16x16x128_f8f6f4 v[96:99], v[8:15], v[216:223], v[96:99]
	s_setprio 0
	s_barrier
	s_mov_b32 m0, s20
	ds_read_b128 v[160:163], v181 offset:16384
	ds_read_b128 v[164:167], v181 offset:17408
	ds_read_b128 v[182:185], v181 offset:18432
	ds_read_b128 v[186:189], v181 offset:19456
	ds_read_b128 v[198:201], v181 offset:20480
	ds_read_b128 v[202:205], v181 offset:21504
	ds_read_b128 v[216:219], v181 offset:22528
	ds_read_b128 v[220:223], v181 offset:23552
	buffer_load_dwordx4 v174, s[56:59], s60 offen lds
	s_mov_b32 m0, s21
	s_add_i32 s61, s60, 0x40000
	buffer_load_dwordx4 v177, s[56:59], s60 offen lds
	s_mov_b32 m0, s23
	s_nop 0
	buffer_load_dwordx4 v174, s[56:59], s61 offen lds
	s_mov_b32 m0, s24
	s_nop 0
	buffer_load_dwordx4 v177, s[56:59], s61 offen lds
	s_mov_b32 m0, s25
	s_nop 0
	buffer_load_dwordx4 v172, s[56:59], s64 offen lds
	s_mov_b32 m0, s26
	s_nop 0
	buffer_load_dwordx4 v175, s[56:59], s64 offen lds
	s_waitcnt vmcnt(8)
	s_waitcnt lgkmcnt(0)
	s_barrier
	s_setprio 1
	s_waitcnt lgkmcnt(0)
	v_mfma_f32_16x16x128_f8f6f4 v[92:95], v[16:23], v[160:167], v[92:95]
	v_mfma_f32_16x16x128_f8f6f4 v[88:91], v[24:31], v[160:167], v[88:91]
	s_waitcnt lgkmcnt(4)
	v_mfma_f32_16x16x128_f8f6f4 v[84:87], v[16:23], v[182:189], v[84:87]
	v_mfma_f32_16x16x128_f8f6f4 v[80:83], v[24:31], v[182:189], v[80:83]
	s_waitcnt lgkmcnt(2)
	v_mfma_f32_16x16x128_f8f6f4 v[72:75], v[16:23], v[198:205], v[72:75]
	v_mfma_f32_16x16x128_f8f6f4 v[64:67], v[24:31], v[198:205], v[64:67]
	s_waitcnt lgkmcnt(0)
	v_mfma_f32_16x16x128_f8f6f4 v[56:59], v[16:23], v[216:223], v[56:59]
	v_mfma_f32_16x16x128_f8f6f4 v[48:51], v[24:31], v[216:223], v[48:51]
	s_setprio 0
	s_setprio 1
	v_mfma_f32_16x16x128_f8f6f4 v[76:79], v[0:7], v[160:167], v[76:79]
	v_mfma_f32_16x16x128_f8f6f4 v[68:71], v[8:15], v[160:167], v[68:71]
	v_mfma_f32_16x16x128_f8f6f4 v[60:63], v[0:7], v[182:189], v[60:63]
	v_mfma_f32_16x16x128_f8f6f4 v[52:55], v[8:15], v[182:189], v[52:55]
	v_mfma_f32_16x16x128_f8f6f4 v[44:47], v[0:7], v[198:205], v[44:47]
	v_mfma_f32_16x16x128_f8f6f4 v[40:43], v[8:15], v[198:205], v[40:43]
	v_mfma_f32_16x16x128_f8f6f4 v[36:39], v[0:7], v[216:223], v[36:39]
	v_mfma_f32_16x16x128_f8f6f4 v[32:35], v[8:15], v[216:223], v[32:35]
	s_setprio 0
	s_barrier
	v_add_u32_e32 v12, s29, v179
	v_add_u32_e32 v28, s36, v179
	ds_read_b128 v[0:3], v12
	ds_read_b128 v[4:7], v12 offset:1024
	ds_read_b128 v[8:11], v12 offset:2048
	ds_read_b128 v[12:15], v12 offset:3072
	ds_read_b128 v[16:19], v28
	ds_read_b128 v[20:23], v28 offset:1024
	ds_read_b128 v[24:27], v28 offset:2048
	ds_read_b128 v[28:31], v28 offset:3072
	s_mov_b32 m0, s27
	ds_read_b128 v[160:163], v181 offset:32768
	ds_read_b128 v[164:167], v181 offset:33792
	ds_read_b128 v[182:185], v181 offset:34816
	ds_read_b128 v[186:189], v181 offset:35840
	ds_read_b128 v[198:201], v181 offset:36864
	ds_read_b128 v[202:205], v181 offset:37888
	ds_read_b128 v[216:219], v181 offset:38912
	ds_read_b128 v[220:223], v181 offset:39936
	buffer_load_dwordx4 v173, s[56:59], s64 offen lds
	s_mov_b32 m0, s28
	s_nop 0
	buffer_load_dwordx4 v176, s[56:59], s64 offen lds
	s_waitcnt vmcnt(8)
	s_waitcnt lgkmcnt(0)
	s_barrier
; #define PG8_STAGE(bufoff, soff, voff) do { _Pragma("unroll") for (int _i = 0; _i < 2; ++_i) \
;         __builtin_amdgcn_raw_ptr_buffer_load_lds(rs, (LAS void*)(lds + (bufoff) + ldsw + _i * 8192), 16, (int)(voff)[_i], (int)(soff), 0, 0); } while (0)
; #define PG8_MM(ai, bj, At, Bt) do { if constexpr (F8) PG8_MMA8(ai, bj, At, Bt); else PG8_MMA(ai, bj, At, Bt); } while (0)
; #define PG8_WAIT_V(n) asm volatile("s_waitcnt vmcnt(" #n ")" ::: "memory")
; #define PG8_WAIT_L(n) asm volatile("s_waitcnt lgkmcnt(" #n ")" ::: "memory")
; #define PG8_BAR __builtin_amdgcn_s_barrier()
; #define PG8_SCHED __builtin_amdgcn_sched_barrier(0)
;     ...
;             PG8_LDB(B0, 0, 0); PG8_LDB(B1, 0, 1); PG8_SCHED; PG8_LDA(At, 0, 0); PG8_STAGE(PG8_SA(1, 1), a1, vA1);
;             PG8_WAIT_V(8); PG8_WAIT_L(0); PG8_BAR; PG8_MM(0, 0, At, B0); PG8_MM(0, 1, At, B1); PG8_BAR; PG8_SCHED;
;             PG8_LDA(At, 0, 1); PG8_STAGE(PG8_SB(0, 0), b2, voffB); PG8_STAGE(PG8_SB(0, 1), b2 + hsB, voffB); PG8_STAGE(PG8_SA(0, 0), a2, w0);
;             PG8_WAIT_V(8); PG8_WAIT_L(0); PG8_BAR; PG8_MM(1, 0, At, B0); PG8_MM(1, 1, At, B1); PG8_BAR; PG8_SCHED;
;             PG8_LDB(B0, 1, 0); PG8_LDB(B1, 1, 1); PG8_SCHED; PG8_LDA(At, 1, 0); PG8_STAGE(PG8_SA(0, 1), a2, w1);
;             PG8_WAIT_V(8); PG8_WAIT_L(0); PG8_BAR; PG8_MM(0, 0, At, B0); PG8_MM(0, 1, At, B1); PG8_BAR; PG8_SCHED;
;             PG8_LDA(At, 1, 1); PG8_STAGE(PG8_SB(1, 0), b3, voffB); PG8_STAGE(PG8_SB(1, 1), b3 + hsB, voffB); PG8_STAGE(PG8_SA(1, 0), a3, w0);
;             PG8_WAIT_V(8); PG8_WAIT_L(0); PG8_BAR; PG8_MM(1, 0, At, B0); PG8_MM(1, 1, At, B1); PG8_BAR; PG8_SCHED;
;     __device__ __forceinline__ void operator()(AccRef acc, const pg8::Unit& u, int wr, int wc, int fr, int fq) const {
;     ...
;             for (int m = 0; m < 4; ++m) { const size_t ro = (size_t)(row0 + ai * 128 + m * 16) * DM + col0;
; #pragma unroll
;                 for (int bj = 0; bj < 2; ++bj) { const u32x4 r = *(const u32x4*)(res + ro + bj * 128);
;                     const f32x4 v0 = acc[ai][bj][m][0] * (1.f / (CAT_SCALE * WOUT_SCALE)), v1 = acc[ai][bj][m][1] * (1.f / (CAT_SCALE * WOUT_SCALE));
	s_setprio 1
	s_waitcnt lgkmcnt(0)
	v_mfma_f32_16x16x128_f8f6f4 v[156:159], v[0:7], v[160:167], v[156:159]
	v_mfma_f32_16x16x128_f8f6f4 v[152:155], v[8:15], v[160:167], v[152:155]
	s_waitcnt lgkmcnt(4)
	v_mfma_f32_16x16x128_f8f6f4 v[148:151], v[0:7], v[182:189], v[148:151]
	v_mfma_f32_16x16x128_f8f6f4 v[144:147], v[8:15], v[182:189], v[144:147]
	s_waitcnt lgkmcnt(2)
	v_mfma_f32_16x16x128_f8f6f4 v[136:139], v[0:7], v[198:205], v[136:139]
	v_mfma_f32_16x16x128_f8f6f4 v[128:131], v[8:15], v[198:205], v[128:131]
	s_waitcnt lgkmcnt(0)
	v_mfma_f32_16x16x128_f8f6f4 v[120:123], v[0:7], v[216:223], v[120:123]
	v_mfma_f32_16x16x128_f8f6f4 v[112:115], v[8:15], v[216:223], v[112:115]
	s_setprio 0
	s_setprio 1
	v_mfma_f32_16x16x128_f8f6f4 v[140:143], v[16:23], v[160:167], v[140:143]
	v_mfma_f32_16x16x128_f8f6f4 v[132:135], v[24:31], v[160:167], v[132:135]
	v_mfma_f32_16x16x128_f8f6f4 v[124:127], v[16:23], v[182:189], v[124:127]
	v_mfma_f32_16x16x128_f8f6f4 v[116:119], v[24:31], v[182:189], v[116:119]
	v_mfma_f32_16x16x128_f8f6f4 v[108:111], v[16:23], v[198:205], v[108:111]
	v_mfma_f32_16x16x128_f8f6f4 v[104:107], v[24:31], v[198:205], v[104:107]
	v_mfma_f32_16x16x128_f8f6f4 v[100:103], v[16:23], v[216:223], v[100:103]
	v_mfma_f32_16x16x128_f8f6f4 v[96:99], v[24:31], v[216:223], v[96:99]
	s_setprio 0
	s_barrier
	s_mov_b32 m0, s30
	s_add_i32 s61, s60, 0x80
	ds_read_b128 v[160:163], v181 offset:49152
	ds_read_b128 v[164:167], v181 offset:50176
	ds_read_b128 v[182:185], v181 offset:51200
	ds_read_b128 v[186:189], v181 offset:52224
	ds_read_b128 v[198:201], v181 offset:53248
	ds_read_b128 v[202:205], v181 offset:54272
	ds_read_b128 v[216:219], v181 offset:55296
	ds_read_b128 v[220:223], v181 offset:56320
	buffer_load_dwordx4 v174, s[56:59], s61 offen lds
	s_mov_b32 m0, s31
	s_add_i32 s60, s60, 0x40080
	buffer_load_dwordx4 v177, s[56:59], s61 offen lds
	s_mov_b32 m0, s37
	s_nop 0
	buffer_load_dwordx4 v174, s[56:59], s60 offen lds
	s_mov_b32 m0, s38
	s_nop 0
	buffer_load_dwordx4 v177, s[56:59], s60 offen lds
	s_mov_b32 m0, s34
	s_nop 0
	buffer_load_dwordx4 v172, s[56:59], s55 offen lds
	s_mov_b32 m0, s35
	s_nop 0
	buffer_load_dwordx4 v175, s[56:59], s55 offen lds
	s_waitcnt vmcnt(8)
	s_waitcnt lgkmcnt(0)
	s_barrier
	s_setprio 1
	s_waitcnt lgkmcnt(0)
	v_mfma_f32_16x16x128_f8f6f4 v[92:95], v[0:7], v[160:167], v[92:95]
	v_mfma_f32_16x16x128_f8f6f4 v[88:91], v[8:15], v[160:167], v[88:91]
	s_waitcnt lgkmcnt(4)
	v_mfma_f32_16x16x128_f8f6f4 v[84:87], v[0:7], v[182:189], v[84:87]
	v_mfma_f32_16x16x128_f8f6f4 v[80:83], v[8:15], v[182:189], v[80:83]
	s_waitcnt lgkmcnt(2)
	v_mfma_f32_16x16x128_f8f6f4 v[72:75], v[0:7], v[198:205], v[72:75]
	v_mfma_f32_16x16x128_f8f6f4 v[64:67], v[8:15], v[198:205], v[64:67]
	s_waitcnt lgkmcnt(0)
	v_mfma_f32_16x16x128_f8f6f4 v[56:59], v[0:7], v[216:223], v[56:59]
	v_mfma_f32_16x16x128_f8f6f4 v[48:51], v[8:15], v[216:223], v[48:51]
	s_setprio 0
	s_setprio 1
	v_mfma_f32_16x16x128_f8f6f4 v[76:79], v[16:23], v[160:167], v[76:79]
	v_mfma_f32_16x16x128_f8f6f4 v[68:71], v[24:31], v[160:167], v[68:71]
	v_mfma_f32_16x16x128_f8f6f4 v[60:63], v[16:23], v[182:189], v[60:63]
	v_mfma_f32_16x16x128_f8f6f4 v[52:55], v[24:31], v[182:189], v[52:55]
	v_mfma_f32_16x16x128_f8f6f4 v[44:47], v[16:23], v[198:205], v[44:47]
	v_mfma_f32_16x16x128_f8f6f4 v[40:43], v[24:31], v[198:205], v[40:43]
	v_mfma_f32_16x16x128_f8f6f4 v[36:39], v[16:23], v[216:223], v[36:39]
	v_mfma_f32_16x16x128_f8f6f4 v[32:35], v[24:31], v[216:223], v[32:35]
	s_setprio 0
	s_barrier
	s_add_i32 s54, s54, 2
	s_addk_i32 s51, 0x100
	s_addk_i32 s53, 0x100
	s_cmp_ge_i32 s54, s4
	s_cbranch_scc0 .LBB0_827
	v_readlane_b32 s60, v255, 33
	v_pk_mul_f32 v[164:165], v[158:159], s[88:89] op_sel_hi:[1,0]
	v_pk_mul_f32 v[166:167], v[156:157], s[88:89] op_sel_hi:[1,0]
	v_pk_mul_f32 v[168:169], v[154:155], s[88:89] op_sel_hi:[1,0]
	v_pk_mul_f32 v[170:171], v[152:153], s[88:89] op_sel_hi:[1,0]
	v_pk_mul_f32 v[156:157], v[142:143], s[88:89] op_sel_hi:[1,0]
	v_pk_mul_f32 v[158:159], v[140:141], s[88:89] op_sel_hi:[1,0]
	v_pk_mul_f32 v[160:161], v[134:135], s[88:89] op_sel_hi:[1,0]
	v_pk_mul_f32 v[162:163], v[132:133], s[88:89] op_sel_hi:[1,0]
	v_pk_mul_f32 v[150:151], v[150:151], s[88:89] op_sel_hi:[1,0]
	v_pk_mul_f32 v[148:149], v[148:149], s[88:89] op_sel_hi:[1,0]
	v_pk_mul_f32 v[152:153], v[146:147], s[88:89] op_sel_hi:[1,0]
	v_pk_mul_f32 v[154:155], v[144:145], s[88:89] op_sel_hi:[1,0]
	v_pk_mul_f32 v[140:141], v[126:127], s[88:89] op_sel_hi:[1,0]
	v_pk_mul_f32 v[142:143], v[124:125], s[88:89] op_sel_hi:[1,0]
	v_pk_mul_f32 v[144:145], v[118:119], s[88:89] op_sel_hi:[1,0]
	v_pk_mul_f32 v[146:147], v[116:117], s[88:89] op_sel_hi:[1,0]
	v_pk_mul_f32 v[132:133], v[138:139], s[88:89] op_sel_hi:[1,0]
	v_pk_mul_f32 v[134:135], v[136:137], s[88:89] op_sel_hi:[1,0]
	v_pk_mul_f32 v[136:137], v[130:131], s[88:89] op_sel_hi:[1,0]
	v_pk_mul_f32 v[138:139], v[128:129], s[88:89] op_sel_hi:[1,0]
	v_pk_mul_f32 v[124:125], v[110:111], s[88:89] op_sel_hi:[1,0]
	v_pk_mul_f32 v[126:127], v[108:109], s[88:89] op_sel_hi:[1,0]
	v_pk_mul_f32 v[128:129], v[106:107], s[88:89] op_sel_hi:[1,0]
	v_pk_mul_f32 v[130:131], v[104:105], s[88:89] op_sel_hi:[1,0]
	v_pk_mul_f32 v[116:117], v[122:123], s[88:89] op_sel_hi:[1,0]
	v_pk_mul_f32 v[118:119], v[120:121], s[88:89] op_sel_hi:[1,0]
	v_pk_mul_f32 v[114:115], v[114:115], s[88:89] op_sel_hi:[1,0]
	v_pk_mul_f32 v[112:113], v[112:113], s[88:89] op_sel_hi:[1,0]
	v_pk_mul_f32 v[104:105], v[102:103], s[88:89] op_sel_hi:[1,0]
	v_pk_mul_f32 v[106:107], v[100:101], s[88:89] op_sel_hi:[1,0]
	v_pk_mul_f32 v[108:109], v[98:99], s[88:89] op_sel_hi:[1,0]
	v_pk_mul_f32 v[110:111], v[96:97], s[88:89] op_sel_hi:[1,0]
; __device__ __forceinline__ unsigned cvt_pk_bf16(float lo, float hi) { unsigned r; asm volatile("v_cvt_pk_bf16_f32 %0, %1, %2" : "=v"(r) : "v"(lo), "v"(hi)); return r; }
; __device__ __forceinline__ float bflo(unsigned w) { return __uint_as_float(w << 16); }
; __device__ __forceinline__ float bfhi(unsigned w) { return __uint_as_float(w & 0xffff0000u); }
; #define PG8_BAR __builtin_amdgcn_s_barrier()
;     ...
;         if constexpr (ALIGN_EPI) { if (wr == 0) PG8_BAR; }
;         if constexpr (F8) asm volatile("s_nop 15\n\ts_nop 15" ::: "memory");
;         E(acc, cur, wr, wc, fr, fq); S.done(cur);
;     __device__ __forceinline__ void operator()(AccRef acc, const pg8::Unit& u, int wr, int wc, int fr, int fq) const {
;     ...
;         for (int ai = 0; ai < 2; ++ai)
; #pragma unroll
;             for (int m = 0; m < 4; ++m) { const size_t ro = (size_t)(row0 + ai * 128 + m * 16) * DM + col0;
; #pragma unroll
;                 for (int bj = 0; bj < 2; ++bj) { const u32x4 r = *(const u32x4*)(res + ro + bj * 128);
;                     const f32x4 v0 = acc[ai][bj][m][0] * (1.f / (CAT_SCALE * WOUT_SCALE)), v1 = acc[ai][bj][m][1] * (1.f / (CAT_SCALE * WOUT_SCALE));
;                     u32x4 w;
;                     w.x = cvt_pk_bf16(v0[0] + ALPHA * bflo(r.x), v0[1] + ALPHA * bfhi(r.x)); w.y = cvt_pk_bf16(v0[2] + ALPHA * bflo(r.y), v0[3] + ALPHA * bfhi(r.y));
;                     w.z = cvt_pk_bf16(v1[0] + ALPHA * bflo(r.z), v1[1] + ALPHA * bfhi(r.z)); w.w = cvt_pk_bf16(v1[2] + ALPHA * bflo(r.w), v1[3] + ALPHA * bfhi(r.w));
;                     *(u32x4*)(C + ro + bj * 128) = w; } }
	v_pk_mul_f32 v[96:97], v[94:95], s[88:89] op_sel_hi:[1,0]
	v_pk_mul_f32 v[98:99], v[92:93], s[88:89] op_sel_hi:[1,0]
	v_pk_mul_f32 v[100:101], v[90:91], s[88:89] op_sel_hi:[1,0]
	v_pk_mul_f32 v[102:103], v[88:89], s[88:89] op_sel_hi:[1,0]
	v_pk_mul_f32 v[88:89], v[78:79], s[88:89] op_sel_hi:[1,0]
	v_pk_mul_f32 v[90:91], v[76:77], s[88:89] op_sel_hi:[1,0]
	v_pk_mul_f32 v[92:93], v[70:71], s[88:89] op_sel_hi:[1,0]
	v_pk_mul_f32 v[94:95], v[68:69], s[88:89] op_sel_hi:[1,0]
	v_pk_mul_f32 v[68:69], v[86:87], s[88:89] op_sel_hi:[1,0]
	v_pk_mul_f32 v[70:71], v[84:85], s[88:89] op_sel_hi:[1,0]
	v_pk_mul_f32 v[76:77], v[82:83], s[88:89] op_sel_hi:[1,0]
	v_pk_mul_f32 v[78:79], v[80:81], s[88:89] op_sel_hi:[1,0]
	v_pk_mul_f32 v[62:63], v[62:63], s[88:89] op_sel_hi:[1,0]
	v_pk_mul_f32 v[60:61], v[60:61], s[88:89] op_sel_hi:[1,0]
	v_pk_mul_f32 v[54:55], v[54:55], s[88:89] op_sel_hi:[1,0]
	v_pk_mul_f32 v[52:53], v[52:53], s[88:89] op_sel_hi:[1,0]
	v_pk_mul_f32 v[24:25], v[74:75], s[88:89] op_sel_hi:[1,0]
	v_pk_mul_f32 v[26:27], v[72:73], s[88:89] op_sel_hi:[1,0]
	v_pk_mul_f32 v[28:29], v[66:67], s[88:89] op_sel_hi:[1,0]
	v_pk_mul_f32 v[30:31], v[64:65], s[88:89] op_sel_hi:[1,0]
	v_pk_mul_f32 v[16:17], v[46:47], s[88:89] op_sel_hi:[1,0]
	v_pk_mul_f32 v[18:19], v[44:45], s[88:89] op_sel_hi:[1,0]
	v_pk_mul_f32 v[20:21], v[42:43], s[88:89] op_sel_hi:[1,0]
	v_pk_mul_f32 v[22:23], v[40:41], s[88:89] op_sel_hi:[1,0]
	v_pk_mul_f32 v[8:9], v[58:59], s[88:89] op_sel_hi:[1,0]
	v_pk_mul_f32 v[10:11], v[56:57], s[88:89] op_sel_hi:[1,0]
	v_pk_mul_f32 v[12:13], v[50:51], s[88:89] op_sel_hi:[1,0]
	v_pk_mul_f32 v[14:15], v[48:49], s[88:89] op_sel_hi:[1,0]
	v_pk_mul_f32 v[0:1], v[38:39], s[88:89] op_sel_hi:[1,0]
	v_pk_mul_f32 v[2:3], v[36:37], s[88:89] op_sel_hi:[1,0]
	v_pk_mul_f32 v[4:5], v[34:35], s[88:89] op_sel_hi:[1,0]
	v_pk_mul_f32 v[6:7], v[32:33], s[88:89] op_sel_hi:[1,0]
	v_readlane_b32 s61, v255, 34
.LBB0_829:
	s_and_b64 vcc, exec, s[12:13]
	s_cbranch_vccz .LBB0_831
	s_barrier
.LBB0_831:
	v_lshl_add_u32 v36, s48, 8, v178
	v_lshl_or_b32 v34, s47, 8, v180
	v_ashrrev_i32_e32 v37, 31, v36
	v_ashrrev_i32_e32 v35, 31, v34
	v_lshlrev_b64 v[32:33], 11, v[36:37]
	v_lshl_add_u64 v[32:33], v[32:33], 0, v[34:35]
	v_lshlrev_b64 v[32:33], 1, v[32:33]
	s_nop 15
	s_nop 15
	v_lshl_add_u64 v[42:43], s[10:11], 0, v[32:33]
	flat_load_dwordx4 v[38:41], v[42:43]
	v_lshl_add_u64 v[48:49], s[8:9], 0, v[32:33]
	s_mov_b64 s[48:49], 0x80000
	s_andn2_b64 vcc, exec, s[0:1]
	s_mov_b64 s[0:1], -1
	s_waitcnt vmcnt(0) lgkmcnt(0)
	v_lshlrev_b32_e32 v37, 16, v38
	v_and_b32_e32 v38, 0xffff0000, v38
	v_lshlrev_b32_e32 v44, 16, v39
	v_and_b32_e32 v39, 0xffff0000, v39
	v_lshlrev_b32_e32 v45, 16, v40
	v_and_b32_e32 v40, 0xffff0000, v40
	v_lshlrev_b32_e32 v46, 16, v41
	v_and_b32_e32 v41, 0xffff0000, v41
	v_fmac_f32_e32 v166, 0x3fd744fd, v37
	v_fmac_f32_e32 v167, 0x3fd744fd, v38
	v_fmac_f32_e32 v164, 0x3fd744fd, v44
	v_fmac_f32_e32 v165, 0x3fd744fd, v39
	v_fmac_f32_e32 v170, 0x3fd744fd, v45
	v_fmac_f32_e32 v171, 0x3fd744fd, v40
	v_fmac_f32_e32 v168, 0x3fd744fd, v46
	v_fmac_f32_e32 v169, 0x3fd744fd, v41
	v_cvt_pk_bf16_f32 v38, v166, v167
	v_cvt_pk_bf16_f32 v39, v164, v165
	v_cvt_pk_bf16_f32 v40, v170, v171
	v_cvt_pk_bf16_f32 v41, v168, v169
	flat_load_dwordx4 v[42:45], v[42:43] offset:256
	v_or_b32_e32 v46, 16, v36
	v_ashrrev_i32_e32 v47, 31, v46
	v_lshlrev_b64 v[46:47], 11, v[46:47]
	v_lshl_add_u64 v[46:47], v[46:47], 0, v[34:35]
	v_lshlrev_b64 v[46:47], 1, v[46:47]
	flat_store_dwordx4 v[48:49], v[38:41]
	v_lshl_add_u64 v[50:51], s[10:11], 0, v[46:47]
	v_lshl_add_u64 v[46:47], s[8:9], 0, v[46:47]
	s_waitcnt vmcnt(0) lgkmcnt(0)
	v_lshlrev_b32_e32 v37, 16, v42
	v_and_b32_e32 v38, 0xffff0000, v42
	v_lshlrev_b32_e32 v39, 16, v43
	v_and_b32_e32 v40, 0xffff0000, v43
	v_lshlrev_b32_e32 v41, 16, v44
	v_and_b32_e32 v42, 0xffff0000, v44
	v_lshlrev_b32_e32 v43, 16, v45
	v_and_b32_e32 v44, 0xffff0000, v45
	v_fmac_f32_e32 v158, 0x3fd744fd, v37
	v_fmac_f32_e32 v159, 0x3fd744fd, v38
	v_fmac_f32_e32 v156, 0x3fd744fd, v39
	v_fmac_f32_e32 v157, 0x3fd744fd, v40
	v_fmac_f32_e32 v162, 0x3fd744fd, v41
	v_fmac_f32_e32 v163, 0x3fd744fd, v42
	v_fmac_f32_e32 v160, 0x3fd744fd, v43
	v_fmac_f32_e32 v161, 0x3fd744fd, v44
	v_cvt_pk_bf16_f32 v38, v158, v159
	v_cvt_pk_bf16_f32 v39, v156, v157
	v_cvt_pk_bf16_f32 v40, v162, v163
	v_cvt_pk_bf16_f32 v41, v160, v161
	flat_store_dwordx4 v[48:49], v[38:41] offset:256
	flat_load_dwordx4 v[38:41], v[50:51]
	v_or_b32_e32 v48, 32, v36
	v_ashrrev_i32_e32 v49, 31, v48
	v_lshlrev_b64 v[48:49], 11, v[48:49]
	v_lshl_add_u64 v[48:49], v[48:49], 0, v[34:35]
	v_lshlrev_b64 v[48:49], 1, v[48:49]
	v_or_b32_e32 v36, 48, v36
	s_waitcnt vmcnt(0) lgkmcnt(0)
	v_lshlrev_b32_e32 v37, 16, v38
	v_and_b32_e32 v38, 0xffff0000, v38
	v_lshlrev_b32_e32 v42, 16, v39
	v_and_b32_e32 v39, 0xffff0000, v39
	v_lshlrev_b32_e32 v43, 16, v40
	v_and_b32_e32 v40, 0xffff0000, v40
	v_lshlrev_b32_e32 v44, 16, v41
	v_and_b32_e32 v41, 0xffff0000, v41
	v_fmac_f32_e32 v148, 0x3fd744fd, v37
	v_fmac_f32_e32 v149, 0x3fd744fd, v38
	v_fmac_f32_e32 v150, 0x3fd744fd, v42
	v_fmac_f32_e32 v151, 0x3fd744fd, v39
	v_fmac_f32_e32 v154, 0x3fd744fd, v43
	v_fmac_f32_e32 v155, 0x3fd744fd, v40
	v_fmac_f32_e32 v152, 0x3fd744fd, v44
	v_fmac_f32_e32 v153, 0x3fd744fd, v41
	v_cvt_pk_bf16_f32 v38, v148, v149
	v_cvt_pk_bf16_f32 v39, v150, v151
	v_cvt_pk_bf16_f32 v40, v154, v155
	v_cvt_pk_bf16_f32 v41, v152, v153
	flat_load_dwordx4 v[42:45], v[50:51] offset:256
	v_lshl_add_u64 v[50:51], s[10:11], 0, v[48:49]
	flat_store_dwordx4 v[46:47], v[38:41]
	v_lshl_add_u64 v[48:49], s[8:9], 0, v[48:49]
	s_waitcnt vmcnt(0) lgkmcnt(0)
; __device__ __forceinline__ unsigned cvt_pk_bf16(float lo, float hi) { unsigned r; asm volatile("v_cvt_pk_bf16_f32 %0, %1, %2" : "=v"(r) : "v"(lo), "v"(hi)); return r; }
; __device__ __forceinline__ float bflo(unsigned w) { return __uint_as_float(w << 16); }
; __device__ __forceinline__ float bfhi(unsigned w) { return __uint_as_float(w & 0xffff0000u); }
;     __device__ __forceinline__ void operator()(AccRef acc, const pg8::Unit& u, int wr, int wc, int fr, int fq) const {
;     ...
;         for (int ai = 0; ai < 2; ++ai)
; #pragma unroll
;             for (int m = 0; m < 4; ++m) { const size_t ro = (size_t)(row0 + ai * 128 + m * 16) * DM + col0;
; #pragma unroll
;                 for (int bj = 0; bj < 2; ++bj) { const u32x4 r = *(const u32x4*)(res + ro + bj * 128);
;                     const f32x4 v0 = acc[ai][bj][m][0] * (1.f / (CAT_SCALE * WOUT_SCALE)), v1 = acc[ai][bj][m][1] * (1.f / (CAT_SCALE * WOUT_SCALE));
;                     u32x4 w;
;                     w.x = cvt_pk_bf16(v0[0] + ALPHA * bflo(r.x), v0[1] + ALPHA * bfhi(r.x)); w.y = cvt_pk_bf16(v0[2] + ALPHA * bflo(r.y), v0[3] + ALPHA * bfhi(r.y));
;                     w.z = cvt_pk_bf16(v1[0] + ALPHA * bflo(r.z), v1[1] + ALPHA * bfhi(r.z)); w.w = cvt_pk_bf16(v1[2] + ALPHA * bflo(r.w), v1[3] + ALPHA * bfhi(r.w));
;                     *(u32x4*)(C + ro + bj * 128) = w; } }
	v_lshlrev_b32_e32 v37, 16, v42
	v_and_b32_e32 v38, 0xffff0000, v42
	v_lshlrev_b32_e32 v39, 16, v43
	v_and_b32_e32 v40, 0xffff0000, v43
	v_lshlrev_b32_e32 v41, 16, v44
	v_and_b32_e32 v42, 0xffff0000, v44
	v_lshlrev_b32_e32 v43, 16, v45
	v_and_b32_e32 v44, 0xffff0000, v45
	v_fmac_f32_e32 v142, 0x3fd744fd, v37
	v_fmac_f32_e32 v143, 0x3fd744fd, v38
	v_fmac_f32_e32 v140, 0x3fd744fd, v39
	v_fmac_f32_e32 v141, 0x3fd744fd, v40
	v_fmac_f32_e32 v146, 0x3fd744fd, v41
	v_fmac_f32_e32 v147, 0x3fd744fd, v42
	v_fmac_f32_e32 v144, 0x3fd744fd, v43
	v_fmac_f32_e32 v145, 0x3fd744fd, v44
	v_cvt_pk_bf16_f32 v38, v142, v143
	v_cvt_pk_bf16_f32 v39, v140, v141
	v_cvt_pk_bf16_f32 v40, v146, v147
	v_cvt_pk_bf16_f32 v41, v144, v145
	flat_store_dwordx4 v[46:47], v[38:41] offset:256
	flat_load_dwordx4 v[38:41], v[50:51]
	s_waitcnt vmcnt(0) lgkmcnt(0)
	v_lshlrev_b32_e32 v37, 16, v38
	v_and_b32_e32 v38, 0xffff0000, v38
	v_lshlrev_b32_e32 v42, 16, v39
	v_and_b32_e32 v39, 0xffff0000, v39
	v_lshlrev_b32_e32 v43, 16, v40
	v_and_b32_e32 v40, 0xffff0000, v40
	v_lshlrev_b32_e32 v44, 16, v41
	v_and_b32_e32 v41, 0xffff0000, v41
	v_fmac_f32_e32 v134, 0x3fd744fd, v37
	v_fmac_f32_e32 v135, 0x3fd744fd, v38
	v_fmac_f32_e32 v132, 0x3fd744fd, v42
	v_fmac_f32_e32 v133, 0x3fd744fd, v39
	v_fmac_f32_e32 v138, 0x3fd744fd, v43
	v_fmac_f32_e32 v139, 0x3fd744fd, v40
	v_fmac_f32_e32 v136, 0x3fd744fd, v44
	v_fmac_f32_e32 v137, 0x3fd744fd, v41
	v_cvt_pk_bf16_f32 v38, v134, v135
	v_cvt_pk_bf16_f32 v39, v132, v133
	v_cvt_pk_bf16_f32 v40, v138, v139
	v_cvt_pk_bf16_f32 v41, v136, v137
	flat_load_dwordx4 v[42:45], v[50:51] offset:256
	v_ashrrev_i32_e32 v37, 31, v36
	v_lshlrev_b64 v[36:37], 11, v[36:37]
	v_lshl_add_u64 v[34:35], v[36:37], 0, v[34:35]
	v_lshlrev_b64 v[46:47], 1, v[34:35]
	flat_store_dwordx4 v[48:49], v[38:41]
	v_lshl_add_u64 v[50:51], s[10:11], 0, v[46:47]
	s_waitcnt vmcnt(0) lgkmcnt(0)
	v_lshlrev_b32_e32 v34, 16, v42
	v_and_b32_e32 v35, 0xffff0000, v42
	v_lshlrev_b32_e32 v36, 16, v43
	v_and_b32_e32 v37, 0xffff0000, v43
	v_lshlrev_b32_e32 v38, 16, v44
	v_and_b32_e32 v39, 0xffff0000, v44
	v_lshlrev_b32_e32 v40, 16, v45
	v_and_b32_e32 v41, 0xffff0000, v45
	v_fmac_f32_e32 v126, 0x3fd744fd, v34
	v_fmac_f32_e32 v127, 0x3fd744fd, v35
	v_fmac_f32_e32 v124, 0x3fd744fd, v36
	v_fmac_f32_e32 v125, 0x3fd744fd, v37
	v_fmac_f32_e32 v130, 0x3fd744fd, v38
	v_fmac_f32_e32 v131, 0x3fd744fd, v39
	v_fmac_f32_e32 v128, 0x3fd744fd, v40
	v_fmac_f32_e32 v129, 0x3fd744fd, v41
	v_cvt_pk_bf16_f32 v34, v126, v127
	v_cvt_pk_bf16_f32 v35, v124, v125
	v_cvt_pk_bf16_f32 v36, v130, v131
	v_cvt_pk_bf16_f32 v37, v128, v129
	flat_store_dwordx4 v[48:49], v[34:37] offset:256
	flat_load_dwordx4 v[34:37], v[50:51]
	v_lshl_add_u64 v[44:45], s[8:9], 0, v[46:47]
	v_lshl_add_u64 v[42:43], v[32:33], 0, s[48:49]
	v_lshl_add_u64 v[46:47], s[10:11], 0, v[42:43]
	s_mov_b64 s[48:49], 0x90000
	v_lshl_add_u64 v[42:43], s[8:9], 0, v[42:43]
	s_waitcnt vmcnt(0) lgkmcnt(0)
	v_lshlrev_b32_e32 v38, 16, v34
	v_and_b32_e32 v34, 0xffff0000, v34
	v_lshlrev_b32_e32 v39, 16, v35
	v_and_b32_e32 v35, 0xffff0000, v35
	v_lshlrev_b32_e32 v40, 16, v36
	v_and_b32_e32 v36, 0xffff0000, v36
	v_lshlrev_b32_e32 v41, 16, v37
	v_and_b32_e32 v37, 0xffff0000, v37
	v_fmac_f32_e32 v118, 0x3fd744fd, v38
	v_fmac_f32_e32 v119, 0x3fd744fd, v34
	v_fmac_f32_e32 v116, 0x3fd744fd, v39
	v_fmac_f32_e32 v117, 0x3fd744fd, v35
	v_fmac_f32_e32 v112, 0x3fd744fd, v40
	v_fmac_f32_e32 v113, 0x3fd744fd, v36
	v_fmac_f32_e32 v114, 0x3fd744fd, v41
	v_fmac_f32_e32 v115, 0x3fd744fd, v37
	v_cvt_pk_bf16_f32 v34, v118, v119
	v_cvt_pk_bf16_f32 v35, v116, v117
	v_cvt_pk_bf16_f32 v36, v112, v113
	v_cvt_pk_bf16_f32 v37, v114, v115
	flat_load_dwordx4 v[38:41], v[50:51] offset:256
	s_nop 0
	flat_store_dwordx4 v[44:45], v[34:37]
	s_waitcnt vmcnt(0) lgkmcnt(0)
	s_nop 0
	v_lshlrev_b32_e32 v34, 16, v38
	v_and_b32_e32 v35, 0xffff0000, v38
	v_lshlrev_b32_e32 v36, 16, v39
	v_and_b32_e32 v37, 0xffff0000, v39
	v_lshlrev_b32_e32 v38, 16, v40
	v_and_b32_e32 v39, 0xffff0000, v40
	v_lshlrev_b32_e32 v40, 16, v41
	v_and_b32_e32 v41, 0xffff0000, v41
	v_fmac_f32_e32 v106, 0x3fd744fd, v34
	v_fmac_f32_e32 v107, 0x3fd744fd, v35
	v_fmac_f32_e32 v104, 0x3fd744fd, v36
	v_fmac_f32_e32 v105, 0x3fd744fd, v37
	v_fmac_f32_e32 v110, 0x3fd744fd, v38
	v_fmac_f32_e32 v111, 0x3fd744fd, v39
	v_fmac_f32_e32 v108, 0x3fd744fd, v40
	v_fmac_f32_e32 v109, 0x3fd744fd, v41
	v_cvt_pk_bf16_f32 v34, v106, v107
	v_cvt_pk_bf16_f32 v35, v104, v105
	v_cvt_pk_bf16_f32 v36, v110, v111
	v_cvt_pk_bf16_f32 v37, v108, v109
	flat_store_dwordx4 v[44:45], v[34:37] offset:256
	flat_load_dwordx4 v[34:37], v[46:47]
	v_lshl_add_u64 v[44:45], v[32:33], 0, s[48:49]
	s_mov_b64 s[48:49], 0xa0000
	s_waitcnt vmcnt(0) lgkmcnt(0)
	v_lshlrev_b32_e32 v38, 16, v34
	v_and_b32_e32 v34, 0xffff0000, v34
	v_lshlrev_b32_e32 v39, 16, v35
	v_and_b32_e32 v35, 0xffff0000, v35
	v_lshlrev_b32_e32 v40, 16, v36
	v_and_b32_e32 v36, 0xffff0000, v36
	v_lshlrev_b32_e32 v41, 16, v37
	v_and_b32_e32 v37, 0xffff0000, v37
	v_fmac_f32_e32 v98, 0x3fd744fd, v38
	v_fmac_f32_e32 v99, 0x3fd744fd, v34
	v_fmac_f32_e32 v96, 0x3fd744fd, v39
	v_fmac_f32_e32 v97, 0x3fd744fd, v35
	v_fmac_f32_e32 v102, 0x3fd744fd, v40
	v_fmac_f32_e32 v103, 0x3fd744fd, v36
	v_fmac_f32_e32 v100, 0x3fd744fd, v41
	v_fmac_f32_e32 v101, 0x3fd744fd, v37
	v_cvt_pk_bf16_f32 v34, v98, v99
	v_cvt_pk_bf16_f32 v35, v96, v97
	v_cvt_pk_bf16_f32 v36, v102, v103
	v_cvt_pk_bf16_f32 v37, v100, v101
	flat_load_dwordx4 v[38:41], v[46:47] offset:256
	v_lshl_add_u64 v[46:47], s[10:11], 0, v[44:45]
	flat_store_dwordx4 v[42:43], v[34:37]
	v_lshl_add_u64 v[44:45], s[8:9], 0, v[44:45]
	s_waitcnt vmcnt(0) lgkmcnt(0)
; __device__ __forceinline__ unsigned cvt_pk_bf16(float lo, float hi) { unsigned r; asm volatile("v_cvt_pk_bf16_f32 %0, %1, %2" : "=v"(r) : "v"(lo), "v"(hi)); return r; }
; __device__ __forceinline__ float bflo(unsigned w) { return __uint_as_float(w << 16); }
; __device__ __forceinline__ float bfhi(unsigned w) { return __uint_as_float(w & 0xffff0000u); }
; #define PG8_BAR __builtin_amdgcn_s_barrier()
;     ...
;         if (!has_next) break;
; #pragma unroll
;         for (int a = 0; a < 2; ++a)
; #pragma unroll
;             for (int b = 0; b < 2; ++b)
; #pragma unroll
;                 for (int m = 0; m < 4; ++m)
; #pragma unroll
;                     for (int n = 0; n < 2; ++n) acc[a][b][m][n] = (f32x4){0.f, 0.f, 0.f, 0.f};
;         cur = nxt; cA = nA; cB = nB; ++ui;
; #pragma unroll
;         for (int _i = 0; _i < 2; ++_i) { vA0[_i] = nA0[_i]; vA1[_i] = nA1[_i]; }
;         if constexpr (ALIGN_EPI) { if (wr == 1) PG8_BAR; }
;     }
;     __device__ __forceinline__ void operator()(AccRef acc, const pg8::Unit& u, int wr, int wc, int fr, int fq) const {
;     ...
;         for (int ai = 0; ai < 2; ++ai)
; #pragma unroll
;             for (int m = 0; m < 4; ++m) { const size_t ro = (size_t)(row0 + ai * 128 + m * 16) * DM + col0;
; #pragma unroll
;                 for (int bj = 0; bj < 2; ++bj) { const u32x4 r = *(const u32x4*)(res + ro + bj * 128);
;                     const f32x4 v0 = acc[ai][bj][m][0] * (1.f / (CAT_SCALE * WOUT_SCALE)), v1 = acc[ai][bj][m][1] * (1.f / (CAT_SCALE * WOUT_SCALE));
;                     u32x4 w;
;                     w.x = cvt_pk_bf16(v0[0] + ALPHA * bflo(r.x), v0[1] + ALPHA * bfhi(r.x)); w.y = cvt_pk_bf16(v0[2] + ALPHA * bflo(r.y), v0[3] + ALPHA * bfhi(r.y));
;                     w.z = cvt_pk_bf16(v1[0] + ALPHA * bflo(r.z), v1[1] + ALPHA * bfhi(r.z)); w.w = cvt_pk_bf16(v1[2] + ALPHA * bflo(r.w), v1[3] + ALPHA * bfhi(r.w));
;                     *(u32x4*)(C + ro + bj * 128) = w; } }
	v_lshlrev_b32_e32 v34, 16, v38
	v_and_b32_e32 v35, 0xffff0000, v38
	v_lshlrev_b32_e32 v36, 16, v39
	v_and_b32_e32 v37, 0xffff0000, v39
	v_lshlrev_b32_e32 v38, 16, v40
	v_and_b32_e32 v39, 0xffff0000, v40
	v_lshlrev_b32_e32 v40, 16, v41
	v_and_b32_e32 v41, 0xffff0000, v41
	v_fmac_f32_e32 v90, 0x3fd744fd, v34
	v_fmac_f32_e32 v91, 0x3fd744fd, v35
	v_fmac_f32_e32 v88, 0x3fd744fd, v36
	v_fmac_f32_e32 v89, 0x3fd744fd, v37
	v_fmac_f32_e32 v94, 0x3fd744fd, v38
	v_fmac_f32_e32 v95, 0x3fd744fd, v39
	v_fmac_f32_e32 v92, 0x3fd744fd, v40
	v_fmac_f32_e32 v93, 0x3fd744fd, v41
	v_cvt_pk_bf16_f32 v34, v90, v91
	v_cvt_pk_bf16_f32 v35, v88, v89
	v_cvt_pk_bf16_f32 v36, v94, v95
	v_cvt_pk_bf16_f32 v37, v92, v93
	flat_store_dwordx4 v[42:43], v[34:37] offset:256
	flat_load_dwordx4 v[34:37], v[46:47]
	v_lshl_add_u64 v[42:43], v[32:33], 0, s[48:49]
	s_mov_b64 s[48:49], 0xb0000
	s_waitcnt vmcnt(0) lgkmcnt(0)
	v_lshlrev_b32_e32 v38, 16, v34
	v_and_b32_e32 v34, 0xffff0000, v34
	v_lshlrev_b32_e32 v39, 16, v35
	v_and_b32_e32 v35, 0xffff0000, v35
	v_lshlrev_b32_e32 v40, 16, v36
	v_and_b32_e32 v36, 0xffff0000, v36
	v_lshlrev_b32_e32 v41, 16, v37
	v_and_b32_e32 v37, 0xffff0000, v37
	v_fmac_f32_e32 v70, 0x3fd744fd, v38
	v_fmac_f32_e32 v71, 0x3fd744fd, v34
	v_fmac_f32_e32 v68, 0x3fd744fd, v39
	v_fmac_f32_e32 v69, 0x3fd744fd, v35
	v_fmac_f32_e32 v78, 0x3fd744fd, v40
	v_fmac_f32_e32 v79, 0x3fd744fd, v36
	v_fmac_f32_e32 v76, 0x3fd744fd, v41
	v_fmac_f32_e32 v77, 0x3fd744fd, v37
	v_cvt_pk_bf16_f32 v34, v70, v71
	v_cvt_pk_bf16_f32 v35, v68, v69
	v_cvt_pk_bf16_f32 v36, v78, v79
	v_cvt_pk_bf16_f32 v37, v76, v77
	flat_load_dwordx4 v[38:41], v[46:47] offset:256
	v_lshl_add_u64 v[46:47], s[10:11], 0, v[42:43]
	flat_store_dwordx4 v[44:45], v[34:37]
	s_waitcnt vmcnt(0) lgkmcnt(0)
	s_nop 0
	v_lshlrev_b32_e32 v34, 16, v38
	v_and_b32_e32 v35, 0xffff0000, v38
	v_lshlrev_b32_e32 v36, 16, v39
	v_and_b32_e32 v37, 0xffff0000, v39
	v_lshlrev_b32_e32 v38, 16, v40
	v_and_b32_e32 v39, 0xffff0000, v40
	v_lshlrev_b32_e32 v40, 16, v41
	v_and_b32_e32 v41, 0xffff0000, v41
	v_fmac_f32_e32 v60, 0x3fd744fd, v34
	v_fmac_f32_e32 v61, 0x3fd744fd, v35
	v_fmac_f32_e32 v62, 0x3fd744fd, v36
	v_fmac_f32_e32 v63, 0x3fd744fd, v37
	v_fmac_f32_e32 v52, 0x3fd744fd, v38
	v_fmac_f32_e32 v53, 0x3fd744fd, v39
	v_fmac_f32_e32 v54, 0x3fd744fd, v40
	v_fmac_f32_e32 v55, 0x3fd744fd, v41
	v_cvt_pk_bf16_f32 v34, v60, v61
	v_cvt_pk_bf16_f32 v35, v62, v63
	v_cvt_pk_bf16_f32 v36, v52, v53
	v_cvt_pk_bf16_f32 v37, v54, v55
	flat_store_dwordx4 v[44:45], v[34:37] offset:256
	flat_load_dwordx4 v[34:37], v[46:47]
	s_waitcnt vmcnt(0) lgkmcnt(0)
	v_lshlrev_b32_e32 v38, 16, v34
	v_and_b32_e32 v34, 0xffff0000, v34
	v_lshlrev_b32_e32 v39, 16, v35
	v_and_b32_e32 v35, 0xffff0000, v35
	v_lshlrev_b32_e32 v40, 16, v36
	v_and_b32_e32 v36, 0xffff0000, v36
	v_lshlrev_b32_e32 v41, 16, v37
	v_and_b32_e32 v37, 0xffff0000, v37
	v_fmac_f32_e32 v26, 0x3fd744fd, v38
	v_fmac_f32_e32 v27, 0x3fd744fd, v34
	v_fmac_f32_e32 v24, 0x3fd744fd, v39
	v_fmac_f32_e32 v25, 0x3fd744fd, v35
	v_fmac_f32_e32 v30, 0x3fd744fd, v40
	v_fmac_f32_e32 v31, 0x3fd744fd, v36
	v_fmac_f32_e32 v28, 0x3fd744fd, v41
	v_fmac_f32_e32 v29, 0x3fd744fd, v37
	v_cvt_pk_bf16_f32 v34, v26, v27
	v_cvt_pk_bf16_f32 v35, v24, v25
	v_cvt_pk_bf16_f32 v36, v30, v31
	v_cvt_pk_bf16_f32 v37, v28, v29
	flat_load_dwordx4 v[24:27], v[46:47] offset:256
	v_lshl_add_u64 v[30:31], s[8:9], 0, v[42:43]
	v_lshl_add_u64 v[28:29], v[32:33], 0, s[48:49]
	flat_store_dwordx4 v[30:31], v[34:37]
	v_lshl_add_u64 v[32:33], s[10:11], 0, v[28:29]
	s_waitcnt vmcnt(0) lgkmcnt(0)
	v_lshlrev_b32_e32 v34, 16, v24
	v_and_b32_e32 v24, 0xffff0000, v24
	v_lshlrev_b32_e32 v35, 16, v25
	v_and_b32_e32 v25, 0xffff0000, v25
	v_lshlrev_b32_e32 v36, 16, v26
	v_and_b32_e32 v26, 0xffff0000, v26
	v_lshlrev_b32_e32 v37, 16, v27
	v_and_b32_e32 v27, 0xffff0000, v27
	v_fmac_f32_e32 v18, 0x3fd744fd, v34
	v_fmac_f32_e32 v19, 0x3fd744fd, v24
	v_fmac_f32_e32 v16, 0x3fd744fd, v35
	v_fmac_f32_e32 v17, 0x3fd744fd, v25
	v_fmac_f32_e32 v22, 0x3fd744fd, v36
	v_fmac_f32_e32 v23, 0x3fd744fd, v26
	v_fmac_f32_e32 v20, 0x3fd744fd, v37
	v_fmac_f32_e32 v21, 0x3fd744fd, v27
	v_cvt_pk_bf16_f32 v24, v18, v19
	v_cvt_pk_bf16_f32 v25, v16, v17
	v_cvt_pk_bf16_f32 v26, v22, v23
	v_cvt_pk_bf16_f32 v27, v20, v21
	flat_store_dwordx4 v[30:31], v[24:27] offset:256
	flat_load_dwordx4 v[16:19], v[32:33]
	s_waitcnt vmcnt(0) lgkmcnt(0)
	v_lshlrev_b32_e32 v20, 16, v16
	v_and_b32_e32 v16, 0xffff0000, v16
	v_lshlrev_b32_e32 v21, 16, v17
	v_and_b32_e32 v17, 0xffff0000, v17
	v_lshlrev_b32_e32 v22, 16, v18
	v_and_b32_e32 v18, 0xffff0000, v18
	v_lshlrev_b32_e32 v23, 16, v19
	v_and_b32_e32 v19, 0xffff0000, v19
	v_fmac_f32_e32 v10, 0x3fd744fd, v20
	v_fmac_f32_e32 v11, 0x3fd744fd, v16
	v_fmac_f32_e32 v8, 0x3fd744fd, v21
	v_fmac_f32_e32 v9, 0x3fd744fd, v17
	v_fmac_f32_e32 v14, 0x3fd744fd, v22
	v_fmac_f32_e32 v15, 0x3fd744fd, v18
	v_fmac_f32_e32 v12, 0x3fd744fd, v23
	v_fmac_f32_e32 v13, 0x3fd744fd, v19
	v_cvt_pk_bf16_f32 v16, v10, v11
	v_cvt_pk_bf16_f32 v17, v8, v9
	v_cvt_pk_bf16_f32 v18, v14, v15
	v_cvt_pk_bf16_f32 v19, v12, v13
	flat_load_dwordx4 v[8:11], v[32:33] offset:256
	v_lshl_add_u64 v[12:13], s[8:9], 0, v[28:29]
	flat_store_dwordx4 v[12:13], v[16:19]
	s_waitcnt vmcnt(0) lgkmcnt(0)
	v_lshlrev_b32_e32 v14, 16, v8
	v_and_b32_e32 v8, 0xffff0000, v8
	v_lshlrev_b32_e32 v15, 16, v9
	v_and_b32_e32 v9, 0xffff0000, v9
	v_lshlrev_b32_e32 v16, 16, v10
	v_and_b32_e32 v10, 0xffff0000, v10
	v_lshlrev_b32_e32 v17, 16, v11
	v_and_b32_e32 v11, 0xffff0000, v11
	v_fmac_f32_e32 v2, 0x3fd744fd, v14
	v_fmac_f32_e32 v3, 0x3fd744fd, v8
	v_fmac_f32_e32 v0, 0x3fd744fd, v15
	v_fmac_f32_e32 v1, 0x3fd744fd, v9
	v_fmac_f32_e32 v6, 0x3fd744fd, v16
	v_fmac_f32_e32 v7, 0x3fd744fd, v10
	v_fmac_f32_e32 v4, 0x3fd744fd, v17
	v_fmac_f32_e32 v5, 0x3fd744fd, v11
	v_cvt_pk_bf16_f32 v8, v2, v3
	v_cvt_pk_bf16_f32 v9, v0, v1
	v_cvt_pk_bf16_f32 v10, v6, v7
	v_cvt_pk_bf16_f32 v11, v4, v5
	flat_store_dwordx4 v[12:13], v[8:11] offset:256
	s_cbranch_vccnz .LBB0_818
	s_andn2_b64 vcc, exec, s[2:3]
	s_cbranch_vccnz .LBB0_817
	s_barrier
	s_branch .LBB0_817

; __global__ void __launch_bounds__(NTHREADS, 2) hybrid_fwd(Args a) {
;     ...
;             for (int v = bid; v < 256; v += G) {
;                 u32x2 raw[2][8];
; #pragma unroll
;                 for (int q = 0; q < 2; ++q)
; #pragma unroll
;                     for (int j = 0; j < 8; ++j) raw[q][j] = __builtin_nontemporal_load((const u32x2*)(YB + (size_t)(v * 32 + wave + 8 * q) * DM + j * 256 + lane * 4));
;                 __syncthreads();
;                 if (tid < 16) hist[tid] = 0;
;                 __syncthreads();
;                 asm volatile("s_waitcnt vmcnt(0)" ::: "memory"); __syncthreads();
.LBB0_887:
	s_add_i32 s6, s22, s51
	s_ashr_i32 s7, s6, 31
	s_add_i32 s8, s6, 8
	s_lshl_b64 s[12:13], s[6:7], 12
	s_ashr_i32 s9, s8, 31
	v_lshl_add_u64 v[16:17], v[26:27], 0, s[12:13]
	s_lshl_b64 s[10:11], s[8:9], 12
	flat_load_dwordx2 v[58:59], v[16:17] nt
	flat_load_dwordx2 v[56:57], v[16:17] offset:512 nt
	flat_load_dwordx2 v[54:55], v[16:17] offset:1024 nt
	flat_load_dwordx2 v[52:53], v[16:17] offset:1536 nt
	flat_load_dwordx2 v[50:51], v[16:17] offset:2048 nt
	flat_load_dwordx2 v[48:49], v[16:17] offset:2560 nt
	flat_load_dwordx2 v[46:47], v[16:17] offset:3072 nt
	flat_load_dwordx2 v[44:45], v[16:17] offset:3584 nt
	v_lshl_add_u64 v[16:17], v[26:27], 0, s[10:11]
	flat_load_dwordx2 v[42:43], v[16:17] nt
	flat_load_dwordx2 v[40:41], v[16:17] offset:512 nt
	flat_load_dwordx2 v[38:39], v[16:17] offset:1024 nt
	flat_load_dwordx2 v[36:37], v[16:17] offset:1536 nt
	flat_load_dwordx2 v[22:23], v[16:17] offset:2048 nt
	flat_load_dwordx2 v[20:21], v[16:17] offset:2560 nt
	flat_load_dwordx2 v[18:19], v[16:17] offset:3072 nt
	s_nop 0
	flat_load_dwordx2 v[16:17], v[16:17] offset:3584 nt
	s_waitcnt vmcnt(0) lgkmcnt(0)
	s_barrier
	s_and_saveexec_b64 s[14:15], s[0:1]
	ds_write_b32 v156, v193
	s_or_b64 exec, exec, s[14:15]
	s_waitcnt lgkmcnt(0)
	s_barrier
	s_waitcnt vmcnt(0)
	s_add_i32 s38, s6, 16
	s_barrier
	s_mov_b64 s[14:15], s[34:35]
	v_lshlrev_b32_e32 v192, 2, v24
	s_mov_b64 s[16:17], s[36:37]
	v_lshl_add_u64 v[94:95], s[14:15], 0, v[192:193]
	v_lshlrev_b32_e32 v66, 16, v58
	v_lshl_add_u64 v[96:97], s[16:17], 0, v[192:193]
	flat_load_dwordx4 v[80:83], v[94:95]
	flat_load_dwordx4 v[86:89], v[96:97]
	v_and_b32_e32 v67, 0xffff0000, v58
	v_lshlrev_b32_e32 v64, 16, v59
	v_and_b32_e32 v65, 0xffff0000, v59
	v_add_f32_e32 v35, v66, v67
	v_add_f32_e32 v58, v64, v65
	v_lshlrev_b32_e32 v74, 16, v56
	v_and_b32_e32 v75, 0xffff0000, v56
	v_lshlrev_b32_e32 v72, 16, v57
	v_and_b32_e32 v73, 0xffff0000, v57
	v_add_f32_e32 v35, v35, v58
	v_add_f32_e32 v56, v74, v75
	v_add_f32_e32 v57, v72, v73
	v_lshlrev_b32_e32 v68, 16, v54
	v_and_b32_e32 v69, 0xffff0000, v54
	v_lshlrev_b32_e32 v70, 16, v55
	v_and_b32_e32 v71, 0xffff0000, v55
	v_add_f32_e32 v35, 0, v35
	v_add_f32_e32 v56, v56, v57
	v_add_f32_e32 v54, v68, v69
	v_add_f32_e32 v55, v70, v71
	v_lshlrev_b32_e32 v60, 16, v52
	v_and_b32_e32 v61, 0xffff0000, v52
	v_lshlrev_b32_e32 v62, 16, v53
	v_and_b32_e32 v63, 0xffff0000, v53
	v_add_f32_e32 v35, v35, v56
	v_add_f32_e32 v54, v54, v55
	v_add_f32_e32 v52, v60, v61
	v_add_f32_e32 v53, v62, v63
	v_add_f32_e32 v35, v35, v54
	v_add_f32_e32 v52, v52, v53
	v_lshlrev_b32_e32 v56, 16, v50
	v_and_b32_e32 v57, 0xffff0000, v50
	v_lshlrev_b32_e32 v58, 16, v51
	v_and_b32_e32 v59, 0xffff0000, v51
	v_add_f32_e32 v35, v35, v52
	v_add_f32_e32 v50, v56, v57
	v_add_f32_e32 v51, v58, v59
	v_lshlrev_b32_e32 v52, 16, v48
	v_and_b32_e32 v53, 0xffff0000, v48
	v_lshlrev_b32_e32 v54, 16, v49
	v_and_b32_e32 v55, 0xffff0000, v49
	v_add_f32_e32 v50, v50, v51
	v_add_f32_e32 v48, v52, v53
	v_add_f32_e32 v49, v54, v55
	v_add_f32_e32 v35, v35, v50
	v_add_f32_e32 v48, v48, v49
	v_add_f32_e32 v35, v35, v48
	v_lshlrev_b32_e32 v48, 16, v46
	v_and_b32_e32 v49, 0xffff0000, v46
	v_lshlrev_b32_e32 v50, 16, v47
	v_and_b32_e32 v51, 0xffff0000, v47
	v_add_f32_e32 v46, v48, v49
	v_add_f32_e32 v47, v50, v51
	v_add_f32_e32 v46, v46, v47
	v_add_f32_e32 v35, v35, v46
	v_lshlrev_b32_e32 v46, 16, v44
	v_and_b32_e32 v47, 0xffff0000, v44
	v_lshlrev_b32_e32 v44, 16, v45
	v_and_b32_e32 v45, 0xffff0000, v45
	v_add_f32_e32 v76, v46, v47
	v_add_f32_e32 v77, v44, v45
	v_add_f32_e32 v76, v76, v77
	v_add_f32_e32 v35, v35, v76
	s_lshl_b64 s[14:15], s[6:7], 11
	s_nop 0
	v_add_f32_dpp v35, v35, v35 quad_perm:[1,0,3,2] row_mask:0xf bank_mask:0xf bound_ctrl:1
	s_nop 1
	v_add_f32_dpp v35, v35, v35 quad_perm:[2,3,0,1] row_mask:0xf bank_mask:0xf bound_ctrl:1
	s_nop 1
	v_add_f32_dpp v35, v35, v35 row_ror:4 row_mask:0xf bank_mask:0xf bound_ctrl:1
	s_nop 1
	v_add_f32_dpp v35, v35, v35 row_ror:8 row_mask:0xf bank_mask:0xf bound_ctrl:1
	v_mov_b32_e32 v76, v35
	s_nop 1
	v_permlane16_swap_b32_e32 v35, v76
	v_add_f32_e32 v35, v35, v76
	v_mov_b32_e32 v76, v35
	s_nop 1
	v_permlane32_swap_b32_e32 v35, v76
	v_add_f32_e32 v35, v35, v76
	v_fmac_f32_e32 v65, 0xba000000, v35
	v_fmac_f32_e32 v67, 0xba000000, v35
	v_fmac_f32_e32 v64, 0xba000000, v35
	v_fmac_f32_e32 v66, 0xba000000, v35
	v_mul_f32_e32 v76, v67, v67
	v_mul_f32_e32 v77, v65, v65
	v_fmac_f32_e32 v76, v66, v66
	v_fmac_f32_e32 v77, v64, v64
	v_fmac_f32_e32 v73, 0xba000000, v35
	v_fmac_f32_e32 v75, 0xba000000, v35
	v_add_f32_e32 v76, v76, v77
	v_fmac_f32_e32 v72, 0xba000000, v35
	v_fmac_f32_e32 v74, 0xba000000, v35
	v_mul_f32_e32 v77, v75, v75
	v_mul_f32_e32 v78, v73, v73
	v_fmac_f32_e32 v77, v74, v74
	v_fmac_f32_e32 v78, v72, v72
	v_add_f32_e32 v77, v77, v78
	v_fmac_f32_e32 v71, 0xba000000, v35
	v_fmac_f32_e32 v69, 0xba000000, v35
	v_add_f32_e32 v76, v76, v77
	v_fmac_f32_e32 v70, 0xba000000, v35
	v_fmac_f32_e32 v68, 0xba000000, v35
	v_mul_f32_e32 v77, v69, v69
	v_mul_f32_e32 v78, v71, v71
	v_fmac_f32_e32 v77, v68, v68
	v_fmac_f32_e32 v78, v70, v70
	v_add_f32_e32 v77, v77, v78
	v_fmac_f32_e32 v63, 0xba000000, v35
	v_fmac_f32_e32 v61, 0xba000000, v35
	v_add_f32_e32 v76, v76, v77
	v_fmac_f32_e32 v62, 0xba000000, v35
	v_fmac_f32_e32 v60, 0xba000000, v35
	v_mul_f32_e32 v77, v61, v61
	v_mul_f32_e32 v78, v63, v63
	v_fmac_f32_e32 v77, v60, v60
	v_fmac_f32_e32 v78, v62, v62
	v_add_f32_e32 v77, v77, v78
	v_fmac_f32_e32 v59, 0xba000000, v35
	v_fmac_f32_e32 v57, 0xba000000, v35
	v_add_f32_e32 v76, v76, v77
	v_fmac_f32_e32 v58, 0xba000000, v35
	v_fmac_f32_e32 v56, 0xba000000, v35
	v_mul_f32_e32 v77, v57, v57
	v_mul_f32_e32 v78, v59, v59
	v_fmac_f32_e32 v77, v56, v56
	v_fmac_f32_e32 v78, v58, v58
	v_add_f32_e32 v77, v77, v78
	v_fmac_f32_e32 v55, 0xba000000, v35
	v_fmac_f32_e32 v53, 0xba000000, v35
	v_add_f32_e32 v76, v76, v77
	v_fmac_f32_e32 v54, 0xba000000, v35
	v_fmac_f32_e32 v52, 0xba000000, v35
	v_mul_f32_e32 v77, v53, v53
	v_mul_f32_e32 v78, v55, v55
	v_fmac_f32_e32 v77, v52, v52
	v_fmac_f32_e32 v78, v54, v54
	v_add_f32_e32 v77, v77, v78
	v_fmac_f32_e32 v51, 0xba000000, v35
	v_fmac_f32_e32 v49, 0xba000000, v35
	v_add_f32_e32 v76, v76, v77
	v_fmac_f32_e32 v50, 0xba000000, v35
	v_fmac_f32_e32 v48, 0xba000000, v35
	v_mul_f32_e32 v77, v49, v49
	v_mul_f32_e32 v78, v51, v51
	v_fmac_f32_e32 v77, v48, v48
	v_fmac_f32_e32 v78, v50, v50
	v_add_f32_e32 v77, v77, v78
	v_fmac_f32_e32 v45, 0xba000000, v35
	v_fmac_f32_e32 v47, 0xba000000, v35
	v_add_f32_e32 v76, v76, v77
	v_fmac_f32_e32 v44, 0xba000000, v35
	v_fmac_f32_e32 v46, 0xba000000, v35
	v_mul_f32_e32 v35, v47, v47
	v_mul_f32_e32 v77, v45, v45
	v_fmac_f32_e32 v35, v46, v46
	v_fmac_f32_e32 v77, v44, v44
	v_add_f32_e32 v35, v35, v77
	v_add_f32_e32 v35, v76, v35
	v_lshl_add_u64 v[78:79], v[30:31], 0, s[14:15]
	s_nop 0
	v_add_f32_dpp v35, v35, v35 quad_perm:[1,0,3,2] row_mask:0xf bank_mask:0xf bound_ctrl:1
	s_nop 1
	v_add_f32_dpp v35, v35, v35 quad_perm:[2,3,0,1] row_mask:0xf bank_mask:0xf bound_ctrl:1
	s_nop 1
	v_add_f32_dpp v35, v35, v35 row_ror:4 row_mask:0xf bank_mask:0xf bound_ctrl:1
	s_nop 1
	v_add_f32_dpp v35, v35, v35 row_ror:8 row_mask:0xf bank_mask:0xf bound_ctrl:1
	v_mov_b32_e32 v76, v35
	s_nop 1
	v_permlane16_swap_b32_e32 v35, v76
	v_add_f32_e32 v35, v35, v76
	v_mov_b32_e32 v76, v35
	s_nop 1
	v_permlane32_swap_b32_e32 v35, v76
	v_add_f32_e32 v35, v35, v76
	v_fmamk_f32 v35, v35, 0x3a000000, v207
	v_rsq_f32_e32 v84, v35
	v_lshl_add_u64 v[76:77], v[28:29], 0, s[12:13]
	v_pk_mul_f32 v[66:67], v[84:85], v[66:67] op_sel_hi:[0,1]
	v_pk_mul_f32 v[90:91], v[84:85], v[64:65] op_sel_hi:[0,1]
	s_waitcnt vmcnt(0) lgkmcnt(0)
	v_pk_fma_f32 v[64:65], v[80:81], v[66:67], v[86:87]
	v_mov_b32_e32 v85, 0
	v_med3_f32 v35, v64, s69, v208
	v_med3_f32 v66, v65, s69, v208
	v_cvt_pk_fp8_f32 v85, v35, v66
	v_pk_fma_f32 v[66:67], v[82:83], v[90:91], v[88:89]
	s_nop 0
	v_med3_f32 v35, v66, s69, v208
	v_med3_f32 v80, v67, s69, v208
	v_cvt_pk_fp8_f32 v85, v35, v80 op_sel:[0,0,1]
	v_cvt_pk_bf16_f32 v80, v64, v65
	v_cvt_pk_bf16_f32 v81, v66, v67
	flat_store_dwordx2 v[76:77], v[80:81] nt
	flat_store_dword v[78:79], v85 nt
	flat_load_dwordx4 v[80:83], v[94:95] offset:1024
	s_nop 0
	flat_load_dwordx4 v[86:89], v[96:97] offset:1024
	v_pk_mul_f32 v[74:75], v[84:85], v[74:75] op_sel_hi:[0,1]
	v_pk_mul_f32 v[90:91], v[84:85], v[72:73] op_sel_hi:[0,1]
	v_mov_b32_e32 v85, 0
	s_waitcnt vmcnt(0) lgkmcnt(0)
	v_pk_fma_f32 v[72:73], v[80:81], v[74:75], v[86:87]
	s_nop 0
	v_med3_f32 v35, v72, s69, v208
	v_med3_f32 v74, v73, s69, v208
	v_cvt_pk_fp8_f32 v85, v35, v74
	v_pk_fma_f32 v[74:75], v[82:83], v[90:91], v[88:89]
	s_nop 0
	v_med3_f32 v35, v74, s69, v208
	v_med3_f32 v80, v75, s69, v208
	v_cvt_pk_fp8_f32 v85, v35, v80 op_sel:[0,0,1]
	v_cvt_pk_bf16_f32 v80, v72, v73
	v_cvt_pk_bf16_f32 v81, v74, v75
	flat_store_dwordx2 v[76:77], v[80:81] offset:512 nt
	flat_store_dword v[78:79], v85 offset:256 nt
	flat_load_dwordx4 v[86:89], v[94:95] offset:2048
	flat_load_dwordx4 v[90:93], v[96:97] offset:2048
	v_pk_mul_f32 v[68:69], v[84:85], v[68:69] op_sel_hi:[0,1]
	v_mov_b32_e32 v35, 0
	v_pk_mul_f32 v[70:71], v[84:85], v[70:71] op_sel_hi:[0,1]
	v_pk_mul_f32 v[60:61], v[84:85], v[60:61] op_sel_hi:[0,1]
	v_pk_mul_f32 v[62:63], v[84:85], v[62:63] op_sel_hi:[0,1]
	v_pk_mul_f32 v[56:57], v[84:85], v[56:57] op_sel_hi:[0,1]
	v_pk_mul_f32 v[58:59], v[84:85], v[58:59] op_sel_hi:[0,1]
	v_pk_mul_f32 v[52:53], v[84:85], v[52:53] op_sel_hi:[0,1]
	v_pk_mul_f32 v[54:55], v[84:85], v[54:55] op_sel_hi:[0,1]
	v_pk_mul_f32 v[48:49], v[84:85], v[48:49] op_sel_hi:[0,1]
	v_pk_mul_f32 v[50:51], v[84:85], v[50:51] op_sel_hi:[0,1]
	v_pk_mul_f32 v[46:47], v[84:85], v[46:47] op_sel_hi:[0,1]
	v_pk_mul_f32 v[44:45], v[84:85], v[44:45] op_sel_hi:[0,1]
	s_waitcnt vmcnt(0) lgkmcnt(0)
	v_pk_fma_f32 v[82:83], v[86:87], v[68:69], v[90:91]
	s_nop 0
	v_med3_f32 v68, v82, s69, v208
	v_med3_f32 v69, v83, s69, v208
	v_cvt_pk_fp8_f32 v35, v68, v69
	v_pk_fma_f32 v[80:81], v[88:89], v[70:71], v[92:93]
	v_add_co_u32_e32 v90, vcc, s33, v94
	v_med3_f32 v68, v80, s69, v208
	v_med3_f32 v69, v81, s69, v208
	v_cvt_pk_fp8_f32 v35, v68, v69 op_sel:[0,0,1]
	v_cvt_pk_bf16_f32 v68, v82, v83
	v_cvt_pk_bf16_f32 v69, v80, v81
	flat_store_dwordx2 v[76:77], v[68:69] offset:1024 nt
	flat_store_dword v[78:79], v35 offset:512 nt
	flat_load_dwordx4 v[68:71], v[94:95] offset:3072
	s_nop 0
	flat_load_dwordx4 v[86:89], v[96:97] offset:3072
	v_addc_co_u32_e32 v91, vcc, 0, v95, vcc
	v_mov_b32_e32 v35, 0
	v_add_co_u32_e32 v96, vcc, s33, v96
	s_waitcnt vmcnt(0) lgkmcnt(0)
	v_pk_fma_f32 v[94:95], v[68:69], v[60:61], v[86:87]
	s_nop 0
	v_med3_f32 v60, v94, s69, v208
	v_med3_f32 v61, v95, s69, v208
	v_cvt_pk_fp8_f32 v35, v60, v61
	v_pk_fma_f32 v[92:93], v[70:71], v[62:63], v[88:89]
	v_addc_co_u32_e32 v97, vcc, 0, v97, vcc
	v_med3_f32 v60, v92, s69, v208
	v_med3_f32 v61, v93, s69, v208
	v_cvt_pk_fp8_f32 v35, v60, v61 op_sel:[0,0,1]
	v_cvt_pk_bf16_f32 v60, v94, v95
	v_cvt_pk_bf16_f32 v61, v92, v93
	flat_store_dwordx2 v[76:77], v[60:61] offset:1536 nt
	flat_store_dword v[78:79], v35 offset:768 nt
	flat_load_dwordx4 v[60:63], v[90:91]
	s_nop 0
	flat_load_dwordx4 v[68:71], v[96:97]
	v_mov_b32_e32 v35, 0
	s_waitcnt vmcnt(0) lgkmcnt(0)
; __global__ void __launch_bounds__(NTHREADS, 2) hybrid_fwd(Args a) {
;     ...
;                     P7_LN(2 * qp, 0, ya);
;                     __builtin_amdgcn_sched_barrier(0);
;                     P7_LN(2 * qp + 1, 1, yb);
	v_pk_fma_f32 v[114:115], v[60:61], v[56:57], v[68:69]
	s_nop 0
	v_med3_f32 v56, v114, s69, v208
	v_med3_f32 v57, v115, s69, v208
	v_cvt_pk_fp8_f32 v35, v56, v57
	v_pk_fma_f32 v[112:113], v[62:63], v[58:59], v[70:71]
	s_nop 0
	v_med3_f32 v56, v112, s69, v208
	v_med3_f32 v57, v113, s69, v208
	v_cvt_pk_fp8_f32 v35, v56, v57 op_sel:[0,0,1]
	v_cvt_pk_bf16_f32 v56, v114, v115
	v_cvt_pk_bf16_f32 v57, v112, v113
	flat_store_dwordx2 v[76:77], v[56:57] offset:2048 nt
	flat_store_dword v[78:79], v35 offset:1024 nt
	flat_load_dwordx4 v[56:59], v[90:91] offset:1024
	s_nop 0
	flat_load_dwordx4 v[60:63], v[96:97] offset:1024
	v_mov_b32_e32 v35, 0
	s_waitcnt vmcnt(0) lgkmcnt(0)
	v_pk_fma_f32 v[118:119], v[56:57], v[52:53], v[60:61]
	s_nop 0
	v_med3_f32 v52, v118, s69, v208
	v_med3_f32 v53, v119, s69, v208
	v_cvt_pk_fp8_f32 v35, v52, v53
	v_pk_fma_f32 v[116:117], v[58:59], v[54:55], v[62:63]
	s_nop 0
	v_med3_f32 v52, v116, s69, v208
	v_med3_f32 v53, v117, s69, v208
	v_cvt_pk_fp8_f32 v35, v52, v53 op_sel:[0,0,1]
	v_cvt_pk_bf16_f32 v52, v118, v119
	v_cvt_pk_bf16_f32 v53, v116, v117
	flat_store_dwordx2 v[76:77], v[52:53] offset:2560 nt
	flat_store_dword v[78:79], v35 offset:1280 nt
	flat_load_dwordx4 v[52:55], v[90:91] offset:2048
	s_nop 0
	flat_load_dwordx4 v[56:59], v[96:97] offset:2048
	v_mov_b32_e32 v35, 0
	s_waitcnt vmcnt(0) lgkmcnt(0)
	v_pk_fma_f32 v[122:123], v[52:53], v[48:49], v[56:57]
	s_nop 0
	v_med3_f32 v48, v122, s69, v208
	v_med3_f32 v49, v123, s69, v208
	v_cvt_pk_fp8_f32 v35, v48, v49
	v_pk_fma_f32 v[120:121], v[54:55], v[50:51], v[58:59]
	s_nop 0
	v_med3_f32 v48, v120, s69, v208
	v_med3_f32 v49, v121, s69, v208
	v_cvt_pk_fp8_f32 v35, v48, v49 op_sel:[0,0,1]
	v_cvt_pk_bf16_f32 v48, v122, v123
	v_cvt_pk_bf16_f32 v49, v120, v121
	flat_store_dwordx2 v[76:77], v[48:49] offset:3072 nt
	flat_store_dword v[78:79], v35 offset:1536 nt
	flat_load_dwordx4 v[48:51], v[90:91] offset:3072
	s_nop 0
	flat_load_dwordx4 v[52:55], v[96:97] offset:3072
	v_mov_b32_e32 v35, 0
	s_waitcnt vmcnt(0) lgkmcnt(0)
	v_pk_fma_f32 v[124:125], v[48:49], v[46:47], v[52:53]
	s_nop 0
	v_med3_f32 v46, v124, s69, v208
	v_med3_f32 v47, v125, s69, v208
	v_mov_b32_e32 v48, 0
	v_cvt_pk_fp8_f32 v48, v46, v47
	v_pk_fma_f32 v[126:127], v[50:51], v[44:45], v[54:55]
	s_nop 0
	v_med3_f32 v44, v126, s69, v208
	v_med3_f32 v45, v127, s69, v208
	v_cvt_pk_fp8_f32 v48, v44, v45 op_sel:[0,0,1]
	v_cvt_pk_bf16_f32 v44, v124, v125
	v_cvt_pk_bf16_f32 v45, v126, v127
	flat_store_dwordx2 v[76:77], v[44:45] offset:3584 nt
	flat_store_dword v[78:79], v48 offset:1792 nt
	v_lshlrev_b32_e32 v84, 16, v42
	v_and_b32_e32 v85, 0xffff0000, v42
	v_lshlrev_b32_e32 v78, 16, v43
	v_and_b32_e32 v79, 0xffff0000, v43
	v_add_f32_e32 v42, v84, v85
	v_add_f32_e32 v43, v78, v79
	v_lshlrev_b32_e32 v76, 16, v40
	v_and_b32_e32 v77, 0xffff0000, v40
	v_lshlrev_b32_e32 v70, 16, v41
	v_and_b32_e32 v71, 0xffff0000, v41
	v_add_f32_e32 v42, v42, v43
	v_add_f32_e32 v40, v76, v77
	v_add_f32_e32 v41, v70, v71
	v_lshlrev_b32_e32 v62, 16, v38
	v_and_b32_e32 v63, 0xffff0000, v38
	v_lshlrev_b32_e32 v68, 16, v39
	v_and_b32_e32 v69, 0xffff0000, v39
	v_add_f32_e32 v42, 0, v42
	v_add_f32_e32 v40, v40, v41
	v_add_f32_e32 v38, v62, v63
	v_add_f32_e32 v39, v68, v69
	v_lshlrev_b32_e32 v58, 16, v36
	v_and_b32_e32 v59, 0xffff0000, v36
	v_lshlrev_b32_e32 v60, 16, v37
	v_and_b32_e32 v61, 0xffff0000, v37
	v_add_f32_e32 v40, v42, v40
	v_add_f32_e32 v38, v38, v39
	v_add_f32_e32 v36, v58, v59
	v_add_f32_e32 v37, v60, v61
	v_lshlrev_b32_e32 v50, 16, v22
	v_and_b32_e32 v51, 0xffff0000, v22
	v_lshlrev_b32_e32 v52, 16, v23
	v_and_b32_e32 v53, 0xffff0000, v23
	v_add_f32_e32 v38, v40, v38
	v_add_f32_e32 v36, v36, v37
	v_add_f32_e32 v22, v50, v51
	v_add_f32_e32 v23, v52, v53
	v_lshlrev_b32_e32 v46, 16, v20
	v_and_b32_e32 v47, 0xffff0000, v20
	v_lshlrev_b32_e32 v48, 16, v21
	v_and_b32_e32 v49, 0xffff0000, v21
	v_add_f32_e32 v36, v38, v36
	v_add_f32_e32 v22, v22, v23
	v_add_f32_e32 v20, v46, v47
	v_add_f32_e32 v21, v48, v49
	v_lshlrev_b32_e32 v40, 16, v18
	v_and_b32_e32 v41, 0xffff0000, v18
	v_lshlrev_b32_e32 v42, 16, v19
	v_and_b32_e32 v43, 0xffff0000, v19
	v_add_f32_e32 v22, v36, v22
	v_add_f32_e32 v20, v20, v21
	v_add_f32_e32 v18, v40, v41
	v_add_f32_e32 v19, v42, v43
	v_lshlrev_b32_e32 v38, 16, v16
	v_and_b32_e32 v39, 0xffff0000, v16
	v_lshlrev_b32_e32 v36, 16, v17
	v_and_b32_e32 v37, 0xffff0000, v17
	v_add_f32_e32 v20, v22, v20
	v_add_f32_e32 v18, v18, v19
	v_add_f32_e32 v16, v38, v39
	v_add_f32_e32 v17, v36, v37
	v_add_f32_e32 v18, v20, v18
	v_add_f32_e32 v16, v16, v17
	v_add_f32_e32 v16, v18, v16
	s_mov_b64 s[12:13], s[34:35]
	s_mov_b64 s[14:15], s[36:37]
	v_add_f32_dpp v16, v16, v16 quad_perm:[1,0,3,2] row_mask:0xf bank_mask:0xf bound_ctrl:1
	v_lshl_add_u64 v[100:101], s[12:13], 0, v[192:193]
	v_lshl_add_u64 v[56:57], v[28:29], 0, s[10:11]
	v_add_f32_dpp v16, v16, v16 quad_perm:[2,3,0,1] row_mask:0xf bank_mask:0xf bound_ctrl:1
	v_lshl_add_u64 v[86:87], s[14:15], 0, v[192:193]
	s_lshl_b64 s[8:9], s[8:9], 11
	v_add_f32_dpp v16, v16, v16 row_ror:4 row_mask:0xf bank_mask:0xf bound_ctrl:1
	v_lshl_add_u64 v[54:55], v[30:31], 0, s[8:9]
	s_nop 0
	v_add_f32_dpp v16, v16, v16 row_ror:8 row_mask:0xf bank_mask:0xf bound_ctrl:1
	v_mov_b32_e32 v17, v16
	s_nop 1
	v_permlane16_swap_b32_e32 v16, v17
	v_add_f32_e32 v16, v16, v17
	v_mov_b32_e32 v17, v16
	s_nop 1
	v_permlane32_swap_b32_e32 v16, v17
	v_add_f32_e32 v16, v16, v17
	v_fmac_f32_e32 v79, 0xba000000, v16
	v_fmac_f32_e32 v85, 0xba000000, v16
	v_fmac_f32_e32 v78, 0xba000000, v16
	v_fmac_f32_e32 v84, 0xba000000, v16
	v_mul_f32_e32 v17, v85, v85
	v_mul_f32_e32 v18, v79, v79
	v_fmac_f32_e32 v17, v84, v84
	v_fmac_f32_e32 v18, v78, v78
	v_fmac_f32_e32 v71, 0xba000000, v16
	v_fmac_f32_e32 v77, 0xba000000, v16
	v_add_f32_e32 v17, v17, v18
	v_fmac_f32_e32 v70, 0xba000000, v16
	v_fmac_f32_e32 v76, 0xba000000, v16
	v_mul_f32_e32 v18, v77, v77
	v_mul_f32_e32 v19, v71, v71
	v_fmac_f32_e32 v18, v76, v76
	v_fmac_f32_e32 v19, v70, v70
	v_add_f32_e32 v18, v18, v19
	v_fmac_f32_e32 v69, 0xba000000, v16
	v_fmac_f32_e32 v63, 0xba000000, v16
	v_add_f32_e32 v17, v17, v18
	v_fmac_f32_e32 v68, 0xba000000, v16
	v_fmac_f32_e32 v62, 0xba000000, v16
	v_mul_f32_e32 v18, v63, v63
	v_mul_f32_e32 v19, v69, v69
	v_fmac_f32_e32 v18, v62, v62
	v_fmac_f32_e32 v19, v68, v68
	v_add_f32_e32 v18, v18, v19
	v_fmac_f32_e32 v61, 0xba000000, v16
	v_fmac_f32_e32 v59, 0xba000000, v16
	v_add_f32_e32 v17, v17, v18
	v_fmac_f32_e32 v60, 0xba000000, v16
	v_fmac_f32_e32 v58, 0xba000000, v16
	v_mul_f32_e32 v18, v59, v59
	v_mul_f32_e32 v19, v61, v61
	v_fmac_f32_e32 v18, v58, v58
	v_fmac_f32_e32 v19, v60, v60
	v_add_f32_e32 v18, v18, v19
	v_fmac_f32_e32 v53, 0xba000000, v16
	v_fmac_f32_e32 v51, 0xba000000, v16
	v_add_f32_e32 v17, v17, v18
	v_fmac_f32_e32 v52, 0xba000000, v16
	v_fmac_f32_e32 v50, 0xba000000, v16
	v_mul_f32_e32 v18, v51, v51
	v_mul_f32_e32 v19, v53, v53
	v_fmac_f32_e32 v18, v50, v50
	v_fmac_f32_e32 v19, v52, v52
	v_add_f32_e32 v18, v18, v19
	v_fmac_f32_e32 v49, 0xba000000, v16
	v_fmac_f32_e32 v47, 0xba000000, v16
	v_add_f32_e32 v17, v17, v18
	v_fmac_f32_e32 v48, 0xba000000, v16
	v_fmac_f32_e32 v46, 0xba000000, v16
	v_mul_f32_e32 v18, v47, v47
	v_mul_f32_e32 v19, v49, v49
	v_fmac_f32_e32 v18, v46, v46
	v_fmac_f32_e32 v19, v48, v48
	v_add_f32_e32 v18, v18, v19
	v_fmac_f32_e32 v43, 0xba000000, v16
	v_fmac_f32_e32 v41, 0xba000000, v16
	v_add_f32_e32 v17, v17, v18
	v_fmac_f32_e32 v42, 0xba000000, v16
	v_fmac_f32_e32 v40, 0xba000000, v16
	v_mul_f32_e32 v18, v41, v41
	v_mul_f32_e32 v19, v43, v43
	v_fmac_f32_e32 v18, v40, v40
	v_fmac_f32_e32 v19, v42, v42
	v_add_f32_e32 v18, v18, v19
	v_fmac_f32_e32 v37, 0xba000000, v16
	v_fmac_f32_e32 v39, 0xba000000, v16
	v_add_f32_e32 v17, v17, v18
	v_fmac_f32_e32 v36, 0xba000000, v16
	v_fmac_f32_e32 v38, 0xba000000, v16
	v_mul_f32_e32 v16, v39, v39
	v_mul_f32_e32 v18, v37, v37
	v_fmac_f32_e32 v16, v38, v38
	v_fmac_f32_e32 v18, v36, v36
	v_add_f32_e32 v16, v16, v18
	v_add_f32_e32 v16, v17, v16
	s_nop 1
	v_add_f32_dpp v16, v16, v16 quad_perm:[1,0,3,2] row_mask:0xf bank_mask:0xf bound_ctrl:1
	s_nop 1
	v_add_f32_dpp v16, v16, v16 quad_perm:[2,3,0,1] row_mask:0xf bank_mask:0xf bound_ctrl:1
	s_nop 1
	v_add_f32_dpp v16, v16, v16 row_ror:4 row_mask:0xf bank_mask:0xf bound_ctrl:1
	s_nop 1
	v_add_f32_dpp v16, v16, v16 row_ror:8 row_mask:0xf bank_mask:0xf bound_ctrl:1
	v_mov_b32_e32 v17, v16
	s_nop 1
	v_permlane16_swap_b32_e32 v16, v17
	v_add_f32_e32 v16, v16, v17
	v_mov_b32_e32 v17, v16
	s_nop 1
	v_permlane32_swap_b32_e32 v16, v17
	v_add_f32_e32 v16, v16, v17
	v_fmamk_f32 v16, v16, 0x3a000000, v207
	v_rsq_f32_e32 v44, v16
	flat_load_dwordx4 v[16:19], v[100:101]
	flat_load_dwordx4 v[20:23], v[86:87]
	v_pk_mul_f32 v[84:85], v[44:45], v[84:85] op_sel_hi:[0,1]
	v_pk_mul_f32 v[78:79], v[44:45], v[78:79] op_sel_hi:[0,1]
	v_pk_mul_f32 v[76:77], v[44:45], v[76:77] op_sel_hi:[0,1]
	v_pk_mul_f32 v[70:71], v[44:45], v[70:71] op_sel_hi:[0,1]
	v_pk_mul_f32 v[62:63], v[44:45], v[62:63] op_sel_hi:[0,1]
	v_pk_mul_f32 v[68:69], v[44:45], v[68:69] op_sel_hi:[0,1]
	v_pk_mul_f32 v[58:59], v[44:45], v[58:59] op_sel_hi:[0,1]
	v_pk_mul_f32 v[60:61], v[44:45], v[60:61] op_sel_hi:[0,1]
	v_pk_mul_f32 v[50:51], v[44:45], v[50:51] op_sel_hi:[0,1]
	v_pk_mul_f32 v[52:53], v[44:45], v[52:53] op_sel_hi:[0,1]
	v_mov_b32_e32 v45, 0
	s_waitcnt vmcnt(0) lgkmcnt(0)
	v_pk_fma_f32 v[128:129], v[18:19], v[78:79], v[22:23]
	v_pk_fma_f32 v[130:131], v[16:17], v[84:85], v[20:21]
	v_mov_b32_e32 v20, 0
	v_cvt_pk_bf16_f32 v16, v130, v131
	v_cvt_pk_bf16_f32 v17, v128, v129
	flat_store_dwordx2 v[56:57], v[16:17] nt
	v_med3_f32 v16, v130, s69, v208
	v_med3_f32 v17, v131, s69, v208
	v_cvt_pk_fp8_f32 v20, v16, v17
	v_med3_f32 v18, v128, s69, v208
	v_med3_f32 v19, v129, s69, v208
	v_cvt_pk_fp8_f32 v20, v18, v19 op_sel:[0,0,1]
	flat_store_dword v[54:55], v20 nt
	flat_load_dwordx4 v[16:19], v[100:101] offset:1024
	s_nop 0
	flat_load_dwordx4 v[20:23], v[86:87] offset:1024
	s_waitcnt vmcnt(0) lgkmcnt(0)
	v_pk_fma_f32 v[104:105], v[18:19], v[70:71], v[22:23]
	v_pk_fma_f32 v[106:107], v[16:17], v[76:77], v[20:21]
	v_mov_b32_e32 v20, 0
	v_cvt_pk_bf16_f32 v16, v106, v107
	v_cvt_pk_bf16_f32 v17, v104, v105
	flat_store_dwordx2 v[56:57], v[16:17] offset:512 nt
	v_med3_f32 v16, v106, s69, v208
	v_med3_f32 v17, v107, s69, v208
	v_cvt_pk_fp8_f32 v20, v16, v17
	v_med3_f32 v18, v104, s69, v208
	v_med3_f32 v19, v105, s69, v208
	v_cvt_pk_fp8_f32 v20, v18, v19 op_sel:[0,0,1]
	flat_store_dword v[54:55], v20 offset:256 nt
	flat_load_dwordx4 v[16:19], v[100:101] offset:2048
	s_nop 0
	flat_load_dwordx4 v[20:23], v[86:87] offset:2048
	s_waitcnt vmcnt(0) lgkmcnt(0)
	v_pk_fma_f32 v[96:97], v[18:19], v[68:69], v[22:23]
	v_pk_fma_f32 v[98:99], v[16:17], v[62:63], v[20:21]
	v_mov_b32_e32 v20, 0
	v_cvt_pk_bf16_f32 v16, v98, v99
	v_cvt_pk_bf16_f32 v17, v96, v97
	flat_store_dwordx2 v[56:57], v[16:17] offset:1024 nt
	v_med3_f32 v16, v98, s69, v208
	v_med3_f32 v17, v99, s69, v208
	v_cvt_pk_fp8_f32 v20, v16, v17
	v_med3_f32 v18, v96, s69, v208
	v_med3_f32 v19, v97, s69, v208
	v_cvt_pk_fp8_f32 v20, v18, v19 op_sel:[0,0,1]
	flat_store_dword v[54:55], v20 offset:512 nt
	flat_load_dwordx4 v[16:19], v[100:101] offset:3072
	s_nop 0
	flat_load_dwordx4 v[20:23], v[86:87] offset:3072
	s_waitcnt vmcnt(0) lgkmcnt(0)
; #define LAS __attribute__((address_space(3)))
; __global__ void __launch_bounds__(NTHREADS, 2) hybrid_fwd(Args a) {
;     ...
;                     if (qp == 0) {
; #pragma unroll
;                         for (int q = 0; q < 2; ++q)
; #pragma unroll
;                             for (int j = 0; j < 8; ++j) raw[q][j] = __builtin_nontemporal_load((const u32x2*)(YB + (size_t)(v * 32 + wave + 8 * (2 + q)) * DM + j * 256 + lane * 4));
;                         __builtin_amdgcn_sched_barrier(0);
;                     }
;                     f32x2 y2[8][4];
; #pragma unroll
;                     for (int j = 0; j < 8; ++j)
; #pragma unroll
;                         for (int c = 0; c < 4; ++c) y2[j][c] = (f32x2){ya[j][c], yb[j][c]};
;                     f32x2 acc2[16];
; #pragma unroll
;                     for (int e = 0; e < 16; ++e) acc2[e] = (f32x2){0.f, 0.f};
; #pragma unroll
;                     for (int j = 0; j < 8; ++j) {
; #pragma unroll
;                         for (int e = 0; e < 16; ++e) { const f32x4 w = *(const LAS f32x4*)(rwT + e * 2052 + j * 256 + lane * 4);
;                             acc2[e] += y2[j][0] * (f32x2){w[0], w[0]}; acc2[e] += y2[j][1] * (f32x2){w[1], w[1]};
;                             acc2[e] += y2[j][2] * (f32x2){w[2], w[2]}; acc2[e] += y2[j][3] * (f32x2){w[3], w[3]}; }
	v_pk_fma_f32 v[88:89], v[18:19], v[60:61], v[22:23]
	v_pk_fma_f32 v[90:91], v[16:17], v[58:59], v[20:21]
	v_mov_b32_e32 v20, 0
	v_cvt_pk_bf16_f32 v16, v90, v91
	v_cvt_pk_bf16_f32 v17, v88, v89
	flat_store_dwordx2 v[56:57], v[16:17] offset:1536 nt
	v_med3_f32 v16, v90, s69, v208
	v_med3_f32 v17, v91, s69, v208
	v_cvt_pk_fp8_f32 v20, v16, v17
	v_med3_f32 v18, v88, s69, v208
	v_med3_f32 v19, v89, s69, v208
	v_add_co_u32_e32 v16, vcc, s33, v100
	v_cvt_pk_fp8_f32 v20, v18, v19 op_sel:[0,0,1]
	s_nop 0
	v_addc_co_u32_e32 v17, vcc, 0, v101, vcc
	v_add_co_u32_e32 v18, vcc, s33, v86
	flat_store_dword v[54:55], v20 offset:768 nt
	s_nop 0
	v_addc_co_u32_e32 v19, vcc, 0, v87, vcc
	flat_load_dwordx4 v[20:23], v[16:17]
	flat_load_dwordx4 v[58:61], v[18:19]
	s_waitcnt vmcnt(0) lgkmcnt(0)
	v_pk_fma_f32 v[84:85], v[22:23], v[52:53], v[60:61]
	v_pk_fma_f32 v[86:87], v[20:21], v[50:51], v[58:59]
	v_med3_f32 v22, v84, s69, v208
	v_cvt_pk_bf16_f32 v20, v86, v87
	v_cvt_pk_bf16_f32 v21, v84, v85
	flat_store_dwordx2 v[56:57], v[20:21] offset:2048 nt
	v_med3_f32 v20, v86, s69, v208
	v_med3_f32 v21, v87, s69, v208
	v_cvt_pk_fp8_f32 v45, v20, v21
	v_med3_f32 v23, v85, s69, v208
	v_cvt_pk_fp8_f32 v45, v22, v23 op_sel:[0,0,1]
	flat_store_dword v[54:55], v45 offset:1024 nt
	flat_load_dwordx4 v[20:23], v[16:17] offset:1024
	flat_load_dwordx4 v[50:53], v[18:19] offset:1024
	v_pk_mul_f32 v[46:47], v[44:45], v[46:47] op_sel_hi:[0,1]
	v_pk_mul_f32 v[48:49], v[44:45], v[48:49] op_sel_hi:[0,1]
	v_mov_b32_e32 v45, 0
	s_waitcnt vmcnt(0) lgkmcnt(0)
	v_pk_fma_f32 v[76:77], v[22:23], v[48:49], v[52:53]
	v_pk_fma_f32 v[78:79], v[20:21], v[46:47], v[50:51]
	v_med3_f32 v22, v76, s69, v208
	v_cvt_pk_bf16_f32 v20, v78, v79
	v_cvt_pk_bf16_f32 v21, v76, v77
	flat_store_dwordx2 v[56:57], v[20:21] offset:2560 nt
	v_med3_f32 v20, v78, s69, v208
	v_med3_f32 v21, v79, s69, v208
	v_cvt_pk_fp8_f32 v45, v20, v21
	v_med3_f32 v23, v77, s69, v208
	v_cvt_pk_fp8_f32 v45, v22, v23 op_sel:[0,0,1]
	flat_store_dword v[54:55], v45 offset:1280 nt
	flat_load_dwordx4 v[20:23], v[16:17] offset:2048
	flat_load_dwordx4 v[46:49], v[18:19] offset:2048
	v_pk_mul_f32 v[40:41], v[44:45], v[40:41] op_sel_hi:[0,1]
	v_pk_mul_f32 v[42:43], v[44:45], v[42:43] op_sel_hi:[0,1]
	v_pk_mul_f32 v[38:39], v[44:45], v[38:39] op_sel_hi:[0,1]
	v_pk_mul_f32 v[36:37], v[44:45], v[36:37] op_sel_hi:[0,1]
	s_waitcnt vmcnt(0) lgkmcnt(0)
	v_pk_fma_f32 v[68:69], v[22:23], v[42:43], v[48:49]
	v_pk_fma_f32 v[70:71], v[20:21], v[40:41], v[46:47]
	v_mov_b32_e32 v40, 0
	v_cvt_pk_bf16_f32 v20, v70, v71
	v_cvt_pk_bf16_f32 v21, v68, v69
	flat_store_dwordx2 v[56:57], v[20:21] offset:3072 nt
	v_med3_f32 v20, v70, s69, v208
	v_med3_f32 v21, v71, s69, v208
	v_cvt_pk_fp8_f32 v40, v20, v21
	v_med3_f32 v22, v68, s69, v208
	v_med3_f32 v23, v69, s69, v208
	v_cvt_pk_fp8_f32 v40, v22, v23 op_sel:[0,0,1]
	flat_store_dword v[54:55], v40 offset:1536 nt
	flat_load_dwordx4 v[20:23], v[16:17] offset:3072
	s_nop 0
	flat_load_dwordx4 v[16:19], v[18:19] offset:3072
	s_waitcnt vmcnt(0) lgkmcnt(0)
	v_pk_fma_f32 v[60:61], v[22:23], v[36:37], v[18:19]
	v_pk_fma_f32 v[62:63], v[20:21], v[38:39], v[16:17]
	v_mov_b32_e32 v20, 0
	v_cvt_pk_bf16_f32 v16, v62, v63
	v_cvt_pk_bf16_f32 v17, v60, v61
	flat_store_dwordx2 v[56:57], v[16:17] offset:3584 nt
	v_med3_f32 v16, v62, s69, v208
	v_med3_f32 v17, v63, s69, v208
	v_cvt_pk_fp8_f32 v20, v16, v17
	v_med3_f32 v18, v60, s69, v208
	v_med3_f32 v19, v61, s69, v208
	v_cvt_pk_fp8_f32 v20, v18, v19 op_sel:[0,0,1]
	flat_store_dword v[54:55], v20 offset:1792 nt
	s_ashr_i32 s39, s38, 31
	s_add_i32 s40, s6, 24
	s_lshl_b64 s[44:45], s[38:39], 12
	s_ashr_i32 s41, s40, 31
	v_lshl_add_u64 v[16:17], v[26:27], 0, s[44:45]
	s_lshl_b64 s[42:43], s[40:41], 12
	flat_load_dwordx2 v[58:59], v[16:17] nt
	flat_load_dwordx2 v[56:57], v[16:17] offset:512 nt
	flat_load_dwordx2 v[54:55], v[16:17] offset:1024 nt
	flat_load_dwordx2 v[52:53], v[16:17] offset:1536 nt
	flat_load_dwordx2 v[50:51], v[16:17] offset:2048 nt
	flat_load_dwordx2 v[48:49], v[16:17] offset:2560 nt
	flat_load_dwordx2 v[46:47], v[16:17] offset:3072 nt
	flat_load_dwordx2 v[44:45], v[16:17] offset:3584 nt
	v_lshl_add_u64 v[16:17], v[26:27], 0, s[42:43]
	flat_load_dwordx2 v[42:43], v[16:17] nt
	flat_load_dwordx2 v[40:41], v[16:17] offset:512 nt
	flat_load_dwordx2 v[38:39], v[16:17] offset:1024 nt
	flat_load_dwordx2 v[36:37], v[16:17] offset:1536 nt
	flat_load_dwordx2 v[22:23], v[16:17] offset:2048 nt
	flat_load_dwordx2 v[20:21], v[16:17] offset:2560 nt
	flat_load_dwordx2 v[18:19], v[16:17] offset:3072 nt
	s_nop 0
	flat_load_dwordx2 v[16:17], v[16:17] offset:3584 nt
	v_add_u32_e32 v238, 0x10000, v25
	ds_read_b128 v[158:161], v25 offset:0
	ds_read_b128 v[162:165], v25 offset:8208
	ds_read_b128 v[166:169], v25 offset:16416
	ds_read_b128 v[170:173], v25 offset:24624
	ds_read_b128 v[174:177], v25 offset:32832
	ds_read_b128 v[178:181], v25 offset:41040
	ds_read_b128 v[182:185], v25 offset:49248
	ds_read_b128 v[186:189], v25 offset:57456
	v_mov_b32_e32 v100, v94
	v_mov_b32_e32 v101, v90
	v_mov_b32_e32 v90, v95
	v_mov_b32_e32 v102, v92
	v_mov_b32_e32 v103, v88
	v_mov_b32_e32 v88, v93
	v_mov_b32_e32 v92, v114
	v_mov_b32_e32 v93, v86
	v_mov_b32_e32 v86, v115
	v_mov_b32_e32 v94, v112
	v_mov_b32_e32 v95, v84
	v_mov_b32_e32 v84, v113
	ds_read_b128 v[198:201], v238 offset:128
	v_mov_b32_e32 v136, v64
	v_mov_b32_e32 v137, v130
	v_mov_b32_e32 v130, v65
	v_mov_b32_e32 v108, v82
	v_mov_b32_e32 v109, v98
	v_mov_b32_e32 v98, v83
	v_mov_b32_e32 v82, v116
	v_mov_b32_e32 v83, v76
	v_mov_b32_e32 v76, v117
	s_waitcnt lgkmcnt(8)
; #define LAS __attribute__((address_space(3)))
; __global__ void __launch_bounds__(NTHREADS, 2) hybrid_fwd(Args a) {
;     ...
;                     for (int j = 0; j < 8; ++j) {
; #pragma unroll
;                         for (int e = 0; e < 16; ++e) { const f32x4 w = *(const LAS f32x4*)(rwT + e * 2052 + j * 256 + lane * 4);
;                             acc2[e] += y2[j][0] * (f32x2){w[0], w[0]}; acc2[e] += y2[j][1] * (f32x2){w[1], w[1]};
;                             acc2[e] += y2[j][2] * (f32x2){w[2], w[2]}; acc2[e] += y2[j][3] * (f32x2){w[3], w[3]}; }
	v_pk_fma_f32 v[116:117], v[136:137], v[158:159], 0 op_sel_hi:[1,0,0]
	v_mov_b32_e32 v138, v66
	v_mov_b32_e32 v139, v128
	v_pk_fma_f32 v[112:113], v[158:159], v[130:131], v[116:117] op_sel:[1,0,0]
	v_mov_b32_e32 v128, v67
	v_pk_fma_f32 v[112:113], v[160:161], v[138:139], v[112:113] op_sel_hi:[0,1,1]
	v_mov_b32_e32 v114, v161
	v_pk_fma_f32 v[112:113], v[114:115], v[128:129], v[112:113] op_sel_hi:[0,1,1]
	ds_read_b128 v[202:205], v238 offset:8336
	v_mov_b32_e32 v110, v80
	v_mov_b32_e32 v111, v96
	v_mov_b32_e32 v96, v81
	v_mov_b32_e32 v80, v118
	v_mov_b32_e32 v81, v78
	v_mov_b32_e32 v78, v119
	s_waitcnt lgkmcnt(8)
	v_pk_fma_f32 v[118:119], v[136:137], v[162:163], 0 op_sel_hi:[1,0,0]
	v_mov_b32_e32 v134, v74
	v_pk_fma_f32 v[114:115], v[162:163], v[130:131], v[118:119] op_sel:[1,0,0]
	v_mov_b32_e32 v135, v104
	v_pk_fma_f32 v[114:115], v[164:165], v[138:139], v[114:115] op_sel_hi:[0,1,1]
	v_mov_b32_e32 v116, v165
	v_pk_fma_f32 v[152:153], v[116:117], v[128:129], v[114:115] op_sel_hi:[0,1,1]
	ds_read_b128 v[216:219], v238 offset:16544
	v_mov_b32_e32 v104, v75
	v_mov_b32_e32 v74, v120
	v_mov_b32_e32 v75, v68
	v_mov_b32_e32 v68, v121
	s_waitcnt lgkmcnt(8)
	v_pk_fma_f32 v[118:119], v[136:137], v[166:167], 0 op_sel_hi:[1,0,0]
	v_mov_b32_e32 v132, v72
	v_pk_fma_f32 v[114:115], v[166:167], v[130:131], v[118:119] op_sel:[1,0,0]
	v_mov_b32_e32 v133, v106
	v_pk_fma_f32 v[114:115], v[168:169], v[138:139], v[114:115] op_sel_hi:[0,1,1]
	v_mov_b32_e32 v116, v169
	v_pk_fma_f32 v[154:155], v[116:117], v[128:129], v[114:115] op_sel_hi:[0,1,1]
	ds_read_b128 v[220:223], v238 offset:24752
	v_mov_b32_e32 v106, v73
	v_mov_b32_e32 v72, v122
	v_mov_b32_e32 v73, v70
	v_mov_b32_e32 v70, v123
	s_waitcnt lgkmcnt(8)
	v_pk_fma_f32 v[118:119], v[136:137], v[170:171], 0 op_sel_hi:[1,0,0]
	v_mov_b32_e32 v66, v124
	v_pk_fma_f32 v[114:115], v[170:171], v[130:131], v[118:119] op_sel:[1,0,0]
	v_mov_b32_e32 v67, v62
	v_pk_fma_f32 v[114:115], v[172:173], v[138:139], v[114:115] op_sel_hi:[0,1,1]
	v_mov_b32_e32 v116, v173
	v_pk_fma_f32 v[114:115], v[116:117], v[128:129], v[114:115] op_sel_hi:[0,1,1]
	ds_read_b128 v[224:227], v238 offset:32960
	v_mov_b32_e32 v62, v125
	v_mov_b32_e32 v64, v126
	v_mov_b32_e32 v65, v60
	v_mov_b32_e32 v60, v127
	s_waitcnt lgkmcnt(8)
	v_pk_fma_f32 v[120:121], v[136:137], v[174:175], 0 op_sel_hi:[1,0,0]
	s_nop 0
	v_pk_fma_f32 v[116:117], v[174:175], v[130:131], v[120:121] op_sel:[1,0,0]
	s_nop 0
	v_pk_fma_f32 v[116:117], v[176:177], v[138:139], v[116:117] op_sel_hi:[0,1,1]
	v_mov_b32_e32 v118, v177
	v_pk_fma_f32 v[116:117], v[118:119], v[128:129], v[116:117] op_sel_hi:[0,1,1]
	ds_read_b128 v[228:231], v238 offset:41168
	s_waitcnt lgkmcnt(8)
	v_pk_fma_f32 v[122:123], v[136:137], v[178:179], 0 op_sel_hi:[1,0,0]
	s_nop 0
	v_pk_fma_f32 v[118:119], v[178:179], v[130:131], v[122:123] op_sel:[1,0,0]
	s_nop 0
	v_pk_fma_f32 v[118:119], v[180:181], v[138:139], v[118:119] op_sel_hi:[0,1,1]
	v_mov_b32_e32 v120, v181
	v_pk_fma_f32 v[118:119], v[120:121], v[128:129], v[118:119] op_sel_hi:[0,1,1]
	ds_read_b128 v[232:235], v238 offset:49376
	s_waitcnt lgkmcnt(8)
	v_pk_fma_f32 v[124:125], v[136:137], v[182:183], 0 op_sel_hi:[1,0,0]
	s_nop 0
	v_pk_fma_f32 v[120:121], v[182:183], v[130:131], v[124:125] op_sel:[1,0,0]
	s_nop 0
	v_pk_fma_f32 v[120:121], v[184:185], v[138:139], v[120:121] op_sel_hi:[0,1,1]
	v_mov_b32_e32 v122, v185
	v_pk_fma_f32 v[120:121], v[122:123], v[128:129], v[120:121] op_sel_hi:[0,1,1]
	ds_read_b128 v[242:245], v238 offset:57584
	s_waitcnt lgkmcnt(8)
	v_pk_fma_f32 v[126:127], v[136:137], v[186:187], 0 op_sel_hi:[1,0,0]
	s_nop 0
	v_pk_fma_f32 v[122:123], v[186:187], v[130:131], v[126:127] op_sel:[1,0,0]
	s_nop 0
	v_pk_fma_f32 v[122:123], v[188:189], v[138:139], v[122:123] op_sel_hi:[0,1,1]
	v_mov_b32_e32 v124, v189
	v_pk_fma_f32 v[122:123], v[124:125], v[128:129], v[122:123] op_sel_hi:[0,1,1]
	ds_read_b128 v[246:249], v25 offset:1024
	s_waitcnt lgkmcnt(8)
	v_pk_fma_f32 v[140:141], v[136:137], v[198:199], 0 op_sel_hi:[1,0,0]
	s_nop 0
	v_pk_fma_f32 v[124:125], v[198:199], v[130:131], v[140:141] op_sel:[1,0,0]
	ds_read_b128 v[250:253], v25 offset:9232
	v_pk_fma_f32 v[124:125], v[200:201], v[138:139], v[124:125] op_sel_hi:[0,1,1]
	v_mov_b32_e32 v126, v201
	v_pk_fma_f32 v[124:125], v[126:127], v[128:129], v[124:125] op_sel_hi:[0,1,1]
	s_waitcnt lgkmcnt(8)
	v_pk_fma_f32 v[126:127], v[136:137], v[202:203], 0 op_sel_hi:[1,0,0]
	s_nop 0
	v_pk_fma_f32 v[126:127], v[202:203], v[130:131], v[126:127] op_sel:[1,0,0]
	v_mov_b32_e32 v140, v205
	v_pk_fma_f32 v[126:127], v[204:205], v[138:139], v[126:127] op_sel_hi:[0,1,1]
	v_pk_fma_f32 v[126:127], v[140:141], v[128:129], v[126:127] op_sel_hi:[0,1,1]
	ds_read_b128 v[158:161], v25 offset:17440
	s_waitcnt lgkmcnt(8)
	v_pk_fma_f32 v[144:145], v[136:137], v[216:217], 0 op_sel_hi:[1,0,0]
	s_nop 0
	v_pk_fma_f32 v[140:141], v[216:217], v[130:131], v[144:145] op_sel:[1,0,0]
	s_nop 0
	v_pk_fma_f32 v[140:141], v[218:219], v[138:139], v[140:141] op_sel_hi:[0,1,1]
	v_mov_b32_e32 v142, v219
	v_pk_fma_f32 v[140:141], v[142:143], v[128:129], v[140:141] op_sel_hi:[0,1,1]
	ds_read_b128 v[162:165], v25 offset:25648
	s_waitcnt lgkmcnt(8)
	v_pk_fma_f32 v[146:147], v[136:137], v[220:221], 0 op_sel_hi:[1,0,0]
	s_nop 0
	v_pk_fma_f32 v[142:143], v[220:221], v[130:131], v[146:147] op_sel:[1,0,0]
	s_nop 0
	v_pk_fma_f32 v[142:143], v[222:223], v[138:139], v[142:143] op_sel_hi:[0,1,1]
	v_mov_b32_e32 v144, v223
	v_pk_fma_f32 v[142:143], v[144:145], v[128:129], v[142:143] op_sel_hi:[0,1,1]
	ds_read_b128 v[166:169], v25 offset:33856
	s_waitcnt lgkmcnt(8)
; #define LAS __attribute__((address_space(3)))
; __global__ void __launch_bounds__(NTHREADS, 2) hybrid_fwd(Args a) {
;     ...
;                     for (int j = 0; j < 8; ++j) {
; #pragma unroll
;                         for (int e = 0; e < 16; ++e) { const f32x4 w = *(const LAS f32x4*)(rwT + e * 2052 + j * 256 + lane * 4);
;                             acc2[e] += y2[j][0] * (f32x2){w[0], w[0]}; acc2[e] += y2[j][1] * (f32x2){w[1], w[1]};
;                             acc2[e] += y2[j][2] * (f32x2){w[2], w[2]}; acc2[e] += y2[j][3] * (f32x2){w[3], w[3]}; }
	v_pk_fma_f32 v[148:149], v[136:137], v[224:225], 0 op_sel_hi:[1,0,0]
	s_nop 0
	v_pk_fma_f32 v[144:145], v[224:225], v[130:131], v[148:149] op_sel:[1,0,0]
	s_nop 0
	v_pk_fma_f32 v[144:145], v[226:227], v[138:139], v[144:145] op_sel_hi:[0,1,1]
	v_mov_b32_e32 v146, v227
	v_pk_fma_f32 v[144:145], v[146:147], v[128:129], v[144:145] op_sel_hi:[0,1,1]
	ds_read_b128 v[170:173], v25 offset:42064
	s_waitcnt lgkmcnt(8)
	v_pk_fma_f32 v[150:151], v[136:137], v[228:229], 0 op_sel_hi:[1,0,0]
	s_nop 0
	v_pk_fma_f32 v[146:147], v[228:229], v[130:131], v[150:151] op_sel:[1,0,0]
	s_nop 0
	v_pk_fma_f32 v[146:147], v[230:231], v[138:139], v[146:147] op_sel_hi:[0,1,1]
	v_mov_b32_e32 v148, v231
	v_pk_fma_f32 v[146:147], v[148:149], v[128:129], v[146:147] op_sel_hi:[0,1,1]
	ds_read_b128 v[174:177], v25 offset:50272
	s_waitcnt lgkmcnt(8)
	v_pk_fma_f32 v[194:195], v[136:137], v[232:233], 0 op_sel_hi:[1,0,0]
	s_nop 0
	v_pk_fma_f32 v[148:149], v[232:233], v[130:131], v[194:195] op_sel:[1,0,0]
	ds_read_b128 v[178:181], v25 offset:58480
	v_pk_fma_f32 v[148:149], v[234:235], v[138:139], v[148:149] op_sel_hi:[0,1,1]
	v_mov_b32_e32 v150, v235
	v_pk_fma_f32 v[148:149], v[150:151], v[128:129], v[148:149] op_sel_hi:[0,1,1]
	s_waitcnt lgkmcnt(8)
	v_pk_fma_f32 v[136:137], v[136:137], v[242:243], 0 op_sel_hi:[1,0,0]
	s_nop 0
	v_pk_fma_f32 v[130:131], v[242:243], v[130:131], v[136:137] op_sel:[1,0,0]
	v_mov_b32_e32 v136, v245
	v_pk_fma_f32 v[130:131], v[244:245], v[138:139], v[130:131] op_sel_hi:[0,1,1]
	v_pk_fma_f32 v[150:151], v[136:137], v[128:129], v[130:131] op_sel_hi:[0,1,1]
	ds_read_b128 v[182:185], v238 offset:1152
	s_waitcnt lgkmcnt(8)
	v_pk_fma_f32 v[112:113], v[132:133], v[246:247], v[112:113] op_sel_hi:[1,0,1]
	s_nop 0
	v_pk_fma_f32 v[112:113], v[246:247], v[106:107], v[112:113] op_sel:[1,0,0]
	v_mov_b32_e32 v128, v249
	v_pk_fma_f32 v[112:113], v[248:249], v[134:135], v[112:113] op_sel_hi:[0,1,1]
	v_pk_fma_f32 v[112:113], v[128:129], v[104:105], v[112:113] op_sel_hi:[0,1,1]
	ds_read_b128 v[186:189], v238 offset:9360
	s_waitcnt lgkmcnt(8)
	v_pk_fma_f32 v[136:137], v[132:133], v[250:251], v[152:153] op_sel_hi:[1,0,1]
	s_nop 0
	v_pk_fma_f32 v[128:129], v[250:251], v[106:107], v[136:137] op_sel:[1,0,0]
	s_nop 0
	v_pk_fma_f32 v[128:129], v[252:253], v[134:135], v[128:129] op_sel_hi:[0,1,1]
	v_mov_b32_e32 v130, v253
	v_pk_fma_f32 v[152:153], v[130:131], v[104:105], v[128:129] op_sel_hi:[0,1,1]
	ds_read_b128 v[198:201], v238 offset:17568
	s_waitcnt lgkmcnt(8)
	v_pk_fma_f32 v[136:137], v[132:133], v[158:159], v[154:155] op_sel_hi:[1,0,1]
	s_nop 0
	v_pk_fma_f32 v[128:129], v[158:159], v[106:107], v[136:137] op_sel:[1,0,0]
	ds_read_b128 v[202:205], v238 offset:25776
	v_pk_fma_f32 v[128:129], v[160:161], v[134:135], v[128:129] op_sel_hi:[0,1,1]
	v_mov_b32_e32 v130, v161
	v_pk_fma_f32 v[128:129], v[130:131], v[104:105], v[128:129] op_sel_hi:[0,1,1]
	s_waitcnt lgkmcnt(8)
	v_pk_fma_f32 v[114:115], v[132:133], v[162:163], v[114:115] op_sel_hi:[1,0,1]
	s_nop 0
	v_pk_fma_f32 v[114:115], v[162:163], v[106:107], v[114:115] op_sel:[1,0,0]
	v_mov_b32_e32 v130, v165
	v_pk_fma_f32 v[114:115], v[164:165], v[134:135], v[114:115] op_sel_hi:[0,1,1]
	ds_read_b128 v[216:219], v238 offset:33984
	v_pk_fma_f32 v[114:115], v[130:131], v[104:105], v[114:115] op_sel_hi:[0,1,1]
	s_waitcnt lgkmcnt(8)
	v_pk_fma_f32 v[116:117], v[132:133], v[166:167], v[116:117] op_sel_hi:[1,0,1]
	s_nop 0
	v_pk_fma_f32 v[116:117], v[166:167], v[106:107], v[116:117] op_sel:[1,0,0]
	v_mov_b32_e32 v130, v169
	v_pk_fma_f32 v[116:117], v[168:169], v[134:135], v[116:117] op_sel_hi:[0,1,1]
	ds_read_b128 v[220:223], v238 offset:42192
	v_pk_fma_f32 v[116:117], v[130:131], v[104:105], v[116:117] op_sel_hi:[0,1,1]
	s_waitcnt lgkmcnt(8)
	v_pk_fma_f32 v[118:119], v[132:133], v[170:171], v[118:119] op_sel_hi:[1,0,1]
	s_nop 0
	v_pk_fma_f32 v[118:119], v[170:171], v[106:107], v[118:119] op_sel:[1,0,0]
	v_mov_b32_e32 v130, v173
	v_pk_fma_f32 v[118:119], v[172:173], v[134:135], v[118:119] op_sel_hi:[0,1,1]
	ds_read_b128 v[224:227], v238 offset:50400
	v_pk_fma_f32 v[118:119], v[130:131], v[104:105], v[118:119] op_sel_hi:[0,1,1]
	s_waitcnt lgkmcnt(8)
	v_pk_fma_f32 v[120:121], v[132:133], v[174:175], v[120:121] op_sel_hi:[1,0,1]
	s_nop 0
	v_pk_fma_f32 v[120:121], v[174:175], v[106:107], v[120:121] op_sel:[1,0,0]
	v_mov_b32_e32 v130, v177
	v_pk_fma_f32 v[120:121], v[176:177], v[134:135], v[120:121] op_sel_hi:[0,1,1]
	ds_read_b128 v[228:231], v238 offset:58608
	v_pk_fma_f32 v[120:121], v[130:131], v[104:105], v[120:121] op_sel_hi:[0,1,1]
	s_waitcnt lgkmcnt(8)
	v_pk_fma_f32 v[122:123], v[132:133], v[178:179], v[122:123] op_sel_hi:[1,0,1]
	s_nop 0
	v_pk_fma_f32 v[122:123], v[178:179], v[106:107], v[122:123] op_sel:[1,0,0]
	v_mov_b32_e32 v130, v181
	v_pk_fma_f32 v[122:123], v[180:181], v[134:135], v[122:123] op_sel_hi:[0,1,1]
	ds_read_b128 v[232:235], v25 offset:2048
	v_pk_fma_f32 v[122:123], v[130:131], v[104:105], v[122:123] op_sel_hi:[0,1,1]
	s_waitcnt lgkmcnt(8)
	v_pk_fma_f32 v[124:125], v[132:133], v[182:183], v[124:125] op_sel_hi:[1,0,1]
	s_nop 0
	v_pk_fma_f32 v[124:125], v[182:183], v[106:107], v[124:125] op_sel:[1,0,0]
	v_mov_b32_e32 v130, v185
	v_pk_fma_f32 v[124:125], v[184:185], v[134:135], v[124:125] op_sel_hi:[0,1,1]
	ds_read_b128 v[242:245], v25 offset:10256
	v_pk_fma_f32 v[124:125], v[130:131], v[104:105], v[124:125] op_sel_hi:[0,1,1]
	s_waitcnt lgkmcnt(8)
	v_pk_fma_f32 v[126:127], v[132:133], v[186:187], v[126:127] op_sel_hi:[1,0,1]
	s_nop 0
	v_pk_fma_f32 v[126:127], v[186:187], v[106:107], v[126:127] op_sel:[1,0,0]
	v_mov_b32_e32 v130, v189
	v_pk_fma_f32 v[126:127], v[188:189], v[134:135], v[126:127] op_sel_hi:[0,1,1]
	ds_read_b128 v[246:249], v25 offset:18464
	v_pk_fma_f32 v[126:127], v[130:131], v[104:105], v[126:127] op_sel_hi:[0,1,1]
	s_waitcnt lgkmcnt(8)
; #define LAS __attribute__((address_space(3)))
; __global__ void __launch_bounds__(NTHREADS, 2) hybrid_fwd(Args a) {
;     ...
;                     for (int j = 0; j < 8; ++j) {
; #pragma unroll
;                         for (int e = 0; e < 16; ++e) { const f32x4 w = *(const LAS f32x4*)(rwT + e * 2052 + j * 256 + lane * 4);
;                             acc2[e] += y2[j][0] * (f32x2){w[0], w[0]}; acc2[e] += y2[j][1] * (f32x2){w[1], w[1]};
;                             acc2[e] += y2[j][2] * (f32x2){w[2], w[2]}; acc2[e] += y2[j][3] * (f32x2){w[3], w[3]}; }
	v_pk_fma_f32 v[130:131], v[132:133], v[198:199], v[140:141] op_sel_hi:[1,0,1]
	s_nop 0
	v_pk_fma_f32 v[130:131], v[198:199], v[106:107], v[130:131] op_sel:[1,0,0]
	v_mov_b32_e32 v136, v201
	v_pk_fma_f32 v[130:131], v[200:201], v[134:135], v[130:131] op_sel_hi:[0,1,1]
	v_pk_fma_f32 v[130:131], v[136:137], v[104:105], v[130:131] op_sel_hi:[0,1,1]
	ds_read_b128 v[250:253], v25 offset:26672
	s_waitcnt lgkmcnt(8)
	v_pk_fma_f32 v[140:141], v[132:133], v[202:203], v[142:143] op_sel_hi:[1,0,1]
	s_nop 0
	v_pk_fma_f32 v[136:137], v[202:203], v[106:107], v[140:141] op_sel:[1,0,0]
	s_nop 0
	v_pk_fma_f32 v[136:137], v[204:205], v[134:135], v[136:137] op_sel_hi:[0,1,1]
	v_mov_b32_e32 v138, v205
	v_pk_fma_f32 v[136:137], v[138:139], v[104:105], v[136:137] op_sel_hi:[0,1,1]
	ds_read_b128 v[162:165], v25 offset:34880
	s_waitcnt lgkmcnt(8)
	v_pk_fma_f32 v[142:143], v[132:133], v[216:217], v[144:145] op_sel_hi:[1,0,1]
	s_nop 0
	v_pk_fma_f32 v[138:139], v[216:217], v[106:107], v[142:143] op_sel:[1,0,0]
	s_nop 0
	v_pk_fma_f32 v[138:139], v[218:219], v[134:135], v[138:139] op_sel_hi:[0,1,1]
	v_mov_b32_e32 v140, v219
	v_pk_fma_f32 v[138:139], v[140:141], v[104:105], v[138:139] op_sel_hi:[0,1,1]
	ds_read_b128 v[166:169], v25 offset:43088
	s_waitcnt lgkmcnt(8)
	v_pk_fma_f32 v[144:145], v[132:133], v[220:221], v[146:147] op_sel_hi:[1,0,1]
	s_nop 0
	v_pk_fma_f32 v[140:141], v[220:221], v[106:107], v[144:145] op_sel:[1,0,0]
	s_nop 0
	v_pk_fma_f32 v[140:141], v[222:223], v[134:135], v[140:141] op_sel_hi:[0,1,1]
	v_mov_b32_e32 v142, v223
	v_pk_fma_f32 v[140:141], v[142:143], v[104:105], v[140:141] op_sel_hi:[0,1,1]
	ds_read_b128 v[170:173], v25 offset:51296
	s_waitcnt lgkmcnt(8)
	v_pk_fma_f32 v[146:147], v[132:133], v[224:225], v[148:149] op_sel_hi:[1,0,1]
	s_nop 0
	v_pk_fma_f32 v[142:143], v[224:225], v[106:107], v[146:147] op_sel:[1,0,0]
	s_nop 0
	v_pk_fma_f32 v[142:143], v[226:227], v[134:135], v[142:143] op_sel_hi:[0,1,1]
	v_mov_b32_e32 v144, v227
	v_pk_fma_f32 v[142:143], v[144:145], v[104:105], v[142:143] op_sel_hi:[0,1,1]
	ds_read_b128 v[174:177], v25 offset:59504
	s_waitcnt lgkmcnt(8)
	v_pk_fma_f32 v[132:133], v[132:133], v[228:229], v[150:151] op_sel_hi:[1,0,1]
	s_nop 0
	v_pk_fma_f32 v[106:107], v[228:229], v[106:107], v[132:133] op_sel:[1,0,0]
	v_mov_b32_e32 v132, v231
	v_pk_fma_f32 v[106:107], v[230:231], v[134:135], v[106:107] op_sel_hi:[0,1,1]
	v_pk_fma_f32 v[144:145], v[132:133], v[104:105], v[106:107] op_sel_hi:[0,1,1]
	ds_read_b128 v[178:181], v238 offset:2176
	ds_read_b128 v[182:185], v238 offset:10384
	s_waitcnt lgkmcnt(8)
	v_pk_fma_f32 v[112:113], v[108:109], v[232:233], v[112:113] op_sel_hi:[1,0,1]
	s_nop 0
	v_pk_fma_f32 v[104:105], v[232:233], v[98:99], v[112:113] op_sel:[1,0,0]
	v_mov_b32_e32 v112, v245
	v_pk_fma_f32 v[104:105], v[234:235], v[110:111], v[104:105] op_sel_hi:[0,1,1]
	v_mov_b32_e32 v106, v235
	v_pk_fma_f32 v[104:105], v[106:107], v[96:97], v[104:105] op_sel_hi:[0,1,1]
	v_pk_fma_f32 v[106:107], v[108:109], v[242:243], v[152:153] op_sel_hi:[1,0,1]
	s_nop 0
	v_pk_fma_f32 v[106:107], v[242:243], v[98:99], v[106:107] op_sel:[1,0,0]
	s_nop 0
	v_pk_fma_f32 v[106:107], v[244:245], v[110:111], v[106:107] op_sel_hi:[0,1,1]
	ds_read_b128 v[186:189], v238 offset:18592
	v_pk_fma_f32 v[146:147], v[112:113], v[96:97], v[106:107] op_sel_hi:[0,1,1]
	s_waitcnt lgkmcnt(8)
	v_pk_fma_f32 v[106:107], v[108:109], v[246:247], v[128:129] op_sel_hi:[1,0,1]
	s_nop 0
	v_pk_fma_f32 v[106:107], v[246:247], v[98:99], v[106:107] op_sel:[1,0,0]
	v_mov_b32_e32 v112, v249
	v_pk_fma_f32 v[106:107], v[248:249], v[110:111], v[106:107] op_sel_hi:[0,1,1]
	ds_read_b128 v[158:161], v238 offset:26800
	v_pk_fma_f32 v[106:107], v[112:113], v[96:97], v[106:107] op_sel_hi:[0,1,1]
	s_waitcnt lgkmcnt(8)
	v_pk_fma_f32 v[112:113], v[108:109], v[250:251], v[114:115] op_sel_hi:[1,0,1]
	s_nop 0
	v_pk_fma_f32 v[112:113], v[250:251], v[98:99], v[112:113] op_sel:[1,0,0]
	v_mov_b32_e32 v114, v253
	v_pk_fma_f32 v[112:113], v[252:253], v[110:111], v[112:113] op_sel_hi:[0,1,1]
	ds_read_b128 v[198:201], v238 offset:35008
	v_pk_fma_f32 v[112:113], v[114:115], v[96:97], v[112:113] op_sel_hi:[0,1,1]
	s_waitcnt lgkmcnt(8)
	v_pk_fma_f32 v[114:115], v[108:109], v[162:163], v[116:117] op_sel_hi:[1,0,1]
	s_nop 0
	v_pk_fma_f32 v[114:115], v[162:163], v[98:99], v[114:115] op_sel:[1,0,0]
	v_mov_b32_e32 v116, v165
	v_pk_fma_f32 v[114:115], v[164:165], v[110:111], v[114:115] op_sel_hi:[0,1,1]
	ds_read_b128 v[202:205], v238 offset:43216
	v_pk_fma_f32 v[114:115], v[116:117], v[96:97], v[114:115] op_sel_hi:[0,1,1]
	s_waitcnt lgkmcnt(8)
	v_pk_fma_f32 v[116:117], v[108:109], v[166:167], v[118:119] op_sel_hi:[1,0,1]
	s_nop 0
	v_pk_fma_f32 v[116:117], v[166:167], v[98:99], v[116:117] op_sel:[1,0,0]
	v_mov_b32_e32 v118, v169
	v_pk_fma_f32 v[116:117], v[168:169], v[110:111], v[116:117] op_sel_hi:[0,1,1]
	ds_read_b128 v[216:219], v238 offset:51424
	v_pk_fma_f32 v[116:117], v[118:119], v[96:97], v[116:117] op_sel_hi:[0,1,1]
	s_waitcnt lgkmcnt(8)
	v_pk_fma_f32 v[118:119], v[108:109], v[170:171], v[120:121] op_sel_hi:[1,0,1]
	s_nop 0
	v_pk_fma_f32 v[118:119], v[170:171], v[98:99], v[118:119] op_sel:[1,0,0]
	v_mov_b32_e32 v120, v173
	v_pk_fma_f32 v[118:119], v[172:173], v[110:111], v[118:119] op_sel_hi:[0,1,1]
	ds_read_b128 v[220:223], v238 offset:59632
	v_pk_fma_f32 v[118:119], v[120:121], v[96:97], v[118:119] op_sel_hi:[0,1,1]
	s_waitcnt lgkmcnt(8)
	v_pk_fma_f32 v[120:121], v[108:109], v[174:175], v[122:123] op_sel_hi:[1,0,1]
	s_nop 0
	v_pk_fma_f32 v[120:121], v[174:175], v[98:99], v[120:121] op_sel:[1,0,0]
	v_mov_b32_e32 v122, v177
	v_pk_fma_f32 v[120:121], v[176:177], v[110:111], v[120:121] op_sel_hi:[0,1,1]
	ds_read_b128 v[224:227], v25 offset:3072
	v_pk_fma_f32 v[120:121], v[122:123], v[96:97], v[120:121] op_sel_hi:[0,1,1]
	s_waitcnt lgkmcnt(8)
; #define LAS __attribute__((address_space(3)))
; __global__ void __launch_bounds__(NTHREADS, 2) hybrid_fwd(Args a) {
;     ...
;                     for (int j = 0; j < 8; ++j) {
; #pragma unroll
;                         for (int e = 0; e < 16; ++e) { const f32x4 w = *(const LAS f32x4*)(rwT + e * 2052 + j * 256 + lane * 4);
;                             acc2[e] += y2[j][0] * (f32x2){w[0], w[0]}; acc2[e] += y2[j][1] * (f32x2){w[1], w[1]};
;                             acc2[e] += y2[j][2] * (f32x2){w[2], w[2]}; acc2[e] += y2[j][3] * (f32x2){w[3], w[3]}; }
	v_pk_fma_f32 v[122:123], v[108:109], v[178:179], v[124:125] op_sel_hi:[1,0,1]
	s_nop 0
	v_pk_fma_f32 v[122:123], v[178:179], v[98:99], v[122:123] op_sel:[1,0,0]
	v_mov_b32_e32 v124, v181
	v_pk_fma_f32 v[122:123], v[180:181], v[110:111], v[122:123] op_sel_hi:[0,1,1]
	ds_read_b128 v[228:231], v25 offset:11280
	v_pk_fma_f32 v[122:123], v[124:125], v[96:97], v[122:123] op_sel_hi:[0,1,1]
	s_waitcnt lgkmcnt(8)
	v_pk_fma_f32 v[124:125], v[108:109], v[182:183], v[126:127] op_sel_hi:[1,0,1]
	s_nop 0
	v_pk_fma_f32 v[124:125], v[182:183], v[98:99], v[124:125] op_sel:[1,0,0]
	v_mov_b32_e32 v126, v185
	v_pk_fma_f32 v[124:125], v[184:185], v[110:111], v[124:125] op_sel_hi:[0,1,1]
	v_pk_fma_f32 v[124:125], v[126:127], v[96:97], v[124:125] op_sel_hi:[0,1,1]
	ds_read_b128 v[232:235], v25 offset:19488
	s_waitcnt lgkmcnt(8)
	v_pk_fma_f32 v[130:131], v[108:109], v[186:187], v[130:131] op_sel_hi:[1,0,1]
	s_nop 0
	v_pk_fma_f32 v[126:127], v[186:187], v[98:99], v[130:131] op_sel:[1,0,0]
	s_nop 0
	v_pk_fma_f32 v[126:127], v[188:189], v[110:111], v[126:127] op_sel_hi:[0,1,1]
	v_mov_b32_e32 v128, v189
	v_pk_fma_f32 v[126:127], v[128:129], v[96:97], v[126:127] op_sel_hi:[0,1,1]
	ds_read_b128 v[242:245], v25 offset:27696
	s_waitcnt lgkmcnt(8)
	v_pk_fma_f32 v[132:133], v[108:109], v[158:159], v[136:137] op_sel_hi:[1,0,1]
	s_nop 0
	v_pk_fma_f32 v[128:129], v[158:159], v[98:99], v[132:133] op_sel:[1,0,0]
	s_nop 0
	v_pk_fma_f32 v[128:129], v[160:161], v[110:111], v[128:129] op_sel_hi:[0,1,1]
	v_mov_b32_e32 v130, v161
	v_pk_fma_f32 v[128:129], v[130:131], v[96:97], v[128:129] op_sel_hi:[0,1,1]
	ds_read_b128 v[246:249], v25 offset:35904
	s_waitcnt lgkmcnt(8)
	v_pk_fma_f32 v[134:135], v[108:109], v[198:199], v[138:139] op_sel_hi:[1,0,1]
	s_nop 0
	v_pk_fma_f32 v[130:131], v[198:199], v[98:99], v[134:135] op_sel:[1,0,0]
	s_nop 0
	v_pk_fma_f32 v[130:131], v[200:201], v[110:111], v[130:131] op_sel_hi:[0,1,1]
	v_mov_b32_e32 v132, v201
	v_pk_fma_f32 v[130:131], v[132:133], v[96:97], v[130:131] op_sel_hi:[0,1,1]
	ds_read_b128 v[250:253], v25 offset:44112
	s_waitcnt lgkmcnt(8)
	v_pk_fma_f32 v[136:137], v[108:109], v[202:203], v[140:141] op_sel_hi:[1,0,1]
	s_nop 0
	v_pk_fma_f32 v[132:133], v[202:203], v[98:99], v[136:137] op_sel:[1,0,0]
	s_nop 0
	v_pk_fma_f32 v[132:133], v[204:205], v[110:111], v[132:133] op_sel_hi:[0,1,1]
	v_mov_b32_e32 v134, v205
	v_pk_fma_f32 v[132:133], v[134:135], v[96:97], v[132:133] op_sel_hi:[0,1,1]
	ds_read_b128 v[162:165], v25 offset:52320
	s_waitcnt lgkmcnt(8)
	v_pk_fma_f32 v[138:139], v[108:109], v[216:217], v[142:143] op_sel_hi:[1,0,1]
	s_nop 0
	v_pk_fma_f32 v[134:135], v[216:217], v[98:99], v[138:139] op_sel:[1,0,0]
	s_nop 0
	v_pk_fma_f32 v[134:135], v[218:219], v[110:111], v[134:135] op_sel_hi:[0,1,1]
	v_mov_b32_e32 v136, v219
	v_pk_fma_f32 v[134:135], v[136:137], v[96:97], v[134:135] op_sel_hi:[0,1,1]
	ds_read_b128 v[166:169], v25 offset:60528
	s_waitcnt lgkmcnt(8)
	v_pk_fma_f32 v[108:109], v[108:109], v[220:221], v[144:145] op_sel_hi:[1,0,1]
	s_nop 0
	v_pk_fma_f32 v[98:99], v[220:221], v[98:99], v[108:109] op_sel:[1,0,0]
	v_mov_b32_e32 v108, v223
	v_pk_fma_f32 v[98:99], v[222:223], v[110:111], v[98:99] op_sel_hi:[0,1,1]
	v_pk_fma_f32 v[136:137], v[108:109], v[96:97], v[98:99] op_sel_hi:[0,1,1]
	ds_read_b128 v[170:173], v238 offset:3200
	ds_read_b128 v[174:177], v238 offset:11408
	s_waitcnt lgkmcnt(8)
	v_pk_fma_f32 v[104:105], v[100:101], v[224:225], v[104:105] op_sel_hi:[1,0,1]
	s_nop 0
	v_pk_fma_f32 v[96:97], v[224:225], v[90:91], v[104:105] op_sel:[1,0,0]
	v_mov_b32_e32 v104, v231
	v_pk_fma_f32 v[96:97], v[226:227], v[102:103], v[96:97] op_sel_hi:[0,1,1]
	v_mov_b32_e32 v98, v227
	v_pk_fma_f32 v[96:97], v[98:99], v[88:89], v[96:97] op_sel_hi:[0,1,1]
	v_pk_fma_f32 v[98:99], v[100:101], v[228:229], v[146:147] op_sel_hi:[1,0,1]
	s_nop 0
	v_pk_fma_f32 v[98:99], v[228:229], v[90:91], v[98:99] op_sel:[1,0,0]
	s_nop 0
	v_pk_fma_f32 v[98:99], v[230:231], v[102:103], v[98:99] op_sel_hi:[0,1,1]
	ds_read_b128 v[178:181], v238 offset:19616
	v_pk_fma_f32 v[138:139], v[104:105], v[88:89], v[98:99] op_sel_hi:[0,1,1]
	s_waitcnt lgkmcnt(8)
	v_pk_fma_f32 v[98:99], v[100:101], v[232:233], v[106:107] op_sel_hi:[1,0,1]
	s_nop 0
	v_pk_fma_f32 v[98:99], v[232:233], v[90:91], v[98:99] op_sel:[1,0,0]
	v_mov_b32_e32 v104, v235
	v_pk_fma_f32 v[98:99], v[234:235], v[102:103], v[98:99] op_sel_hi:[0,1,1]
	v_pk_fma_f32 v[98:99], v[104:105], v[88:89], v[98:99] op_sel_hi:[0,1,1]
	ds_read_b128 v[182:185], v238 offset:27824
	s_waitcnt lgkmcnt(8)
	v_pk_fma_f32 v[108:109], v[100:101], v[242:243], v[112:113] op_sel_hi:[1,0,1]
	s_nop 0
	v_pk_fma_f32 v[104:105], v[242:243], v[90:91], v[108:109] op_sel:[1,0,0]
	s_nop 0
	v_pk_fma_f32 v[104:105], v[244:245], v[102:103], v[104:105] op_sel_hi:[0,1,1]
	v_mov_b32_e32 v106, v245
	v_pk_fma_f32 v[104:105], v[106:107], v[88:89], v[104:105] op_sel_hi:[0,1,1]
	ds_read_b128 v[186:189], v238 offset:36032
	s_waitcnt lgkmcnt(8)
	v_pk_fma_f32 v[110:111], v[100:101], v[246:247], v[114:115] op_sel_hi:[1,0,1]
	s_nop 0
	v_pk_fma_f32 v[106:107], v[246:247], v[90:91], v[110:111] op_sel:[1,0,0]
	s_nop 0
	v_pk_fma_f32 v[106:107], v[248:249], v[102:103], v[106:107] op_sel_hi:[0,1,1]
	v_mov_b32_e32 v108, v249
	v_pk_fma_f32 v[106:107], v[108:109], v[88:89], v[106:107] op_sel_hi:[0,1,1]
	ds_read_b128 v[158:161], v238 offset:44240
	s_waitcnt lgkmcnt(8)
	v_pk_fma_f32 v[112:113], v[100:101], v[250:251], v[116:117] op_sel_hi:[1,0,1]
	s_nop 0
	v_pk_fma_f32 v[108:109], v[250:251], v[90:91], v[112:113] op_sel:[1,0,0]
	s_nop 0
	v_pk_fma_f32 v[108:109], v[252:253], v[102:103], v[108:109] op_sel_hi:[0,1,1]
	v_mov_b32_e32 v110, v253
	v_pk_fma_f32 v[108:109], v[110:111], v[88:89], v[108:109] op_sel_hi:[0,1,1]
	ds_read_b128 v[198:201], v238 offset:52448
	s_waitcnt lgkmcnt(8)
; #define LAS __attribute__((address_space(3)))
; __global__ void __launch_bounds__(NTHREADS, 2) hybrid_fwd(Args a) {
;     ...
;                     for (int j = 0; j < 8; ++j) {
; #pragma unroll
;                         for (int e = 0; e < 16; ++e) { const f32x4 w = *(const LAS f32x4*)(rwT + e * 2052 + j * 256 + lane * 4);
;                             acc2[e] += y2[j][0] * (f32x2){w[0], w[0]}; acc2[e] += y2[j][1] * (f32x2){w[1], w[1]};
;                             acc2[e] += y2[j][2] * (f32x2){w[2], w[2]}; acc2[e] += y2[j][3] * (f32x2){w[3], w[3]}; }
	v_pk_fma_f32 v[114:115], v[100:101], v[162:163], v[118:119] op_sel_hi:[1,0,1]
	s_nop 0
	v_pk_fma_f32 v[110:111], v[162:163], v[90:91], v[114:115] op_sel:[1,0,0]
	s_nop 0
	v_pk_fma_f32 v[110:111], v[164:165], v[102:103], v[110:111] op_sel_hi:[0,1,1]
	v_mov_b32_e32 v112, v165
	v_pk_fma_f32 v[110:111], v[112:113], v[88:89], v[110:111] op_sel_hi:[0,1,1]
	ds_read_b128 v[202:205], v238 offset:60656
	s_waitcnt lgkmcnt(8)
	v_pk_fma_f32 v[116:117], v[100:101], v[166:167], v[120:121] op_sel_hi:[1,0,1]
	s_nop 0
	v_pk_fma_f32 v[112:113], v[166:167], v[90:91], v[116:117] op_sel:[1,0,0]
	s_nop 0
	v_pk_fma_f32 v[112:113], v[168:169], v[102:103], v[112:113] op_sel_hi:[0,1,1]
	v_mov_b32_e32 v114, v169
	v_pk_fma_f32 v[112:113], v[114:115], v[88:89], v[112:113] op_sel_hi:[0,1,1]
	ds_read_b128 v[216:219], v25 offset:4096
	s_waitcnt lgkmcnt(8)
	v_pk_fma_f32 v[118:119], v[100:101], v[170:171], v[122:123] op_sel_hi:[1,0,1]
	s_nop 0
	v_pk_fma_f32 v[114:115], v[170:171], v[90:91], v[118:119] op_sel:[1,0,0]
	s_nop 0
	v_pk_fma_f32 v[114:115], v[172:173], v[102:103], v[114:115] op_sel_hi:[0,1,1]
	v_mov_b32_e32 v116, v173
	v_pk_fma_f32 v[114:115], v[116:117], v[88:89], v[114:115] op_sel_hi:[0,1,1]
	ds_read_b128 v[220:223], v25 offset:12304
	s_waitcnt lgkmcnt(8)
	v_pk_fma_f32 v[120:121], v[100:101], v[174:175], v[124:125] op_sel_hi:[1,0,1]
	s_nop 0
	v_pk_fma_f32 v[116:117], v[174:175], v[90:91], v[120:121] op_sel:[1,0,0]
	s_nop 0
	v_pk_fma_f32 v[116:117], v[176:177], v[102:103], v[116:117] op_sel_hi:[0,1,1]
	v_mov_b32_e32 v118, v177
	v_pk_fma_f32 v[116:117], v[118:119], v[88:89], v[116:117] op_sel_hi:[0,1,1]
	ds_read_b128 v[224:227], v25 offset:20512
	s_waitcnt lgkmcnt(8)
	v_pk_fma_f32 v[122:123], v[100:101], v[178:179], v[126:127] op_sel_hi:[1,0,1]
	s_nop 0
	v_pk_fma_f32 v[118:119], v[178:179], v[90:91], v[122:123] op_sel:[1,0,0]
	s_nop 0
	v_pk_fma_f32 v[118:119], v[180:181], v[102:103], v[118:119] op_sel_hi:[0,1,1]
	v_mov_b32_e32 v120, v181
	v_pk_fma_f32 v[118:119], v[120:121], v[88:89], v[118:119] op_sel_hi:[0,1,1]
	ds_read_b128 v[228:231], v25 offset:28720
	s_waitcnt lgkmcnt(8)
	v_pk_fma_f32 v[124:125], v[100:101], v[182:183], v[128:129] op_sel_hi:[1,0,1]
	s_nop 0
	v_pk_fma_f32 v[120:121], v[182:183], v[90:91], v[124:125] op_sel:[1,0,0]
	s_nop 0
	v_pk_fma_f32 v[120:121], v[184:185], v[102:103], v[120:121] op_sel_hi:[0,1,1]
	v_mov_b32_e32 v122, v185
	v_pk_fma_f32 v[120:121], v[122:123], v[88:89], v[120:121] op_sel_hi:[0,1,1]
	ds_read_b128 v[232:235], v25 offset:36928
	s_waitcnt lgkmcnt(8)
	v_pk_fma_f32 v[126:127], v[100:101], v[186:187], v[130:131] op_sel_hi:[1,0,1]
	s_nop 0
	v_pk_fma_f32 v[122:123], v[186:187], v[90:91], v[126:127] op_sel:[1,0,0]
	s_nop 0
	v_pk_fma_f32 v[122:123], v[188:189], v[102:103], v[122:123] op_sel_hi:[0,1,1]
	v_mov_b32_e32 v124, v189
	v_pk_fma_f32 v[122:123], v[124:125], v[88:89], v[122:123] op_sel_hi:[0,1,1]
	ds_read_b128 v[242:245], v25 offset:45136
	s_waitcnt lgkmcnt(8)
	v_pk_fma_f32 v[128:129], v[100:101], v[158:159], v[132:133] op_sel_hi:[1,0,1]
	s_nop 0
	v_pk_fma_f32 v[124:125], v[158:159], v[90:91], v[128:129] op_sel:[1,0,0]
	s_nop 0
	v_pk_fma_f32 v[124:125], v[160:161], v[102:103], v[124:125] op_sel_hi:[0,1,1]
	v_mov_b32_e32 v126, v161
	v_pk_fma_f32 v[124:125], v[126:127], v[88:89], v[124:125] op_sel_hi:[0,1,1]
	ds_read_b128 v[246:249], v25 offset:53344
	s_waitcnt lgkmcnt(8)
	v_pk_fma_f32 v[130:131], v[100:101], v[198:199], v[134:135] op_sel_hi:[1,0,1]
	s_nop 0
	v_pk_fma_f32 v[126:127], v[198:199], v[90:91], v[130:131] op_sel:[1,0,0]
	s_nop 0
	v_pk_fma_f32 v[126:127], v[200:201], v[102:103], v[126:127] op_sel_hi:[0,1,1]
	v_mov_b32_e32 v128, v201
	v_pk_fma_f32 v[126:127], v[128:129], v[88:89], v[126:127] op_sel_hi:[0,1,1]
	ds_read_b128 v[250:253], v25 offset:61552
	s_waitcnt lgkmcnt(8)
	v_pk_fma_f32 v[100:101], v[100:101], v[202:203], v[136:137] op_sel_hi:[1,0,1]
	s_nop 0
	v_pk_fma_f32 v[90:91], v[202:203], v[90:91], v[100:101] op_sel:[1,0,0]
	v_mov_b32_e32 v100, v205
	v_pk_fma_f32 v[90:91], v[204:205], v[102:103], v[90:91] op_sel_hi:[0,1,1]
	v_pk_fma_f32 v[128:129], v[100:101], v[88:89], v[90:91] op_sel_hi:[0,1,1]
	ds_read_b128 v[162:165], v238 offset:4224
	ds_read_b128 v[166:169], v238 offset:12432
	s_waitcnt lgkmcnt(8)
	v_pk_fma_f32 v[96:97], v[92:93], v[216:217], v[96:97] op_sel_hi:[1,0,1]
	s_nop 0
	v_pk_fma_f32 v[88:89], v[216:217], v[86:87], v[96:97] op_sel:[1,0,0]
	v_mov_b32_e32 v96, v223
	v_pk_fma_f32 v[88:89], v[218:219], v[94:95], v[88:89] op_sel_hi:[0,1,1]
	v_mov_b32_e32 v90, v219
	v_pk_fma_f32 v[88:89], v[90:91], v[84:85], v[88:89] op_sel_hi:[0,1,1]
	v_pk_fma_f32 v[90:91], v[92:93], v[220:221], v[138:139] op_sel_hi:[1,0,1]
	s_nop 0
	v_pk_fma_f32 v[90:91], v[220:221], v[86:87], v[90:91] op_sel:[1,0,0]
	s_nop 0
	v_pk_fma_f32 v[90:91], v[222:223], v[94:95], v[90:91] op_sel_hi:[0,1,1]
	ds_read_b128 v[170:173], v238 offset:20640
	v_pk_fma_f32 v[130:131], v[96:97], v[84:85], v[90:91] op_sel_hi:[0,1,1]
	s_waitcnt lgkmcnt(8)
	v_pk_fma_f32 v[90:91], v[92:93], v[224:225], v[98:99] op_sel_hi:[1,0,1]
	s_nop 0
	v_pk_fma_f32 v[90:91], v[224:225], v[86:87], v[90:91] op_sel:[1,0,0]
	v_mov_b32_e32 v96, v227
	v_pk_fma_f32 v[90:91], v[226:227], v[94:95], v[90:91] op_sel_hi:[0,1,1]
	v_pk_fma_f32 v[90:91], v[96:97], v[84:85], v[90:91] op_sel_hi:[0,1,1]
	ds_read_b128 v[174:177], v238 offset:28848
	s_waitcnt lgkmcnt(8)
	v_pk_fma_f32 v[100:101], v[92:93], v[228:229], v[104:105] op_sel_hi:[1,0,1]
	s_nop 0
	v_pk_fma_f32 v[96:97], v[228:229], v[86:87], v[100:101] op_sel:[1,0,0]
	s_nop 0
	v_pk_fma_f32 v[96:97], v[230:231], v[94:95], v[96:97] op_sel_hi:[0,1,1]
	v_mov_b32_e32 v98, v231
	v_pk_fma_f32 v[96:97], v[98:99], v[84:85], v[96:97] op_sel_hi:[0,1,1]
	ds_read_b128 v[178:181], v238 offset:37056
	s_waitcnt lgkmcnt(8)
; #define LAS __attribute__((address_space(3)))
; __global__ void __launch_bounds__(NTHREADS, 2) hybrid_fwd(Args a) {
;     ...
;                     for (int j = 0; j < 8; ++j) {
; #pragma unroll
;                         for (int e = 0; e < 16; ++e) { const f32x4 w = *(const LAS f32x4*)(rwT + e * 2052 + j * 256 + lane * 4);
;                             acc2[e] += y2[j][0] * (f32x2){w[0], w[0]}; acc2[e] += y2[j][1] * (f32x2){w[1], w[1]};
;                             acc2[e] += y2[j][2] * (f32x2){w[2], w[2]}; acc2[e] += y2[j][3] * (f32x2){w[3], w[3]}; }
	v_pk_fma_f32 v[102:103], v[92:93], v[232:233], v[106:107] op_sel_hi:[1,0,1]
	s_nop 0
	v_pk_fma_f32 v[98:99], v[232:233], v[86:87], v[102:103] op_sel:[1,0,0]
	s_nop 0
	v_pk_fma_f32 v[98:99], v[234:235], v[94:95], v[98:99] op_sel_hi:[0,1,1]
	v_mov_b32_e32 v100, v235
	v_pk_fma_f32 v[98:99], v[100:101], v[84:85], v[98:99] op_sel_hi:[0,1,1]
	ds_read_b128 v[182:185], v238 offset:45264
	s_waitcnt lgkmcnt(8)
	v_pk_fma_f32 v[104:105], v[92:93], v[242:243], v[108:109] op_sel_hi:[1,0,1]
	s_nop 0
	v_pk_fma_f32 v[100:101], v[242:243], v[86:87], v[104:105] op_sel:[1,0,0]
	s_nop 0
	v_pk_fma_f32 v[100:101], v[244:245], v[94:95], v[100:101] op_sel_hi:[0,1,1]
	v_mov_b32_e32 v102, v245
	v_pk_fma_f32 v[100:101], v[102:103], v[84:85], v[100:101] op_sel_hi:[0,1,1]
	ds_read_b128 v[186:189], v238 offset:53472
	s_waitcnt lgkmcnt(8)
	v_pk_fma_f32 v[106:107], v[92:93], v[246:247], v[110:111] op_sel_hi:[1,0,1]
	s_nop 0
	v_pk_fma_f32 v[102:103], v[246:247], v[86:87], v[106:107] op_sel:[1,0,0]
	s_nop 0
	v_pk_fma_f32 v[102:103], v[248:249], v[94:95], v[102:103] op_sel_hi:[0,1,1]
	v_mov_b32_e32 v104, v249
	v_pk_fma_f32 v[102:103], v[104:105], v[84:85], v[102:103] op_sel_hi:[0,1,1]
	ds_read_b128 v[158:161], v238 offset:61680
	s_waitcnt lgkmcnt(8)
	v_pk_fma_f32 v[108:109], v[92:93], v[250:251], v[112:113] op_sel_hi:[1,0,1]
	s_nop 0
	v_pk_fma_f32 v[104:105], v[250:251], v[86:87], v[108:109] op_sel:[1,0,0]
	s_nop 0
	v_pk_fma_f32 v[104:105], v[252:253], v[94:95], v[104:105] op_sel_hi:[0,1,1]
	v_mov_b32_e32 v106, v253
	v_pk_fma_f32 v[104:105], v[106:107], v[84:85], v[104:105] op_sel_hi:[0,1,1]
	ds_read_b128 v[198:201], v25 offset:5120
	s_waitcnt lgkmcnt(8)
	v_pk_fma_f32 v[110:111], v[92:93], v[162:163], v[114:115] op_sel_hi:[1,0,1]
	s_nop 0
	v_pk_fma_f32 v[106:107], v[162:163], v[86:87], v[110:111] op_sel:[1,0,0]
	s_nop 0
	v_pk_fma_f32 v[106:107], v[164:165], v[94:95], v[106:107] op_sel_hi:[0,1,1]
	v_mov_b32_e32 v108, v165
	v_pk_fma_f32 v[106:107], v[108:109], v[84:85], v[106:107] op_sel_hi:[0,1,1]
	ds_read_b128 v[202:205], v25 offset:13328
	s_waitcnt lgkmcnt(8)
	v_pk_fma_f32 v[112:113], v[92:93], v[166:167], v[116:117] op_sel_hi:[1,0,1]
	s_nop 0
	v_pk_fma_f32 v[108:109], v[166:167], v[86:87], v[112:113] op_sel:[1,0,0]
	s_nop 0
	v_pk_fma_f32 v[108:109], v[168:169], v[94:95], v[108:109] op_sel_hi:[0,1,1]
	v_mov_b32_e32 v110, v169
	v_pk_fma_f32 v[108:109], v[110:111], v[84:85], v[108:109] op_sel_hi:[0,1,1]
	ds_read_b128 v[216:219], v25 offset:21536
	s_waitcnt lgkmcnt(8)
	v_pk_fma_f32 v[114:115], v[92:93], v[170:171], v[118:119] op_sel_hi:[1,0,1]
	s_nop 0
	v_pk_fma_f32 v[110:111], v[170:171], v[86:87], v[114:115] op_sel:[1,0,0]
	s_nop 0
	v_pk_fma_f32 v[110:111], v[172:173], v[94:95], v[110:111] op_sel_hi:[0,1,1]
	v_mov_b32_e32 v112, v173
	v_pk_fma_f32 v[110:111], v[112:113], v[84:85], v[110:111] op_sel_hi:[0,1,1]
	ds_read_b128 v[220:223], v25 offset:29744
	s_waitcnt lgkmcnt(8)
	v_pk_fma_f32 v[116:117], v[92:93], v[174:175], v[120:121] op_sel_hi:[1,0,1]
	s_nop 0
	v_pk_fma_f32 v[112:113], v[174:175], v[86:87], v[116:117] op_sel:[1,0,0]
	s_nop 0
	v_pk_fma_f32 v[112:113], v[176:177], v[94:95], v[112:113] op_sel_hi:[0,1,1]
	v_mov_b32_e32 v114, v177
	v_pk_fma_f32 v[112:113], v[114:115], v[84:85], v[112:113] op_sel_hi:[0,1,1]
	ds_read_b128 v[224:227], v25 offset:37952
	s_waitcnt lgkmcnt(8)
	v_pk_fma_f32 v[118:119], v[92:93], v[178:179], v[122:123] op_sel_hi:[1,0,1]
	s_nop 0
	v_pk_fma_f32 v[114:115], v[178:179], v[86:87], v[118:119] op_sel:[1,0,0]
	s_nop 0
	v_pk_fma_f32 v[114:115], v[180:181], v[94:95], v[114:115] op_sel_hi:[0,1,1]
	v_mov_b32_e32 v116, v181
	v_pk_fma_f32 v[114:115], v[116:117], v[84:85], v[114:115] op_sel_hi:[0,1,1]
	ds_read_b128 v[228:231], v25 offset:46160
	s_waitcnt lgkmcnt(8)
	v_pk_fma_f32 v[120:121], v[92:93], v[182:183], v[124:125] op_sel_hi:[1,0,1]
	s_nop 0
	v_pk_fma_f32 v[116:117], v[182:183], v[86:87], v[120:121] op_sel:[1,0,0]
	s_nop 0
	v_pk_fma_f32 v[116:117], v[184:185], v[94:95], v[116:117] op_sel_hi:[0,1,1]
	v_mov_b32_e32 v118, v185
	v_pk_fma_f32 v[116:117], v[118:119], v[84:85], v[116:117] op_sel_hi:[0,1,1]
	ds_read_b128 v[232:235], v25 offset:54368
	s_waitcnt lgkmcnt(8)
	v_pk_fma_f32 v[122:123], v[92:93], v[186:187], v[126:127] op_sel_hi:[1,0,1]
	s_nop 0
	v_pk_fma_f32 v[118:119], v[186:187], v[86:87], v[122:123] op_sel:[1,0,0]
	s_nop 0
	v_pk_fma_f32 v[118:119], v[188:189], v[94:95], v[118:119] op_sel_hi:[0,1,1]
	v_mov_b32_e32 v120, v189
	v_pk_fma_f32 v[118:119], v[120:121], v[84:85], v[118:119] op_sel_hi:[0,1,1]
	ds_read_b128 v[242:245], v25 offset:62576
	s_waitcnt lgkmcnt(8)
	v_pk_fma_f32 v[92:93], v[92:93], v[158:159], v[128:129] op_sel_hi:[1,0,1]
	s_nop 0
	v_pk_fma_f32 v[86:87], v[158:159], v[86:87], v[92:93] op_sel:[1,0,0]
	v_mov_b32_e32 v92, v161
	v_pk_fma_f32 v[86:87], v[160:161], v[94:95], v[86:87] op_sel_hi:[0,1,1]
	v_pk_fma_f32 v[120:121], v[92:93], v[84:85], v[86:87] op_sel_hi:[0,1,1]
	ds_read_b128 v[246:249], v238 offset:5248
	s_waitcnt lgkmcnt(8)
	v_pk_fma_f32 v[88:89], v[80:81], v[198:199], v[88:89] op_sel_hi:[1,0,1]
	s_nop 0
	v_pk_fma_f32 v[84:85], v[198:199], v[78:79], v[88:89] op_sel:[1,0,0]
	s_nop 0
	v_pk_fma_f32 v[84:85], v[200:201], v[82:83], v[84:85] op_sel_hi:[0,1,1]
	v_mov_b32_e32 v86, v201
	v_pk_fma_f32 v[84:85], v[86:87], v[76:77], v[84:85] op_sel_hi:[0,1,1]
	ds_read_b128 v[250:253], v238 offset:13456
	s_waitcnt lgkmcnt(8)
	v_pk_fma_f32 v[92:93], v[80:81], v[202:203], v[130:131] op_sel_hi:[1,0,1]
	s_nop 0
	v_pk_fma_f32 v[86:87], v[202:203], v[78:79], v[92:93] op_sel:[1,0,0]
	s_nop 0
	v_pk_fma_f32 v[86:87], v[204:205], v[82:83], v[86:87] op_sel_hi:[0,1,1]
	v_mov_b32_e32 v88, v205
	v_pk_fma_f32 v[122:123], v[88:89], v[76:77], v[86:87] op_sel_hi:[0,1,1]
	ds_read_b128 v[162:165], v238 offset:21664
	s_waitcnt lgkmcnt(8)
; #define LAS __attribute__((address_space(3)))
; __global__ void __launch_bounds__(NTHREADS, 2) hybrid_fwd(Args a) {
;     ...
;                     for (int j = 0; j < 8; ++j) {
; #pragma unroll
;                         for (int e = 0; e < 16; ++e) { const f32x4 w = *(const LAS f32x4*)(rwT + e * 2052 + j * 256 + lane * 4);
;                             acc2[e] += y2[j][0] * (f32x2){w[0], w[0]}; acc2[e] += y2[j][1] * (f32x2){w[1], w[1]};
;                             acc2[e] += y2[j][2] * (f32x2){w[2], w[2]}; acc2[e] += y2[j][3] * (f32x2){w[3], w[3]}; }
	v_pk_fma_f32 v[90:91], v[80:81], v[216:217], v[90:91] op_sel_hi:[1,0,1]
	s_nop 0
	v_pk_fma_f32 v[86:87], v[216:217], v[78:79], v[90:91] op_sel:[1,0,0]
	s_nop 0
	v_pk_fma_f32 v[86:87], v[218:219], v[82:83], v[86:87] op_sel_hi:[0,1,1]
	v_mov_b32_e32 v88, v219
	v_pk_fma_f32 v[86:87], v[88:89], v[76:77], v[86:87] op_sel_hi:[0,1,1]
	ds_read_b128 v[166:169], v238 offset:29872
	s_waitcnt lgkmcnt(8)
	v_pk_fma_f32 v[92:93], v[80:81], v[220:221], v[96:97] op_sel_hi:[1,0,1]
	s_nop 0
	v_pk_fma_f32 v[88:89], v[220:221], v[78:79], v[92:93] op_sel:[1,0,0]
	s_nop 0
	v_pk_fma_f32 v[88:89], v[222:223], v[82:83], v[88:89] op_sel_hi:[0,1,1]
	v_mov_b32_e32 v90, v223
	v_pk_fma_f32 v[88:89], v[90:91], v[76:77], v[88:89] op_sel_hi:[0,1,1]
	ds_read_b128 v[170:173], v238 offset:38080
	s_waitcnt lgkmcnt(8)
	v_pk_fma_f32 v[94:95], v[80:81], v[224:225], v[98:99] op_sel_hi:[1,0,1]
	s_nop 0
	v_pk_fma_f32 v[90:91], v[224:225], v[78:79], v[94:95] op_sel:[1,0,0]
	s_nop 0
	v_pk_fma_f32 v[90:91], v[226:227], v[82:83], v[90:91] op_sel_hi:[0,1,1]
	v_mov_b32_e32 v92, v227
	v_pk_fma_f32 v[90:91], v[92:93], v[76:77], v[90:91] op_sel_hi:[0,1,1]
	ds_read_b128 v[174:177], v238 offset:46288
	s_waitcnt lgkmcnt(8)
	v_pk_fma_f32 v[96:97], v[80:81], v[228:229], v[100:101] op_sel_hi:[1,0,1]
	s_nop 0
	v_pk_fma_f32 v[92:93], v[228:229], v[78:79], v[96:97] op_sel:[1,0,0]
	s_nop 0
	v_pk_fma_f32 v[92:93], v[230:231], v[82:83], v[92:93] op_sel_hi:[0,1,1]
	v_mov_b32_e32 v94, v231
	v_pk_fma_f32 v[92:93], v[94:95], v[76:77], v[92:93] op_sel_hi:[0,1,1]
	ds_read_b128 v[178:181], v238 offset:54496
	s_waitcnt lgkmcnt(8)
	v_pk_fma_f32 v[98:99], v[80:81], v[232:233], v[102:103] op_sel_hi:[1,0,1]
	s_nop 0
	v_pk_fma_f32 v[94:95], v[232:233], v[78:79], v[98:99] op_sel:[1,0,0]
	s_nop 0
	v_pk_fma_f32 v[94:95], v[234:235], v[82:83], v[94:95] op_sel_hi:[0,1,1]
	v_mov_b32_e32 v96, v235
	v_pk_fma_f32 v[94:95], v[96:97], v[76:77], v[94:95] op_sel_hi:[0,1,1]
	ds_read_b128 v[182:185], v238 offset:62704
	s_waitcnt lgkmcnt(8)
	v_pk_fma_f32 v[100:101], v[80:81], v[242:243], v[104:105] op_sel_hi:[1,0,1]
	s_nop 0
	v_pk_fma_f32 v[96:97], v[242:243], v[78:79], v[100:101] op_sel:[1,0,0]
	s_nop 0
	v_pk_fma_f32 v[96:97], v[244:245], v[82:83], v[96:97] op_sel_hi:[0,1,1]
	v_mov_b32_e32 v98, v245
	v_pk_fma_f32 v[96:97], v[98:99], v[76:77], v[96:97] op_sel_hi:[0,1,1]
	ds_read_b128 v[186:189], v25 offset:6144
	s_waitcnt lgkmcnt(8)
	v_pk_fma_f32 v[102:103], v[80:81], v[246:247], v[106:107] op_sel_hi:[1,0,1]
	s_nop 0
	v_pk_fma_f32 v[98:99], v[246:247], v[78:79], v[102:103] op_sel:[1,0,0]
	s_nop 0
	v_pk_fma_f32 v[98:99], v[248:249], v[82:83], v[98:99] op_sel_hi:[0,1,1]
	v_mov_b32_e32 v100, v249
	v_pk_fma_f32 v[98:99], v[100:101], v[76:77], v[98:99] op_sel_hi:[0,1,1]
	ds_read_b128 v[158:161], v25 offset:14352
	s_waitcnt lgkmcnt(8)
	v_pk_fma_f32 v[104:105], v[80:81], v[250:251], v[108:109] op_sel_hi:[1,0,1]
	s_nop 0
	v_pk_fma_f32 v[100:101], v[250:251], v[78:79], v[104:105] op_sel:[1,0,0]
	s_nop 0
	v_pk_fma_f32 v[100:101], v[252:253], v[82:83], v[100:101] op_sel_hi:[0,1,1]
	v_mov_b32_e32 v102, v253
	v_pk_fma_f32 v[100:101], v[102:103], v[76:77], v[100:101] op_sel_hi:[0,1,1]
	ds_read_b128 v[198:201], v25 offset:22560
	s_waitcnt lgkmcnt(8)
	v_pk_fma_f32 v[106:107], v[80:81], v[162:163], v[110:111] op_sel_hi:[1,0,1]
	s_nop 0
	v_pk_fma_f32 v[102:103], v[162:163], v[78:79], v[106:107] op_sel:[1,0,0]
	s_nop 0
	v_pk_fma_f32 v[102:103], v[164:165], v[82:83], v[102:103] op_sel_hi:[0,1,1]
	v_mov_b32_e32 v104, v165
	v_pk_fma_f32 v[102:103], v[104:105], v[76:77], v[102:103] op_sel_hi:[0,1,1]
	ds_read_b128 v[202:205], v25 offset:30768
	s_waitcnt lgkmcnt(8)
	v_pk_fma_f32 v[108:109], v[80:81], v[166:167], v[112:113] op_sel_hi:[1,0,1]
	s_nop 0
	v_pk_fma_f32 v[104:105], v[166:167], v[78:79], v[108:109] op_sel:[1,0,0]
	s_nop 0
	v_pk_fma_f32 v[104:105], v[168:169], v[82:83], v[104:105] op_sel_hi:[0,1,1]
	v_mov_b32_e32 v106, v169
	v_pk_fma_f32 v[104:105], v[106:107], v[76:77], v[104:105] op_sel_hi:[0,1,1]
	ds_read_b128 v[216:219], v25 offset:38976
	s_waitcnt lgkmcnt(8)
	v_pk_fma_f32 v[110:111], v[80:81], v[170:171], v[114:115] op_sel_hi:[1,0,1]
	s_nop 0
	v_pk_fma_f32 v[106:107], v[170:171], v[78:79], v[110:111] op_sel:[1,0,0]
	s_nop 0
	v_pk_fma_f32 v[106:107], v[172:173], v[82:83], v[106:107] op_sel_hi:[0,1,1]
	v_mov_b32_e32 v108, v173
	v_pk_fma_f32 v[106:107], v[108:109], v[76:77], v[106:107] op_sel_hi:[0,1,1]
	ds_read_b128 v[220:223], v25 offset:47184
	s_waitcnt lgkmcnt(8)
	v_pk_fma_f32 v[112:113], v[80:81], v[174:175], v[116:117] op_sel_hi:[1,0,1]
	s_nop 0
	v_pk_fma_f32 v[108:109], v[174:175], v[78:79], v[112:113] op_sel:[1,0,0]
	s_nop 0
	v_pk_fma_f32 v[108:109], v[176:177], v[82:83], v[108:109] op_sel_hi:[0,1,1]
	v_mov_b32_e32 v110, v177
	v_pk_fma_f32 v[108:109], v[110:111], v[76:77], v[108:109] op_sel_hi:[0,1,1]
	ds_read_b128 v[224:227], v25 offset:55392
	s_waitcnt lgkmcnt(8)
	v_pk_fma_f32 v[114:115], v[80:81], v[178:179], v[118:119] op_sel_hi:[1,0,1]
	s_nop 0
	v_pk_fma_f32 v[110:111], v[178:179], v[78:79], v[114:115] op_sel:[1,0,0]
	s_nop 0
	v_pk_fma_f32 v[110:111], v[180:181], v[82:83], v[110:111] op_sel_hi:[0,1,1]
	v_mov_b32_e32 v112, v181
	v_pk_fma_f32 v[110:111], v[112:113], v[76:77], v[110:111] op_sel_hi:[0,1,1]
	ds_read_b128 v[228:231], v25 offset:63600
	s_waitcnt lgkmcnt(8)
	v_pk_fma_f32 v[80:81], v[80:81], v[182:183], v[120:121] op_sel_hi:[1,0,1]
	s_nop 0
	v_pk_fma_f32 v[78:79], v[182:183], v[78:79], v[80:81] op_sel:[1,0,0]
	v_mov_b32_e32 v80, v185
	v_pk_fma_f32 v[78:79], v[184:185], v[82:83], v[78:79] op_sel_hi:[0,1,1]
	v_pk_fma_f32 v[112:113], v[80:81], v[76:77], v[78:79] op_sel_hi:[0,1,1]
	ds_read_b128 v[232:235], v238 offset:6272
	s_waitcnt lgkmcnt(8)
; #define LAS __attribute__((address_space(3)))
; __global__ void __launch_bounds__(NTHREADS, 2) hybrid_fwd(Args a) {
;     ...
;                     for (int j = 0; j < 8; ++j) {
; #pragma unroll
;                         for (int e = 0; e < 16; ++e) { const f32x4 w = *(const LAS f32x4*)(rwT + e * 2052 + j * 256 + lane * 4);
;                             acc2[e] += y2[j][0] * (f32x2){w[0], w[0]}; acc2[e] += y2[j][1] * (f32x2){w[1], w[1]};
;                             acc2[e] += y2[j][2] * (f32x2){w[2], w[2]}; acc2[e] += y2[j][3] * (f32x2){w[3], w[3]}; }
	v_pk_fma_f32 v[80:81], v[72:73], v[186:187], v[84:85] op_sel_hi:[1,0,1]
	s_nop 0
	v_pk_fma_f32 v[76:77], v[186:187], v[70:71], v[80:81] op_sel:[1,0,0]
	s_nop 0
	v_pk_fma_f32 v[76:77], v[188:189], v[74:75], v[76:77] op_sel_hi:[0,1,1]
	v_mov_b32_e32 v78, v189
	v_pk_fma_f32 v[76:77], v[78:79], v[68:69], v[76:77] op_sel_hi:[0,1,1]
	ds_read_b128 v[242:245], v238 offset:14480
	s_waitcnt lgkmcnt(8)
	v_pk_fma_f32 v[82:83], v[72:73], v[158:159], v[122:123] op_sel_hi:[1,0,1]
	s_nop 0
	v_pk_fma_f32 v[78:79], v[158:159], v[70:71], v[82:83] op_sel:[1,0,0]
	s_nop 0
	v_pk_fma_f32 v[78:79], v[160:161], v[74:75], v[78:79] op_sel_hi:[0,1,1]
	v_mov_b32_e32 v80, v161
	v_pk_fma_f32 v[114:115], v[80:81], v[68:69], v[78:79] op_sel_hi:[0,1,1]
	ds_read_b128 v[246:249], v238 offset:22688
	s_waitcnt lgkmcnt(8)
	v_pk_fma_f32 v[82:83], v[72:73], v[198:199], v[86:87] op_sel_hi:[1,0,1]
	s_nop 0
	v_pk_fma_f32 v[78:79], v[198:199], v[70:71], v[82:83] op_sel:[1,0,0]
	s_nop 0
	v_pk_fma_f32 v[78:79], v[200:201], v[74:75], v[78:79] op_sel_hi:[0,1,1]
	v_mov_b32_e32 v80, v201
	v_pk_fma_f32 v[78:79], v[80:81], v[68:69], v[78:79] op_sel_hi:[0,1,1]
	ds_read_b128 v[250:253], v238 offset:30896
	s_waitcnt lgkmcnt(8)
	v_pk_fma_f32 v[84:85], v[72:73], v[202:203], v[88:89] op_sel_hi:[1,0,1]
	s_nop 0
	v_pk_fma_f32 v[80:81], v[202:203], v[70:71], v[84:85] op_sel:[1,0,0]
	s_nop 0
	v_pk_fma_f32 v[80:81], v[204:205], v[74:75], v[80:81] op_sel_hi:[0,1,1]
	v_mov_b32_e32 v82, v205
	v_pk_fma_f32 v[80:81], v[82:83], v[68:69], v[80:81] op_sel_hi:[0,1,1]
	ds_read_b128 v[162:165], v238 offset:39104
	s_waitcnt lgkmcnt(8)
	v_pk_fma_f32 v[86:87], v[72:73], v[216:217], v[90:91] op_sel_hi:[1,0,1]
	s_nop 0
	v_pk_fma_f32 v[82:83], v[216:217], v[70:71], v[86:87] op_sel:[1,0,0]
	s_nop 0
	v_pk_fma_f32 v[82:83], v[218:219], v[74:75], v[82:83] op_sel_hi:[0,1,1]
	v_mov_b32_e32 v84, v219
	v_pk_fma_f32 v[82:83], v[84:85], v[68:69], v[82:83] op_sel_hi:[0,1,1]
	ds_read_b128 v[166:169], v238 offset:47312
	s_waitcnt lgkmcnt(8)
	v_pk_fma_f32 v[88:89], v[72:73], v[220:221], v[92:93] op_sel_hi:[1,0,1]
	s_nop 0
	v_pk_fma_f32 v[84:85], v[220:221], v[70:71], v[88:89] op_sel:[1,0,0]
	s_nop 0
	v_pk_fma_f32 v[84:85], v[222:223], v[74:75], v[84:85] op_sel_hi:[0,1,1]
	v_mov_b32_e32 v86, v223
	v_pk_fma_f32 v[84:85], v[86:87], v[68:69], v[84:85] op_sel_hi:[0,1,1]
	ds_read_b128 v[170:173], v238 offset:55520
	s_waitcnt lgkmcnt(8)
	v_pk_fma_f32 v[90:91], v[72:73], v[224:225], v[94:95] op_sel_hi:[1,0,1]
	s_nop 0
	v_pk_fma_f32 v[86:87], v[224:225], v[70:71], v[90:91] op_sel:[1,0,0]
	s_nop 0
	v_pk_fma_f32 v[86:87], v[226:227], v[74:75], v[86:87] op_sel_hi:[0,1,1]
	v_mov_b32_e32 v88, v227
	v_pk_fma_f32 v[86:87], v[88:89], v[68:69], v[86:87] op_sel_hi:[0,1,1]
	ds_read_b128 v[174:177], v238 offset:63728
	s_waitcnt lgkmcnt(8)
	v_pk_fma_f32 v[92:93], v[72:73], v[228:229], v[96:97] op_sel_hi:[1,0,1]
	s_nop 0
	v_pk_fma_f32 v[88:89], v[228:229], v[70:71], v[92:93] op_sel:[1,0,0]
	s_nop 0
	v_pk_fma_f32 v[88:89], v[230:231], v[74:75], v[88:89] op_sel_hi:[0,1,1]
	v_mov_b32_e32 v90, v231
	v_pk_fma_f32 v[88:89], v[90:91], v[68:69], v[88:89] op_sel_hi:[0,1,1]
	ds_read_b128 v[178:181], v25 offset:7168
	s_waitcnt lgkmcnt(8)
	v_pk_fma_f32 v[94:95], v[72:73], v[232:233], v[98:99] op_sel_hi:[1,0,1]
	s_nop 0
	v_pk_fma_f32 v[90:91], v[232:233], v[70:71], v[94:95] op_sel:[1,0,0]
	s_nop 0
	v_pk_fma_f32 v[90:91], v[234:235], v[74:75], v[90:91] op_sel_hi:[0,1,1]
	v_mov_b32_e32 v92, v235
	v_pk_fma_f32 v[90:91], v[92:93], v[68:69], v[90:91] op_sel_hi:[0,1,1]
	ds_read_b128 v[182:185], v25 offset:15376
	s_waitcnt lgkmcnt(8)
	v_pk_fma_f32 v[96:97], v[72:73], v[242:243], v[100:101] op_sel_hi:[1,0,1]
	s_nop 0
	v_pk_fma_f32 v[92:93], v[242:243], v[70:71], v[96:97] op_sel:[1,0,0]
	s_nop 0
	v_pk_fma_f32 v[92:93], v[244:245], v[74:75], v[92:93] op_sel_hi:[0,1,1]
	v_mov_b32_e32 v94, v245
	v_pk_fma_f32 v[92:93], v[94:95], v[68:69], v[92:93] op_sel_hi:[0,1,1]
	ds_read_b128 v[186:189], v25 offset:23584
	s_waitcnt lgkmcnt(8)
	v_pk_fma_f32 v[98:99], v[72:73], v[246:247], v[102:103] op_sel_hi:[1,0,1]
	s_nop 0
	v_pk_fma_f32 v[94:95], v[246:247], v[70:71], v[98:99] op_sel:[1,0,0]
	s_nop 0
	v_pk_fma_f32 v[94:95], v[248:249], v[74:75], v[94:95] op_sel_hi:[0,1,1]
	v_mov_b32_e32 v96, v249
	v_pk_fma_f32 v[94:95], v[96:97], v[68:69], v[94:95] op_sel_hi:[0,1,1]
	ds_read_b128 v[158:161], v25 offset:31792
	s_waitcnt lgkmcnt(8)
	v_pk_fma_f32 v[100:101], v[72:73], v[250:251], v[104:105] op_sel_hi:[1,0,1]
	s_nop 0
	v_pk_fma_f32 v[96:97], v[250:251], v[70:71], v[100:101] op_sel:[1,0,0]
	s_nop 0
	v_pk_fma_f32 v[96:97], v[252:253], v[74:75], v[96:97] op_sel_hi:[0,1,1]
	v_mov_b32_e32 v98, v253
	v_pk_fma_f32 v[96:97], v[98:99], v[68:69], v[96:97] op_sel_hi:[0,1,1]
	ds_read_b128 v[198:201], v25 offset:40000
	s_waitcnt lgkmcnt(8)
	v_pk_fma_f32 v[102:103], v[72:73], v[162:163], v[106:107] op_sel_hi:[1,0,1]
	s_nop 0
	v_pk_fma_f32 v[98:99], v[162:163], v[70:71], v[102:103] op_sel:[1,0,0]
	s_nop 0
	v_pk_fma_f32 v[98:99], v[164:165], v[74:75], v[98:99] op_sel_hi:[0,1,1]
	v_mov_b32_e32 v100, v165
	v_pk_fma_f32 v[98:99], v[100:101], v[68:69], v[98:99] op_sel_hi:[0,1,1]
	ds_read_b128 v[202:205], v25 offset:48208
	s_waitcnt lgkmcnt(8)
	v_pk_fma_f32 v[104:105], v[72:73], v[166:167], v[108:109] op_sel_hi:[1,0,1]
	s_nop 0
	v_pk_fma_f32 v[100:101], v[166:167], v[70:71], v[104:105] op_sel:[1,0,0]
	s_nop 0
	v_pk_fma_f32 v[100:101], v[168:169], v[74:75], v[100:101] op_sel_hi:[0,1,1]
	v_mov_b32_e32 v102, v169
	v_pk_fma_f32 v[100:101], v[102:103], v[68:69], v[100:101] op_sel_hi:[0,1,1]
	ds_read_b128 v[216:219], v25 offset:56416
	s_waitcnt lgkmcnt(8)
; #define LAS __attribute__((address_space(3)))
; __global__ void __launch_bounds__(NTHREADS, 2) hybrid_fwd(Args a) {
;     ...
;                     for (int j = 0; j < 8; ++j) {
; #pragma unroll
;                         for (int e = 0; e < 16; ++e) { const f32x4 w = *(const LAS f32x4*)(rwT + e * 2052 + j * 256 + lane * 4);
;                             acc2[e] += y2[j][0] * (f32x2){w[0], w[0]}; acc2[e] += y2[j][1] * (f32x2){w[1], w[1]};
;                             acc2[e] += y2[j][2] * (f32x2){w[2], w[2]}; acc2[e] += y2[j][3] * (f32x2){w[3], w[3]}; }
	v_pk_fma_f32 v[106:107], v[72:73], v[170:171], v[110:111] op_sel_hi:[1,0,1]
	s_nop 0
	v_pk_fma_f32 v[102:103], v[170:171], v[70:71], v[106:107] op_sel:[1,0,0]
	s_nop 0
	v_pk_fma_f32 v[102:103], v[172:173], v[74:75], v[102:103] op_sel_hi:[0,1,1]
	v_mov_b32_e32 v104, v173
	v_pk_fma_f32 v[102:103], v[104:105], v[68:69], v[102:103] op_sel_hi:[0,1,1]
	ds_read_b128 v[220:223], v25 offset:64624
	s_waitcnt lgkmcnt(8)
	v_pk_fma_f32 v[72:73], v[72:73], v[174:175], v[112:113] op_sel_hi:[1,0,1]
	s_nop 0
	v_pk_fma_f32 v[70:71], v[174:175], v[70:71], v[72:73] op_sel:[1,0,0]
	v_mov_b32_e32 v72, v177
	v_pk_fma_f32 v[70:71], v[176:177], v[74:75], v[70:71] op_sel_hi:[0,1,1]
	v_pk_fma_f32 v[104:105], v[72:73], v[68:69], v[70:71] op_sel_hi:[0,1,1]
	ds_read_b128 v[224:227], v238 offset:7296
	s_waitcnt lgkmcnt(8)
	v_pk_fma_f32 v[72:73], v[66:67], v[178:179], v[76:77] op_sel_hi:[1,0,1]
	s_nop 0
	v_pk_fma_f32 v[68:69], v[178:179], v[62:63], v[72:73] op_sel:[1,0,0]
	s_nop 0
	v_pk_fma_f32 v[68:69], v[180:181], v[64:65], v[68:69] op_sel_hi:[0,1,1]
	v_mov_b32_e32 v70, v181
	v_pk_fma_f32 v[68:69], v[70:71], v[60:61], v[68:69] op_sel_hi:[0,1,1]
	ds_read_b128 v[228:231], v238 offset:15504
	s_waitcnt lgkmcnt(8)
	v_pk_fma_f32 v[74:75], v[66:67], v[182:183], v[114:115] op_sel_hi:[1,0,1]
	s_nop 0
	v_pk_fma_f32 v[70:71], v[182:183], v[62:63], v[74:75] op_sel:[1,0,0]
	s_nop 0
	v_pk_fma_f32 v[70:71], v[184:185], v[64:65], v[70:71] op_sel_hi:[0,1,1]
	v_mov_b32_e32 v72, v185
	v_pk_fma_f32 v[70:71], v[72:73], v[60:61], v[70:71] op_sel_hi:[0,1,1]
	ds_read_b128 v[232:235], v238 offset:23712
	s_waitcnt lgkmcnt(8)
	v_pk_fma_f32 v[76:77], v[66:67], v[186:187], v[78:79] op_sel_hi:[1,0,1]
	s_nop 0
	v_pk_fma_f32 v[72:73], v[186:187], v[62:63], v[76:77] op_sel:[1,0,0]
	s_nop 0
	v_pk_fma_f32 v[72:73], v[188:189], v[64:65], v[72:73] op_sel_hi:[0,1,1]
	v_mov_b32_e32 v74, v189
	v_pk_fma_f32 v[72:73], v[74:75], v[60:61], v[72:73] op_sel_hi:[0,1,1]
	ds_read_b128 v[242:245], v238 offset:31920
	s_waitcnt lgkmcnt(8)
	v_pk_fma_f32 v[78:79], v[66:67], v[158:159], v[80:81] op_sel_hi:[1,0,1]
	s_nop 0
	v_pk_fma_f32 v[74:75], v[158:159], v[62:63], v[78:79] op_sel:[1,0,0]
	ds_read_b128 v[246:249], v238 offset:40128
	v_pk_fma_f32 v[74:75], v[160:161], v[64:65], v[74:75] op_sel_hi:[0,1,1]
	v_mov_b32_e32 v76, v161
	v_pk_fma_f32 v[76:77], v[76:77], v[60:61], v[74:75] op_sel_hi:[0,1,1]
	s_waitcnt lgkmcnt(8)
	v_pk_fma_f32 v[74:75], v[66:67], v[198:199], v[82:83] op_sel_hi:[1,0,1]
	s_nop 0
	v_pk_fma_f32 v[74:75], v[198:199], v[62:63], v[74:75] op_sel:[1,0,0]
	v_mov_b32_e32 v78, v201
	v_pk_fma_f32 v[74:75], v[200:201], v[64:65], v[74:75] op_sel_hi:[0,1,1]
	v_pk_fma_f32 v[74:75], v[78:79], v[60:61], v[74:75] op_sel_hi:[0,1,1]
	ds_read_b128 v[250:253], v238 offset:48336
	s_waitcnt lgkmcnt(8)
	v_pk_fma_f32 v[82:83], v[66:67], v[202:203], v[84:85] op_sel_hi:[1,0,1]
	s_nop 0
	v_pk_fma_f32 v[78:79], v[202:203], v[62:63], v[82:83] op_sel:[1,0,0]
	s_nop 0
	v_pk_fma_f32 v[78:79], v[204:205], v[64:65], v[78:79] op_sel_hi:[0,1,1]
	v_mov_b32_e32 v80, v205
	v_pk_fma_f32 v[78:79], v[80:81], v[60:61], v[78:79] op_sel_hi:[0,1,1]
	ds_read_b128 v[162:165], v238 offset:56544
	s_waitcnt lgkmcnt(8)
	v_pk_fma_f32 v[84:85], v[66:67], v[216:217], v[86:87] op_sel_hi:[1,0,1]
	s_nop 0
	v_pk_fma_f32 v[80:81], v[216:217], v[62:63], v[84:85] op_sel:[1,0,0]
	s_nop 0
	v_pk_fma_f32 v[80:81], v[218:219], v[64:65], v[80:81] op_sel_hi:[0,1,1]
	v_mov_b32_e32 v82, v219
	v_pk_fma_f32 v[80:81], v[82:83], v[60:61], v[80:81] op_sel_hi:[0,1,1]
	ds_read_b128 v[166:169], v238 offset:64752
	s_waitcnt lgkmcnt(8)
	v_pk_fma_f32 v[86:87], v[66:67], v[220:221], v[88:89] op_sel_hi:[1,0,1]
	s_nop 0
	v_pk_fma_f32 v[82:83], v[220:221], v[62:63], v[86:87] op_sel:[1,0,0]
	s_nop 0
	v_pk_fma_f32 v[82:83], v[222:223], v[64:65], v[82:83] op_sel_hi:[0,1,1]
	v_mov_b32_e32 v84, v223
	v_pk_fma_f32 v[82:83], v[84:85], v[60:61], v[82:83] op_sel_hi:[0,1,1]
	s_waitcnt lgkmcnt(7)
	v_pk_fma_f32 v[88:89], v[66:67], v[224:225], v[90:91] op_sel_hi:[1,0,1]
	s_nop 0
	v_pk_fma_f32 v[84:85], v[224:225], v[62:63], v[88:89] op_sel:[1,0,0]
	s_nop 0
	v_pk_fma_f32 v[84:85], v[226:227], v[64:65], v[84:85] op_sel_hi:[0,1,1]
	v_mov_b32_e32 v86, v227
	v_pk_fma_f32 v[84:85], v[86:87], v[60:61], v[84:85] op_sel_hi:[0,1,1]
	s_waitcnt lgkmcnt(6)
	v_pk_fma_f32 v[90:91], v[66:67], v[228:229], v[92:93] op_sel_hi:[1,0,1]
	s_nop 0
	v_pk_fma_f32 v[86:87], v[228:229], v[62:63], v[90:91] op_sel:[1,0,0]
	s_nop 0
	v_pk_fma_f32 v[86:87], v[230:231], v[64:65], v[86:87] op_sel_hi:[0,1,1]
	v_mov_b32_e32 v88, v231
	v_pk_fma_f32 v[86:87], v[88:89], v[60:61], v[86:87] op_sel_hi:[0,1,1]
	s_waitcnt lgkmcnt(5)
	v_pk_fma_f32 v[92:93], v[66:67], v[232:233], v[94:95] op_sel_hi:[1,0,1]
	s_nop 0
	v_pk_fma_f32 v[88:89], v[232:233], v[62:63], v[92:93] op_sel:[1,0,0]
	s_nop 0
	v_pk_fma_f32 v[88:89], v[234:235], v[64:65], v[88:89] op_sel_hi:[0,1,1]
	v_mov_b32_e32 v90, v235
	v_pk_fma_f32 v[88:89], v[90:91], v[60:61], v[88:89] op_sel_hi:[0,1,1]
	s_waitcnt lgkmcnt(4)
	v_pk_fma_f32 v[94:95], v[66:67], v[242:243], v[96:97] op_sel_hi:[1,0,1]
	s_nop 0
	v_pk_fma_f32 v[90:91], v[242:243], v[62:63], v[94:95] op_sel:[1,0,0]
	s_nop 0
	v_pk_fma_f32 v[90:91], v[244:245], v[64:65], v[90:91] op_sel_hi:[0,1,1]
	v_mov_b32_e32 v92, v245
	v_pk_fma_f32 v[90:91], v[92:93], v[60:61], v[90:91] op_sel_hi:[0,1,1]
	s_waitcnt lgkmcnt(3)
	v_pk_fma_f32 v[96:97], v[66:67], v[246:247], v[98:99] op_sel_hi:[1,0,1]
	s_nop 0
	v_pk_fma_f32 v[92:93], v[246:247], v[62:63], v[96:97] op_sel:[1,0,0]
	s_nop 0
	v_pk_fma_f32 v[92:93], v[248:249], v[64:65], v[92:93] op_sel_hi:[0,1,1]
	v_mov_b32_e32 v94, v249
	v_pk_fma_f32 v[92:93], v[94:95], v[60:61], v[92:93] op_sel_hi:[0,1,1]
	s_waitcnt lgkmcnt(2)
; #define LAS __attribute__((address_space(3)))
; __global__ void __launch_bounds__(NTHREADS, 2) hybrid_fwd(Args a) {
;     ...
;                     for (int j = 0; j < 8; ++j) {
; #pragma unroll
;                         for (int e = 0; e < 16; ++e) { const f32x4 w = *(const LAS f32x4*)(rwT + e * 2052 + j * 256 + lane * 4);
;                             acc2[e] += y2[j][0] * (f32x2){w[0], w[0]}; acc2[e] += y2[j][1] * (f32x2){w[1], w[1]};
;                             acc2[e] += y2[j][2] * (f32x2){w[2], w[2]}; acc2[e] += y2[j][3] * (f32x2){w[3], w[3]}; }
;                         __builtin_amdgcn_sched_barrier(0);
;                     }
;                     float acca[16], accb[16];
; #pragma unroll
;                     for (int e = 0; e < 16; ++e) { acca[e] = acc2[e][0]; accb[e] = acc2[e][1]; }
;                     P7_PICK(2 * qp, acca);
	v_pk_fma_f32 v[98:99], v[66:67], v[250:251], v[100:101] op_sel_hi:[1,0,1]
	s_nop 0
	v_pk_fma_f32 v[94:95], v[250:251], v[62:63], v[98:99] op_sel:[1,0,0]
	s_nop 0
	v_pk_fma_f32 v[94:95], v[252:253], v[64:65], v[94:95] op_sel_hi:[0,1,1]
	v_mov_b32_e32 v96, v253
	v_pk_fma_f32 v[94:95], v[96:97], v[60:61], v[94:95] op_sel_hi:[0,1,1]
	s_waitcnt lgkmcnt(1)
	v_pk_fma_f32 v[100:101], v[66:67], v[162:163], v[102:103] op_sel_hi:[1,0,1]
	s_nop 0
	v_pk_fma_f32 v[96:97], v[162:163], v[62:63], v[100:101] op_sel:[1,0,0]
	s_nop 0
	v_pk_fma_f32 v[96:97], v[164:165], v[64:65], v[96:97] op_sel_hi:[0,1,1]
	v_mov_b32_e32 v98, v165
	v_pk_fma_f32 v[96:97], v[98:99], v[60:61], v[96:97] op_sel_hi:[0,1,1]
	s_waitcnt lgkmcnt(0)
	v_pk_fma_f32 v[66:67], v[66:67], v[166:167], v[104:105] op_sel_hi:[1,0,1]
	s_nop 0
	v_pk_fma_f32 v[62:63], v[166:167], v[62:63], v[66:67] op_sel:[1,0,0]
	s_nop 0
	v_pk_fma_f32 v[62:63], v[168:169], v[64:65], v[62:63] op_sel_hi:[0,1,1]
	v_mov_b32_e32 v64, v169
	v_pk_fma_f32 v[60:61], v[64:65], v[60:61], v[62:63] op_sel_hi:[0,1,1]
	v_add_f32_dpp v62, v68, v68 quad_perm:[1,0,3,2] row_mask:0xf bank_mask:0xf bound_ctrl:1
	s_nop 0
	v_add_f32_dpp v60, v60, v60 quad_perm:[1,0,3,2] row_mask:0xf bank_mask:0xf bound_ctrl:1
	v_add_f32_dpp v68, v94, v94 quad_perm:[1,0,3,2] row_mask:0xf bank_mask:0xf bound_ctrl:1
	v_add_f32_dpp v62, v62, v62 quad_perm:[2,3,0,1] row_mask:0xf bank_mask:0xf bound_ctrl:1
	v_add_f32_dpp v60, v60, v60 quad_perm:[2,3,0,1] row_mask:0xf bank_mask:0xf bound_ctrl:1
	v_add_f32_dpp v68, v68, v68 quad_perm:[2,3,0,1] row_mask:0xf bank_mask:0xf bound_ctrl:1
	v_add_f32_dpp v62, v62, v62 row_ror:4 row_mask:0xf bank_mask:0xf bound_ctrl:1
	v_add_f32_dpp v60, v60, v60 row_ror:4 row_mask:0xf bank_mask:0xf bound_ctrl:1
	v_add_f32_dpp v68, v68, v68 row_ror:4 row_mask:0xf bank_mask:0xf bound_ctrl:1
	v_add_f32_dpp v62, v62, v62 row_ror:8 row_mask:0xf bank_mask:0xf bound_ctrl:1
	v_mov_b32_e32 v63, v62
	s_nop 1
	v_permlane16_swap_b32_e32 v62, v63
	v_add_f32_e32 v62, v62, v63
	v_mov_b32_e32 v63, v62
	s_nop 1
	v_permlane32_swap_b32_e32 v62, v63
	v_add_f32_e32 v62, v62, v63
	s_nop 0
	v_add_f32_dpp v63, v70, v70 quad_perm:[1,0,3,2] row_mask:0xf bank_mask:0xf bound_ctrl:1
	v_mul_f32_e32 v62, 0xbfb8aa3b, v62
	v_exp_f32_e32 v62, v62
	v_add_f32_dpp v63, v63, v63 quad_perm:[2,3,0,1] row_mask:0xf bank_mask:0xf bound_ctrl:1
	v_add_f32_dpp v60, v60, v60 row_ror:8 row_mask:0xf bank_mask:0xf bound_ctrl:1
	v_add_f32_dpp v68, v68, v68 row_ror:8 row_mask:0xf bank_mask:0xf bound_ctrl:1
	v_add_f32_dpp v63, v63, v63 row_ror:4 row_mask:0xf bank_mask:0xf bound_ctrl:1
	v_add_f32_e32 v62, 1.0, v62
	v_rcp_f32_e32 v62, v62
	v_add_f32_dpp v63, v63, v63 row_ror:8 row_mask:0xf bank_mask:0xf bound_ctrl:1
	v_mov_b32_e32 v64, v63
	s_nop 1
	v_permlane16_swap_b32_e32 v63, v64
	v_add_f32_e32 v63, v63, v64
	v_mov_b32_e32 v64, v63
	s_nop 1
	v_permlane32_swap_b32_e32 v63, v64
	v_add_f32_e32 v63, v63, v64
	s_nop 0
	v_add_f32_dpp v64, v72, v72 quad_perm:[1,0,3,2] row_mask:0xf bank_mask:0xf bound_ctrl:1
	v_mul_f32_e32 v63, 0xbfb8aa3b, v63
	v_exp_f32_e32 v63, v63
	v_add_f32_dpp v64, v64, v64 quad_perm:[2,3,0,1] row_mask:0xf bank_mask:0xf bound_ctrl:1
	v_add_f32_dpp v72, v96, v96 quad_perm:[1,0,3,2] row_mask:0xf bank_mask:0xf bound_ctrl:1
	v_mov_b32_e32 v70, v68
	v_add_f32_dpp v64, v64, v64 row_ror:4 row_mask:0xf bank_mask:0xf bound_ctrl:1
	v_add_f32_e32 v63, 1.0, v63
	v_rcp_f32_e32 v63, v63
	v_add_f32_dpp v64, v64, v64 row_ror:8 row_mask:0xf bank_mask:0xf bound_ctrl:1
	v_mov_b32_e32 v65, v64
	s_nop 1
	v_permlane16_swap_b32_e32 v64, v65
	v_add_f32_e32 v64, v64, v65
	v_mov_b32_e32 v65, v64
	s_nop 1
	v_permlane32_swap_b32_e32 v64, v65
	v_add_f32_e32 v64, v64, v65
	s_nop 0
	v_add_f32_dpp v65, v76, v76 quad_perm:[1,0,3,2] row_mask:0xf bank_mask:0xf bound_ctrl:1
	v_mul_f32_e32 v64, 0xbfb8aa3b, v64
	v_exp_f32_e32 v64, v64
	v_add_f32_dpp v65, v65, v65 quad_perm:[2,3,0,1] row_mask:0xf bank_mask:0xf bound_ctrl:1
	v_mov_b32_e32 v76, v60
	s_nop 1
	v_permlane16_swap_b32_e32 v60, v76
	v_add_f32_dpp v65, v65, v65 row_ror:4 row_mask:0xf bank_mask:0xf bound_ctrl:1
	v_add_f32_e32 v64, 1.0, v64
	v_rcp_f32_e32 v102, v64
	v_add_f32_dpp v65, v65, v65 row_ror:8 row_mask:0xf bank_mask:0xf bound_ctrl:1
	v_mov_b32_e32 v66, v65
	s_nop 1
	v_permlane16_swap_b32_e32 v65, v66
	v_add_f32_e32 v65, v65, v66
	v_mov_b32_e32 v66, v65
	s_nop 1
	v_permlane32_swap_b32_e32 v65, v66
	v_add_f32_e32 v65, v65, v66
	s_nop 0
	v_add_f32_dpp v66, v74, v74 quad_perm:[1,0,3,2] row_mask:0xf bank_mask:0xf bound_ctrl:1
	v_mul_f32_e32 v65, 0xbfb8aa3b, v65
	v_exp_f32_e32 v65, v65
	v_add_f32_dpp v66, v66, v66 quad_perm:[2,3,0,1] row_mask:0xf bank_mask:0xf bound_ctrl:1
	v_add_f32_e32 v111, v14, v102
	v_add_f32_e32 v76, v60, v76
	v_add_f32_dpp v66, v66, v66 row_ror:4 row_mask:0xf bank_mask:0xf bound_ctrl:1
	v_add_f32_e32 v64, 1.0, v65
	v_rcp_f32_e32 v104, v64
	v_add_f32_dpp v66, v66, v66 row_ror:8 row_mask:0xf bank_mask:0xf bound_ctrl:1
	v_mov_b32_e32 v67, v66
	s_nop 1
	v_permlane16_swap_b32_e32 v66, v67
	v_add_f32_e32 v101, v66, v67
	s_nop 0
	v_add_f32_dpp v66, v78, v78 quad_perm:[1,0,3,2] row_mask:0xf bank_mask:0xf bound_ctrl:1
	v_pk_add_f32 v[64:65], v[12:13], v[62:63]
	v_add_f32_e32 v112, v15, v104
	v_add_f32_dpp v66, v66, v66 quad_perm:[2,3,0,1] row_mask:0xf bank_mask:0xf bound_ctrl:1
	v_cmp_gt_f32_e32 vcc, v65, v64
	v_add_f32_dpp v72, v72, v72 quad_perm:[2,3,0,1] row_mask:0xf bank_mask:0xf bound_ctrl:1
	v_add_f32_dpp v66, v66, v66 row_ror:4 row_mask:0xf bank_mask:0xf bound_ctrl:1
	v_cndmask_b32_e32 v60, v64, v65, vcc
	v_cmp_gt_f32_e64 s[6:7], v111, v60
	v_add_f32_dpp v66, v66, v66 row_ror:8 row_mask:0xf bank_mask:0xf bound_ctrl:1
	v_mov_b32_e32 v67, v66
	s_nop 1
	v_permlane16_swap_b32_e32 v66, v67
	v_add_f32_e32 v105, v66, v67
	s_nop 0
	v_add_f32_dpp v66, v80, v80 quad_perm:[1,0,3,2] row_mask:0xf bank_mask:0xf bound_ctrl:1
	v_cndmask_b32_e64 v80, 0, 1, vcc
	v_cndmask_b32_e64 v60, v60, v111, s[6:7]
	v_add_f32_dpp v66, v66, v66 quad_perm:[2,3,0,1] row_mask:0xf bank_mask:0xf bound_ctrl:1
	v_cndmask_b32_e64 v80, v80, 2, s[6:7]
	v_cmp_ngt_f32_e64 s[8:9], v112, v60
	v_add_f32_dpp v66, v66, v66 row_ror:4 row_mask:0xf bank_mask:0xf bound_ctrl:1
	v_add_f32_dpp v72, v72, v72 row_ror:4 row_mask:0xf bank_mask:0xf bound_ctrl:1
	v_permlane16_swap_b32_e32 v68, v70
	v_add_f32_dpp v66, v66, v66 row_ror:8 row_mask:0xf bank_mask:0xf bound_ctrl:1
	v_mov_b32_e32 v67, v66
	s_nop 1
	v_permlane16_swap_b32_e32 v66, v67
	v_add_f32_e32 v107, v66, v67
	s_nop 0
	v_add_f32_dpp v66, v82, v82 quad_perm:[1,0,3,2] row_mask:0xf bank_mask:0xf bound_ctrl:1
	v_add_f32_dpp v72, v72, v72 row_ror:8 row_mask:0xf bank_mask:0xf bound_ctrl:1
	v_mov_b32_e32 v74, v72
	v_add_f32_dpp v66, v66, v66 quad_perm:[2,3,0,1] row_mask:0xf bank_mask:0xf bound_ctrl:1
	s_nop 0
	v_permlane16_swap_b32_e32 v72, v74
	v_add_f32_dpp v66, v66, v66 row_ror:4 row_mask:0xf bank_mask:0xf bound_ctrl:1
	v_add_f32_e32 v68, v68, v70
	v_add_f32_e32 v72, v72, v74
	v_add_f32_dpp v66, v66, v66 row_ror:8 row_mask:0xf bank_mask:0xf bound_ctrl:1
	v_mov_b32_e32 v67, v66
	s_nop 1
	v_permlane16_swap_b32_e32 v66, v67
	v_add_f32_e32 v109, v66, v67
	s_nop 0
	v_add_f32_dpp v66, v84, v84 quad_perm:[1,0,3,2] row_mask:0xf bank_mask:0xf bound_ctrl:1
	v_cndmask_b32_e64 v94, v112, v60, s[8:9]
	v_mov_b32_e32 v103, v101
	v_add_f32_dpp v66, v66, v66 quad_perm:[2,3,0,1] row_mask:0xf bank_mask:0xf bound_ctrl:1
	v_mov_b32_e32 v106, v105
	v_mov_b32_e32 v108, v107
	v_add_f32_dpp v66, v66, v66 row_ror:4 row_mask:0xf bank_mask:0xf bound_ctrl:1
	v_mov_b32_e32 v110, v109
	v_mov_b32_e32 v70, v68
	v_add_f32_dpp v66, v66, v66 row_ror:8 row_mask:0xf bank_mask:0xf bound_ctrl:1
	v_mov_b32_e32 v67, v66
	s_nop 1
	v_permlane16_swap_b32_e32 v66, v67
	v_add_f32_e32 v82, v66, v67
	s_nop 0
	v_add_f32_dpp v66, v86, v86 quad_perm:[1,0,3,2] row_mask:0xf bank_mask:0xf bound_ctrl:1
	v_mov_b32_e32 v84, v82
	v_mov_b32_e32 v74, v72
	v_add_f32_dpp v66, v66, v66 quad_perm:[2,3,0,1] row_mask:0xf bank_mask:0xf bound_ctrl:1
	v_mov_b32_e32 v78, v76
	v_permlane32_swap_b32_e32 v101, v103
	v_add_f32_dpp v66, v66, v66 row_ror:4 row_mask:0xf bank_mask:0xf bound_ctrl:1
	v_permlane32_swap_b32_e32 v105, v106
	s_nop 0
	v_add_f32_dpp v66, v66, v66 row_ror:8 row_mask:0xf bank_mask:0xf bound_ctrl:1
	v_mov_b32_e32 v67, v66
	s_nop 1
	v_permlane16_swap_b32_e32 v66, v67
	v_add_f32_e32 v86, v66, v67
	s_nop 0
	v_add_f32_dpp v66, v88, v88 quad_perm:[1,0,3,2] row_mask:0xf bank_mask:0xf bound_ctrl:1
	v_mov_b32_e32 v98, v86
	v_permlane32_swap_b32_e32 v107, v108
	v_add_f32_dpp v66, v66, v66 quad_perm:[2,3,0,1] row_mask:0xf bank_mask:0xf bound_ctrl:1
	v_permlane32_swap_b32_e32 v109, v110
	s_nop 0
	v_add_f32_dpp v66, v66, v66 row_ror:4 row_mask:0xf bank_mask:0xf bound_ctrl:1
	v_permlane32_swap_b32_e32 v82, v84
	s_nop 0
	v_add_f32_dpp v66, v66, v66 row_ror:8 row_mask:0xf bank_mask:0xf bound_ctrl:1
	v_mov_b32_e32 v67, v66
	s_nop 1
	v_permlane16_swap_b32_e32 v66, v67
	v_add_f32_e32 v88, v66, v67
	s_nop 0
	v_add_f32_dpp v66, v90, v90 quad_perm:[1,0,3,2] row_mask:0xf bank_mask:0xf bound_ctrl:1
	v_mov_b32_e32 v99, v88
	v_permlane32_swap_b32_e32 v86, v98
	v_add_f32_dpp v66, v66, v66 quad_perm:[2,3,0,1] row_mask:0xf bank_mask:0xf bound_ctrl:1
	v_permlane32_swap_b32_e32 v88, v99
	s_nop 0
	v_add_f32_dpp v66, v66, v66 row_ror:4 row_mask:0xf bank_mask:0xf bound_ctrl:1
	v_permlane32_swap_b32_e32 v68, v70
	s_nop 0
	v_add_f32_dpp v66, v66, v66 row_ror:8 row_mask:0xf bank_mask:0xf bound_ctrl:1
	v_mov_b32_e32 v67, v66
	s_nop 1
	v_permlane16_swap_b32_e32 v66, v67
	v_add_f32_e32 v90, v66, v67
	s_nop 0
	v_add_f32_dpp v66, v92, v92 quad_perm:[1,0,3,2] row_mask:0xf bank_mask:0xf bound_ctrl:1
	v_cndmask_b32_e64 v92, 3, v80, s[8:9]
	v_mov_b32_e32 v80, 0xff800000
	v_cmp_eq_u32_e64 s[10:11], 0, v92
	v_cmp_nlg_f32_e64 s[12:13], v64, v80
	s_or_b64 s[10:11], s[10:11], s[12:13]
	v_cndmask_b32_e64 v64, v64, v80, s[10:11]
	v_cmp_ne_u32_e64 s[12:13], 1, v92
	v_cmp_gt_f32_e64 s[14:15], v65, v64
	s_and_b64 s[12:13], s[12:13], s[14:15]
	v_cndmask_b32_e64 v64, v64, v65, s[12:13]
	v_add_f32_dpp v66, v66, v66 quad_perm:[2,3,0,1] row_mask:0xf bank_mask:0xf bound_ctrl:1
	v_cmp_ne_u32_e64 s[14:15], 2, v92
	v_cmp_gt_f32_e64 s[16:17], v111, v64
	v_add_f32_dpp v66, v66, v66 row_ror:4 row_mask:0xf bank_mask:0xf bound_ctrl:1
	s_and_b64 s[14:15], s[14:15], s[16:17]
	v_cndmask_b32_e64 v64, v64, v111, s[14:15]
	v_add_f32_dpp v66, v66, v66 row_ror:8 row_mask:0xf bank_mask:0xf bound_ctrl:1
	v_mov_b32_e32 v67, v66
	v_cmp_gt_f32_e64 s[16:17], v112, v64
	s_nop 0
	v_permlane16_swap_b32_e32 v66, v67
	s_and_b64 s[16:17], s[8:9], s[16:17]
	v_add_f32_e32 v66, v66, v67
	v_cndmask_b32_e64 v64, v64, v112, s[16:17]
	v_mov_b32_e32 v100, v90
	v_mov_b32_e32 v67, v66
	v_add_f32_e32 v94, v94, v64
	v_permlane32_swap_b32_e32 v90, v100
	v_permlane32_swap_b32_e32 v66, v67
	v_permlane32_swap_b32_e32 v72, v74
	v_permlane32_swap_b32_e32 v76, v78
	v_mov_b32_e32 v60, 1
	v_cmp_lg_f32_e64 s[18:19], v94, v80
	v_mov_b32_e32 v65, 0
	v_mov_b32_e32 v64, 0
	s_and_saveexec_b64 s[46:47], s[18:19]
	s_cbranch_execz .LBB0_891
	v_cndmask_b32_e64 v35, 0, 1, s[12:13]
	v_cndmask_b32_e64 v35, v35, 2, s[14:15]
	v_cndmask_b32_e64 v60, v35, 3, s[16:17]
	v_cndmask_b32_e64 v35, v62, 0, s[10:11]
	v_cndmask_b32_e64 v35, v35, v63, s[12:13]
	v_cndmask_b32_e32 v62, v62, v63, vcc
	v_cndmask_b32_e64 v35, v35, v102, s[14:15]
	v_cndmask_b32_e64 v62, v62, v102, s[6:7]
	v_cndmask_b32_e64 v35, v35, v104, s[16:17]
	v_cndmask_b32_e64 v65, v104, v62, s[8:9]
	v_mov_b32_e32 v64, v92
	v_mov_b32_e32 v80, v94

.LBB0_909:
	s_or_b64 exec, exec, s[6:7]
	s_waitcnt vmcnt(0)
	v_lshlrev_b32_e32 v80, 16, v58
	v_and_b32_e32 v81, 0xffff0000, v58
	v_lshlrev_b32_e32 v78, 16, v59
	v_and_b32_e32 v79, 0xffff0000, v59
	v_add_f32_e32 v35, v80, v81
	v_add_f32_e32 v58, v78, v79
	v_lshlrev_b32_e32 v62, 16, v56
	v_and_b32_e32 v63, 0xffff0000, v56
	v_lshlrev_b32_e32 v60, 16, v57
	v_and_b32_e32 v61, 0xffff0000, v57
	v_add_f32_e32 v35, v35, v58
	v_add_f32_e32 v56, v62, v63
	v_add_f32_e32 v57, v60, v61
	v_lshlrev_b32_e32 v68, 16, v54
	v_and_b32_e32 v69, 0xffff0000, v54
	v_lshlrev_b32_e32 v70, 16, v55
	v_and_b32_e32 v71, 0xffff0000, v55
	v_add_f32_e32 v35, 0, v35
	v_add_f32_e32 v56, v56, v57
	v_add_f32_e32 v54, v68, v69
	v_add_f32_e32 v55, v70, v71
	v_lshlrev_b32_e32 v72, 16, v52
	v_and_b32_e32 v73, 0xffff0000, v52
	v_lshlrev_b32_e32 v74, 16, v53
	v_and_b32_e32 v75, 0xffff0000, v53
	v_add_f32_e32 v35, v35, v56
	v_add_f32_e32 v54, v54, v55
	v_add_f32_e32 v52, v72, v73
	v_add_f32_e32 v53, v74, v75
	v_lshlrev_b32_e32 v64, 16, v50
	v_and_b32_e32 v65, 0xffff0000, v50
	v_lshlrev_b32_e32 v66, 16, v51
	v_and_b32_e32 v67, 0xffff0000, v51
	v_add_f32_e32 v35, v35, v54
	v_add_f32_e32 v52, v52, v53
	v_add_f32_e32 v50, v64, v65
	v_add_f32_e32 v51, v66, v67
	v_lshlrev_b32_e32 v56, 16, v48
	v_and_b32_e32 v57, 0xffff0000, v48
	v_lshlrev_b32_e32 v58, 16, v49
	v_and_b32_e32 v59, 0xffff0000, v49
	v_add_f32_e32 v35, v35, v52
	v_add_f32_e32 v50, v50, v51
	v_add_f32_e32 v48, v56, v57
	v_add_f32_e32 v49, v58, v59
	v_lshlrev_b32_e32 v52, 16, v46
	v_and_b32_e32 v53, 0xffff0000, v46
	v_lshlrev_b32_e32 v54, 16, v47
	v_and_b32_e32 v55, 0xffff0000, v47
	v_add_f32_e32 v35, v35, v50
	v_add_f32_e32 v48, v48, v49
	v_add_f32_e32 v46, v52, v53
	v_add_f32_e32 v47, v54, v55
	v_add_f32_e32 v35, v35, v48
	v_add_f32_e32 v46, v46, v47
	v_add_f32_e32 v35, v35, v46
	v_lshlrev_b32_e32 v46, 16, v44
	v_and_b32_e32 v47, 0xffff0000, v44
	v_lshlrev_b32_e32 v44, 16, v45
	v_and_b32_e32 v45, 0xffff0000, v45
	v_add_f32_e32 v48, v46, v47
	v_add_f32_e32 v49, v44, v45
	v_add_f32_e32 v48, v48, v49
	v_add_f32_e32 v35, v35, v48
	s_mov_b64 s[6:7], s[34:35]
	s_mov_b64 s[8:9], s[36:37]
	v_add_f32_dpp v35, v35, v35 quad_perm:[1,0,3,2] row_mask:0xf bank_mask:0xf bound_ctrl:1
	v_lshl_add_u64 v[92:93], s[6:7], 0, v[192:193]
	s_lshl_b64 s[6:7], s[38:39], 11
	v_add_f32_dpp v35, v35, v35 quad_perm:[2,3,0,1] row_mask:0xf bank_mask:0xf bound_ctrl:1
	v_lshl_add_u64 v[94:95], s[8:9], 0, v[192:193]
	v_add_co_u32_e32 v98, vcc, s33, v92
	v_add_f32_dpp v35, v35, v35 row_ror:4 row_mask:0xf bank_mask:0xf bound_ctrl:1
	s_nop 0
	v_addc_co_u32_e32 v99, vcc, 0, v93, vcc
	v_add_f32_dpp v35, v35, v35 row_ror:8 row_mask:0xf bank_mask:0xf bound_ctrl:1
	v_mov_b32_e32 v48, v35
	s_nop 1
	v_permlane16_swap_b32_e32 v35, v48
	v_add_f32_e32 v35, v35, v48
	v_mov_b32_e32 v48, v35
	s_nop 1
	v_permlane32_swap_b32_e32 v35, v48
	v_add_f32_e32 v35, v35, v48
	v_fmac_f32_e32 v79, 0xba000000, v35
	v_fmac_f32_e32 v81, 0xba000000, v35
	v_fmac_f32_e32 v78, 0xba000000, v35
	v_fmac_f32_e32 v80, 0xba000000, v35
	v_mul_f32_e32 v48, v81, v81
	v_mul_f32_e32 v49, v79, v79
	v_fmac_f32_e32 v48, v80, v80
	v_fmac_f32_e32 v49, v78, v78
	v_fmac_f32_e32 v61, 0xba000000, v35
	v_fmac_f32_e32 v63, 0xba000000, v35
	v_add_f32_e32 v48, v48, v49
	v_fmac_f32_e32 v60, 0xba000000, v35
	v_fmac_f32_e32 v62, 0xba000000, v35
	v_mul_f32_e32 v49, v63, v63
	v_mul_f32_e32 v50, v61, v61
	v_fmac_f32_e32 v49, v62, v62
	v_fmac_f32_e32 v50, v60, v60
	v_add_f32_e32 v49, v49, v50
	v_add_f32_e32 v76, v48, v49
	flat_load_dwordx4 v[48:51], v[92:93]
	flat_load_dwordx4 v[84:87], v[94:95]
	v_fmac_f32_e32 v71, 0xba000000, v35
	v_fmac_f32_e32 v69, 0xba000000, v35
	v_fmac_f32_e32 v70, 0xba000000, v35
	v_fmac_f32_e32 v68, 0xba000000, v35
	v_mul_f32_e32 v77, v69, v69
	v_mul_f32_e32 v82, v71, v71
	v_fmac_f32_e32 v77, v68, v68
	v_fmac_f32_e32 v82, v70, v70
	v_add_f32_e32 v77, v77, v82
	v_fmac_f32_e32 v75, 0xba000000, v35
	v_fmac_f32_e32 v73, 0xba000000, v35
	v_add_f32_e32 v76, v76, v77
	v_fmac_f32_e32 v74, 0xba000000, v35
	v_fmac_f32_e32 v72, 0xba000000, v35
	v_mul_f32_e32 v77, v73, v73
	v_mul_f32_e32 v82, v75, v75
	v_fmac_f32_e32 v77, v72, v72
	v_fmac_f32_e32 v82, v74, v74
	v_add_f32_e32 v77, v77, v82
	v_fmac_f32_e32 v67, 0xba000000, v35
	v_fmac_f32_e32 v65, 0xba000000, v35
	v_add_f32_e32 v76, v76, v77
	v_fmac_f32_e32 v66, 0xba000000, v35
	v_fmac_f32_e32 v64, 0xba000000, v35
	v_mul_f32_e32 v77, v65, v65
	v_mul_f32_e32 v82, v67, v67
	v_fmac_f32_e32 v77, v64, v64
	v_fmac_f32_e32 v82, v66, v66
	v_add_f32_e32 v77, v77, v82
	v_fmac_f32_e32 v59, 0xba000000, v35
	v_fmac_f32_e32 v57, 0xba000000, v35
	v_add_f32_e32 v76, v76, v77
	v_fmac_f32_e32 v58, 0xba000000, v35
	v_fmac_f32_e32 v56, 0xba000000, v35
	v_mul_f32_e32 v77, v57, v57
	v_mul_f32_e32 v82, v59, v59
	v_fmac_f32_e32 v77, v56, v56
	v_fmac_f32_e32 v82, v58, v58
	v_add_f32_e32 v77, v77, v82
	v_fmac_f32_e32 v55, 0xba000000, v35
	v_fmac_f32_e32 v53, 0xba000000, v35
	v_add_f32_e32 v76, v76, v77
	v_fmac_f32_e32 v54, 0xba000000, v35
	v_fmac_f32_e32 v52, 0xba000000, v35
	v_mul_f32_e32 v77, v53, v53
	v_mul_f32_e32 v82, v55, v55
	v_fmac_f32_e32 v77, v52, v52
	v_fmac_f32_e32 v82, v54, v54
	v_add_f32_e32 v77, v77, v82
	v_fmac_f32_e32 v45, 0xba000000, v35
	v_fmac_f32_e32 v47, 0xba000000, v35
	v_add_f32_e32 v76, v76, v77
	v_fmac_f32_e32 v44, 0xba000000, v35
	v_fmac_f32_e32 v46, 0xba000000, v35
	v_mul_f32_e32 v35, v47, v47
	v_mul_f32_e32 v77, v45, v45
	v_fmac_f32_e32 v35, v46, v46
	v_fmac_f32_e32 v77, v44, v44
	v_add_f32_e32 v35, v35, v77
	v_add_f32_e32 v35, v76, v35
	v_lshl_add_u64 v[82:83], v[30:31], 0, s[6:7]
	v_add_co_u32_e32 v100, vcc, s33, v94
	v_add_f32_dpp v35, v35, v35 quad_perm:[1,0,3,2] row_mask:0xf bank_mask:0xf bound_ctrl:1
	s_nop 0
	v_addc_co_u32_e32 v101, vcc, 0, v95, vcc
	v_add_f32_dpp v35, v35, v35 quad_perm:[2,3,0,1] row_mask:0xf bank_mask:0xf bound_ctrl:1
	s_nop 1
	v_add_f32_dpp v35, v35, v35 row_ror:4 row_mask:0xf bank_mask:0xf bound_ctrl:1
	s_nop 1
	v_add_f32_dpp v35, v35, v35 row_ror:8 row_mask:0xf bank_mask:0xf bound_ctrl:1
	v_mov_b32_e32 v76, v35
	s_nop 1
	v_permlane16_swap_b32_e32 v35, v76
	v_add_f32_e32 v35, v35, v76
	v_mov_b32_e32 v76, v35
	s_nop 1
	v_permlane32_swap_b32_e32 v35, v76
	v_add_f32_e32 v35, v35, v76
	v_fmamk_f32 v35, v35, 0x3a000000, v207
	v_rsq_f32_e32 v96, v35
	v_lshl_add_u64 v[76:77], v[28:29], 0, s[44:45]
	v_pk_mul_f32 v[80:81], v[96:97], v[80:81] op_sel_hi:[0,1]
	s_waitcnt vmcnt(0) lgkmcnt(0)
	v_pk_fma_f32 v[48:49], v[48:49], v[80:81], v[84:85]
	v_mov_b32_e32 v81, 0
	v_med3_f32 v35, v48, s69, v208
	v_med3_f32 v80, v49, s69, v208
	v_cvt_pk_fp8_f32 v81, v35, v80
	v_pk_mul_f32 v[78:79], v[96:97], v[78:79] op_sel_hi:[0,1]
	v_pk_fma_f32 v[50:51], v[50:51], v[78:79], v[86:87]
	v_pk_mul_f32 v[62:63], v[96:97], v[62:63] op_sel_hi:[0,1]
	v_med3_f32 v35, v50, s69, v208
	v_med3_f32 v78, v51, s69, v208
	v_cvt_pk_fp8_f32 v81, v35, v78 op_sel:[0,0,1]
	v_cvt_pk_bf16_f32 v78, v48, v49
	v_cvt_pk_bf16_f32 v79, v50, v51
	flat_store_dwordx2 v[76:77], v[78:79] nt
	flat_store_dword v[82:83], v81 nt
	flat_load_dwordx4 v[78:81], v[92:93] offset:1024
	s_nop 0
	flat_load_dwordx4 v[84:87], v[94:95] offset:1024
	v_pk_mul_f32 v[88:89], v[96:97], v[60:61] op_sel_hi:[0,1]
	v_pk_mul_f32 v[68:69], v[96:97], v[68:69] op_sel_hi:[0,1]
	v_pk_mul_f32 v[72:73], v[96:97], v[72:73] op_sel_hi:[0,1]
	v_pk_mul_f32 v[74:75], v[96:97], v[74:75] op_sel_hi:[0,1]
	v_pk_mul_f32 v[64:65], v[96:97], v[64:65] op_sel_hi:[0,1]
	v_pk_mul_f32 v[66:67], v[96:97], v[66:67] op_sel_hi:[0,1]
	v_pk_mul_f32 v[56:57], v[96:97], v[56:57] op_sel_hi:[0,1]
	v_pk_mul_f32 v[58:59], v[96:97], v[58:59] op_sel_hi:[0,1]
	v_pk_mul_f32 v[52:53], v[96:97], v[52:53] op_sel_hi:[0,1]
	v_pk_mul_f32 v[54:55], v[96:97], v[54:55] op_sel_hi:[0,1]
	v_pk_mul_f32 v[46:47], v[96:97], v[46:47] op_sel_hi:[0,1]
	v_pk_mul_f32 v[44:45], v[96:97], v[44:45] op_sel_hi:[0,1]
	s_waitcnt vmcnt(0) lgkmcnt(0)
	v_pk_fma_f32 v[60:61], v[78:79], v[62:63], v[84:85]
	s_nop 0
	v_med3_f32 v35, v60, s69, v208
	v_med3_f32 v62, v61, s69, v208
	v_mov_b32_e32 v84, 0
	v_cvt_pk_fp8_f32 v84, v35, v62
	v_pk_fma_f32 v[62:63], v[80:81], v[88:89], v[86:87]
	v_pk_mul_f32 v[88:89], v[96:97], v[70:71] op_sel_hi:[0,1]
	v_med3_f32 v35, v62, s69, v208
	v_med3_f32 v78, v63, s69, v208
	v_cvt_pk_fp8_f32 v84, v35, v78 op_sel:[0,0,1]
	v_cvt_pk_bf16_f32 v78, v60, v61
	v_cvt_pk_bf16_f32 v79, v62, v63
	flat_store_dwordx2 v[76:77], v[78:79] offset:512 nt
	flat_store_dword v[82:83], v84 offset:256 nt
	flat_load_dwordx4 v[78:81], v[92:93] offset:2048
	s_nop 0
	flat_load_dwordx4 v[84:87], v[94:95] offset:2048
	v_mov_b32_e32 v35, 0
	s_waitcnt vmcnt(0) lgkmcnt(0)
	v_pk_fma_f32 v[70:71], v[78:79], v[68:69], v[84:85]
	s_nop 0
	v_med3_f32 v68, v70, s69, v208
	v_med3_f32 v69, v71, s69, v208
	v_cvt_pk_fp8_f32 v35, v68, v69
	v_pk_fma_f32 v[68:69], v[80:81], v[88:89], v[86:87]
	s_nop 0
	v_med3_f32 v78, v68, s69, v208
	v_med3_f32 v79, v69, s69, v208
	v_cvt_pk_fp8_f32 v35, v78, v79 op_sel:[0,0,1]
	v_cvt_pk_bf16_f32 v78, v70, v71
	v_cvt_pk_bf16_f32 v79, v68, v69
	flat_store_dwordx2 v[76:77], v[78:79] offset:1024 nt
	flat_store_dword v[82:83], v35 offset:512 nt
	flat_load_dwordx4 v[84:87], v[92:93] offset:3072
	flat_load_dwordx4 v[88:91], v[94:95] offset:3072
	v_mov_b32_e32 v35, 0
	s_waitcnt vmcnt(0) lgkmcnt(0)
	v_pk_fma_f32 v[80:81], v[84:85], v[72:73], v[88:89]
	s_nop 0
	v_med3_f32 v72, v80, s69, v208
	v_med3_f32 v73, v81, s69, v208
	v_cvt_pk_fp8_f32 v35, v72, v73
	v_pk_fma_f32 v[78:79], v[86:87], v[74:75], v[90:91]
	s_nop 0
	v_med3_f32 v72, v78, s69, v208
	v_med3_f32 v73, v79, s69, v208
	v_cvt_pk_fp8_f32 v35, v72, v73 op_sel:[0,0,1]
	v_cvt_pk_bf16_f32 v72, v80, v81
	v_cvt_pk_bf16_f32 v73, v78, v79
	flat_store_dwordx2 v[76:77], v[72:73] offset:1536 nt
	flat_store_dword v[82:83], v35 offset:768 nt
	flat_load_dwordx4 v[72:75], v[98:99]
	s_nop 0
	flat_load_dwordx4 v[86:89], v[100:101]
	v_mov_b32_e32 v35, 0
	s_waitcnt vmcnt(0) lgkmcnt(0)
	v_pk_fma_f32 v[86:87], v[72:73], v[64:65], v[86:87]
	s_nop 0
	v_med3_f32 v64, v86, s69, v208
	v_med3_f32 v65, v87, s69, v208
	v_cvt_pk_fp8_f32 v35, v64, v65
	v_pk_fma_f32 v[84:85], v[74:75], v[66:67], v[88:89]
	s_nop 0
	v_med3_f32 v64, v84, s69, v208
	v_med3_f32 v65, v85, s69, v208
	v_cvt_pk_fp8_f32 v35, v64, v65 op_sel:[0,0,1]
	v_cvt_pk_bf16_f32 v64, v86, v87
	v_cvt_pk_bf16_f32 v65, v84, v85
	flat_store_dwordx2 v[76:77], v[64:65] offset:2048 nt
	flat_store_dword v[82:83], v35 offset:1024 nt
	flat_load_dwordx4 v[64:67], v[98:99] offset:1024
	s_nop 0
	flat_load_dwordx4 v[72:75], v[100:101] offset:1024
	v_mov_b32_e32 v35, 0
	s_waitcnt vmcnt(0) lgkmcnt(0)
	v_pk_fma_f32 v[90:91], v[64:65], v[56:57], v[72:73]
	s_nop 0
	v_med3_f32 v56, v90, s69, v208
	v_med3_f32 v57, v91, s69, v208
	v_cvt_pk_fp8_f32 v35, v56, v57
	v_pk_fma_f32 v[88:89], v[66:67], v[58:59], v[74:75]
	s_nop 0
	v_med3_f32 v56, v88, s69, v208
	v_med3_f32 v57, v89, s69, v208
	v_cvt_pk_fp8_f32 v35, v56, v57 op_sel:[0,0,1]
	v_cvt_pk_bf16_f32 v56, v90, v91
	v_cvt_pk_bf16_f32 v57, v88, v89
	flat_store_dwordx2 v[76:77], v[56:57] offset:2560 nt
	flat_store_dword v[82:83], v35 offset:1280 nt
	flat_load_dwordx4 v[56:59], v[98:99] offset:2048
	s_nop 0
	flat_load_dwordx4 v[64:67], v[100:101] offset:2048
	v_mov_b32_e32 v35, 0
	s_waitcnt vmcnt(0) lgkmcnt(0)
	v_pk_fma_f32 v[94:95], v[56:57], v[52:53], v[64:65]
	s_nop 0
	v_med3_f32 v52, v94, s69, v208
	v_med3_f32 v53, v95, s69, v208
	v_cvt_pk_fp8_f32 v35, v52, v53
	v_pk_fma_f32 v[92:93], v[58:59], v[54:55], v[66:67]
	s_nop 0
	v_med3_f32 v52, v92, s69, v208
	v_med3_f32 v53, v93, s69, v208
	v_cvt_pk_fp8_f32 v35, v52, v53 op_sel:[0,0,1]
	v_cvt_pk_bf16_f32 v52, v94, v95
	v_cvt_pk_bf16_f32 v53, v92, v93
	flat_store_dwordx2 v[76:77], v[52:53] offset:3072 nt
	flat_store_dword v[82:83], v35 offset:1536 nt
	flat_load_dwordx4 v[52:55], v[98:99] offset:3072
	s_nop 0
	flat_load_dwordx4 v[56:59], v[100:101] offset:3072
	v_mov_b32_e32 v35, 0
	s_waitcnt vmcnt(0) lgkmcnt(0)
	v_pk_fma_f32 v[96:97], v[52:53], v[46:47], v[56:57]
	s_nop 0
	v_med3_f32 v46, v96, s69, v208
	v_med3_f32 v47, v97, s69, v208
	v_mov_b32_e32 v52, 0
	v_cvt_pk_fp8_f32 v52, v46, v47
	v_pk_fma_f32 v[98:99], v[54:55], v[44:45], v[58:59]
	s_nop 0
	v_med3_f32 v44, v98, s69, v208
	v_med3_f32 v45, v99, s69, v208
	v_cvt_pk_fp8_f32 v52, v44, v45 op_sel:[0,0,1]
	v_cvt_pk_bf16_f32 v44, v96, v97
	v_cvt_pk_bf16_f32 v45, v98, v99
	flat_store_dwordx2 v[76:77], v[44:45] offset:3584 nt
	flat_store_dword v[82:83], v52 offset:1792 nt
	v_lshlrev_b32_e32 v102, 16, v42
	v_and_b32_e32 v103, 0xffff0000, v42
	v_lshlrev_b32_e32 v100, 16, v43
	v_and_b32_e32 v101, 0xffff0000, v43
	v_add_f32_e32 v42, v102, v103
	v_add_f32_e32 v43, v100, v101
	v_lshlrev_b32_e32 v74, 16, v40
	v_and_b32_e32 v75, 0xffff0000, v40
	v_lshlrev_b32_e32 v72, 16, v41
	v_and_b32_e32 v73, 0xffff0000, v41
	v_add_f32_e32 v42, v42, v43
	v_add_f32_e32 v40, v74, v75
	v_add_f32_e32 v41, v72, v73
	v_lshlrev_b32_e32 v64, 16, v38
	v_and_b32_e32 v65, 0xffff0000, v38
	v_lshlrev_b32_e32 v66, 16, v39
	v_and_b32_e32 v67, 0xffff0000, v39
	v_add_f32_e32 v42, 0, v42
	v_add_f32_e32 v40, v40, v41
	v_add_f32_e32 v38, v64, v65
	v_add_f32_e32 v39, v66, v67
	v_lshlrev_b32_e32 v56, 16, v36
	v_and_b32_e32 v57, 0xffff0000, v36
	v_lshlrev_b32_e32 v58, 16, v37
	v_and_b32_e32 v59, 0xffff0000, v37
	v_add_f32_e32 v40, v42, v40
	v_add_f32_e32 v38, v38, v39
	v_add_f32_e32 v36, v56, v57
	v_add_f32_e32 v37, v58, v59
	v_lshlrev_b32_e32 v52, 16, v22
	v_and_b32_e32 v53, 0xffff0000, v22
	v_lshlrev_b32_e32 v54, 16, v23
	v_and_b32_e32 v55, 0xffff0000, v23
	v_add_f32_e32 v38, v40, v38
	v_add_f32_e32 v36, v36, v37
	v_add_f32_e32 v22, v52, v53
	v_add_f32_e32 v23, v54, v55
	v_add_f32_e32 v36, v38, v36
	v_add_f32_e32 v22, v22, v23
	v_lshlrev_b32_e32 v44, 16, v20
	v_and_b32_e32 v45, 0xffff0000, v20
	v_lshlrev_b32_e32 v46, 16, v21
	v_and_b32_e32 v47, 0xffff0000, v21
	v_add_f32_e32 v22, v36, v22
	v_add_f32_e32 v20, v44, v45
	v_add_f32_e32 v21, v46, v47
	v_lshlrev_b32_e32 v36, 16, v18
	v_and_b32_e32 v37, 0xffff0000, v18
	v_lshlrev_b32_e32 v38, 16, v19
	v_and_b32_e32 v39, 0xffff0000, v19
	v_add_f32_e32 v20, v20, v21
	v_add_f32_e32 v18, v36, v37
	v_add_f32_e32 v19, v38, v39
	v_lshlrev_b32_e32 v42, 16, v16
	v_and_b32_e32 v43, 0xffff0000, v16
	v_lshlrev_b32_e32 v40, 16, v17
	v_and_b32_e32 v41, 0xffff0000, v17
	v_add_f32_e32 v20, v22, v20
	v_add_f32_e32 v18, v18, v19
	v_add_f32_e32 v16, v42, v43
	v_add_f32_e32 v17, v40, v41
	v_add_f32_e32 v18, v20, v18
	v_add_f32_e32 v16, v16, v17
	v_add_f32_e32 v16, v18, v16
	s_mov_b64 s[6:7], s[34:35]
	s_mov_b64 s[8:9], s[36:37]
	v_add_f32_dpp v16, v16, v16 quad_perm:[1,0,3,2] row_mask:0xf bank_mask:0xf bound_ctrl:1
	v_lshl_add_u64 v[108:109], s[6:7], 0, v[192:193]
	v_lshl_add_u64 v[104:105], v[28:29], 0, s[42:43]
	v_add_f32_dpp v16, v16, v16 quad_perm:[2,3,0,1] row_mask:0xf bank_mask:0xf bound_ctrl:1
	v_lshl_add_u64 v[106:107], s[8:9], 0, v[192:193]
	s_lshl_b64 s[6:7], s[40:41], 11
	v_add_f32_dpp v16, v16, v16 row_ror:4 row_mask:0xf bank_mask:0xf bound_ctrl:1
	v_lshl_add_u64 v[82:83], v[30:31], 0, s[6:7]
	s_nop 0
	v_add_f32_dpp v16, v16, v16 row_ror:8 row_mask:0xf bank_mask:0xf bound_ctrl:1
	v_mov_b32_e32 v17, v16
	s_nop 1
	v_permlane16_swap_b32_e32 v16, v17
	v_add_f32_e32 v16, v16, v17
	v_mov_b32_e32 v17, v16
	s_nop 1
	v_permlane32_swap_b32_e32 v16, v17
	v_add_f32_e32 v16, v16, v17
	v_fmac_f32_e32 v101, 0xba000000, v16
	v_fmac_f32_e32 v103, 0xba000000, v16
	v_fmac_f32_e32 v100, 0xba000000, v16
	v_fmac_f32_e32 v102, 0xba000000, v16
	v_mul_f32_e32 v17, v103, v103
	v_mul_f32_e32 v18, v101, v101
	v_fmac_f32_e32 v17, v102, v102
	v_fmac_f32_e32 v18, v100, v100
	v_fmac_f32_e32 v73, 0xba000000, v16
	v_fmac_f32_e32 v75, 0xba000000, v16
	v_add_f32_e32 v17, v17, v18
	v_fmac_f32_e32 v72, 0xba000000, v16
	v_fmac_f32_e32 v74, 0xba000000, v16
	v_mul_f32_e32 v18, v75, v75
	v_mul_f32_e32 v19, v73, v73
	v_fmac_f32_e32 v18, v74, v74
	v_fmac_f32_e32 v19, v72, v72
	v_add_f32_e32 v18, v18, v19
	v_fmac_f32_e32 v67, 0xba000000, v16
	v_fmac_f32_e32 v65, 0xba000000, v16
	v_add_f32_e32 v17, v17, v18
	v_fmac_f32_e32 v66, 0xba000000, v16
	v_fmac_f32_e32 v64, 0xba000000, v16
	v_mul_f32_e32 v18, v65, v65
	v_mul_f32_e32 v19, v67, v67
	v_fmac_f32_e32 v18, v64, v64
	v_fmac_f32_e32 v19, v66, v66
	v_add_f32_e32 v18, v18, v19
	v_fmac_f32_e32 v59, 0xba000000, v16
	v_fmac_f32_e32 v57, 0xba000000, v16
	v_add_f32_e32 v17, v17, v18
	v_fmac_f32_e32 v58, 0xba000000, v16
	v_fmac_f32_e32 v56, 0xba000000, v16
	v_mul_f32_e32 v18, v57, v57
	v_mul_f32_e32 v19, v59, v59
	v_fmac_f32_e32 v18, v56, v56
	v_fmac_f32_e32 v19, v58, v58
	v_add_f32_e32 v18, v18, v19
	v_fmac_f32_e32 v55, 0xba000000, v16
	v_fmac_f32_e32 v53, 0xba000000, v16
	v_add_f32_e32 v17, v17, v18
	v_fmac_f32_e32 v54, 0xba000000, v16
	v_fmac_f32_e32 v52, 0xba000000, v16
	v_mul_f32_e32 v18, v53, v53
	v_mul_f32_e32 v19, v55, v55
	v_fmac_f32_e32 v18, v52, v52
	v_fmac_f32_e32 v19, v54, v54
	v_add_f32_e32 v18, v18, v19
	v_fmac_f32_e32 v47, 0xba000000, v16
	v_fmac_f32_e32 v45, 0xba000000, v16
	v_add_f32_e32 v17, v17, v18
	v_fmac_f32_e32 v46, 0xba000000, v16
	v_fmac_f32_e32 v44, 0xba000000, v16
	v_mul_f32_e32 v18, v45, v45
	v_mul_f32_e32 v19, v47, v47
	v_fmac_f32_e32 v18, v44, v44
	v_fmac_f32_e32 v19, v46, v46
	v_add_f32_e32 v18, v18, v19
	v_fmac_f32_e32 v39, 0xba000000, v16
	v_fmac_f32_e32 v37, 0xba000000, v16
	v_add_f32_e32 v17, v17, v18
	v_fmac_f32_e32 v38, 0xba000000, v16
	v_fmac_f32_e32 v36, 0xba000000, v16
	v_mul_f32_e32 v18, v37, v37
	v_mul_f32_e32 v19, v39, v39
	v_fmac_f32_e32 v18, v36, v36
	v_fmac_f32_e32 v19, v38, v38
	v_add_f32_e32 v18, v18, v19
	v_fmac_f32_e32 v41, 0xba000000, v16
	v_fmac_f32_e32 v43, 0xba000000, v16
	v_add_f32_e32 v17, v17, v18
	v_fmac_f32_e32 v40, 0xba000000, v16
	v_fmac_f32_e32 v42, 0xba000000, v16
	v_mul_f32_e32 v16, v43, v43
	v_mul_f32_e32 v18, v41, v41
	v_fmac_f32_e32 v16, v42, v42
	v_fmac_f32_e32 v18, v40, v40
	v_add_f32_e32 v16, v16, v18
	v_add_f32_e32 v16, v17, v16
	s_nop 1
	v_add_f32_dpp v16, v16, v16 quad_perm:[1,0,3,2] row_mask:0xf bank_mask:0xf bound_ctrl:1
	s_nop 1
	v_add_f32_dpp v16, v16, v16 quad_perm:[2,3,0,1] row_mask:0xf bank_mask:0xf bound_ctrl:1
	s_nop 1
	v_add_f32_dpp v16, v16, v16 row_ror:4 row_mask:0xf bank_mask:0xf bound_ctrl:1
	s_nop 1
	v_add_f32_dpp v16, v16, v16 row_ror:8 row_mask:0xf bank_mask:0xf bound_ctrl:1
	v_mov_b32_e32 v17, v16
	s_nop 1
	v_permlane16_swap_b32_e32 v16, v17
	v_add_f32_e32 v16, v16, v17
	v_mov_b32_e32 v17, v16
	s_nop 1
	v_permlane32_swap_b32_e32 v16, v17
	v_add_f32_e32 v16, v16, v17
	v_fmamk_f32 v16, v16, 0x3a000000, v207
	v_rsq_f32_e32 v76, v16
	flat_load_dwordx4 v[16:19], v[108:109]
	flat_load_dwordx4 v[20:23], v[106:107]
	v_pk_mul_f32 v[102:103], v[76:77], v[102:103] op_sel_hi:[0,1]
	v_pk_mul_f32 v[100:101], v[76:77], v[100:101] op_sel_hi:[0,1]
	v_pk_mul_f32 v[74:75], v[76:77], v[74:75] op_sel_hi:[0,1]
	v_pk_mul_f32 v[72:73], v[76:77], v[72:73] op_sel_hi:[0,1]
	v_pk_mul_f32 v[110:111], v[76:77], v[64:65] op_sel_hi:[0,1]
	v_pk_mul_f32 v[64:65], v[76:77], v[66:67] op_sel_hi:[0,1]
	s_waitcnt vmcnt(0) lgkmcnt(0)
	v_pk_fma_f32 v[100:101], v[18:19], v[100:101], v[22:23]
	v_pk_fma_f32 v[102:103], v[16:17], v[102:103], v[20:21]
	v_mov_b32_e32 v20, 0
	v_cvt_pk_bf16_f32 v16, v102, v103
	v_cvt_pk_bf16_f32 v17, v100, v101
	flat_store_dwordx2 v[104:105], v[16:17] nt
	v_med3_f32 v16, v102, s69, v208
	v_med3_f32 v17, v103, s69, v208
	v_cvt_pk_fp8_f32 v20, v16, v17
	v_med3_f32 v18, v100, s69, v208
	v_med3_f32 v19, v101, s69, v208
	v_cvt_pk_fp8_f32 v20, v18, v19 op_sel:[0,0,1]
	flat_store_dword v[82:83], v20 nt
	flat_load_dwordx4 v[16:19], v[108:109] offset:1024
	s_nop 0
	flat_load_dwordx4 v[20:23], v[106:107] offset:1024
	s_waitcnt vmcnt(0) lgkmcnt(0)
	v_pk_fma_f32 v[72:73], v[18:19], v[72:73], v[22:23]
	v_pk_fma_f32 v[74:75], v[16:17], v[74:75], v[20:21]
	v_mov_b32_e32 v20, 0
	v_cvt_pk_bf16_f32 v16, v74, v75
	v_cvt_pk_bf16_f32 v17, v72, v73
	flat_store_dwordx2 v[104:105], v[16:17] offset:512 nt
	v_med3_f32 v16, v74, s69, v208
	v_med3_f32 v17, v75, s69, v208
	v_cvt_pk_fp8_f32 v20, v16, v17
	v_med3_f32 v18, v72, s69, v208
	v_med3_f32 v19, v73, s69, v208
	v_cvt_pk_fp8_f32 v20, v18, v19 op_sel:[0,0,1]
	flat_store_dword v[82:83], v20 offset:256 nt
	flat_load_dwordx4 v[16:19], v[108:109] offset:2048
	s_nop 0
	flat_load_dwordx4 v[20:23], v[106:107] offset:2048
	s_waitcnt vmcnt(0) lgkmcnt(0)
	v_pk_fma_f32 v[64:65], v[18:19], v[64:65], v[22:23]
	v_pk_fma_f32 v[66:67], v[16:17], v[110:111], v[20:21]
	v_mov_b32_e32 v20, 0
	v_cvt_pk_bf16_f32 v16, v66, v67
	v_cvt_pk_bf16_f32 v17, v64, v65
	flat_store_dwordx2 v[104:105], v[16:17] offset:1024 nt
	v_med3_f32 v16, v66, s69, v208
	v_med3_f32 v17, v67, s69, v208
	v_cvt_pk_fp8_f32 v20, v16, v17
	v_med3_f32 v18, v64, s69, v208
	v_med3_f32 v19, v65, s69, v208
	v_pk_mul_f32 v[110:111], v[76:77], v[56:57] op_sel_hi:[0,1]
	v_cvt_pk_fp8_f32 v20, v18, v19 op_sel:[0,0,1]
	v_pk_mul_f32 v[56:57], v[76:77], v[58:59] op_sel_hi:[0,1]
	flat_store_dword v[82:83], v20 offset:512 nt
	flat_load_dwordx4 v[16:19], v[108:109] offset:3072
	s_nop 0
	flat_load_dwordx4 v[20:23], v[106:107] offset:3072
	s_waitcnt vmcnt(0) lgkmcnt(0)
	v_pk_fma_f32 v[56:57], v[18:19], v[56:57], v[22:23]
	v_pk_fma_f32 v[58:59], v[16:17], v[110:111], v[20:21]
	v_mov_b32_e32 v20, 0
	v_cvt_pk_bf16_f32 v16, v58, v59
	v_cvt_pk_bf16_f32 v17, v56, v57
	flat_store_dwordx2 v[104:105], v[16:17] offset:1536 nt
	v_med3_f32 v16, v58, s69, v208
	v_med3_f32 v17, v59, s69, v208
	v_cvt_pk_fp8_f32 v20, v16, v17
	v_med3_f32 v18, v56, s69, v208
	v_med3_f32 v19, v57, s69, v208
	v_add_co_u32_e32 v16, vcc, s33, v108
	v_cvt_pk_fp8_f32 v20, v18, v19 op_sel:[0,0,1]
	s_nop 0
	v_addc_co_u32_e32 v17, vcc, 0, v109, vcc
	v_add_co_u32_e32 v18, vcc, s33, v106
	flat_store_dword v[82:83], v20 offset:768 nt
	s_nop 0
	v_addc_co_u32_e32 v19, vcc, 0, v107, vcc
	flat_load_dwordx4 v[20:23], v[16:17]
	flat_load_dwordx4 v[106:109], v[18:19]
	v_pk_mul_f32 v[110:111], v[76:77], v[52:53] op_sel_hi:[0,1]
	v_pk_mul_f32 v[52:53], v[76:77], v[54:55] op_sel_hi:[0,1]
	v_mov_b32_e32 v77, 0
	s_waitcnt vmcnt(0) lgkmcnt(0)
	v_pk_fma_f32 v[52:53], v[22:23], v[52:53], v[108:109]
	v_pk_fma_f32 v[54:55], v[20:21], v[110:111], v[106:107]
	v_med3_f32 v22, v52, s69, v208
	v_cvt_pk_bf16_f32 v20, v54, v55
	v_cvt_pk_bf16_f32 v21, v52, v53
	flat_store_dwordx2 v[104:105], v[20:21] offset:2048 nt
	v_med3_f32 v20, v54, s69, v208
	v_med3_f32 v21, v55, s69, v208
	v_cvt_pk_fp8_f32 v77, v20, v21
	v_med3_f32 v23, v53, s69, v208
	v_cvt_pk_fp8_f32 v77, v22, v23 op_sel:[0,0,1]
	flat_store_dword v[82:83], v77 offset:1024 nt
	flat_load_dwordx4 v[20:23], v[16:17] offset:1024
	flat_load_dwordx4 v[106:109], v[18:19] offset:1024
	v_pk_mul_f32 v[110:111], v[76:77], v[44:45] op_sel_hi:[0,1]
	v_pk_mul_f32 v[44:45], v[76:77], v[46:47] op_sel_hi:[0,1]
	v_mov_b32_e32 v77, 0
	s_waitcnt vmcnt(0) lgkmcnt(0)
	v_pk_fma_f32 v[44:45], v[22:23], v[44:45], v[108:109]
	v_pk_fma_f32 v[46:47], v[20:21], v[110:111], v[106:107]
	v_med3_f32 v22, v44, s69, v208
	v_cvt_pk_bf16_f32 v20, v46, v47
	v_cvt_pk_bf16_f32 v21, v44, v45
	flat_store_dwordx2 v[104:105], v[20:21] offset:2560 nt
	v_med3_f32 v20, v46, s69, v208
	v_med3_f32 v21, v47, s69, v208
	v_cvt_pk_fp8_f32 v77, v20, v21
	v_med3_f32 v23, v45, s69, v208
	v_cvt_pk_fp8_f32 v77, v22, v23 op_sel:[0,0,1]
	flat_store_dword v[82:83], v77 offset:1280 nt
	flat_load_dwordx4 v[20:23], v[16:17] offset:2048
	flat_load_dwordx4 v[106:109], v[18:19] offset:2048
	v_pk_mul_f32 v[110:111], v[76:77], v[36:37] op_sel_hi:[0,1]
	v_pk_mul_f32 v[36:37], v[76:77], v[38:39] op_sel_hi:[0,1]
	v_mov_b32_e32 v77, 0
	s_waitcnt vmcnt(0) lgkmcnt(0)
	v_pk_fma_f32 v[36:37], v[22:23], v[36:37], v[108:109]
	v_pk_fma_f32 v[38:39], v[20:21], v[110:111], v[106:107]
	v_med3_f32 v22, v36, s69, v208
	v_cvt_pk_bf16_f32 v20, v38, v39
	v_cvt_pk_bf16_f32 v21, v36, v37
	flat_store_dwordx2 v[104:105], v[20:21] offset:3072 nt
	v_med3_f32 v20, v38, s69, v208
	v_med3_f32 v21, v39, s69, v208
	v_cvt_pk_fp8_f32 v77, v20, v21
	v_med3_f32 v23, v37, s69, v208
	v_cvt_pk_fp8_f32 v77, v22, v23 op_sel:[0,0,1]
	flat_store_dword v[82:83], v77 offset:1536 nt
	flat_load_dwordx4 v[20:23], v[16:17] offset:3072
	flat_load_dwordx4 v[106:109], v[18:19] offset:3072
	v_pk_mul_f32 v[18:19], v[76:77], v[42:43] op_sel_hi:[0,1]
	v_pk_mul_f32 v[16:17], v[76:77], v[40:41] op_sel_hi:[0,1]
	v_mov_b32_e32 v40, 0
	s_waitcnt vmcnt(0) lgkmcnt(0)
; #define LAS __attribute__((address_space(3)))
; __global__ void __launch_bounds__(NTHREADS, 2) hybrid_fwd(Args a) {
;     ...
;                     for (int j = 0; j < 8; ++j) {
; #pragma unroll
;                         for (int e = 0; e < 16; ++e) { const f32x4 w = *(const LAS f32x4*)(rwT + e * 2052 + j * 256 + lane * 4);
;                             acc2[e] += y2[j][0] * (f32x2){w[0], w[0]}; acc2[e] += y2[j][1] * (f32x2){w[1], w[1]};
;                             acc2[e] += y2[j][2] * (f32x2){w[2], w[2]}; acc2[e] += y2[j][3] * (f32x2){w[3], w[3]}; }
;                         __builtin_amdgcn_sched_barrier(0);
;                     }
	v_pk_fma_f32 v[16:17], v[22:23], v[16:17], v[108:109]
	v_pk_fma_f32 v[18:19], v[20:21], v[18:19], v[106:107]
	v_med3_f32 v22, v16, s69, v208
	v_cvt_pk_bf16_f32 v20, v18, v19
	v_cvt_pk_bf16_f32 v21, v16, v17
	flat_store_dwordx2 v[104:105], v[20:21] offset:3584 nt
	v_med3_f32 v20, v18, s69, v208
	v_med3_f32 v21, v19, s69, v208
	v_cvt_pk_fp8_f32 v40, v20, v21
	v_med3_f32 v23, v17, s69, v208
	v_cvt_pk_fp8_f32 v40, v22, v23 op_sel:[0,0,1]
	flat_store_dword v[82:83], v40 offset:1792 nt
	v_add_u32_e32 v238, 0x10000, v25
	ds_read_b128 v[158:161], v25 offset:0
	ds_read_b128 v[162:165], v25 offset:8208
	ds_read_b128 v[166:169], v25 offset:16416
	ds_read_b128 v[170:173], v25 offset:24624
	ds_read_b128 v[174:177], v25 offset:32832
	ds_read_b128 v[178:181], v25 offset:41040
	ds_read_b128 v[182:185], v25 offset:49248
	ds_read_b128 v[186:189], v25 offset:57456
	v_mov_b32_e32 v76, v70
	v_mov_b32_e32 v77, v66
	v_mov_b32_e32 v66, v71
	v_mov_b32_e32 v82, v68
	v_mov_b32_e32 v83, v64
	v_mov_b32_e32 v64, v69
	v_mov_b32_e32 v68, v80
	v_mov_b32_e32 v69, v58
	v_mov_b32_e32 v58, v81
	v_mov_b32_e32 v70, v78
	v_mov_b32_e32 v71, v56
	v_mov_b32_e32 v56, v79
	ds_read_b128 v[198:201], v238 offset:128
	v_mov_b32_e32 v108, v48
	v_mov_b32_e32 v109, v102
	v_mov_b32_e32 v102, v49
	v_mov_b32_e32 v106, v62
	v_mov_b32_e32 v107, v72
	v_mov_b32_e32 v72, v63
	v_mov_b32_e32 v62, v84
	v_mov_b32_e32 v63, v52
	v_mov_b32_e32 v52, v85
	s_waitcnt lgkmcnt(8)
	v_pk_fma_f32 v[84:85], v[108:109], v[158:159], 0 op_sel_hi:[1,0,0]
	v_mov_b32_e32 v104, v60
	v_mov_b32_e32 v105, v74
	v_mov_b32_e32 v74, v61
	v_mov_b32_e32 v60, v86
	v_mov_b32_e32 v61, v54
	v_mov_b32_e32 v54, v87
	v_pk_fma_f32 v[78:79], v[158:159], v[102:103], v[84:85] op_sel:[1,0,0]
	ds_read_b128 v[202:205], v238 offset:8336
	v_mov_b32_e32 v110, v50
	v_mov_b32_e32 v111, v100
	v_mov_b32_e32 v100, v51
	v_pk_fma_f32 v[78:79], v[160:161], v[110:111], v[78:79] op_sel_hi:[0,1,1]
	v_mov_b32_e32 v80, v161
	v_pk_fma_f32 v[78:79], v[80:81], v[100:101], v[78:79] op_sel_hi:[0,1,1]
	s_waitcnt lgkmcnt(8)
	v_pk_fma_f32 v[80:81], v[108:109], v[162:163], 0 op_sel_hi:[1,0,0]
	v_mov_b32_e32 v50, v88
	v_pk_fma_f32 v[80:81], v[162:163], v[102:103], v[80:81] op_sel:[1,0,0]
	v_mov_b32_e32 v84, v165
	v_pk_fma_f32 v[80:81], v[164:165], v[110:111], v[80:81] op_sel_hi:[0,1,1]
	v_pk_fma_f32 v[120:121], v[84:85], v[100:101], v[80:81] op_sel_hi:[0,1,1]
	ds_read_b128 v[216:219], v238 offset:16544
	v_mov_b32_e32 v51, v44
	v_mov_b32_e32 v44, v89
	v_mov_b32_e32 v48, v90
	v_mov_b32_e32 v49, v46
	s_waitcnt lgkmcnt(8)
	v_pk_fma_f32 v[80:81], v[108:109], v[166:167], 0 op_sel_hi:[1,0,0]
	v_mov_b32_e32 v46, v91
	v_pk_fma_f32 v[80:81], v[166:167], v[102:103], v[80:81] op_sel:[1,0,0]
	v_mov_b32_e32 v84, v169
	v_pk_fma_f32 v[80:81], v[168:169], v[110:111], v[80:81] op_sel_hi:[0,1,1]
	v_pk_fma_f32 v[122:123], v[84:85], v[100:101], v[80:81] op_sel_hi:[0,1,1]
	ds_read_b128 v[220:223], v238 offset:24752
	v_mov_b32_e32 v42, v92
	v_mov_b32_e32 v43, v36
	v_mov_b32_e32 v36, v93
	v_mov_b32_e32 v40, v94
	s_waitcnt lgkmcnt(8)
	v_pk_fma_f32 v[80:81], v[108:109], v[170:171], 0 op_sel_hi:[1,0,0]
	v_mov_b32_e32 v41, v38
	v_pk_fma_f32 v[80:81], v[170:171], v[102:103], v[80:81] op_sel:[1,0,0]
	v_mov_b32_e32 v84, v173
	v_pk_fma_f32 v[80:81], v[172:173], v[110:111], v[80:81] op_sel_hi:[0,1,1]
	v_pk_fma_f32 v[80:81], v[84:85], v[100:101], v[80:81] op_sel_hi:[0,1,1]
	ds_read_b128 v[224:227], v238 offset:32960
	v_mov_b32_e32 v38, v95
	v_mov_b32_e32 v22, v96
	v_mov_b32_e32 v23, v18
	v_mov_b32_e32 v18, v97
	s_waitcnt lgkmcnt(8)
	v_pk_fma_f32 v[88:89], v[108:109], v[174:175], 0 op_sel_hi:[1,0,0]
	v_mov_b32_e32 v20, v98
	v_pk_fma_f32 v[84:85], v[174:175], v[102:103], v[88:89] op_sel:[1,0,0]
	v_mov_b32_e32 v21, v16
	v_pk_fma_f32 v[84:85], v[176:177], v[110:111], v[84:85] op_sel_hi:[0,1,1]
	v_mov_b32_e32 v86, v177
	v_pk_fma_f32 v[84:85], v[86:87], v[100:101], v[84:85] op_sel_hi:[0,1,1]
	ds_read_b128 v[228:231], v238 offset:41168
	v_mov_b32_e32 v16, v99
	s_waitcnt lgkmcnt(8)
	v_pk_fma_f32 v[90:91], v[108:109], v[178:179], 0 op_sel_hi:[1,0,0]
	s_nop 0
	v_pk_fma_f32 v[86:87], v[178:179], v[102:103], v[90:91] op_sel:[1,0,0]
	s_nop 0
	v_pk_fma_f32 v[86:87], v[180:181], v[110:111], v[86:87] op_sel_hi:[0,1,1]
	v_mov_b32_e32 v88, v181
	v_pk_fma_f32 v[86:87], v[88:89], v[100:101], v[86:87] op_sel_hi:[0,1,1]
	ds_read_b128 v[232:235], v238 offset:49376
	s_waitcnt lgkmcnt(8)
	v_pk_fma_f32 v[92:93], v[108:109], v[182:183], 0 op_sel_hi:[1,0,0]
	s_nop 0
	v_pk_fma_f32 v[88:89], v[182:183], v[102:103], v[92:93] op_sel:[1,0,0]
	s_nop 0
	v_pk_fma_f32 v[88:89], v[184:185], v[110:111], v[88:89] op_sel_hi:[0,1,1]
	v_mov_b32_e32 v90, v185
	v_pk_fma_f32 v[88:89], v[90:91], v[100:101], v[88:89] op_sel_hi:[0,1,1]
	ds_read_b128 v[242:245], v238 offset:57584
	s_waitcnt lgkmcnt(8)
	v_pk_fma_f32 v[94:95], v[108:109], v[186:187], 0 op_sel_hi:[1,0,0]
	s_nop 0
	v_pk_fma_f32 v[90:91], v[186:187], v[102:103], v[94:95] op_sel:[1,0,0]
	s_nop 0
	v_pk_fma_f32 v[90:91], v[188:189], v[110:111], v[90:91] op_sel_hi:[0,1,1]
	v_mov_b32_e32 v92, v189
	v_pk_fma_f32 v[90:91], v[92:93], v[100:101], v[90:91] op_sel_hi:[0,1,1]
	ds_read_b128 v[246:249], v25 offset:1024
	s_waitcnt lgkmcnt(8)
	v_pk_fma_f32 v[96:97], v[108:109], v[198:199], 0 op_sel_hi:[1,0,0]
	s_nop 0
	v_pk_fma_f32 v[92:93], v[198:199], v[102:103], v[96:97] op_sel:[1,0,0]
	s_nop 0
	v_pk_fma_f32 v[92:93], v[200:201], v[110:111], v[92:93] op_sel_hi:[0,1,1]
	v_mov_b32_e32 v94, v201
	v_pk_fma_f32 v[92:93], v[94:95], v[100:101], v[92:93] op_sel_hi:[0,1,1]
	ds_read_b128 v[250:253], v25 offset:9232
	s_waitcnt lgkmcnt(8)
; #define LAS __attribute__((address_space(3)))
; __global__ void __launch_bounds__(NTHREADS, 2) hybrid_fwd(Args a) {
;     ...
;                     for (int j = 0; j < 8; ++j) {
; #pragma unroll
;                         for (int e = 0; e < 16; ++e) { const f32x4 w = *(const LAS f32x4*)(rwT + e * 2052 + j * 256 + lane * 4);
;                             acc2[e] += y2[j][0] * (f32x2){w[0], w[0]}; acc2[e] += y2[j][1] * (f32x2){w[1], w[1]};
;                             acc2[e] += y2[j][2] * (f32x2){w[2], w[2]}; acc2[e] += y2[j][3] * (f32x2){w[3], w[3]}; }
;                         __builtin_amdgcn_sched_barrier(0);
;                     }
	v_pk_fma_f32 v[98:99], v[108:109], v[202:203], 0 op_sel_hi:[1,0,0]
	s_nop 0
	v_pk_fma_f32 v[94:95], v[202:203], v[102:103], v[98:99] op_sel:[1,0,0]
	s_nop 0
	v_pk_fma_f32 v[94:95], v[204:205], v[110:111], v[94:95] op_sel_hi:[0,1,1]
	v_mov_b32_e32 v96, v205
	v_pk_fma_f32 v[94:95], v[96:97], v[100:101], v[94:95] op_sel_hi:[0,1,1]
	ds_read_b128 v[158:161], v25 offset:17440
	s_waitcnt lgkmcnt(8)
	v_pk_fma_f32 v[112:113], v[108:109], v[216:217], 0 op_sel_hi:[1,0,0]
	s_nop 0
	v_pk_fma_f32 v[96:97], v[216:217], v[102:103], v[112:113] op_sel:[1,0,0]
	ds_read_b128 v[162:165], v25 offset:25648
	v_pk_fma_f32 v[96:97], v[218:219], v[110:111], v[96:97] op_sel_hi:[0,1,1]
	v_mov_b32_e32 v98, v219
	v_pk_fma_f32 v[96:97], v[98:99], v[100:101], v[96:97] op_sel_hi:[0,1,1]
	s_waitcnt lgkmcnt(8)
	v_pk_fma_f32 v[98:99], v[108:109], v[220:221], 0 op_sel_hi:[1,0,0]
	s_nop 0
	v_pk_fma_f32 v[98:99], v[220:221], v[102:103], v[98:99] op_sel:[1,0,0]
	v_mov_b32_e32 v112, v223
	v_pk_fma_f32 v[98:99], v[222:223], v[110:111], v[98:99] op_sel_hi:[0,1,1]
	v_pk_fma_f32 v[98:99], v[112:113], v[100:101], v[98:99] op_sel_hi:[0,1,1]
	ds_read_b128 v[166:169], v25 offset:33856
	s_waitcnt lgkmcnt(8)
	v_pk_fma_f32 v[116:117], v[108:109], v[224:225], 0 op_sel_hi:[1,0,0]
	s_nop 0
	v_pk_fma_f32 v[112:113], v[224:225], v[102:103], v[116:117] op_sel:[1,0,0]
	s_nop 0
	v_pk_fma_f32 v[112:113], v[226:227], v[110:111], v[112:113] op_sel_hi:[0,1,1]
	v_mov_b32_e32 v114, v227
	v_pk_fma_f32 v[112:113], v[114:115], v[100:101], v[112:113] op_sel_hi:[0,1,1]
	ds_read_b128 v[170:173], v25 offset:42064
	s_waitcnt lgkmcnt(8)
	v_pk_fma_f32 v[118:119], v[108:109], v[228:229], 0 op_sel_hi:[1,0,0]
	s_nop 0
	v_pk_fma_f32 v[114:115], v[228:229], v[102:103], v[118:119] op_sel:[1,0,0]
	s_nop 0
	v_pk_fma_f32 v[114:115], v[230:231], v[110:111], v[114:115] op_sel_hi:[0,1,1]
	v_mov_b32_e32 v116, v231
	v_pk_fma_f32 v[114:115], v[116:117], v[100:101], v[114:115] op_sel_hi:[0,1,1]
	ds_read_b128 v[174:177], v25 offset:50272
	s_waitcnt lgkmcnt(8)
	v_pk_fma_f32 v[124:125], v[108:109], v[232:233], 0 op_sel_hi:[1,0,0]
	s_nop 0
	v_pk_fma_f32 v[116:117], v[232:233], v[102:103], v[124:125] op_sel:[1,0,0]
	ds_read_b128 v[178:181], v25 offset:58480
	v_pk_fma_f32 v[116:117], v[234:235], v[110:111], v[116:117] op_sel_hi:[0,1,1]
	v_mov_b32_e32 v118, v235
	v_pk_fma_f32 v[116:117], v[118:119], v[100:101], v[116:117] op_sel_hi:[0,1,1]
	s_waitcnt lgkmcnt(8)
	v_pk_fma_f32 v[108:109], v[108:109], v[242:243], 0 op_sel_hi:[1,0,0]
	s_nop 0
	v_pk_fma_f32 v[102:103], v[242:243], v[102:103], v[108:109] op_sel:[1,0,0]
	v_mov_b32_e32 v108, v245
	v_pk_fma_f32 v[102:103], v[244:245], v[110:111], v[102:103] op_sel_hi:[0,1,1]
	v_pk_fma_f32 v[118:119], v[108:109], v[100:101], v[102:103] op_sel_hi:[0,1,1]
	ds_read_b128 v[182:185], v238 offset:1152
	s_waitcnt lgkmcnt(8)
	v_pk_fma_f32 v[78:79], v[104:105], v[246:247], v[78:79] op_sel_hi:[1,0,1]
	s_nop 0
	v_pk_fma_f32 v[78:79], v[246:247], v[74:75], v[78:79] op_sel:[1,0,0]
	v_mov_b32_e32 v100, v249
	v_pk_fma_f32 v[78:79], v[248:249], v[106:107], v[78:79] op_sel_hi:[0,1,1]
	v_pk_fma_f32 v[78:79], v[100:101], v[72:73], v[78:79] op_sel_hi:[0,1,1]
	ds_read_b128 v[186:189], v238 offset:9360
	s_waitcnt lgkmcnt(8)
	v_pk_fma_f32 v[108:109], v[104:105], v[250:251], v[120:121] op_sel_hi:[1,0,1]
	s_nop 0
	v_pk_fma_f32 v[100:101], v[250:251], v[74:75], v[108:109] op_sel:[1,0,0]
	s_nop 0
	v_pk_fma_f32 v[100:101], v[252:253], v[106:107], v[100:101] op_sel_hi:[0,1,1]
	v_mov_b32_e32 v102, v253
	v_pk_fma_f32 v[120:121], v[102:103], v[72:73], v[100:101] op_sel_hi:[0,1,1]
	ds_read_b128 v[198:201], v238 offset:17568
	s_waitcnt lgkmcnt(8)
	v_pk_fma_f32 v[108:109], v[104:105], v[158:159], v[122:123] op_sel_hi:[1,0,1]
	s_nop 0
	v_pk_fma_f32 v[100:101], v[158:159], v[74:75], v[108:109] op_sel:[1,0,0]
	ds_read_b128 v[202:205], v238 offset:25776
	v_pk_fma_f32 v[100:101], v[160:161], v[106:107], v[100:101] op_sel_hi:[0,1,1]
	v_mov_b32_e32 v102, v161
	v_pk_fma_f32 v[100:101], v[102:103], v[72:73], v[100:101] op_sel_hi:[0,1,1]
	s_waitcnt lgkmcnt(8)
	v_pk_fma_f32 v[80:81], v[104:105], v[162:163], v[80:81] op_sel_hi:[1,0,1]
	s_nop 0
	v_pk_fma_f32 v[80:81], v[162:163], v[74:75], v[80:81] op_sel:[1,0,0]
	v_mov_b32_e32 v102, v165
	v_pk_fma_f32 v[80:81], v[164:165], v[106:107], v[80:81] op_sel_hi:[0,1,1]
	ds_read_b128 v[216:219], v238 offset:33984
	v_pk_fma_f32 v[80:81], v[102:103], v[72:73], v[80:81] op_sel_hi:[0,1,1]
	s_waitcnt lgkmcnt(8)
	v_pk_fma_f32 v[84:85], v[104:105], v[166:167], v[84:85] op_sel_hi:[1,0,1]
	s_nop 0
	v_pk_fma_f32 v[84:85], v[166:167], v[74:75], v[84:85] op_sel:[1,0,0]
	v_mov_b32_e32 v102, v169
	v_pk_fma_f32 v[84:85], v[168:169], v[106:107], v[84:85] op_sel_hi:[0,1,1]
	ds_read_b128 v[220:223], v238 offset:42192
	v_pk_fma_f32 v[84:85], v[102:103], v[72:73], v[84:85] op_sel_hi:[0,1,1]
	s_waitcnt lgkmcnt(8)
	v_pk_fma_f32 v[86:87], v[104:105], v[170:171], v[86:87] op_sel_hi:[1,0,1]
	s_nop 0
	v_pk_fma_f32 v[86:87], v[170:171], v[74:75], v[86:87] op_sel:[1,0,0]
	v_mov_b32_e32 v102, v173
	v_pk_fma_f32 v[86:87], v[172:173], v[106:107], v[86:87] op_sel_hi:[0,1,1]
	ds_read_b128 v[224:227], v238 offset:50400
	v_pk_fma_f32 v[86:87], v[102:103], v[72:73], v[86:87] op_sel_hi:[0,1,1]
	s_waitcnt lgkmcnt(8)
	v_pk_fma_f32 v[88:89], v[104:105], v[174:175], v[88:89] op_sel_hi:[1,0,1]
	s_nop 0
	v_pk_fma_f32 v[88:89], v[174:175], v[74:75], v[88:89] op_sel:[1,0,0]
	v_mov_b32_e32 v102, v177
	v_pk_fma_f32 v[88:89], v[176:177], v[106:107], v[88:89] op_sel_hi:[0,1,1]
	ds_read_b128 v[228:231], v238 offset:58608
	v_pk_fma_f32 v[88:89], v[102:103], v[72:73], v[88:89] op_sel_hi:[0,1,1]
	s_waitcnt lgkmcnt(8)
; #define LAS __attribute__((address_space(3)))
; __global__ void __launch_bounds__(NTHREADS, 2) hybrid_fwd(Args a) {
;     ...
;                     for (int j = 0; j < 8; ++j) {
; #pragma unroll
;                         for (int e = 0; e < 16; ++e) { const f32x4 w = *(const LAS f32x4*)(rwT + e * 2052 + j * 256 + lane * 4);
;                             acc2[e] += y2[j][0] * (f32x2){w[0], w[0]}; acc2[e] += y2[j][1] * (f32x2){w[1], w[1]};
;                             acc2[e] += y2[j][2] * (f32x2){w[2], w[2]}; acc2[e] += y2[j][3] * (f32x2){w[3], w[3]}; }
;                         __builtin_amdgcn_sched_barrier(0);
;                     }
	v_pk_fma_f32 v[90:91], v[104:105], v[178:179], v[90:91] op_sel_hi:[1,0,1]
	s_nop 0
	v_pk_fma_f32 v[90:91], v[178:179], v[74:75], v[90:91] op_sel:[1,0,0]
	v_mov_b32_e32 v102, v181
	v_pk_fma_f32 v[90:91], v[180:181], v[106:107], v[90:91] op_sel_hi:[0,1,1]
	ds_read_b128 v[232:235], v25 offset:2048
	v_pk_fma_f32 v[90:91], v[102:103], v[72:73], v[90:91] op_sel_hi:[0,1,1]
	s_waitcnt lgkmcnt(8)
	v_pk_fma_f32 v[92:93], v[104:105], v[182:183], v[92:93] op_sel_hi:[1,0,1]
	s_nop 0
	v_pk_fma_f32 v[92:93], v[182:183], v[74:75], v[92:93] op_sel:[1,0,0]
	v_mov_b32_e32 v102, v185
	v_pk_fma_f32 v[92:93], v[184:185], v[106:107], v[92:93] op_sel_hi:[0,1,1]
	ds_read_b128 v[242:245], v25 offset:10256
	v_pk_fma_f32 v[92:93], v[102:103], v[72:73], v[92:93] op_sel_hi:[0,1,1]
	s_waitcnt lgkmcnt(8)
	v_pk_fma_f32 v[94:95], v[104:105], v[186:187], v[94:95] op_sel_hi:[1,0,1]
	s_nop 0
	v_pk_fma_f32 v[94:95], v[186:187], v[74:75], v[94:95] op_sel:[1,0,0]
	v_mov_b32_e32 v102, v189
	v_pk_fma_f32 v[94:95], v[188:189], v[106:107], v[94:95] op_sel_hi:[0,1,1]
	ds_read_b128 v[246:249], v25 offset:18464
	v_pk_fma_f32 v[94:95], v[102:103], v[72:73], v[94:95] op_sel_hi:[0,1,1]
	s_waitcnt lgkmcnt(8)
	v_pk_fma_f32 v[96:97], v[104:105], v[198:199], v[96:97] op_sel_hi:[1,0,1]
	s_nop 0
	v_pk_fma_f32 v[96:97], v[198:199], v[74:75], v[96:97] op_sel:[1,0,0]
	v_mov_b32_e32 v102, v201
	v_pk_fma_f32 v[96:97], v[200:201], v[106:107], v[96:97] op_sel_hi:[0,1,1]
	ds_read_b128 v[250:253], v25 offset:26672
	v_pk_fma_f32 v[96:97], v[102:103], v[72:73], v[96:97] op_sel_hi:[0,1,1]
	s_waitcnt lgkmcnt(8)
	v_pk_fma_f32 v[98:99], v[104:105], v[202:203], v[98:99] op_sel_hi:[1,0,1]
	s_nop 0
	v_pk_fma_f32 v[98:99], v[202:203], v[74:75], v[98:99] op_sel:[1,0,0]
	v_mov_b32_e32 v102, v205
	v_pk_fma_f32 v[98:99], v[204:205], v[106:107], v[98:99] op_sel_hi:[0,1,1]
	ds_read_b128 v[162:165], v25 offset:34880
	v_pk_fma_f32 v[98:99], v[102:103], v[72:73], v[98:99] op_sel_hi:[0,1,1]
	s_waitcnt lgkmcnt(8)
	v_pk_fma_f32 v[102:103], v[104:105], v[216:217], v[112:113] op_sel_hi:[1,0,1]
	s_nop 0
	v_pk_fma_f32 v[102:103], v[216:217], v[74:75], v[102:103] op_sel:[1,0,0]
	v_mov_b32_e32 v108, v219
	v_pk_fma_f32 v[102:103], v[218:219], v[106:107], v[102:103] op_sel_hi:[0,1,1]
	v_pk_fma_f32 v[102:103], v[108:109], v[72:73], v[102:103] op_sel_hi:[0,1,1]
	ds_read_b128 v[166:169], v25 offset:43088
	s_waitcnt lgkmcnt(8)
	v_pk_fma_f32 v[112:113], v[104:105], v[220:221], v[114:115] op_sel_hi:[1,0,1]
	s_nop 0
	v_pk_fma_f32 v[108:109], v[220:221], v[74:75], v[112:113] op_sel:[1,0,0]
	s_nop 0
	v_pk_fma_f32 v[108:109], v[222:223], v[106:107], v[108:109] op_sel_hi:[0,1,1]
	v_mov_b32_e32 v110, v223
	v_pk_fma_f32 v[108:109], v[110:111], v[72:73], v[108:109] op_sel_hi:[0,1,1]
	ds_read_b128 v[170:173], v25 offset:51296
	s_waitcnt lgkmcnt(8)
	v_pk_fma_f32 v[114:115], v[104:105], v[224:225], v[116:117] op_sel_hi:[1,0,1]
	s_nop 0
	v_pk_fma_f32 v[110:111], v[224:225], v[74:75], v[114:115] op_sel:[1,0,0]
	s_nop 0
	v_pk_fma_f32 v[110:111], v[226:227], v[106:107], v[110:111] op_sel_hi:[0,1,1]
	v_mov_b32_e32 v112, v227
	v_pk_fma_f32 v[110:111], v[112:113], v[72:73], v[110:111] op_sel_hi:[0,1,1]
	ds_read_b128 v[174:177], v25 offset:59504
	s_waitcnt lgkmcnt(8)
	v_pk_fma_f32 v[104:105], v[104:105], v[228:229], v[118:119] op_sel_hi:[1,0,1]
	s_nop 0
	v_pk_fma_f32 v[74:75], v[228:229], v[74:75], v[104:105] op_sel:[1,0,0]
	v_mov_b32_e32 v104, v231
	v_pk_fma_f32 v[74:75], v[230:231], v[106:107], v[74:75] op_sel_hi:[0,1,1]
	v_pk_fma_f32 v[104:105], v[104:105], v[72:73], v[74:75] op_sel_hi:[0,1,1]
	ds_read_b128 v[178:181], v238 offset:2176
	ds_read_b128 v[182:185], v238 offset:10384
	s_waitcnt lgkmcnt(8)
	v_pk_fma_f32 v[78:79], v[76:77], v[232:233], v[78:79] op_sel_hi:[1,0,1]
	s_nop 0
	v_pk_fma_f32 v[72:73], v[232:233], v[66:67], v[78:79] op_sel:[1,0,0]
	v_mov_b32_e32 v78, v245
	v_pk_fma_f32 v[72:73], v[234:235], v[82:83], v[72:73] op_sel_hi:[0,1,1]
	v_mov_b32_e32 v74, v235
	v_pk_fma_f32 v[72:73], v[74:75], v[64:65], v[72:73] op_sel_hi:[0,1,1]
	v_pk_fma_f32 v[74:75], v[76:77], v[242:243], v[120:121] op_sel_hi:[1,0,1]
	s_nop 0
	v_pk_fma_f32 v[74:75], v[242:243], v[66:67], v[74:75] op_sel:[1,0,0]
	s_nop 0
	v_pk_fma_f32 v[74:75], v[244:245], v[82:83], v[74:75] op_sel_hi:[0,1,1]
	ds_read_b128 v[186:189], v238 offset:18592
	v_pk_fma_f32 v[106:107], v[78:79], v[64:65], v[74:75] op_sel_hi:[0,1,1]
	s_waitcnt lgkmcnt(8)
	v_pk_fma_f32 v[74:75], v[76:77], v[246:247], v[100:101] op_sel_hi:[1,0,1]
	s_nop 0
	v_pk_fma_f32 v[74:75], v[246:247], v[66:67], v[74:75] op_sel:[1,0,0]
	v_mov_b32_e32 v78, v249
	v_pk_fma_f32 v[74:75], v[248:249], v[82:83], v[74:75] op_sel_hi:[0,1,1]
	ds_read_b128 v[198:201], v238 offset:26800
	v_pk_fma_f32 v[74:75], v[78:79], v[64:65], v[74:75] op_sel_hi:[0,1,1]
	s_waitcnt lgkmcnt(8)
	v_pk_fma_f32 v[78:79], v[76:77], v[250:251], v[80:81] op_sel_hi:[1,0,1]
	s_nop 0
	v_pk_fma_f32 v[78:79], v[250:251], v[66:67], v[78:79] op_sel:[1,0,0]
	v_mov_b32_e32 v80, v253
	v_pk_fma_f32 v[78:79], v[252:253], v[82:83], v[78:79] op_sel_hi:[0,1,1]
	ds_read_b128 v[202:205], v238 offset:35008
	v_pk_fma_f32 v[78:79], v[80:81], v[64:65], v[78:79] op_sel_hi:[0,1,1]
	s_waitcnt lgkmcnt(8)
	v_pk_fma_f32 v[80:81], v[76:77], v[162:163], v[84:85] op_sel_hi:[1,0,1]
	s_nop 0
	v_pk_fma_f32 v[80:81], v[162:163], v[66:67], v[80:81] op_sel:[1,0,0]
	v_mov_b32_e32 v84, v165
	v_pk_fma_f32 v[80:81], v[164:165], v[82:83], v[80:81] op_sel_hi:[0,1,1]
	ds_read_b128 v[158:161], v238 offset:51424
	v_pk_fma_f32 v[80:81], v[84:85], v[64:65], v[80:81] op_sel_hi:[0,1,1]
	s_waitcnt lgkmcnt(8)
; #define LAS __attribute__((address_space(3)))
; __global__ void __launch_bounds__(NTHREADS, 2) hybrid_fwd(Args a) {
;     ...
;                     for (int j = 0; j < 8; ++j) {
; #pragma unroll
;                         for (int e = 0; e < 16; ++e) { const f32x4 w = *(const LAS f32x4*)(rwT + e * 2052 + j * 256 + lane * 4);
;                             acc2[e] += y2[j][0] * (f32x2){w[0], w[0]}; acc2[e] += y2[j][1] * (f32x2){w[1], w[1]};
;                             acc2[e] += y2[j][2] * (f32x2){w[2], w[2]}; acc2[e] += y2[j][3] * (f32x2){w[3], w[3]}; }
;                         __builtin_amdgcn_sched_barrier(0);
;                     }
	v_pk_fma_f32 v[84:85], v[76:77], v[166:167], v[86:87] op_sel_hi:[1,0,1]
	s_nop 0
	v_pk_fma_f32 v[84:85], v[166:167], v[66:67], v[84:85] op_sel:[1,0,0]
	v_mov_b32_e32 v86, v169
	v_pk_fma_f32 v[84:85], v[168:169], v[82:83], v[84:85] op_sel_hi:[0,1,1]
	ds_read_b128 v[216:219], v238 offset:43216
	v_pk_fma_f32 v[84:85], v[86:87], v[64:65], v[84:85] op_sel_hi:[0,1,1]
	s_waitcnt lgkmcnt(8)
	v_pk_fma_f32 v[86:87], v[76:77], v[170:171], v[88:89] op_sel_hi:[1,0,1]
	s_nop 0
	v_pk_fma_f32 v[86:87], v[170:171], v[66:67], v[86:87] op_sel:[1,0,0]
	v_mov_b32_e32 v88, v173
	v_pk_fma_f32 v[86:87], v[172:173], v[82:83], v[86:87] op_sel_hi:[0,1,1]
	ds_read_b128 v[220:223], v238 offset:59632
	v_pk_fma_f32 v[86:87], v[88:89], v[64:65], v[86:87] op_sel_hi:[0,1,1]
	s_waitcnt lgkmcnt(8)
	v_pk_fma_f32 v[88:89], v[76:77], v[174:175], v[90:91] op_sel_hi:[1,0,1]
	s_nop 0
	v_pk_fma_f32 v[88:89], v[174:175], v[66:67], v[88:89] op_sel:[1,0,0]
	v_mov_b32_e32 v90, v177
	v_pk_fma_f32 v[88:89], v[176:177], v[82:83], v[88:89] op_sel_hi:[0,1,1]
	ds_read_b128 v[224:227], v25 offset:3072
	v_pk_fma_f32 v[88:89], v[90:91], v[64:65], v[88:89] op_sel_hi:[0,1,1]
	s_waitcnt lgkmcnt(8)
	v_pk_fma_f32 v[90:91], v[76:77], v[178:179], v[92:93] op_sel_hi:[1,0,1]
	s_nop 0
	v_pk_fma_f32 v[90:91], v[178:179], v[66:67], v[90:91] op_sel:[1,0,0]
	v_mov_b32_e32 v92, v181
	v_pk_fma_f32 v[90:91], v[180:181], v[82:83], v[90:91] op_sel_hi:[0,1,1]
	ds_read_b128 v[228:231], v25 offset:11280
	v_pk_fma_f32 v[90:91], v[92:93], v[64:65], v[90:91] op_sel_hi:[0,1,1]
	s_waitcnt lgkmcnt(8)
	v_pk_fma_f32 v[92:93], v[76:77], v[182:183], v[94:95] op_sel_hi:[1,0,1]
	s_nop 0
	v_pk_fma_f32 v[92:93], v[182:183], v[66:67], v[92:93] op_sel:[1,0,0]
	v_mov_b32_e32 v94, v185
	v_pk_fma_f32 v[92:93], v[184:185], v[82:83], v[92:93] op_sel_hi:[0,1,1]
	ds_read_b128 v[232:235], v25 offset:19488
	v_pk_fma_f32 v[92:93], v[94:95], v[64:65], v[92:93] op_sel_hi:[0,1,1]
	s_waitcnt lgkmcnt(8)
	v_pk_fma_f32 v[94:95], v[76:77], v[186:187], v[96:97] op_sel_hi:[1,0,1]
	s_nop 0
	v_pk_fma_f32 v[94:95], v[186:187], v[66:67], v[94:95] op_sel:[1,0,0]
	v_mov_b32_e32 v96, v189
	v_pk_fma_f32 v[94:95], v[188:189], v[82:83], v[94:95] op_sel_hi:[0,1,1]
	ds_read_b128 v[242:245], v25 offset:27696
	v_pk_fma_f32 v[94:95], v[96:97], v[64:65], v[94:95] op_sel_hi:[0,1,1]
	s_waitcnt lgkmcnt(8)
	v_pk_fma_f32 v[96:97], v[76:77], v[198:199], v[98:99] op_sel_hi:[1,0,1]
	s_nop 0
	v_pk_fma_f32 v[96:97], v[198:199], v[66:67], v[96:97] op_sel:[1,0,0]
	v_mov_b32_e32 v98, v201
	v_pk_fma_f32 v[96:97], v[200:201], v[82:83], v[96:97] op_sel_hi:[0,1,1]
	v_pk_fma_f32 v[96:97], v[98:99], v[64:65], v[96:97] op_sel_hi:[0,1,1]
	ds_read_b128 v[246:249], v25 offset:35904
	ds_read_b128 v[250:253], v25 offset:44112
	s_waitcnt lgkmcnt(8)
	v_pk_fma_f32 v[102:103], v[76:77], v[202:203], v[102:103] op_sel_hi:[1,0,1]
	s_nop 0
	v_pk_fma_f32 v[98:99], v[202:203], v[66:67], v[102:103] op_sel:[1,0,0]
	s_nop 0
	v_pk_fma_f32 v[98:99], v[204:205], v[82:83], v[98:99] op_sel_hi:[0,1,1]
	v_mov_b32_e32 v100, v205
	v_pk_fma_f32 v[98:99], v[100:101], v[64:65], v[98:99] op_sel_hi:[0,1,1]
	ds_read_b128 v[162:165], v25 offset:52320
	s_waitcnt lgkmcnt(8)
	v_pk_fma_f32 v[108:109], v[76:77], v[216:217], v[108:109] op_sel_hi:[1,0,1]
	s_nop 0
	v_pk_fma_f32 v[100:101], v[216:217], v[66:67], v[108:109] op_sel:[1,0,0]
	v_mov_b32_e32 v108, v161
	v_pk_fma_f32 v[100:101], v[218:219], v[82:83], v[100:101] op_sel_hi:[0,1,1]
	v_mov_b32_e32 v102, v219
	v_pk_fma_f32 v[100:101], v[102:103], v[64:65], v[100:101] op_sel_hi:[0,1,1]
	v_pk_fma_f32 v[102:103], v[76:77], v[158:159], v[110:111] op_sel_hi:[1,0,1]
	s_nop 0
	v_pk_fma_f32 v[102:103], v[158:159], v[66:67], v[102:103] op_sel:[1,0,0]
	s_nop 0
	v_pk_fma_f32 v[102:103], v[160:161], v[82:83], v[102:103] op_sel_hi:[0,1,1]
	v_pk_fma_f32 v[102:103], v[108:109], v[64:65], v[102:103] op_sel_hi:[0,1,1]
	ds_read_b128 v[166:169], v25 offset:60528
	s_waitcnt lgkmcnt(8)
	v_pk_fma_f32 v[76:77], v[76:77], v[220:221], v[104:105] op_sel_hi:[1,0,1]
	s_nop 0
	v_pk_fma_f32 v[66:67], v[220:221], v[66:67], v[76:77] op_sel:[1,0,0]
	v_mov_b32_e32 v76, v223
	v_pk_fma_f32 v[66:67], v[222:223], v[82:83], v[66:67] op_sel_hi:[0,1,1]
	v_pk_fma_f32 v[104:105], v[76:77], v[64:65], v[66:67] op_sel_hi:[0,1,1]
	ds_read_b128 v[170:173], v238 offset:3200
	ds_read_b128 v[174:177], v238 offset:11408
	s_waitcnt lgkmcnt(8)
	v_pk_fma_f32 v[72:73], v[68:69], v[224:225], v[72:73] op_sel_hi:[1,0,1]
	s_nop 0
	v_pk_fma_f32 v[64:65], v[224:225], v[58:59], v[72:73] op_sel:[1,0,0]
	v_mov_b32_e32 v72, v231
	v_pk_fma_f32 v[64:65], v[226:227], v[70:71], v[64:65] op_sel_hi:[0,1,1]
	v_mov_b32_e32 v66, v227
	v_pk_fma_f32 v[64:65], v[66:67], v[56:57], v[64:65] op_sel_hi:[0,1,1]
	v_pk_fma_f32 v[66:67], v[68:69], v[228:229], v[106:107] op_sel_hi:[1,0,1]
	s_nop 0
	v_pk_fma_f32 v[66:67], v[228:229], v[58:59], v[66:67] op_sel:[1,0,0]
	s_nop 0
	v_pk_fma_f32 v[66:67], v[230:231], v[70:71], v[66:67] op_sel_hi:[0,1,1]
	ds_read_b128 v[178:181], v238 offset:19616
	v_pk_fma_f32 v[106:107], v[72:73], v[56:57], v[66:67] op_sel_hi:[0,1,1]
	s_waitcnt lgkmcnt(8)
	v_pk_fma_f32 v[66:67], v[68:69], v[232:233], v[74:75] op_sel_hi:[1,0,1]
	s_nop 0
	v_pk_fma_f32 v[66:67], v[232:233], v[58:59], v[66:67] op_sel:[1,0,0]
	v_mov_b32_e32 v72, v235
	v_pk_fma_f32 v[66:67], v[234:235], v[70:71], v[66:67] op_sel_hi:[0,1,1]
	v_pk_fma_f32 v[66:67], v[72:73], v[56:57], v[66:67] op_sel_hi:[0,1,1]
	ds_read_b128 v[182:185], v238 offset:27824
	s_waitcnt lgkmcnt(8)
; #define LAS __attribute__((address_space(3)))
; __global__ void __launch_bounds__(NTHREADS, 2) hybrid_fwd(Args a) {
;     ...
;                     for (int j = 0; j < 8; ++j) {
; #pragma unroll
;                         for (int e = 0; e < 16; ++e) { const f32x4 w = *(const LAS f32x4*)(rwT + e * 2052 + j * 256 + lane * 4);
;                             acc2[e] += y2[j][0] * (f32x2){w[0], w[0]}; acc2[e] += y2[j][1] * (f32x2){w[1], w[1]};
;                             acc2[e] += y2[j][2] * (f32x2){w[2], w[2]}; acc2[e] += y2[j][3] * (f32x2){w[3], w[3]}; }
;                         __builtin_amdgcn_sched_barrier(0);
;                     }
	v_pk_fma_f32 v[76:77], v[68:69], v[242:243], v[78:79] op_sel_hi:[1,0,1]
	s_nop 0
	v_pk_fma_f32 v[72:73], v[242:243], v[58:59], v[76:77] op_sel:[1,0,0]
	s_nop 0
	v_pk_fma_f32 v[72:73], v[244:245], v[70:71], v[72:73] op_sel_hi:[0,1,1]
	v_mov_b32_e32 v74, v245
	v_pk_fma_f32 v[72:73], v[74:75], v[56:57], v[72:73] op_sel_hi:[0,1,1]
	ds_read_b128 v[186:189], v238 offset:36032
	s_waitcnt lgkmcnt(8)
	v_pk_fma_f32 v[78:79], v[68:69], v[246:247], v[80:81] op_sel_hi:[1,0,1]
	s_nop 0
	v_pk_fma_f32 v[74:75], v[246:247], v[58:59], v[78:79] op_sel:[1,0,0]
	s_nop 0
	v_pk_fma_f32 v[74:75], v[248:249], v[70:71], v[74:75] op_sel_hi:[0,1,1]
	v_mov_b32_e32 v76, v249
	v_pk_fma_f32 v[74:75], v[76:77], v[56:57], v[74:75] op_sel_hi:[0,1,1]
	ds_read_b128 v[198:201], v238 offset:44240
	s_waitcnt lgkmcnt(8)
	v_pk_fma_f32 v[80:81], v[68:69], v[250:251], v[84:85] op_sel_hi:[1,0,1]
	s_nop 0
	v_pk_fma_f32 v[76:77], v[250:251], v[58:59], v[80:81] op_sel:[1,0,0]
	s_nop 0
	v_pk_fma_f32 v[76:77], v[252:253], v[70:71], v[76:77] op_sel_hi:[0,1,1]
	v_mov_b32_e32 v78, v253
	v_pk_fma_f32 v[76:77], v[78:79], v[56:57], v[76:77] op_sel_hi:[0,1,1]
	ds_read_b128 v[202:205], v238 offset:52448
	s_waitcnt lgkmcnt(8)
	v_pk_fma_f32 v[82:83], v[68:69], v[162:163], v[86:87] op_sel_hi:[1,0,1]
	s_nop 0
	v_pk_fma_f32 v[78:79], v[162:163], v[58:59], v[82:83] op_sel:[1,0,0]
	s_nop 0
	v_pk_fma_f32 v[78:79], v[164:165], v[70:71], v[78:79] op_sel_hi:[0,1,1]
	v_mov_b32_e32 v80, v165
	v_pk_fma_f32 v[78:79], v[80:81], v[56:57], v[78:79] op_sel_hi:[0,1,1]
	ds_read_b128 v[216:219], v238 offset:60656
	s_waitcnt lgkmcnt(8)
	v_pk_fma_f32 v[84:85], v[68:69], v[166:167], v[88:89] op_sel_hi:[1,0,1]
	s_nop 0
	v_pk_fma_f32 v[80:81], v[166:167], v[58:59], v[84:85] op_sel:[1,0,0]
	s_nop 0
	v_pk_fma_f32 v[80:81], v[168:169], v[70:71], v[80:81] op_sel_hi:[0,1,1]
	v_mov_b32_e32 v82, v169
	v_pk_fma_f32 v[80:81], v[82:83], v[56:57], v[80:81] op_sel_hi:[0,1,1]
	ds_read_b128 v[158:161], v25 offset:4096
	s_waitcnt lgkmcnt(8)
	v_pk_fma_f32 v[86:87], v[68:69], v[170:171], v[90:91] op_sel_hi:[1,0,1]
	s_nop 0
	v_pk_fma_f32 v[82:83], v[170:171], v[58:59], v[86:87] op_sel:[1,0,0]
	s_nop 0
	v_pk_fma_f32 v[82:83], v[172:173], v[70:71], v[82:83] op_sel_hi:[0,1,1]
	v_mov_b32_e32 v84, v173
	v_pk_fma_f32 v[82:83], v[84:85], v[56:57], v[82:83] op_sel_hi:[0,1,1]
	ds_read_b128 v[220:223], v25 offset:12304
	s_waitcnt lgkmcnt(8)
	v_pk_fma_f32 v[88:89], v[68:69], v[174:175], v[92:93] op_sel_hi:[1,0,1]
	s_nop 0
	v_pk_fma_f32 v[84:85], v[174:175], v[58:59], v[88:89] op_sel:[1,0,0]
	s_nop 0
	v_pk_fma_f32 v[84:85], v[176:177], v[70:71], v[84:85] op_sel_hi:[0,1,1]
	v_mov_b32_e32 v86, v177
	v_pk_fma_f32 v[84:85], v[86:87], v[56:57], v[84:85] op_sel_hi:[0,1,1]
	ds_read_b128 v[224:227], v25 offset:20512
	s_waitcnt lgkmcnt(8)
	v_pk_fma_f32 v[90:91], v[68:69], v[178:179], v[94:95] op_sel_hi:[1,0,1]
	s_nop 0
	v_pk_fma_f32 v[86:87], v[178:179], v[58:59], v[90:91] op_sel:[1,0,0]
	s_nop 0
	v_pk_fma_f32 v[86:87], v[180:181], v[70:71], v[86:87] op_sel_hi:[0,1,1]
	v_mov_b32_e32 v88, v181
	v_pk_fma_f32 v[86:87], v[88:89], v[56:57], v[86:87] op_sel_hi:[0,1,1]
	ds_read_b128 v[228:231], v25 offset:28720
	s_waitcnt lgkmcnt(8)
	v_pk_fma_f32 v[92:93], v[68:69], v[182:183], v[96:97] op_sel_hi:[1,0,1]
	s_nop 0
	v_pk_fma_f32 v[88:89], v[182:183], v[58:59], v[92:93] op_sel:[1,0,0]
	s_nop 0
	v_pk_fma_f32 v[88:89], v[184:185], v[70:71], v[88:89] op_sel_hi:[0,1,1]
	v_mov_b32_e32 v90, v185
	v_pk_fma_f32 v[88:89], v[90:91], v[56:57], v[88:89] op_sel_hi:[0,1,1]
	ds_read_b128 v[232:235], v25 offset:36928
	s_waitcnt lgkmcnt(8)
	v_pk_fma_f32 v[94:95], v[68:69], v[186:187], v[98:99] op_sel_hi:[1,0,1]
	s_nop 0
	v_pk_fma_f32 v[90:91], v[186:187], v[58:59], v[94:95] op_sel:[1,0,0]
	s_nop 0
	v_pk_fma_f32 v[90:91], v[188:189], v[70:71], v[90:91] op_sel_hi:[0,1,1]
	v_mov_b32_e32 v92, v189
	v_pk_fma_f32 v[90:91], v[92:93], v[56:57], v[90:91] op_sel_hi:[0,1,1]
	ds_read_b128 v[242:245], v25 offset:45136
	s_waitcnt lgkmcnt(8)
	v_pk_fma_f32 v[96:97], v[68:69], v[198:199], v[100:101] op_sel_hi:[1,0,1]
	s_nop 0
	v_pk_fma_f32 v[92:93], v[198:199], v[58:59], v[96:97] op_sel:[1,0,0]
	s_nop 0
	v_pk_fma_f32 v[92:93], v[200:201], v[70:71], v[92:93] op_sel_hi:[0,1,1]
	v_mov_b32_e32 v94, v201
	v_pk_fma_f32 v[92:93], v[94:95], v[56:57], v[92:93] op_sel_hi:[0,1,1]
	ds_read_b128 v[246:249], v25 offset:53344
	s_waitcnt lgkmcnt(8)
	v_pk_fma_f32 v[98:99], v[68:69], v[202:203], v[102:103] op_sel_hi:[1,0,1]
	s_nop 0
	v_pk_fma_f32 v[94:95], v[202:203], v[58:59], v[98:99] op_sel:[1,0,0]
	s_nop 0
	v_pk_fma_f32 v[94:95], v[204:205], v[70:71], v[94:95] op_sel_hi:[0,1,1]
	v_mov_b32_e32 v96, v205
	v_pk_fma_f32 v[94:95], v[96:97], v[56:57], v[94:95] op_sel_hi:[0,1,1]
	ds_read_b128 v[250:253], v25 offset:61552
	s_waitcnt lgkmcnt(8)
	v_pk_fma_f32 v[68:69], v[68:69], v[216:217], v[104:105] op_sel_hi:[1,0,1]
	s_nop 0
	v_pk_fma_f32 v[58:59], v[216:217], v[58:59], v[68:69] op_sel:[1,0,0]
	v_mov_b32_e32 v68, v219
	v_pk_fma_f32 v[58:59], v[218:219], v[70:71], v[58:59] op_sel_hi:[0,1,1]
	v_pk_fma_f32 v[96:97], v[68:69], v[56:57], v[58:59] op_sel_hi:[0,1,1]
	ds_read_b128 v[162:165], v238 offset:4224
	ds_read_b128 v[166:169], v238 offset:12432
	s_waitcnt lgkmcnt(8)
	v_pk_fma_f32 v[64:65], v[60:61], v[158:159], v[64:65] op_sel_hi:[1,0,1]
	s_nop 0
	v_pk_fma_f32 v[56:57], v[158:159], v[54:55], v[64:65] op_sel:[1,0,0]
	v_mov_b32_e32 v64, v223
	v_pk_fma_f32 v[56:57], v[160:161], v[62:63], v[56:57] op_sel_hi:[0,1,1]
	v_mov_b32_e32 v58, v161
	v_pk_fma_f32 v[56:57], v[58:59], v[52:53], v[56:57] op_sel_hi:[0,1,1]
	v_pk_fma_f32 v[58:59], v[60:61], v[220:221], v[106:107] op_sel_hi:[1,0,1]
	s_nop 0
	v_pk_fma_f32 v[58:59], v[220:221], v[54:55], v[58:59] op_sel:[1,0,0]
	s_nop 0
	v_pk_fma_f32 v[58:59], v[222:223], v[62:63], v[58:59] op_sel_hi:[0,1,1]
	ds_read_b128 v[170:173], v238 offset:20640
	v_pk_fma_f32 v[98:99], v[64:65], v[52:53], v[58:59] op_sel_hi:[0,1,1]
	s_waitcnt lgkmcnt(8)
; #define LAS __attribute__((address_space(3)))
; __global__ void __launch_bounds__(NTHREADS, 2) hybrid_fwd(Args a) {
;     ...
;                     for (int j = 0; j < 8; ++j) {
; #pragma unroll
;                         for (int e = 0; e < 16; ++e) { const f32x4 w = *(const LAS f32x4*)(rwT + e * 2052 + j * 256 + lane * 4);
;                             acc2[e] += y2[j][0] * (f32x2){w[0], w[0]}; acc2[e] += y2[j][1] * (f32x2){w[1], w[1]};
;                             acc2[e] += y2[j][2] * (f32x2){w[2], w[2]}; acc2[e] += y2[j][3] * (f32x2){w[3], w[3]}; }
;                         __builtin_amdgcn_sched_barrier(0);
;                     }
	v_pk_fma_f32 v[58:59], v[60:61], v[224:225], v[66:67] op_sel_hi:[1,0,1]
	s_nop 0
	v_pk_fma_f32 v[58:59], v[224:225], v[54:55], v[58:59] op_sel:[1,0,0]
	v_mov_b32_e32 v64, v227
	v_pk_fma_f32 v[58:59], v[226:227], v[62:63], v[58:59] op_sel_hi:[0,1,1]
	v_pk_fma_f32 v[58:59], v[64:65], v[52:53], v[58:59] op_sel_hi:[0,1,1]
	ds_read_b128 v[174:177], v238 offset:28848
	s_waitcnt lgkmcnt(8)
	v_pk_fma_f32 v[68:69], v[60:61], v[228:229], v[72:73] op_sel_hi:[1,0,1]
	s_nop 0
	v_pk_fma_f32 v[64:65], v[228:229], v[54:55], v[68:69] op_sel:[1,0,0]
	s_nop 0
	v_pk_fma_f32 v[64:65], v[230:231], v[62:63], v[64:65] op_sel_hi:[0,1,1]
	v_mov_b32_e32 v66, v231
	v_pk_fma_f32 v[64:65], v[66:67], v[52:53], v[64:65] op_sel_hi:[0,1,1]
	ds_read_b128 v[178:181], v238 offset:37056
	s_waitcnt lgkmcnt(8)
	v_pk_fma_f32 v[70:71], v[60:61], v[232:233], v[74:75] op_sel_hi:[1,0,1]
	s_nop 0
	v_pk_fma_f32 v[66:67], v[232:233], v[54:55], v[70:71] op_sel:[1,0,0]
	s_nop 0
	v_pk_fma_f32 v[66:67], v[234:235], v[62:63], v[66:67] op_sel_hi:[0,1,1]
	v_mov_b32_e32 v68, v235
	v_pk_fma_f32 v[66:67], v[68:69], v[52:53], v[66:67] op_sel_hi:[0,1,1]
	ds_read_b128 v[182:185], v238 offset:45264
	s_waitcnt lgkmcnt(8)
	v_pk_fma_f32 v[72:73], v[60:61], v[242:243], v[76:77] op_sel_hi:[1,0,1]
	s_nop 0
	v_pk_fma_f32 v[68:69], v[242:243], v[54:55], v[72:73] op_sel:[1,0,0]
	s_nop 0
	v_pk_fma_f32 v[68:69], v[244:245], v[62:63], v[68:69] op_sel_hi:[0,1,1]
	v_mov_b32_e32 v70, v245
	v_pk_fma_f32 v[68:69], v[70:71], v[52:53], v[68:69] op_sel_hi:[0,1,1]
	ds_read_b128 v[186:189], v238 offset:53472
	s_waitcnt lgkmcnt(8)
	v_pk_fma_f32 v[74:75], v[60:61], v[246:247], v[78:79] op_sel_hi:[1,0,1]
	s_nop 0
	v_pk_fma_f32 v[70:71], v[246:247], v[54:55], v[74:75] op_sel:[1,0,0]
	s_nop 0
	v_pk_fma_f32 v[70:71], v[248:249], v[62:63], v[70:71] op_sel_hi:[0,1,1]
	v_mov_b32_e32 v72, v249
	v_pk_fma_f32 v[70:71], v[72:73], v[52:53], v[70:71] op_sel_hi:[0,1,1]
	ds_read_b128 v[198:201], v238 offset:61680
	s_waitcnt lgkmcnt(8)
	v_pk_fma_f32 v[76:77], v[60:61], v[250:251], v[80:81] op_sel_hi:[1,0,1]
	s_nop 0
	v_pk_fma_f32 v[72:73], v[250:251], v[54:55], v[76:77] op_sel:[1,0,0]
	s_nop 0
	v_pk_fma_f32 v[72:73], v[252:253], v[62:63], v[72:73] op_sel_hi:[0,1,1]
	v_mov_b32_e32 v74, v253
	v_pk_fma_f32 v[72:73], v[74:75], v[52:53], v[72:73] op_sel_hi:[0,1,1]
	ds_read_b128 v[202:205], v25 offset:5120
	s_waitcnt lgkmcnt(8)
	v_pk_fma_f32 v[78:79], v[60:61], v[162:163], v[82:83] op_sel_hi:[1,0,1]
	s_nop 0
	v_pk_fma_f32 v[74:75], v[162:163], v[54:55], v[78:79] op_sel:[1,0,0]
	s_nop 0
	v_pk_fma_f32 v[74:75], v[164:165], v[62:63], v[74:75] op_sel_hi:[0,1,1]
	v_mov_b32_e32 v76, v165
	v_pk_fma_f32 v[74:75], v[76:77], v[52:53], v[74:75] op_sel_hi:[0,1,1]
	ds_read_b128 v[216:219], v25 offset:13328
	s_waitcnt lgkmcnt(8)
	v_pk_fma_f32 v[80:81], v[60:61], v[166:167], v[84:85] op_sel_hi:[1,0,1]
	s_nop 0
	v_pk_fma_f32 v[76:77], v[166:167], v[54:55], v[80:81] op_sel:[1,0,0]
	s_nop 0
	v_pk_fma_f32 v[76:77], v[168:169], v[62:63], v[76:77] op_sel_hi:[0,1,1]
	v_mov_b32_e32 v78, v169
	v_pk_fma_f32 v[76:77], v[78:79], v[52:53], v[76:77] op_sel_hi:[0,1,1]
	ds_read_b128 v[158:161], v25 offset:21536
	s_waitcnt lgkmcnt(8)
	v_pk_fma_f32 v[82:83], v[60:61], v[170:171], v[86:87] op_sel_hi:[1,0,1]
	s_nop 0
	v_pk_fma_f32 v[78:79], v[170:171], v[54:55], v[82:83] op_sel:[1,0,0]
	s_nop 0
	v_pk_fma_f32 v[78:79], v[172:173], v[62:63], v[78:79] op_sel_hi:[0,1,1]
	v_mov_b32_e32 v80, v173
	v_pk_fma_f32 v[78:79], v[80:81], v[52:53], v[78:79] op_sel_hi:[0,1,1]
	ds_read_b128 v[220:223], v25 offset:29744
	s_waitcnt lgkmcnt(8)
	v_pk_fma_f32 v[84:85], v[60:61], v[174:175], v[88:89] op_sel_hi:[1,0,1]
	s_nop 0
	v_pk_fma_f32 v[80:81], v[174:175], v[54:55], v[84:85] op_sel:[1,0,0]
	s_nop 0
	v_pk_fma_f32 v[80:81], v[176:177], v[62:63], v[80:81] op_sel_hi:[0,1,1]
	v_mov_b32_e32 v82, v177
	v_pk_fma_f32 v[80:81], v[82:83], v[52:53], v[80:81] op_sel_hi:[0,1,1]
	ds_read_b128 v[224:227], v25 offset:37952
	s_waitcnt lgkmcnt(8)
	v_pk_fma_f32 v[86:87], v[60:61], v[178:179], v[90:91] op_sel_hi:[1,0,1]
	s_nop 0
	v_pk_fma_f32 v[82:83], v[178:179], v[54:55], v[86:87] op_sel:[1,0,0]
	s_nop 0
	v_pk_fma_f32 v[82:83], v[180:181], v[62:63], v[82:83] op_sel_hi:[0,1,1]
	v_mov_b32_e32 v84, v181
	v_pk_fma_f32 v[82:83], v[84:85], v[52:53], v[82:83] op_sel_hi:[0,1,1]
	ds_read_b128 v[228:231], v25 offset:46160
	s_waitcnt lgkmcnt(8)
	v_pk_fma_f32 v[88:89], v[60:61], v[182:183], v[92:93] op_sel_hi:[1,0,1]
	s_nop 0
	v_pk_fma_f32 v[84:85], v[182:183], v[54:55], v[88:89] op_sel:[1,0,0]
	s_nop 0
	v_pk_fma_f32 v[84:85], v[184:185], v[62:63], v[84:85] op_sel_hi:[0,1,1]
	v_mov_b32_e32 v86, v185
	v_pk_fma_f32 v[84:85], v[86:87], v[52:53], v[84:85] op_sel_hi:[0,1,1]
	ds_read_b128 v[232:235], v25 offset:54368
	s_waitcnt lgkmcnt(8)
	v_pk_fma_f32 v[90:91], v[60:61], v[186:187], v[94:95] op_sel_hi:[1,0,1]
	s_nop 0
	v_pk_fma_f32 v[86:87], v[186:187], v[54:55], v[90:91] op_sel:[1,0,0]
	s_nop 0
	v_pk_fma_f32 v[86:87], v[188:189], v[62:63], v[86:87] op_sel_hi:[0,1,1]
	v_mov_b32_e32 v88, v189
	v_pk_fma_f32 v[86:87], v[88:89], v[52:53], v[86:87] op_sel_hi:[0,1,1]
	ds_read_b128 v[242:245], v25 offset:62576
	s_waitcnt lgkmcnt(8)
	v_pk_fma_f32 v[60:61], v[60:61], v[198:199], v[96:97] op_sel_hi:[1,0,1]
	s_nop 0
	v_pk_fma_f32 v[54:55], v[198:199], v[54:55], v[60:61] op_sel:[1,0,0]
	v_mov_b32_e32 v60, v201
	v_pk_fma_f32 v[54:55], v[200:201], v[62:63], v[54:55] op_sel_hi:[0,1,1]
	v_pk_fma_f32 v[88:89], v[60:61], v[52:53], v[54:55] op_sel_hi:[0,1,1]
	ds_read_b128 v[246:249], v238 offset:5248
	s_waitcnt lgkmcnt(8)
; #define LAS __attribute__((address_space(3)))
; __global__ void __launch_bounds__(NTHREADS, 2) hybrid_fwd(Args a) {
;     ...
;                     for (int j = 0; j < 8; ++j) {
; #pragma unroll
;                         for (int e = 0; e < 16; ++e) { const f32x4 w = *(const LAS f32x4*)(rwT + e * 2052 + j * 256 + lane * 4);
;                             acc2[e] += y2[j][0] * (f32x2){w[0], w[0]}; acc2[e] += y2[j][1] * (f32x2){w[1], w[1]};
;                             acc2[e] += y2[j][2] * (f32x2){w[2], w[2]}; acc2[e] += y2[j][3] * (f32x2){w[3], w[3]}; }
;                         __builtin_amdgcn_sched_barrier(0);
;                     }
	v_pk_fma_f32 v[56:57], v[48:49], v[202:203], v[56:57] op_sel_hi:[1,0,1]
	s_nop 0
	v_pk_fma_f32 v[52:53], v[202:203], v[46:47], v[56:57] op_sel:[1,0,0]
	s_nop 0
	v_pk_fma_f32 v[52:53], v[204:205], v[50:51], v[52:53] op_sel_hi:[0,1,1]
	v_mov_b32_e32 v54, v205
	v_pk_fma_f32 v[52:53], v[54:55], v[44:45], v[52:53] op_sel_hi:[0,1,1]
	ds_read_b128 v[250:253], v238 offset:13456
	s_waitcnt lgkmcnt(8)
	v_pk_fma_f32 v[60:61], v[48:49], v[216:217], v[98:99] op_sel_hi:[1,0,1]
	s_nop 0
	v_pk_fma_f32 v[54:55], v[216:217], v[46:47], v[60:61] op_sel:[1,0,0]
	s_nop 0
	v_pk_fma_f32 v[54:55], v[218:219], v[50:51], v[54:55] op_sel_hi:[0,1,1]
	v_mov_b32_e32 v56, v219
	v_pk_fma_f32 v[90:91], v[56:57], v[44:45], v[54:55] op_sel_hi:[0,1,1]
	ds_read_b128 v[162:165], v238 offset:21664
	s_waitcnt lgkmcnt(8)
	v_pk_fma_f32 v[58:59], v[48:49], v[158:159], v[58:59] op_sel_hi:[1,0,1]
	s_nop 0
	v_pk_fma_f32 v[54:55], v[158:159], v[46:47], v[58:59] op_sel:[1,0,0]
	s_nop 0
	v_pk_fma_f32 v[54:55], v[160:161], v[50:51], v[54:55] op_sel_hi:[0,1,1]
	v_mov_b32_e32 v56, v161
	v_pk_fma_f32 v[54:55], v[56:57], v[44:45], v[54:55] op_sel_hi:[0,1,1]
	ds_read_b128 v[166:169], v238 offset:29872
	s_waitcnt lgkmcnt(8)
	v_pk_fma_f32 v[60:61], v[48:49], v[220:221], v[64:65] op_sel_hi:[1,0,1]
	s_nop 0
	v_pk_fma_f32 v[56:57], v[220:221], v[46:47], v[60:61] op_sel:[1,0,0]
	s_nop 0
	v_pk_fma_f32 v[56:57], v[222:223], v[50:51], v[56:57] op_sel_hi:[0,1,1]
	v_mov_b32_e32 v58, v223
	v_pk_fma_f32 v[56:57], v[58:59], v[44:45], v[56:57] op_sel_hi:[0,1,1]
	ds_read_b128 v[170:173], v238 offset:38080
	s_waitcnt lgkmcnt(8)
	v_pk_fma_f32 v[62:63], v[48:49], v[224:225], v[66:67] op_sel_hi:[1,0,1]
	s_nop 0
	v_pk_fma_f32 v[58:59], v[224:225], v[46:47], v[62:63] op_sel:[1,0,0]
	s_nop 0
	v_pk_fma_f32 v[58:59], v[226:227], v[50:51], v[58:59] op_sel_hi:[0,1,1]
	v_mov_b32_e32 v60, v227
	v_pk_fma_f32 v[58:59], v[60:61], v[44:45], v[58:59] op_sel_hi:[0,1,1]
	ds_read_b128 v[174:177], v238 offset:46288
	s_waitcnt lgkmcnt(8)
	v_pk_fma_f32 v[64:65], v[48:49], v[228:229], v[68:69] op_sel_hi:[1,0,1]
	s_nop 0
	v_pk_fma_f32 v[60:61], v[228:229], v[46:47], v[64:65] op_sel:[1,0,0]
	s_nop 0
	v_pk_fma_f32 v[60:61], v[230:231], v[50:51], v[60:61] op_sel_hi:[0,1,1]
	v_mov_b32_e32 v62, v231
	v_pk_fma_f32 v[60:61], v[62:63], v[44:45], v[60:61] op_sel_hi:[0,1,1]
	ds_read_b128 v[178:181], v238 offset:54496
	s_waitcnt lgkmcnt(8)
	v_pk_fma_f32 v[66:67], v[48:49], v[232:233], v[70:71] op_sel_hi:[1,0,1]
	s_nop 0
	v_pk_fma_f32 v[62:63], v[232:233], v[46:47], v[66:67] op_sel:[1,0,0]
	s_nop 0
	v_pk_fma_f32 v[62:63], v[234:235], v[50:51], v[62:63] op_sel_hi:[0,1,1]
	v_mov_b32_e32 v64, v235
	v_pk_fma_f32 v[62:63], v[64:65], v[44:45], v[62:63] op_sel_hi:[0,1,1]
	ds_read_b128 v[182:185], v238 offset:62704
	s_waitcnt lgkmcnt(8)
	v_pk_fma_f32 v[68:69], v[48:49], v[242:243], v[72:73] op_sel_hi:[1,0,1]
	s_nop 0
	v_pk_fma_f32 v[64:65], v[242:243], v[46:47], v[68:69] op_sel:[1,0,0]
	s_nop 0
	v_pk_fma_f32 v[64:65], v[244:245], v[50:51], v[64:65] op_sel_hi:[0,1,1]
	v_mov_b32_e32 v66, v245
	v_pk_fma_f32 v[64:65], v[66:67], v[44:45], v[64:65] op_sel_hi:[0,1,1]
	ds_read_b128 v[186:189], v25 offset:6144
	s_waitcnt lgkmcnt(8)
	v_pk_fma_f32 v[70:71], v[48:49], v[246:247], v[74:75] op_sel_hi:[1,0,1]
	s_nop 0
	v_pk_fma_f32 v[66:67], v[246:247], v[46:47], v[70:71] op_sel:[1,0,0]
	s_nop 0
	v_pk_fma_f32 v[66:67], v[248:249], v[50:51], v[66:67] op_sel_hi:[0,1,1]
	v_mov_b32_e32 v68, v249
	v_pk_fma_f32 v[66:67], v[68:69], v[44:45], v[66:67] op_sel_hi:[0,1,1]
	ds_read_b128 v[198:201], v25 offset:14352
	s_waitcnt lgkmcnt(8)
	v_pk_fma_f32 v[72:73], v[48:49], v[250:251], v[76:77] op_sel_hi:[1,0,1]
	s_nop 0
	v_pk_fma_f32 v[68:69], v[250:251], v[46:47], v[72:73] op_sel:[1,0,0]
	s_nop 0
	v_pk_fma_f32 v[68:69], v[252:253], v[50:51], v[68:69] op_sel_hi:[0,1,1]
	v_mov_b32_e32 v70, v253
	v_pk_fma_f32 v[68:69], v[70:71], v[44:45], v[68:69] op_sel_hi:[0,1,1]
	ds_read_b128 v[202:205], v25 offset:22560
	s_waitcnt lgkmcnt(8)
	v_pk_fma_f32 v[74:75], v[48:49], v[162:163], v[78:79] op_sel_hi:[1,0,1]
	s_nop 0
	v_pk_fma_f32 v[70:71], v[162:163], v[46:47], v[74:75] op_sel:[1,0,0]
	s_nop 0
	v_pk_fma_f32 v[70:71], v[164:165], v[50:51], v[70:71] op_sel_hi:[0,1,1]
	v_mov_b32_e32 v72, v165
	v_pk_fma_f32 v[70:71], v[72:73], v[44:45], v[70:71] op_sel_hi:[0,1,1]
	ds_read_b128 v[216:219], v25 offset:30768
	s_waitcnt lgkmcnt(8)
	v_pk_fma_f32 v[76:77], v[48:49], v[166:167], v[80:81] op_sel_hi:[1,0,1]
	s_nop 0
	v_pk_fma_f32 v[72:73], v[166:167], v[46:47], v[76:77] op_sel:[1,0,0]
	s_nop 0
	v_pk_fma_f32 v[72:73], v[168:169], v[50:51], v[72:73] op_sel_hi:[0,1,1]
	v_mov_b32_e32 v74, v169
	v_pk_fma_f32 v[72:73], v[74:75], v[44:45], v[72:73] op_sel_hi:[0,1,1]
	ds_read_b128 v[158:161], v25 offset:38976
	s_waitcnt lgkmcnt(8)
	v_pk_fma_f32 v[78:79], v[48:49], v[170:171], v[82:83] op_sel_hi:[1,0,1]
	s_nop 0
	v_pk_fma_f32 v[74:75], v[170:171], v[46:47], v[78:79] op_sel:[1,0,0]
	s_nop 0
	v_pk_fma_f32 v[74:75], v[172:173], v[50:51], v[74:75] op_sel_hi:[0,1,1]
	v_mov_b32_e32 v76, v173
	v_pk_fma_f32 v[74:75], v[76:77], v[44:45], v[74:75] op_sel_hi:[0,1,1]
	ds_read_b128 v[220:223], v25 offset:47184
	s_waitcnt lgkmcnt(8)
	v_pk_fma_f32 v[80:81], v[48:49], v[174:175], v[84:85] op_sel_hi:[1,0,1]
	s_nop 0
	v_pk_fma_f32 v[76:77], v[174:175], v[46:47], v[80:81] op_sel:[1,0,0]
	s_nop 0
	v_pk_fma_f32 v[76:77], v[176:177], v[50:51], v[76:77] op_sel_hi:[0,1,1]
	v_mov_b32_e32 v78, v177
	v_pk_fma_f32 v[76:77], v[78:79], v[44:45], v[76:77] op_sel_hi:[0,1,1]
	ds_read_b128 v[224:227], v25 offset:55392
	s_waitcnt lgkmcnt(8)
; #define LAS __attribute__((address_space(3)))
; __global__ void __launch_bounds__(NTHREADS, 2) hybrid_fwd(Args a) {
;     ...
;                     for (int j = 0; j < 8; ++j) {
; #pragma unroll
;                         for (int e = 0; e < 16; ++e) { const f32x4 w = *(const LAS f32x4*)(rwT + e * 2052 + j * 256 + lane * 4);
;                             acc2[e] += y2[j][0] * (f32x2){w[0], w[0]}; acc2[e] += y2[j][1] * (f32x2){w[1], w[1]};
;                             acc2[e] += y2[j][2] * (f32x2){w[2], w[2]}; acc2[e] += y2[j][3] * (f32x2){w[3], w[3]}; }
;                         __builtin_amdgcn_sched_barrier(0);
;                     }
	v_pk_fma_f32 v[82:83], v[48:49], v[178:179], v[86:87] op_sel_hi:[1,0,1]
	s_nop 0
	v_pk_fma_f32 v[78:79], v[178:179], v[46:47], v[82:83] op_sel:[1,0,0]
	s_nop 0
	v_pk_fma_f32 v[78:79], v[180:181], v[50:51], v[78:79] op_sel_hi:[0,1,1]
	v_mov_b32_e32 v80, v181
	v_pk_fma_f32 v[78:79], v[80:81], v[44:45], v[78:79] op_sel_hi:[0,1,1]
	ds_read_b128 v[228:231], v25 offset:63600
	s_waitcnt lgkmcnt(8)
	v_pk_fma_f32 v[48:49], v[48:49], v[182:183], v[88:89] op_sel_hi:[1,0,1]
	s_nop 0
	v_pk_fma_f32 v[46:47], v[182:183], v[46:47], v[48:49] op_sel:[1,0,0]
	v_mov_b32_e32 v48, v185
	v_pk_fma_f32 v[46:47], v[184:185], v[50:51], v[46:47] op_sel_hi:[0,1,1]
	v_pk_fma_f32 v[80:81], v[48:49], v[44:45], v[46:47] op_sel_hi:[0,1,1]
	ds_read_b128 v[232:235], v238 offset:6272
	s_waitcnt lgkmcnt(8)
	v_pk_fma_f32 v[48:49], v[40:41], v[186:187], v[52:53] op_sel_hi:[1,0,1]
	s_nop 0
	v_pk_fma_f32 v[44:45], v[186:187], v[38:39], v[48:49] op_sel:[1,0,0]
	s_nop 0
	v_pk_fma_f32 v[44:45], v[188:189], v[42:43], v[44:45] op_sel_hi:[0,1,1]
	v_mov_b32_e32 v46, v189
	v_pk_fma_f32 v[44:45], v[46:47], v[36:37], v[44:45] op_sel_hi:[0,1,1]
	ds_read_b128 v[242:245], v238 offset:14480
	s_waitcnt lgkmcnt(8)
	v_pk_fma_f32 v[50:51], v[40:41], v[198:199], v[90:91] op_sel_hi:[1,0,1]
	s_nop 0
	v_pk_fma_f32 v[46:47], v[198:199], v[38:39], v[50:51] op_sel:[1,0,0]
	s_nop 0
	v_pk_fma_f32 v[46:47], v[200:201], v[42:43], v[46:47] op_sel_hi:[0,1,1]
	v_mov_b32_e32 v48, v201
	v_pk_fma_f32 v[82:83], v[48:49], v[36:37], v[46:47] op_sel_hi:[0,1,1]
	ds_read_b128 v[246:249], v238 offset:22688
	s_waitcnt lgkmcnt(8)
	v_pk_fma_f32 v[50:51], v[40:41], v[202:203], v[54:55] op_sel_hi:[1,0,1]
	s_nop 0
	v_pk_fma_f32 v[46:47], v[202:203], v[38:39], v[50:51] op_sel:[1,0,0]
	s_nop 0
	v_pk_fma_f32 v[46:47], v[204:205], v[42:43], v[46:47] op_sel_hi:[0,1,1]
	v_mov_b32_e32 v48, v205
	v_pk_fma_f32 v[46:47], v[48:49], v[36:37], v[46:47] op_sel_hi:[0,1,1]
	ds_read_b128 v[250:253], v238 offset:30896
	s_waitcnt lgkmcnt(8)
	v_pk_fma_f32 v[52:53], v[40:41], v[216:217], v[56:57] op_sel_hi:[1,0,1]
	s_nop 0
	v_pk_fma_f32 v[48:49], v[216:217], v[38:39], v[52:53] op_sel:[1,0,0]
	s_nop 0
	v_pk_fma_f32 v[48:49], v[218:219], v[42:43], v[48:49] op_sel_hi:[0,1,1]
	v_mov_b32_e32 v50, v219
	v_pk_fma_f32 v[48:49], v[50:51], v[36:37], v[48:49] op_sel_hi:[0,1,1]
	ds_read_b128 v[162:165], v238 offset:39104
	s_waitcnt lgkmcnt(8)
	v_pk_fma_f32 v[54:55], v[40:41], v[158:159], v[58:59] op_sel_hi:[1,0,1]
	s_nop 0
	v_pk_fma_f32 v[50:51], v[158:159], v[38:39], v[54:55] op_sel:[1,0,0]
	s_nop 0
	v_pk_fma_f32 v[50:51], v[160:161], v[42:43], v[50:51] op_sel_hi:[0,1,1]
	v_mov_b32_e32 v52, v161
	v_pk_fma_f32 v[50:51], v[52:53], v[36:37], v[50:51] op_sel_hi:[0,1,1]
	ds_read_b128 v[166:169], v238 offset:47312
	s_waitcnt lgkmcnt(8)
	v_pk_fma_f32 v[56:57], v[40:41], v[220:221], v[60:61] op_sel_hi:[1,0,1]
	s_nop 0
	v_pk_fma_f32 v[52:53], v[220:221], v[38:39], v[56:57] op_sel:[1,0,0]
	s_nop 0
	v_pk_fma_f32 v[52:53], v[222:223], v[42:43], v[52:53] op_sel_hi:[0,1,1]
	v_mov_b32_e32 v54, v223
	v_pk_fma_f32 v[52:53], v[54:55], v[36:37], v[52:53] op_sel_hi:[0,1,1]
	ds_read_b128 v[170:173], v238 offset:55520
	s_waitcnt lgkmcnt(8)
	v_pk_fma_f32 v[58:59], v[40:41], v[224:225], v[62:63] op_sel_hi:[1,0,1]
	s_nop 0
	v_pk_fma_f32 v[54:55], v[224:225], v[38:39], v[58:59] op_sel:[1,0,0]
	s_nop 0
	v_pk_fma_f32 v[54:55], v[226:227], v[42:43], v[54:55] op_sel_hi:[0,1,1]
	v_mov_b32_e32 v56, v227
	v_pk_fma_f32 v[54:55], v[56:57], v[36:37], v[54:55] op_sel_hi:[0,1,1]
	ds_read_b128 v[174:177], v238 offset:63728
	s_waitcnt lgkmcnt(8)
	v_pk_fma_f32 v[60:61], v[40:41], v[228:229], v[64:65] op_sel_hi:[1,0,1]
	s_nop 0
	v_pk_fma_f32 v[56:57], v[228:229], v[38:39], v[60:61] op_sel:[1,0,0]
	s_nop 0
	v_pk_fma_f32 v[56:57], v[230:231], v[42:43], v[56:57] op_sel_hi:[0,1,1]
	v_mov_b32_e32 v58, v231
	v_pk_fma_f32 v[56:57], v[58:59], v[36:37], v[56:57] op_sel_hi:[0,1,1]
	ds_read_b128 v[178:181], v25 offset:7168
	s_waitcnt lgkmcnt(8)
	v_pk_fma_f32 v[62:63], v[40:41], v[232:233], v[66:67] op_sel_hi:[1,0,1]
	s_nop 0
	v_pk_fma_f32 v[58:59], v[232:233], v[38:39], v[62:63] op_sel:[1,0,0]
	s_nop 0
	v_pk_fma_f32 v[58:59], v[234:235], v[42:43], v[58:59] op_sel_hi:[0,1,1]
	v_mov_b32_e32 v60, v235
	v_pk_fma_f32 v[58:59], v[60:61], v[36:37], v[58:59] op_sel_hi:[0,1,1]
	ds_read_b128 v[182:185], v25 offset:15376
	s_waitcnt lgkmcnt(8)
	v_pk_fma_f32 v[64:65], v[40:41], v[242:243], v[68:69] op_sel_hi:[1,0,1]
	s_nop 0
	v_pk_fma_f32 v[60:61], v[242:243], v[38:39], v[64:65] op_sel:[1,0,0]
	s_nop 0
	v_pk_fma_f32 v[60:61], v[244:245], v[42:43], v[60:61] op_sel_hi:[0,1,1]
	v_mov_b32_e32 v62, v245
	v_pk_fma_f32 v[60:61], v[62:63], v[36:37], v[60:61] op_sel_hi:[0,1,1]
	ds_read_b128 v[186:189], v25 offset:23584
	s_waitcnt lgkmcnt(8)
	v_pk_fma_f32 v[66:67], v[40:41], v[246:247], v[70:71] op_sel_hi:[1,0,1]
	s_nop 0
	v_pk_fma_f32 v[62:63], v[246:247], v[38:39], v[66:67] op_sel:[1,0,0]
	s_nop 0
	v_pk_fma_f32 v[62:63], v[248:249], v[42:43], v[62:63] op_sel_hi:[0,1,1]
	v_mov_b32_e32 v64, v249
	v_pk_fma_f32 v[62:63], v[64:65], v[36:37], v[62:63] op_sel_hi:[0,1,1]
	ds_read_b128 v[198:201], v25 offset:31792
	s_waitcnt lgkmcnt(8)
	v_pk_fma_f32 v[68:69], v[40:41], v[250:251], v[72:73] op_sel_hi:[1,0,1]
	s_nop 0
	v_pk_fma_f32 v[64:65], v[250:251], v[38:39], v[68:69] op_sel:[1,0,0]
	s_nop 0
	v_pk_fma_f32 v[64:65], v[252:253], v[42:43], v[64:65] op_sel_hi:[0,1,1]
	v_mov_b32_e32 v66, v253
	v_pk_fma_f32 v[64:65], v[66:67], v[36:37], v[64:65] op_sel_hi:[0,1,1]
	ds_read_b128 v[202:205], v25 offset:40000
	s_waitcnt lgkmcnt(8)
; #define LAS __attribute__((address_space(3)))
; __global__ void __launch_bounds__(NTHREADS, 2) hybrid_fwd(Args a) {
;     ...
;                     for (int j = 0; j < 8; ++j) {
; #pragma unroll
;                         for (int e = 0; e < 16; ++e) { const f32x4 w = *(const LAS f32x4*)(rwT + e * 2052 + j * 256 + lane * 4);
;                             acc2[e] += y2[j][0] * (f32x2){w[0], w[0]}; acc2[e] += y2[j][1] * (f32x2){w[1], w[1]};
;                             acc2[e] += y2[j][2] * (f32x2){w[2], w[2]}; acc2[e] += y2[j][3] * (f32x2){w[3], w[3]}; }
;                         __builtin_amdgcn_sched_barrier(0);
;                     }
	v_pk_fma_f32 v[70:71], v[40:41], v[162:163], v[74:75] op_sel_hi:[1,0,1]
	s_nop 0
	v_pk_fma_f32 v[66:67], v[162:163], v[38:39], v[70:71] op_sel:[1,0,0]
	s_nop 0
	v_pk_fma_f32 v[66:67], v[164:165], v[42:43], v[66:67] op_sel_hi:[0,1,1]
	v_mov_b32_e32 v68, v165
	v_pk_fma_f32 v[66:67], v[68:69], v[36:37], v[66:67] op_sel_hi:[0,1,1]
	ds_read_b128 v[216:219], v25 offset:48208
	s_waitcnt lgkmcnt(8)
	v_pk_fma_f32 v[72:73], v[40:41], v[166:167], v[76:77] op_sel_hi:[1,0,1]
	s_nop 0
	v_pk_fma_f32 v[68:69], v[166:167], v[38:39], v[72:73] op_sel:[1,0,0]
	s_nop 0
	v_pk_fma_f32 v[68:69], v[168:169], v[42:43], v[68:69] op_sel_hi:[0,1,1]
	v_mov_b32_e32 v70, v169
	v_pk_fma_f32 v[68:69], v[70:71], v[36:37], v[68:69] op_sel_hi:[0,1,1]
	ds_read_b128 v[158:161], v25 offset:56416
	s_waitcnt lgkmcnt(8)
	v_pk_fma_f32 v[74:75], v[40:41], v[170:171], v[78:79] op_sel_hi:[1,0,1]
	s_nop 0
	v_pk_fma_f32 v[70:71], v[170:171], v[38:39], v[74:75] op_sel:[1,0,0]
	s_nop 0
	v_pk_fma_f32 v[70:71], v[172:173], v[42:43], v[70:71] op_sel_hi:[0,1,1]
	v_mov_b32_e32 v72, v173
	v_pk_fma_f32 v[70:71], v[72:73], v[36:37], v[70:71] op_sel_hi:[0,1,1]
	ds_read_b128 v[220:223], v25 offset:64624
	s_waitcnt lgkmcnt(8)
	v_pk_fma_f32 v[40:41], v[40:41], v[174:175], v[80:81] op_sel_hi:[1,0,1]
	s_nop 0
	v_pk_fma_f32 v[38:39], v[174:175], v[38:39], v[40:41] op_sel:[1,0,0]
	v_mov_b32_e32 v40, v177
	v_pk_fma_f32 v[38:39], v[176:177], v[42:43], v[38:39] op_sel_hi:[0,1,1]
	v_pk_fma_f32 v[72:73], v[40:41], v[36:37], v[38:39] op_sel_hi:[0,1,1]
	ds_read_b128 v[224:227], v238 offset:7296
	s_waitcnt lgkmcnt(8)
	v_pk_fma_f32 v[40:41], v[22:23], v[178:179], v[44:45] op_sel_hi:[1,0,1]
	s_nop 0
	v_pk_fma_f32 v[36:37], v[178:179], v[18:19], v[40:41] op_sel:[1,0,0]
	s_nop 0
	v_pk_fma_f32 v[36:37], v[180:181], v[20:21], v[36:37] op_sel_hi:[0,1,1]
	v_mov_b32_e32 v38, v181
	v_pk_fma_f32 v[36:37], v[38:39], v[16:17], v[36:37] op_sel_hi:[0,1,1]
	ds_read_b128 v[228:231], v238 offset:15504
	s_waitcnt lgkmcnt(8)
	v_pk_fma_f32 v[42:43], v[22:23], v[182:183], v[82:83] op_sel_hi:[1,0,1]
	s_nop 0
	v_pk_fma_f32 v[38:39], v[182:183], v[18:19], v[42:43] op_sel:[1,0,0]
	s_nop 0
	v_pk_fma_f32 v[38:39], v[184:185], v[20:21], v[38:39] op_sel_hi:[0,1,1]
	v_mov_b32_e32 v40, v185
	v_pk_fma_f32 v[38:39], v[40:41], v[16:17], v[38:39] op_sel_hi:[0,1,1]
	ds_read_b128 v[232:235], v238 offset:23712
	s_waitcnt lgkmcnt(8)
	v_pk_fma_f32 v[44:45], v[22:23], v[186:187], v[46:47] op_sel_hi:[1,0,1]
	s_nop 0
	v_pk_fma_f32 v[40:41], v[186:187], v[18:19], v[44:45] op_sel:[1,0,0]
	s_nop 0
	v_pk_fma_f32 v[40:41], v[188:189], v[20:21], v[40:41] op_sel_hi:[0,1,1]
	v_mov_b32_e32 v42, v189
	v_pk_fma_f32 v[40:41], v[42:43], v[16:17], v[40:41] op_sel_hi:[0,1,1]
	ds_read_b128 v[242:245], v238 offset:31920
	s_waitcnt lgkmcnt(8)
	v_pk_fma_f32 v[46:47], v[22:23], v[198:199], v[48:49] op_sel_hi:[1,0,1]
	s_nop 0
	v_pk_fma_f32 v[42:43], v[198:199], v[18:19], v[46:47] op_sel:[1,0,0]
	ds_read_b128 v[246:249], v238 offset:40128
	v_pk_fma_f32 v[42:43], v[200:201], v[20:21], v[42:43] op_sel_hi:[0,1,1]
	v_mov_b32_e32 v44, v201
	v_pk_fma_f32 v[44:45], v[44:45], v[16:17], v[42:43] op_sel_hi:[0,1,1]
	s_waitcnt lgkmcnt(8)
	v_pk_fma_f32 v[42:43], v[22:23], v[202:203], v[50:51] op_sel_hi:[1,0,1]
	s_nop 0
	v_pk_fma_f32 v[42:43], v[202:203], v[18:19], v[42:43] op_sel:[1,0,0]
	v_mov_b32_e32 v46, v205
	v_pk_fma_f32 v[42:43], v[204:205], v[20:21], v[42:43] op_sel_hi:[0,1,1]
	v_pk_fma_f32 v[42:43], v[46:47], v[16:17], v[42:43] op_sel_hi:[0,1,1]
	ds_read_b128 v[250:253], v238 offset:48336
	s_waitcnt lgkmcnt(8)
	v_pk_fma_f32 v[50:51], v[22:23], v[216:217], v[52:53] op_sel_hi:[1,0,1]
	s_nop 0
	v_pk_fma_f32 v[46:47], v[216:217], v[18:19], v[50:51] op_sel:[1,0,0]
	s_nop 0
	v_pk_fma_f32 v[46:47], v[218:219], v[20:21], v[46:47] op_sel_hi:[0,1,1]
	v_mov_b32_e32 v48, v219
	v_pk_fma_f32 v[46:47], v[48:49], v[16:17], v[46:47] op_sel_hi:[0,1,1]
	ds_read_b128 v[162:165], v238 offset:56544
	s_waitcnt lgkmcnt(8)
	v_pk_fma_f32 v[52:53], v[22:23], v[158:159], v[54:55] op_sel_hi:[1,0,1]
	s_nop 0
	v_pk_fma_f32 v[48:49], v[158:159], v[18:19], v[52:53] op_sel:[1,0,0]
	s_nop 0
	v_pk_fma_f32 v[48:49], v[160:161], v[20:21], v[48:49] op_sel_hi:[0,1,1]
	v_mov_b32_e32 v50, v161
	v_pk_fma_f32 v[48:49], v[50:51], v[16:17], v[48:49] op_sel_hi:[0,1,1]
	ds_read_b128 v[166:169], v238 offset:64752
	s_waitcnt lgkmcnt(8)
	v_pk_fma_f32 v[54:55], v[22:23], v[220:221], v[56:57] op_sel_hi:[1,0,1]
	s_nop 0
	v_pk_fma_f32 v[50:51], v[220:221], v[18:19], v[54:55] op_sel:[1,0,0]
	s_nop 0
	v_pk_fma_f32 v[50:51], v[222:223], v[20:21], v[50:51] op_sel_hi:[0,1,1]
	v_mov_b32_e32 v52, v223
	v_pk_fma_f32 v[50:51], v[52:53], v[16:17], v[50:51] op_sel_hi:[0,1,1]
	s_waitcnt lgkmcnt(7)
	v_pk_fma_f32 v[56:57], v[22:23], v[224:225], v[58:59] op_sel_hi:[1,0,1]
	s_nop 0
	v_pk_fma_f32 v[52:53], v[224:225], v[18:19], v[56:57] op_sel:[1,0,0]
	s_nop 0
	v_pk_fma_f32 v[52:53], v[226:227], v[20:21], v[52:53] op_sel_hi:[0,1,1]
	v_mov_b32_e32 v54, v227
	v_pk_fma_f32 v[52:53], v[54:55], v[16:17], v[52:53] op_sel_hi:[0,1,1]
	s_waitcnt lgkmcnt(6)
	v_pk_fma_f32 v[58:59], v[22:23], v[228:229], v[60:61] op_sel_hi:[1,0,1]
	s_nop 0
	v_pk_fma_f32 v[54:55], v[228:229], v[18:19], v[58:59] op_sel:[1,0,0]
	s_nop 0
	v_pk_fma_f32 v[54:55], v[230:231], v[20:21], v[54:55] op_sel_hi:[0,1,1]
	v_mov_b32_e32 v56, v231
	v_pk_fma_f32 v[54:55], v[56:57], v[16:17], v[54:55] op_sel_hi:[0,1,1]
	s_waitcnt lgkmcnt(5)
	v_pk_fma_f32 v[60:61], v[22:23], v[232:233], v[62:63] op_sel_hi:[1,0,1]
	s_nop 0
	v_pk_fma_f32 v[56:57], v[232:233], v[18:19], v[60:61] op_sel:[1,0,0]
	s_nop 0
	v_pk_fma_f32 v[56:57], v[234:235], v[20:21], v[56:57] op_sel_hi:[0,1,1]
	v_mov_b32_e32 v58, v235
	v_pk_fma_f32 v[56:57], v[58:59], v[16:17], v[56:57] op_sel_hi:[0,1,1]
	s_waitcnt lgkmcnt(4)
; #define LAS __attribute__((address_space(3)))
; __global__ void __launch_bounds__(NTHREADS, 2) hybrid_fwd(Args a) {
;     ...
;                     for (int j = 0; j < 8; ++j) {
; #pragma unroll
;                         for (int e = 0; e < 16; ++e) { const f32x4 w = *(const LAS f32x4*)(rwT + e * 2052 + j * 256 + lane * 4);
;                             acc2[e] += y2[j][0] * (f32x2){w[0], w[0]}; acc2[e] += y2[j][1] * (f32x2){w[1], w[1]};
;                             acc2[e] += y2[j][2] * (f32x2){w[2], w[2]}; acc2[e] += y2[j][3] * (f32x2){w[3], w[3]}; }
;                         __builtin_amdgcn_sched_barrier(0);
;                     }
	v_pk_fma_f32 v[62:63], v[22:23], v[242:243], v[64:65] op_sel_hi:[1,0,1]
	s_nop 0
	v_pk_fma_f32 v[58:59], v[242:243], v[18:19], v[62:63] op_sel:[1,0,0]
	s_nop 0
	v_pk_fma_f32 v[58:59], v[244:245], v[20:21], v[58:59] op_sel_hi:[0,1,1]
	v_mov_b32_e32 v60, v245
	v_pk_fma_f32 v[58:59], v[60:61], v[16:17], v[58:59] op_sel_hi:[0,1,1]
	s_waitcnt lgkmcnt(3)
	v_pk_fma_f32 v[64:65], v[22:23], v[246:247], v[66:67] op_sel_hi:[1,0,1]
	s_nop 0
	v_pk_fma_f32 v[60:61], v[246:247], v[18:19], v[64:65] op_sel:[1,0,0]
	s_nop 0
	v_pk_fma_f32 v[60:61], v[248:249], v[20:21], v[60:61] op_sel_hi:[0,1,1]
	v_mov_b32_e32 v62, v249
	v_pk_fma_f32 v[60:61], v[62:63], v[16:17], v[60:61] op_sel_hi:[0,1,1]
	s_waitcnt lgkmcnt(2)
	v_pk_fma_f32 v[66:67], v[22:23], v[250:251], v[68:69] op_sel_hi:[1,0,1]
	s_nop 0
	v_pk_fma_f32 v[62:63], v[250:251], v[18:19], v[66:67] op_sel:[1,0,0]
	s_nop 0
	v_pk_fma_f32 v[62:63], v[252:253], v[20:21], v[62:63] op_sel_hi:[0,1,1]
	v_mov_b32_e32 v64, v253
	v_pk_fma_f32 v[62:63], v[64:65], v[16:17], v[62:63] op_sel_hi:[0,1,1]
	s_waitcnt lgkmcnt(1)
	v_pk_fma_f32 v[68:69], v[22:23], v[162:163], v[70:71] op_sel_hi:[1,0,1]
	s_nop 0
	v_pk_fma_f32 v[64:65], v[162:163], v[18:19], v[68:69] op_sel:[1,0,0]
	s_nop 0
	v_pk_fma_f32 v[64:65], v[164:165], v[20:21], v[64:65] op_sel_hi:[0,1,1]
	v_mov_b32_e32 v66, v165
	v_pk_fma_f32 v[64:65], v[66:67], v[16:17], v[64:65] op_sel_hi:[0,1,1]
	s_waitcnt lgkmcnt(0)
	v_pk_fma_f32 v[22:23], v[22:23], v[166:167], v[72:73] op_sel_hi:[1,0,1]
	s_nop 0
	v_pk_fma_f32 v[18:19], v[166:167], v[18:19], v[22:23] op_sel:[1,0,0]
	s_nop 0
	v_pk_fma_f32 v[18:19], v[168:169], v[20:21], v[18:19] op_sel_hi:[0,1,1]
	v_mov_b32_e32 v20, v169
	v_pk_fma_f32 v[16:17], v[20:21], v[16:17], v[18:19] op_sel_hi:[0,1,1]
	v_add_f32_dpp v18, v36, v36 quad_perm:[1,0,3,2] row_mask:0xf bank_mask:0xf bound_ctrl:1
	s_nop 0
	v_add_f32_dpp v16, v16, v16 quad_perm:[1,0,3,2] row_mask:0xf bank_mask:0xf bound_ctrl:1
	v_add_f32_dpp v36, v62, v62 quad_perm:[1,0,3,2] row_mask:0xf bank_mask:0xf bound_ctrl:1
	v_add_f32_dpp v18, v18, v18 quad_perm:[2,3,0,1] row_mask:0xf bank_mask:0xf bound_ctrl:1
	v_add_f32_dpp v16, v16, v16 quad_perm:[2,3,0,1] row_mask:0xf bank_mask:0xf bound_ctrl:1
	v_add_f32_dpp v36, v36, v36 quad_perm:[2,3,0,1] row_mask:0xf bank_mask:0xf bound_ctrl:1
	v_add_f32_dpp v18, v18, v18 row_ror:4 row_mask:0xf bank_mask:0xf bound_ctrl:1
	v_add_f32_dpp v16, v16, v16 row_ror:4 row_mask:0xf bank_mask:0xf bound_ctrl:1
	v_add_f32_dpp v36, v36, v36 row_ror:4 row_mask:0xf bank_mask:0xf bound_ctrl:1
	v_add_f32_dpp v18, v18, v18 row_ror:8 row_mask:0xf bank_mask:0xf bound_ctrl:1
	v_mov_b32_e32 v19, v18
	s_nop 1
	v_permlane16_swap_b32_e32 v18, v19
	v_add_f32_e32 v18, v18, v19
	v_mov_b32_e32 v19, v18
	s_nop 1
	v_permlane32_swap_b32_e32 v18, v19
	v_add_f32_e32 v18, v18, v19
	s_nop 0
	v_add_f32_dpp v19, v38, v38 quad_perm:[1,0,3,2] row_mask:0xf bank_mask:0xf bound_ctrl:1
	v_mul_f32_e32 v18, 0xbfb8aa3b, v18
	v_exp_f32_e32 v18, v18
	v_add_f32_dpp v19, v19, v19 quad_perm:[2,3,0,1] row_mask:0xf bank_mask:0xf bound_ctrl:1
	v_add_f32_dpp v16, v16, v16 row_ror:8 row_mask:0xf bank_mask:0xf bound_ctrl:1
	v_add_f32_dpp v36, v36, v36 row_ror:8 row_mask:0xf bank_mask:0xf bound_ctrl:1
	v_add_f32_dpp v19, v19, v19 row_ror:4 row_mask:0xf bank_mask:0xf bound_ctrl:1
	v_add_f32_e32 v18, 1.0, v18
	v_rcp_f32_e32 v18, v18
	v_add_f32_dpp v19, v19, v19 row_ror:8 row_mask:0xf bank_mask:0xf bound_ctrl:1
	v_mov_b32_e32 v20, v19
	s_nop 1
	v_permlane16_swap_b32_e32 v19, v20
	v_add_f32_e32 v19, v19, v20
	v_mov_b32_e32 v20, v19
	s_nop 1
	v_permlane32_swap_b32_e32 v19, v20
	v_add_f32_e32 v19, v19, v20
	s_nop 0
	v_add_f32_dpp v20, v40, v40 quad_perm:[1,0,3,2] row_mask:0xf bank_mask:0xf bound_ctrl:1
	v_mul_f32_e32 v19, 0xbfb8aa3b, v19
	v_exp_f32_e32 v19, v19
	v_add_f32_dpp v20, v20, v20 quad_perm:[2,3,0,1] row_mask:0xf bank_mask:0xf bound_ctrl:1
	v_add_f32_dpp v40, v64, v64 quad_perm:[1,0,3,2] row_mask:0xf bank_mask:0xf bound_ctrl:1
	v_mov_b32_e32 v38, v36
	v_add_f32_dpp v20, v20, v20 row_ror:4 row_mask:0xf bank_mask:0xf bound_ctrl:1
	v_add_f32_e32 v19, 1.0, v19
	v_rcp_f32_e32 v19, v19
	v_add_f32_dpp v20, v20, v20 row_ror:8 row_mask:0xf bank_mask:0xf bound_ctrl:1
	v_mov_b32_e32 v21, v20
	s_nop 1
	v_permlane16_swap_b32_e32 v20, v21
	v_add_f32_e32 v20, v20, v21
	v_mov_b32_e32 v21, v20
	s_nop 1
	v_permlane32_swap_b32_e32 v20, v21
	v_add_f32_e32 v20, v20, v21
	s_nop 0
	v_add_f32_dpp v21, v44, v44 quad_perm:[1,0,3,2] row_mask:0xf bank_mask:0xf bound_ctrl:1
	v_mul_f32_e32 v20, 0xbfb8aa3b, v20
	v_exp_f32_e32 v20, v20
	v_add_f32_dpp v21, v21, v21 quad_perm:[2,3,0,1] row_mask:0xf bank_mask:0xf bound_ctrl:1
	v_mov_b32_e32 v44, v16
	s_nop 1
	v_permlane16_swap_b32_e32 v16, v44
	v_add_f32_dpp v21, v21, v21 row_ror:4 row_mask:0xf bank_mask:0xf bound_ctrl:1
	v_add_f32_e32 v20, 1.0, v20
	v_rcp_f32_e32 v70, v20
	v_add_f32_dpp v21, v21, v21 row_ror:8 row_mask:0xf bank_mask:0xf bound_ctrl:1
	v_mov_b32_e32 v22, v21
	s_nop 1
	v_permlane16_swap_b32_e32 v21, v22
	v_add_f32_e32 v21, v21, v22
	v_mov_b32_e32 v22, v21
	s_nop 1
	v_permlane32_swap_b32_e32 v21, v22
	v_add_f32_e32 v21, v21, v22
	s_nop 0
	v_add_f32_dpp v22, v42, v42 quad_perm:[1,0,3,2] row_mask:0xf bank_mask:0xf bound_ctrl:1
	v_mul_f32_e32 v21, 0xbfb8aa3b, v21
	v_exp_f32_e32 v21, v21
	v_add_f32_dpp v22, v22, v22 quad_perm:[2,3,0,1] row_mask:0xf bank_mask:0xf bound_ctrl:1
	v_add_f32_e32 v79, v14, v70
	v_add_f32_e32 v44, v16, v44
	v_add_f32_dpp v22, v22, v22 row_ror:4 row_mask:0xf bank_mask:0xf bound_ctrl:1
	v_add_f32_e32 v20, 1.0, v21
	v_rcp_f32_e32 v72, v20
	v_add_f32_dpp v22, v22, v22 row_ror:8 row_mask:0xf bank_mask:0xf bound_ctrl:1
	v_mov_b32_e32 v23, v22
	s_nop 1
	v_permlane16_swap_b32_e32 v22, v23
	v_add_f32_e32 v69, v22, v23
	s_nop 0
	v_add_f32_dpp v22, v46, v46 quad_perm:[1,0,3,2] row_mask:0xf bank_mask:0xf bound_ctrl:1
	v_pk_add_f32 v[20:21], v[12:13], v[18:19]
	v_add_f32_e32 v80, v15, v72
	v_add_f32_dpp v22, v22, v22 quad_perm:[2,3,0,1] row_mask:0xf bank_mask:0xf bound_ctrl:1
	v_cmp_gt_f32_e32 vcc, v21, v20
	v_add_f32_dpp v40, v40, v40 quad_perm:[2,3,0,1] row_mask:0xf bank_mask:0xf bound_ctrl:1
	v_add_f32_dpp v22, v22, v22 row_ror:4 row_mask:0xf bank_mask:0xf bound_ctrl:1
	v_cndmask_b32_e32 v16, v20, v21, vcc
	v_cmp_gt_f32_e64 s[6:7], v79, v16
	v_add_f32_dpp v22, v22, v22 row_ror:8 row_mask:0xf bank_mask:0xf bound_ctrl:1
	v_mov_b32_e32 v23, v22
	s_nop 1
	v_permlane16_swap_b32_e32 v22, v23
	v_add_f32_e32 v73, v22, v23
	s_nop 0
	v_add_f32_dpp v22, v48, v48 quad_perm:[1,0,3,2] row_mask:0xf bank_mask:0xf bound_ctrl:1
	v_cndmask_b32_e64 v48, 0, 1, vcc
	v_cndmask_b32_e64 v16, v16, v79, s[6:7]
	v_add_f32_dpp v22, v22, v22 quad_perm:[2,3,0,1] row_mask:0xf bank_mask:0xf bound_ctrl:1
	v_cndmask_b32_e64 v48, v48, 2, s[6:7]
	v_cmp_ngt_f32_e64 s[8:9], v80, v16
	v_add_f32_dpp v22, v22, v22 row_ror:4 row_mask:0xf bank_mask:0xf bound_ctrl:1
	v_add_f32_dpp v40, v40, v40 row_ror:4 row_mask:0xf bank_mask:0xf bound_ctrl:1
	v_permlane16_swap_b32_e32 v36, v38
	v_add_f32_dpp v22, v22, v22 row_ror:8 row_mask:0xf bank_mask:0xf bound_ctrl:1
	v_mov_b32_e32 v23, v22
	s_nop 1
	v_permlane16_swap_b32_e32 v22, v23
	v_add_f32_e32 v75, v22, v23
	s_nop 0
	v_add_f32_dpp v22, v50, v50 quad_perm:[1,0,3,2] row_mask:0xf bank_mask:0xf bound_ctrl:1
	v_add_f32_dpp v40, v40, v40 row_ror:8 row_mask:0xf bank_mask:0xf bound_ctrl:1
	v_mov_b32_e32 v42, v40
	v_add_f32_dpp v22, v22, v22 quad_perm:[2,3,0,1] row_mask:0xf bank_mask:0xf bound_ctrl:1
	s_nop 0
	v_permlane16_swap_b32_e32 v40, v42
	v_add_f32_dpp v22, v22, v22 row_ror:4 row_mask:0xf bank_mask:0xf bound_ctrl:1
	v_add_f32_e32 v36, v36, v38
	v_add_f32_e32 v40, v40, v42
	v_add_f32_dpp v22, v22, v22 row_ror:8 row_mask:0xf bank_mask:0xf bound_ctrl:1
	v_mov_b32_e32 v23, v22
	s_nop 1
	v_permlane16_swap_b32_e32 v22, v23
	v_add_f32_e32 v77, v22, v23
	s_nop 0
	v_add_f32_dpp v22, v52, v52 quad_perm:[1,0,3,2] row_mask:0xf bank_mask:0xf bound_ctrl:1
	v_cndmask_b32_e64 v62, v80, v16, s[8:9]
	v_mov_b32_e32 v71, v69
	v_add_f32_dpp v22, v22, v22 quad_perm:[2,3,0,1] row_mask:0xf bank_mask:0xf bound_ctrl:1
	v_mov_b32_e32 v74, v73
	v_mov_b32_e32 v76, v75
	v_add_f32_dpp v22, v22, v22 row_ror:4 row_mask:0xf bank_mask:0xf bound_ctrl:1
	v_mov_b32_e32 v78, v77
	v_mov_b32_e32 v38, v36
	v_add_f32_dpp v22, v22, v22 row_ror:8 row_mask:0xf bank_mask:0xf bound_ctrl:1
	v_mov_b32_e32 v23, v22
	s_nop 1
	v_permlane16_swap_b32_e32 v22, v23
	v_add_f32_e32 v50, v22, v23
	s_nop 0
	v_add_f32_dpp v22, v54, v54 quad_perm:[1,0,3,2] row_mask:0xf bank_mask:0xf bound_ctrl:1
	v_mov_b32_e32 v52, v50
	v_mov_b32_e32 v42, v40
	v_add_f32_dpp v22, v22, v22 quad_perm:[2,3,0,1] row_mask:0xf bank_mask:0xf bound_ctrl:1
	v_mov_b32_e32 v46, v44
	v_permlane32_swap_b32_e32 v69, v71
	v_add_f32_dpp v22, v22, v22 row_ror:4 row_mask:0xf bank_mask:0xf bound_ctrl:1
	v_permlane32_swap_b32_e32 v73, v74
	s_nop 0
	v_add_f32_dpp v22, v22, v22 row_ror:8 row_mask:0xf bank_mask:0xf bound_ctrl:1
	v_mov_b32_e32 v23, v22
	s_nop 1
	v_permlane16_swap_b32_e32 v22, v23
	v_add_f32_e32 v54, v22, v23
	s_nop 0
	v_add_f32_dpp v22, v56, v56 quad_perm:[1,0,3,2] row_mask:0xf bank_mask:0xf bound_ctrl:1
	v_mov_b32_e32 v66, v54
	v_permlane32_swap_b32_e32 v75, v76
	v_add_f32_dpp v22, v22, v22 quad_perm:[2,3,0,1] row_mask:0xf bank_mask:0xf bound_ctrl:1
	v_permlane32_swap_b32_e32 v77, v78
	s_nop 0
	v_add_f32_dpp v22, v22, v22 row_ror:4 row_mask:0xf bank_mask:0xf bound_ctrl:1
	v_permlane32_swap_b32_e32 v50, v52
	s_nop 0
	v_add_f32_dpp v22, v22, v22 row_ror:8 row_mask:0xf bank_mask:0xf bound_ctrl:1
	v_mov_b32_e32 v23, v22
	s_nop 1
	v_permlane16_swap_b32_e32 v22, v23
	v_add_f32_e32 v56, v22, v23
	s_nop 0
	v_add_f32_dpp v22, v58, v58 quad_perm:[1,0,3,2] row_mask:0xf bank_mask:0xf bound_ctrl:1
	v_mov_b32_e32 v67, v56
	v_permlane32_swap_b32_e32 v54, v66
	v_add_f32_dpp v22, v22, v22 quad_perm:[2,3,0,1] row_mask:0xf bank_mask:0xf bound_ctrl:1
	v_permlane32_swap_b32_e32 v56, v67
	s_nop 0
	v_add_f32_dpp v22, v22, v22 row_ror:4 row_mask:0xf bank_mask:0xf bound_ctrl:1
	v_permlane32_swap_b32_e32 v36, v38
	s_nop 0
	v_add_f32_dpp v22, v22, v22 row_ror:8 row_mask:0xf bank_mask:0xf bound_ctrl:1
	v_mov_b32_e32 v23, v22
	s_nop 1
	v_permlane16_swap_b32_e32 v22, v23
	v_add_f32_e32 v58, v22, v23
	s_nop 0
	v_add_f32_dpp v22, v60, v60 quad_perm:[1,0,3,2] row_mask:0xf bank_mask:0xf bound_ctrl:1
	v_cndmask_b32_e64 v60, 3, v48, s[8:9]
	v_mov_b32_e32 v48, 0xff800000
	v_cmp_eq_u32_e64 s[10:11], 0, v60
	v_cmp_nlg_f32_e64 s[12:13], v20, v48
	s_or_b64 s[10:11], s[10:11], s[12:13]
	v_cndmask_b32_e64 v20, v20, v48, s[10:11]
	v_cmp_ne_u32_e64 s[12:13], 1, v60
	v_cmp_gt_f32_e64 s[14:15], v21, v20
	s_and_b64 s[12:13], s[12:13], s[14:15]
	v_cndmask_b32_e64 v20, v20, v21, s[12:13]
	v_add_f32_dpp v22, v22, v22 quad_perm:[2,3,0,1] row_mask:0xf bank_mask:0xf bound_ctrl:1
	v_cmp_ne_u32_e64 s[14:15], 2, v60
	v_cmp_gt_f32_e64 s[16:17], v79, v20
	v_add_f32_dpp v22, v22, v22 row_ror:4 row_mask:0xf bank_mask:0xf bound_ctrl:1
	s_and_b64 s[14:15], s[14:15], s[16:17]
	v_cndmask_b32_e64 v20, v20, v79, s[14:15]
	v_add_f32_dpp v22, v22, v22 row_ror:8 row_mask:0xf bank_mask:0xf bound_ctrl:1
	v_mov_b32_e32 v23, v22
	v_cmp_gt_f32_e64 s[16:17], v80, v20
	s_nop 0
	v_permlane16_swap_b32_e32 v22, v23
	s_and_b64 s[16:17], s[8:9], s[16:17]
	v_add_f32_e32 v22, v22, v23
	v_cndmask_b32_e64 v20, v20, v80, s[16:17]
	v_mov_b32_e32 v68, v58
	v_mov_b32_e32 v23, v22
	v_add_f32_e32 v62, v62, v20
	v_permlane32_swap_b32_e32 v58, v68
	v_permlane32_swap_b32_e32 v22, v23
	v_permlane32_swap_b32_e32 v40, v42
	v_permlane32_swap_b32_e32 v44, v46
	v_mov_b32_e32 v16, 1
	v_cmp_lg_f32_e64 s[18:19], v62, v48
	v_mov_b32_e32 v21, 0
	v_mov_b32_e32 v20, 0
	s_and_saveexec_b64 s[38:39], s[18:19]
	s_cbranch_execz .LBB0_911
	v_cndmask_b32_e64 v20, v18, 0, s[10:11]
	v_cndmask_b32_e64 v16, 0, 1, s[12:13]
	v_cndmask_b32_e64 v20, v20, v19, s[12:13]
	v_cndmask_b32_e32 v18, v18, v19, vcc
	v_cndmask_b32_e64 v16, v16, 2, s[14:15]
	v_cndmask_b32_e64 v20, v20, v70, s[14:15]
	v_cndmask_b32_e64 v18, v18, v70, s[6:7]
	v_cndmask_b32_e64 v16, v16, 3, s[16:17]
	v_cndmask_b32_e64 v35, v20, v72, s[16:17]
	v_cndmask_b32_e64 v21, v72, v18, s[8:9]
	v_mov_b32_e32 v20, v60
	v_mov_b32_e32 v48, v62

; #define PG8_BAR __builtin_amdgcn_s_barrier()
;     ...
;         if constexpr (ALIGN_EPI) { if (wr == 0) PG8_BAR; }
;         if constexpr (F8) asm volatile("s_nop 15\n\ts_nop 15" ::: "memory");
;     __device__ __forceinline__ void operator()(AccRef acc, const pg8::Unit& u, int wr, int wc, int fr, int fq) const {
;     ...
;         for (int ai = 0; ai < 2; ++ai)
; #pragma unroll
;             for (int m = 0; m < 4; ++m) { const int row = row0 + ai * 128 + m * 16; const float s = sw[u.lb + u.pb - u.pm * 256 + row] * (Y2_SCALE / (H_SCALE * W2_SCALE)); unsigned char* rowp = O + (size_t)row * DM + col0;
; #pragma unroll
;                 for (int bj = 0; bj < 2; ++bj) { const f32x4 v0 = acc[ai][bj][m][0] * s, v1 = acc[ai][bj][m][1] * s;
;                     u32x2 w; w.x = cvt4_fp8(v0[0], v0[1], v0[2], v0[3]); w.y = cvt4_fp8(v1[0], v1[1], v1[2], v1[3]);
;                     *(u32x2*)(rowp + bj * 128) = w; } }
.LBB0_1099:
	s_and_b64 vcc, exec, s[16:17]
	s_cbranch_vccz .LBB0_1101
	s_barrier
.LBB0_1101:
	s_add_i32 s2, s94, s93
	v_add_u32_e32 v4, s2, v166
	v_ashrrev_i32_e32 v5, 31, v4
	s_nop 15
	s_nop 15
	v_lshl_add_u64 v[4:5], v[4:5], 2, s[12:13]
	flat_load_dword v3, v[4:5]
	s_lshl_b32 s0, s91, 8
	v_add_u32_e32 v2, s0, v166
	v_lshl_or_b32 v0, s92, 8, v168
	v_ashrrev_i32_e32 v1, 31, v0
	s_sub_i32 s0, s2, s0
	s_mov_b64 s[2:3], -1
	s_andn2_b64 vcc, exec, s[18:19]
	s_waitcnt vmcnt(0) lgkmcnt(0)
	v_mul_f32_e32 v4, 0x3d800000, v3
	v_ashrrev_i32_e32 v3, 31, v2
	v_pk_mul_f32 v[8:9], v[154:155], v[4:5] op_sel_hi:[1,0]
	v_pk_mul_f32 v[10:11], v[152:153], v[4:5] op_sel_hi:[1,0]
	v_lshlrev_b64 v[6:7], 11, v[2:3]
	v_pk_mul_f32 v[12:13], v[158:159], v[4:5] op_sel_hi:[1,0]
	v_pk_mul_f32 v[14:15], v[156:157], v[4:5] op_sel_hi:[1,0]
	v_med3_f32 v3, v10, s69, v208
	v_med3_f32 v5, v11, s69, v208
	v_med3_f32 v10, v8, s69, v208
	v_mov_b32_e32 v8, v193
	v_cvt_pk_fp8_f32 v8, v3, v5
	v_med3_f32 v9, v9, s69, v208
	v_med3_f32 v3, v14, s69, v208
	v_med3_f32 v5, v15, s69, v208
	v_cvt_pk_fp8_f32 v8, v10, v9 op_sel:[0,0,1]
	v_mov_b32_e32 v9, v193
	v_cvt_pk_fp8_f32 v9, v3, v5
	v_med3_f32 v10, v12, s69, v208
	v_med3_f32 v11, v13, s69, v208
	v_lshl_add_u64 v[6:7], s[10:11], 0, v[6:7]
	v_cvt_pk_fp8_f32 v9, v10, v11 op_sel:[0,0,1]
	v_lshl_add_u64 v[6:7], v[6:7], 0, v[0:1]
	v_pk_mul_f32 v[10:11], v[148:149], v[4:5] op_sel_hi:[1,0]
	v_pk_mul_f32 v[12:13], v[146:147], v[4:5] op_sel_hi:[1,0]
	flat_store_dwordx2 v[6:7], v[8:9]
	v_pk_mul_f32 v[8:9], v[150:151], v[4:5] op_sel_hi:[1,0]
	v_med3_f32 v3, v10, s69, v208
	v_med3_f32 v10, v11, s69, v208
	v_med3_f32 v11, v8, s69, v208
	v_mov_b32_e32 v8, v193
	v_cvt_pk_fp8_f32 v8, v3, v10
	v_pk_mul_f32 v[4:5], v[144:145], v[4:5] op_sel_hi:[1,0]
	v_med3_f32 v9, v9, s69, v208
	v_med3_f32 v3, v4, s69, v208
	v_cvt_pk_fp8_f32 v8, v11, v9 op_sel:[0,0,1]
	v_med3_f32 v4, v5, s69, v208
	v_mov_b32_e32 v9, v193
	v_cvt_pk_fp8_f32 v9, v3, v4
	v_med3_f32 v5, v12, s69, v208
	v_med3_f32 v10, v13, s69, v208
	v_or_b32_e32 v4, 16, v2
	v_cvt_pk_fp8_f32 v9, v5, v10 op_sel:[0,0,1]
	v_ashrrev_i32_e32 v5, 31, v4
	flat_store_dwordx2 v[6:7], v[8:9] offset:128
	v_add_u32_e32 v6, s0, v4
	v_ashrrev_i32_e32 v7, 31, v6
	v_lshl_add_u64 v[6:7], v[6:7], 2, s[12:13]
	flat_load_dword v3, v[6:7]
	v_lshlrev_b64 v[4:5], 11, v[4:5]
	v_lshl_add_u64 v[4:5], s[10:11], 0, v[4:5]
	v_lshl_add_u64 v[4:5], v[4:5], 0, v[0:1]
	s_waitcnt vmcnt(0) lgkmcnt(0)
	v_mul_f32_e32 v6, 0x3d800000, v3
	v_pk_mul_f32 v[8:9], v[142:143], v[6:7] op_sel_hi:[1,0]
	v_pk_mul_f32 v[10:11], v[140:141], v[6:7] op_sel_hi:[1,0]
	v_pk_mul_f32 v[12:13], v[138:139], v[6:7] op_sel_hi:[1,0]
	v_pk_mul_f32 v[14:15], v[136:137], v[6:7] op_sel_hi:[1,0]
	v_med3_f32 v3, v10, s69, v208
	v_med3_f32 v7, v11, s69, v208
	v_med3_f32 v10, v8, s69, v208
	v_mov_b32_e32 v8, v193
	v_cvt_pk_fp8_f32 v8, v3, v7
	v_med3_f32 v9, v9, s69, v208
	v_med3_f32 v3, v14, s69, v208
	v_med3_f32 v7, v15, s69, v208
	v_cvt_pk_fp8_f32 v8, v10, v9 op_sel:[0,0,1]
	v_mov_b32_e32 v9, v193
	v_cvt_pk_fp8_f32 v9, v3, v7
	v_med3_f32 v10, v12, s69, v208
	v_med3_f32 v11, v13, s69, v208
	v_pk_mul_f32 v[12:13], v[130:131], v[6:7] op_sel_hi:[1,0]
	v_cvt_pk_fp8_f32 v9, v10, v11 op_sel:[0,0,1]
	v_pk_mul_f32 v[10:11], v[132:133], v[6:7] op_sel_hi:[1,0]
	flat_store_dwordx2 v[4:5], v[8:9]
	v_pk_mul_f32 v[8:9], v[134:135], v[6:7] op_sel_hi:[1,0]
	v_med3_f32 v3, v10, s69, v208
	v_med3_f32 v10, v11, s69, v208
	v_med3_f32 v11, v8, s69, v208
	v_mov_b32_e32 v8, v193
	v_cvt_pk_fp8_f32 v8, v3, v10
	v_pk_mul_f32 v[6:7], v[128:129], v[6:7] op_sel_hi:[1,0]
	v_med3_f32 v9, v9, s69, v208
	v_med3_f32 v3, v6, s69, v208
	v_cvt_pk_fp8_f32 v8, v11, v9 op_sel:[0,0,1]
	v_med3_f32 v6, v7, s69, v208
	v_mov_b32_e32 v9, v193
	v_cvt_pk_fp8_f32 v9, v3, v6
	v_med3_f32 v7, v12, s69, v208
	v_med3_f32 v10, v13, s69, v208
	v_cvt_pk_fp8_f32 v9, v7, v10 op_sel:[0,0,1]
	flat_store_dwordx2 v[4:5], v[8:9] offset:128
	v_or_b32_e32 v4, 32, v2
	v_add_u32_e32 v6, s0, v4
	v_ashrrev_i32_e32 v7, 31, v6
	v_lshl_add_u64 v[6:7], v[6:7], 2, s[12:13]
	flat_load_dword v3, v[6:7]
	v_ashrrev_i32_e32 v5, 31, v4
	v_lshlrev_b64 v[4:5], 11, v[4:5]
	v_lshl_add_u64 v[4:5], s[10:11], 0, v[4:5]
	v_lshl_add_u64 v[4:5], v[4:5], 0, v[0:1]
	s_waitcnt vmcnt(0) lgkmcnt(0)
	v_mul_f32_e32 v6, 0x3d800000, v3
	v_pk_mul_f32 v[8:9], v[126:127], v[6:7] op_sel_hi:[1,0]
	v_pk_mul_f32 v[10:11], v[124:125], v[6:7] op_sel_hi:[1,0]
	v_pk_mul_f32 v[12:13], v[122:123], v[6:7] op_sel_hi:[1,0]
	v_pk_mul_f32 v[14:15], v[120:121], v[6:7] op_sel_hi:[1,0]
	v_med3_f32 v3, v10, s69, v208
	v_med3_f32 v7, v11, s69, v208
	v_med3_f32 v10, v8, s69, v208
	v_mov_b32_e32 v8, v193
	v_cvt_pk_fp8_f32 v8, v3, v7
	v_med3_f32 v9, v9, s69, v208
	v_med3_f32 v3, v14, s69, v208
	v_med3_f32 v7, v15, s69, v208
	v_cvt_pk_fp8_f32 v8, v10, v9 op_sel:[0,0,1]
	v_mov_b32_e32 v9, v193
	v_cvt_pk_fp8_f32 v9, v3, v7
	v_med3_f32 v10, v12, s69, v208
	v_med3_f32 v11, v13, s69, v208
	v_pk_mul_f32 v[12:13], v[114:115], v[6:7] op_sel_hi:[1,0]
	v_cvt_pk_fp8_f32 v9, v10, v11 op_sel:[0,0,1]
	v_pk_mul_f32 v[10:11], v[116:117], v[6:7] op_sel_hi:[1,0]
	flat_store_dwordx2 v[4:5], v[8:9]
	v_pk_mul_f32 v[8:9], v[118:119], v[6:7] op_sel_hi:[1,0]
	v_med3_f32 v3, v10, s69, v208
	v_med3_f32 v10, v11, s69, v208
	v_med3_f32 v11, v8, s69, v208
	v_mov_b32_e32 v8, v193
	v_cvt_pk_fp8_f32 v8, v3, v10
	v_pk_mul_f32 v[6:7], v[112:113], v[6:7] op_sel_hi:[1,0]
	v_med3_f32 v9, v9, s69, v208
	v_med3_f32 v3, v6, s69, v208
	v_cvt_pk_fp8_f32 v8, v11, v9 op_sel:[0,0,1]
	v_med3_f32 v6, v7, s69, v208
	v_mov_b32_e32 v9, v193
	v_cvt_pk_fp8_f32 v9, v3, v6
	v_med3_f32 v7, v12, s69, v208
	v_med3_f32 v10, v13, s69, v208
	v_cvt_pk_fp8_f32 v9, v7, v10 op_sel:[0,0,1]
	flat_store_dwordx2 v[4:5], v[8:9] offset:128
	v_or_b32_e32 v4, 48, v2
	v_add_u32_e32 v6, s0, v4
	v_ashrrev_i32_e32 v7, 31, v6
	v_lshl_add_u64 v[6:7], v[6:7], 2, s[12:13]
	flat_load_dword v3, v[6:7]
	v_ashrrev_i32_e32 v5, 31, v4
	v_lshlrev_b64 v[4:5], 11, v[4:5]
	v_lshl_add_u64 v[4:5], s[10:11], 0, v[4:5]
	v_lshl_add_u64 v[4:5], v[4:5], 0, v[0:1]
	s_waitcnt vmcnt(0) lgkmcnt(0)
;     __device__ __forceinline__ void operator()(AccRef acc, const pg8::Unit& u, int wr, int wc, int fr, int fq) const {
;     ...
;         for (int ai = 0; ai < 2; ++ai)
; #pragma unroll
;             for (int m = 0; m < 4; ++m) { const int row = row0 + ai * 128 + m * 16; const float s = sw[u.lb + u.pb - u.pm * 256 + row] * (Y2_SCALE / (H_SCALE * W2_SCALE)); unsigned char* rowp = O + (size_t)row * DM + col0;
; #pragma unroll
;                 for (int bj = 0; bj < 2; ++bj) { const f32x4 v0 = acc[ai][bj][m][0] * s, v1 = acc[ai][bj][m][1] * s;
;                     u32x2 w; w.x = cvt4_fp8(v0[0], v0[1], v0[2], v0[3]); w.y = cvt4_fp8(v1[0], v1[1], v1[2], v1[3]);
;                     *(u32x2*)(rowp + bj * 128) = w; } }
	v_mul_f32_e32 v6, 0x3d800000, v3
	v_pk_mul_f32 v[8:9], v[110:111], v[6:7] op_sel_hi:[1,0]
	v_pk_mul_f32 v[10:11], v[108:109], v[6:7] op_sel_hi:[1,0]
	v_pk_mul_f32 v[12:13], v[106:107], v[6:7] op_sel_hi:[1,0]
	v_pk_mul_f32 v[14:15], v[104:105], v[6:7] op_sel_hi:[1,0]
	v_med3_f32 v3, v10, s69, v208
	v_med3_f32 v7, v11, s69, v208
	v_med3_f32 v10, v8, s69, v208
	v_mov_b32_e32 v8, v193
	v_cvt_pk_fp8_f32 v8, v3, v7
	v_med3_f32 v9, v9, s69, v208
	v_med3_f32 v3, v14, s69, v208
	v_med3_f32 v7, v15, s69, v208
	v_cvt_pk_fp8_f32 v8, v10, v9 op_sel:[0,0,1]
	v_mov_b32_e32 v9, v193
	v_cvt_pk_fp8_f32 v9, v3, v7
	v_med3_f32 v10, v12, s69, v208
	v_med3_f32 v11, v13, s69, v208
	v_pk_mul_f32 v[12:13], v[98:99], v[6:7] op_sel_hi:[1,0]
	v_cvt_pk_fp8_f32 v9, v10, v11 op_sel:[0,0,1]
	v_pk_mul_f32 v[10:11], v[100:101], v[6:7] op_sel_hi:[1,0]
	flat_store_dwordx2 v[4:5], v[8:9]
	v_pk_mul_f32 v[8:9], v[102:103], v[6:7] op_sel_hi:[1,0]
	v_med3_f32 v3, v10, s69, v208
	v_med3_f32 v10, v11, s69, v208
	v_med3_f32 v11, v8, s69, v208
	v_mov_b32_e32 v8, v193
	v_cvt_pk_fp8_f32 v8, v3, v10
	v_pk_mul_f32 v[6:7], v[96:97], v[6:7] op_sel_hi:[1,0]
	v_med3_f32 v9, v9, s69, v208
	v_med3_f32 v3, v6, s69, v208
	v_cvt_pk_fp8_f32 v8, v11, v9 op_sel:[0,0,1]
	v_med3_f32 v6, v7, s69, v208
	v_mov_b32_e32 v9, v193
	v_cvt_pk_fp8_f32 v9, v3, v6
	v_med3_f32 v7, v12, s69, v208
	v_med3_f32 v10, v13, s69, v208
	v_cvt_pk_fp8_f32 v9, v7, v10 op_sel:[0,0,1]
	flat_store_dwordx2 v[4:5], v[8:9] offset:128
	v_add_u32_e32 v4, 0x80, v2
	v_add_u32_e32 v6, s0, v4
	v_ashrrev_i32_e32 v7, 31, v6
	v_lshl_add_u64 v[6:7], v[6:7], 2, s[12:13]
	flat_load_dword v3, v[6:7]
	v_ashrrev_i32_e32 v5, 31, v4
	v_lshlrev_b64 v[4:5], 11, v[4:5]
	v_lshl_add_u64 v[4:5], s[10:11], 0, v[4:5]
	v_lshl_add_u64 v[4:5], v[4:5], 0, v[0:1]
	s_waitcnt vmcnt(0) lgkmcnt(0)
	v_mul_f32_e32 v6, 0x3d800000, v3
	v_pk_mul_f32 v[8:9], v[94:95], v[6:7] op_sel_hi:[1,0]
	v_pk_mul_f32 v[10:11], v[92:93], v[6:7] op_sel_hi:[1,0]
	v_pk_mul_f32 v[12:13], v[90:91], v[6:7] op_sel_hi:[1,0]
	v_pk_mul_f32 v[14:15], v[88:89], v[6:7] op_sel_hi:[1,0]
	v_med3_f32 v3, v10, s69, v208
	v_med3_f32 v7, v11, s69, v208
	v_med3_f32 v10, v8, s69, v208
	v_mov_b32_e32 v8, v193
	v_cvt_pk_fp8_f32 v8, v3, v7
	v_med3_f32 v9, v9, s69, v208
	v_med3_f32 v3, v14, s69, v208
	v_med3_f32 v7, v15, s69, v208
	v_cvt_pk_fp8_f32 v8, v10, v9 op_sel:[0,0,1]
	v_mov_b32_e32 v9, v193
	v_cvt_pk_fp8_f32 v9, v3, v7
	v_med3_f32 v10, v12, s69, v208
	v_med3_f32 v11, v13, s69, v208
	v_pk_mul_f32 v[12:13], v[82:83], v[6:7] op_sel_hi:[1,0]
	v_cvt_pk_fp8_f32 v9, v10, v11 op_sel:[0,0,1]
	v_pk_mul_f32 v[10:11], v[84:85], v[6:7] op_sel_hi:[1,0]
	flat_store_dwordx2 v[4:5], v[8:9]
	v_pk_mul_f32 v[8:9], v[86:87], v[6:7] op_sel_hi:[1,0]
	v_med3_f32 v3, v10, s69, v208
	v_med3_f32 v10, v11, s69, v208
	v_med3_f32 v11, v8, s69, v208
	v_mov_b32_e32 v8, v193
	v_cvt_pk_fp8_f32 v8, v3, v10
	v_pk_mul_f32 v[6:7], v[80:81], v[6:7] op_sel_hi:[1,0]
	v_med3_f32 v9, v9, s69, v208
	v_med3_f32 v3, v6, s69, v208
	v_cvt_pk_fp8_f32 v8, v11, v9 op_sel:[0,0,1]
	v_med3_f32 v6, v7, s69, v208
	v_mov_b32_e32 v9, v193
	v_cvt_pk_fp8_f32 v9, v3, v6
	v_med3_f32 v7, v12, s69, v208
	v_med3_f32 v10, v13, s69, v208
	v_cvt_pk_fp8_f32 v9, v7, v10 op_sel:[0,0,1]
	flat_store_dwordx2 v[4:5], v[8:9] offset:128
	v_add_u32_e32 v4, 0x90, v2
	v_add_u32_e32 v6, s0, v4
	v_ashrrev_i32_e32 v7, 31, v6
	v_lshl_add_u64 v[6:7], v[6:7], 2, s[12:13]
	flat_load_dword v3, v[6:7]
	v_ashrrev_i32_e32 v5, 31, v4
	v_lshlrev_b64 v[4:5], 11, v[4:5]
	v_lshl_add_u64 v[4:5], s[10:11], 0, v[4:5]
	v_lshl_add_u64 v[4:5], v[4:5], 0, v[0:1]
	s_waitcnt vmcnt(0) lgkmcnt(0)
; #define PG8_BAR __builtin_amdgcn_s_barrier()
;     ...
;         if (!has_next) break;
; #pragma unroll
;         for (int a = 0; a < 2; ++a)
; #pragma unroll
;             for (int b = 0; b < 2; ++b)
; #pragma unroll
;                 for (int m = 0; m < 4; ++m)
; #pragma unroll
;                     for (int n = 0; n < 2; ++n) acc[a][b][m][n] = (f32x4){0.f, 0.f, 0.f, 0.f};
;         cur = nxt; cA = nA; cB = nB; ++ui;
; #pragma unroll
;         for (int _i = 0; _i < 2; ++_i) { vA0[_i] = nA0[_i]; vA1[_i] = nA1[_i]; }
;         if constexpr (ALIGN_EPI) { if (wr == 1) PG8_BAR; }
;     __device__ __forceinline__ void operator()(AccRef acc, const pg8::Unit& u, int wr, int wc, int fr, int fq) const {
;     ...
;         for (int ai = 0; ai < 2; ++ai)
; #pragma unroll
;             for (int m = 0; m < 4; ++m) { const int row = row0 + ai * 128 + m * 16; const float s = sw[u.lb + u.pb - u.pm * 256 + row] * (Y2_SCALE / (H_SCALE * W2_SCALE)); unsigned char* rowp = O + (size_t)row * DM + col0;
; #pragma unroll
;                 for (int bj = 0; bj < 2; ++bj) { const f32x4 v0 = acc[ai][bj][m][0] * s, v1 = acc[ai][bj][m][1] * s;
;                     u32x2 w; w.x = cvt4_fp8(v0[0], v0[1], v0[2], v0[3]); w.y = cvt4_fp8(v1[0], v1[1], v1[2], v1[3]);
;                     *(u32x2*)(rowp + bj * 128) = w; } }
	v_mul_f32_e32 v6, 0x3d800000, v3
	v_pk_mul_f32 v[8:9], v[78:79], v[6:7] op_sel_hi:[1,0]
	v_pk_mul_f32 v[10:11], v[76:77], v[6:7] op_sel_hi:[1,0]
	v_pk_mul_f32 v[12:13], v[74:75], v[6:7] op_sel_hi:[1,0]
	v_pk_mul_f32 v[14:15], v[72:73], v[6:7] op_sel_hi:[1,0]
	v_med3_f32 v3, v10, s69, v208
	v_med3_f32 v7, v11, s69, v208
	v_med3_f32 v10, v8, s69, v208
	v_mov_b32_e32 v8, v193
	v_cvt_pk_fp8_f32 v8, v3, v7
	v_med3_f32 v9, v9, s69, v208
	v_med3_f32 v3, v14, s69, v208
	v_med3_f32 v7, v15, s69, v208
	v_cvt_pk_fp8_f32 v8, v10, v9 op_sel:[0,0,1]
	v_mov_b32_e32 v9, v193
	v_cvt_pk_fp8_f32 v9, v3, v7
	v_med3_f32 v10, v12, s69, v208
	v_med3_f32 v11, v13, s69, v208
	v_pk_mul_f32 v[12:13], v[66:67], v[6:7] op_sel_hi:[1,0]
	v_cvt_pk_fp8_f32 v9, v10, v11 op_sel:[0,0,1]
	v_pk_mul_f32 v[10:11], v[68:69], v[6:7] op_sel_hi:[1,0]
	flat_store_dwordx2 v[4:5], v[8:9]
	v_pk_mul_f32 v[8:9], v[70:71], v[6:7] op_sel_hi:[1,0]
	v_med3_f32 v3, v10, s69, v208
	v_med3_f32 v10, v11, s69, v208
	v_med3_f32 v11, v8, s69, v208
	v_mov_b32_e32 v8, v193
	v_cvt_pk_fp8_f32 v8, v3, v10
	v_pk_mul_f32 v[6:7], v[64:65], v[6:7] op_sel_hi:[1,0]
	v_med3_f32 v9, v9, s69, v208
	v_med3_f32 v3, v6, s69, v208
	v_cvt_pk_fp8_f32 v8, v11, v9 op_sel:[0,0,1]
	v_med3_f32 v6, v7, s69, v208
	v_mov_b32_e32 v9, v193
	v_cvt_pk_fp8_f32 v9, v3, v6
	v_med3_f32 v7, v12, s69, v208
	v_med3_f32 v10, v13, s69, v208
	v_cvt_pk_fp8_f32 v9, v7, v10 op_sel:[0,0,1]
	flat_store_dwordx2 v[4:5], v[8:9] offset:128
	v_add_u32_e32 v4, 0xa0, v2
	v_add_u32_e32 v6, s0, v4
	v_ashrrev_i32_e32 v7, 31, v6
	v_lshl_add_u64 v[6:7], v[6:7], 2, s[12:13]
	flat_load_dword v3, v[6:7]
	v_ashrrev_i32_e32 v5, 31, v4
	v_lshlrev_b64 v[4:5], 11, v[4:5]
	v_lshl_add_u64 v[4:5], s[10:11], 0, v[4:5]
	v_lshl_add_u64 v[4:5], v[4:5], 0, v[0:1]
	v_add_u32_e32 v2, 0xb0, v2
	s_waitcnt vmcnt(0) lgkmcnt(0)
	v_mul_f32_e32 v6, 0x3d800000, v3
	v_pk_mul_f32 v[8:9], v[62:63], v[6:7] op_sel_hi:[1,0]
	v_pk_mul_f32 v[10:11], v[60:61], v[6:7] op_sel_hi:[1,0]
	v_pk_mul_f32 v[12:13], v[58:59], v[6:7] op_sel_hi:[1,0]
	v_pk_mul_f32 v[14:15], v[56:57], v[6:7] op_sel_hi:[1,0]
	v_med3_f32 v3, v10, s69, v208
	v_med3_f32 v7, v11, s69, v208
	v_med3_f32 v10, v8, s69, v208
	v_mov_b32_e32 v8, v193
	v_cvt_pk_fp8_f32 v8, v3, v7
	v_med3_f32 v9, v9, s69, v208
	v_med3_f32 v3, v14, s69, v208
	v_med3_f32 v7, v15, s69, v208
	v_cvt_pk_fp8_f32 v8, v10, v9 op_sel:[0,0,1]
	v_mov_b32_e32 v9, v193
	v_cvt_pk_fp8_f32 v9, v3, v7
	v_med3_f32 v10, v12, s69, v208
	v_med3_f32 v11, v13, s69, v208
	v_pk_mul_f32 v[12:13], v[50:51], v[6:7] op_sel_hi:[1,0]
	v_cvt_pk_fp8_f32 v9, v10, v11 op_sel:[0,0,1]
	v_pk_mul_f32 v[10:11], v[52:53], v[6:7] op_sel_hi:[1,0]
	flat_store_dwordx2 v[4:5], v[8:9]
	v_pk_mul_f32 v[8:9], v[54:55], v[6:7] op_sel_hi:[1,0]
	v_med3_f32 v3, v10, s69, v208
	v_med3_f32 v10, v11, s69, v208
	v_med3_f32 v11, v8, s69, v208
	v_mov_b32_e32 v8, v193
	v_cvt_pk_fp8_f32 v8, v3, v10
	v_pk_mul_f32 v[6:7], v[48:49], v[6:7] op_sel_hi:[1,0]
	v_med3_f32 v9, v9, s69, v208
	v_med3_f32 v3, v6, s69, v208
	v_cvt_pk_fp8_f32 v8, v11, v9 op_sel:[0,0,1]
	v_med3_f32 v6, v7, s69, v208
	v_mov_b32_e32 v9, v193
	v_cvt_pk_fp8_f32 v9, v3, v6
	v_med3_f32 v7, v12, s69, v208
	v_med3_f32 v10, v13, s69, v208
	v_cvt_pk_fp8_f32 v9, v7, v10 op_sel:[0,0,1]
	flat_store_dwordx2 v[4:5], v[8:9] offset:128
	v_add_u32_e32 v4, s0, v2
	v_ashrrev_i32_e32 v5, 31, v4
	v_lshl_add_u64 v[4:5], v[4:5], 2, s[12:13]
	flat_load_dword v3, v[4:5]
	s_waitcnt vmcnt(0) lgkmcnt(0)
	v_mul_f32_e32 v4, 0x3d800000, v3
	v_ashrrev_i32_e32 v3, 31, v2
	v_lshlrev_b64 v[2:3], 11, v[2:3]
	v_lshl_add_u64 v[2:3], s[10:11], 0, v[2:3]
	v_lshl_add_u64 v[0:1], v[2:3], 0, v[0:1]
	v_pk_mul_f32 v[2:3], v[46:47], v[4:5] op_sel_hi:[1,0]
	v_pk_mul_f32 v[6:7], v[44:45], v[4:5] op_sel_hi:[1,0]
	v_pk_mul_f32 v[8:9], v[42:43], v[4:5] op_sel_hi:[1,0]
	v_pk_mul_f32 v[10:11], v[40:41], v[4:5] op_sel_hi:[1,0]
	v_med3_f32 v5, v6, s69, v208
	v_med3_f32 v6, v7, s69, v208
	v_med3_f32 v7, v2, s69, v208
	v_mov_b32_e32 v2, v193
	v_cvt_pk_fp8_f32 v2, v5, v6
	v_med3_f32 v3, v3, s69, v208
	v_med3_f32 v5, v10, s69, v208
	v_med3_f32 v6, v11, s69, v208
	v_cvt_pk_fp8_f32 v2, v7, v3 op_sel:[0,0,1]
	v_mov_b32_e32 v3, v193
	v_cvt_pk_fp8_f32 v3, v5, v6
	v_med3_f32 v7, v8, s69, v208
	v_med3_f32 v8, v9, s69, v208
	v_cvt_pk_fp8_f32 v3, v7, v8 op_sel:[0,0,1]
	v_pk_mul_f32 v[6:7], v[36:37], v[4:5] op_sel_hi:[1,0]
	v_pk_mul_f32 v[8:9], v[34:35], v[4:5] op_sel_hi:[1,0]
	v_med3_f32 v6, v6, s69, v208
	flat_store_dwordx2 v[0:1], v[2:3]
	v_pk_mul_f32 v[2:3], v[38:39], v[4:5] op_sel_hi:[1,0]
	v_med3_f32 v7, v7, s69, v208
	v_med3_f32 v10, v2, s69, v208
	v_mov_b32_e32 v2, v193
	v_cvt_pk_fp8_f32 v2, v6, v7
	v_pk_mul_f32 v[4:5], v[32:33], v[4:5] op_sel_hi:[1,0]
	v_med3_f32 v3, v3, s69, v208
	v_med3_f32 v4, v4, s69, v208
	v_cvt_pk_fp8_f32 v2, v10, v3 op_sel:[0,0,1]
	v_med3_f32 v5, v5, s69, v208
	v_mov_b32_e32 v3, v193
	v_cvt_pk_fp8_f32 v3, v4, v5
	v_med3_f32 v6, v8, s69, v208
	v_med3_f32 v7, v9, s69, v208
	v_cvt_pk_fp8_f32 v3, v6, v7 op_sel:[0,0,1]
	flat_store_dwordx2 v[0:1], v[2:3] offset:128
	s_cbranch_vccnz .LBB0_1089
	s_andn2_b64 vcc, exec, s[8:9]
	s_cbranch_vccnz .LBB0_1088
	s_barrier
	s_branch .LBB0_1088

; #define PG8_BAR __builtin_amdgcn_s_barrier()
;     ...
;         if constexpr (ALIGN_EPI) { if (wr == 0) PG8_BAR; }
;         if constexpr (F8) asm volatile("s_nop 15\n\ts_nop 15" ::: "memory");
;     __device__ __forceinline__ void operator()(AccRef acc, const pg8::Unit& u, int wr, int wc, int fr, int fq) const {
;     ...
;         for (int ai = 0; ai < 2; ++ai)
; #pragma unroll
;             for (int m = 0; m < 4; ++m) { const int row = row0 + ai * 128 + m * 16; const float s = sw[u.lb + u.pb - u.pm * 256 + row] * (Y2_SCALE / (H_SCALE * W2_SCALE)); unsigned char* rowp = O + (size_t)row * DM + col0;
; #pragma unroll
;                 for (int bj = 0; bj < 2; ++bj) { const f32x4 v0 = acc[ai][bj][m][0] * s, v1 = acc[ai][bj][m][1] * s;
;                     u32x2 w; w.x = cvt4_fp8(v0[0], v0[1], v0[2], v0[3]); w.y = cvt4_fp8(v1[0], v1[1], v1[2], v1[3]);
;                     *(u32x2*)(rowp + bj * 128) = w; } }
.LBB0_1210:
	s_add_i32 s19, s93, s92
	v_add_u32_e32 v4, s19, v168
	v_ashrrev_i32_e32 v5, 31, v4
	s_nop 15
	s_nop 15
	v_lshl_add_u64 v[4:5], v[4:5], 2, s[12:13]
	flat_load_dword v3, v[4:5]
	s_lshl_b32 s18, s82, 8
	v_add_u32_e32 v2, s18, v168
	v_lshl_or_b32 v0, s91, 8, v170
	v_ashrrev_i32_e32 v1, 31, v0
	s_sub_i32 s18, s19, s18
	s_and_b64 vcc, exec, s[0:1]
	s_waitcnt vmcnt(0) lgkmcnt(0)
	v_mul_f32_e32 v4, 0x3d800000, v3
	v_ashrrev_i32_e32 v3, 31, v2
	v_pk_mul_f32 v[8:9], v[154:155], v[4:5] op_sel_hi:[1,0]
	v_pk_mul_f32 v[10:11], v[152:153], v[4:5] op_sel_hi:[1,0]
	v_lshlrev_b64 v[6:7], 11, v[2:3]
	v_pk_mul_f32 v[12:13], v[158:159], v[4:5] op_sel_hi:[1,0]
	v_pk_mul_f32 v[14:15], v[156:157], v[4:5] op_sel_hi:[1,0]
	v_med3_f32 v3, v10, s69, v208
	v_med3_f32 v5, v11, s69, v208
	v_med3_f32 v10, v8, s69, v208
	v_mov_b32_e32 v8, v193
	v_cvt_pk_fp8_f32 v8, v3, v5
	v_med3_f32 v9, v9, s69, v208
	v_med3_f32 v3, v14, s69, v208
	v_med3_f32 v5, v15, s69, v208
	v_cvt_pk_fp8_f32 v8, v10, v9 op_sel:[0,0,1]
	v_mov_b32_e32 v9, v193
	v_cvt_pk_fp8_f32 v9, v3, v5
	v_med3_f32 v10, v12, s69, v208
	v_med3_f32 v11, v13, s69, v208
	v_lshl_add_u64 v[6:7], s[10:11], 0, v[6:7]
	v_cvt_pk_fp8_f32 v9, v10, v11 op_sel:[0,0,1]
	v_lshl_add_u64 v[6:7], v[6:7], 0, v[0:1]
	v_pk_mul_f32 v[10:11], v[148:149], v[4:5] op_sel_hi:[1,0]
	v_pk_mul_f32 v[12:13], v[146:147], v[4:5] op_sel_hi:[1,0]
	flat_store_dwordx2 v[6:7], v[8:9]
	v_pk_mul_f32 v[8:9], v[150:151], v[4:5] op_sel_hi:[1,0]
	v_med3_f32 v3, v10, s69, v208
	v_med3_f32 v10, v11, s69, v208
	v_med3_f32 v11, v8, s69, v208
	v_mov_b32_e32 v8, v193
	v_cvt_pk_fp8_f32 v8, v3, v10
	v_pk_mul_f32 v[4:5], v[144:145], v[4:5] op_sel_hi:[1,0]
	v_med3_f32 v9, v9, s69, v208
	v_med3_f32 v3, v4, s69, v208
	v_cvt_pk_fp8_f32 v8, v11, v9 op_sel:[0,0,1]
	v_med3_f32 v4, v5, s69, v208
	v_mov_b32_e32 v9, v193
	v_cvt_pk_fp8_f32 v9, v3, v4
	v_med3_f32 v5, v12, s69, v208
	v_med3_f32 v10, v13, s69, v208
	v_or_b32_e32 v4, 16, v2
	v_cvt_pk_fp8_f32 v9, v5, v10 op_sel:[0,0,1]
	v_ashrrev_i32_e32 v5, 31, v4
	flat_store_dwordx2 v[6:7], v[8:9] offset:128
	v_add_u32_e32 v6, s18, v4
	v_ashrrev_i32_e32 v7, 31, v6
	v_lshl_add_u64 v[6:7], v[6:7], 2, s[12:13]
	flat_load_dword v3, v[6:7]
	v_lshlrev_b64 v[4:5], 11, v[4:5]
	v_lshl_add_u64 v[4:5], s[10:11], 0, v[4:5]
	v_lshl_add_u64 v[4:5], v[4:5], 0, v[0:1]
	s_waitcnt vmcnt(0) lgkmcnt(0)
	v_mul_f32_e32 v6, 0x3d800000, v3
	v_pk_mul_f32 v[8:9], v[142:143], v[6:7] op_sel_hi:[1,0]
	v_pk_mul_f32 v[10:11], v[140:141], v[6:7] op_sel_hi:[1,0]
	v_pk_mul_f32 v[12:13], v[138:139], v[6:7] op_sel_hi:[1,0]
	v_pk_mul_f32 v[14:15], v[136:137], v[6:7] op_sel_hi:[1,0]
	v_med3_f32 v3, v10, s69, v208
	v_med3_f32 v7, v11, s69, v208
	v_med3_f32 v10, v8, s69, v208
	v_mov_b32_e32 v8, v193
	v_cvt_pk_fp8_f32 v8, v3, v7
	v_med3_f32 v9, v9, s69, v208
	v_med3_f32 v3, v14, s69, v208
	v_med3_f32 v7, v15, s69, v208
	v_cvt_pk_fp8_f32 v8, v10, v9 op_sel:[0,0,1]
	v_mov_b32_e32 v9, v193
	v_cvt_pk_fp8_f32 v9, v3, v7
	v_med3_f32 v10, v12, s69, v208
	v_med3_f32 v11, v13, s69, v208
	v_pk_mul_f32 v[12:13], v[130:131], v[6:7] op_sel_hi:[1,0]
	v_cvt_pk_fp8_f32 v9, v10, v11 op_sel:[0,0,1]
	v_pk_mul_f32 v[10:11], v[132:133], v[6:7] op_sel_hi:[1,0]
	flat_store_dwordx2 v[4:5], v[8:9]
	v_pk_mul_f32 v[8:9], v[134:135], v[6:7] op_sel_hi:[1,0]
	v_med3_f32 v3, v10, s69, v208
	v_med3_f32 v10, v11, s69, v208
	v_med3_f32 v11, v8, s69, v208
	v_mov_b32_e32 v8, v193
	v_cvt_pk_fp8_f32 v8, v3, v10
	v_pk_mul_f32 v[6:7], v[128:129], v[6:7] op_sel_hi:[1,0]
	v_med3_f32 v9, v9, s69, v208
	v_med3_f32 v3, v6, s69, v208
	v_cvt_pk_fp8_f32 v8, v11, v9 op_sel:[0,0,1]
	v_med3_f32 v6, v7, s69, v208
	v_mov_b32_e32 v9, v193
	v_cvt_pk_fp8_f32 v9, v3, v6
	v_med3_f32 v7, v12, s69, v208
	v_med3_f32 v10, v13, s69, v208
	v_cvt_pk_fp8_f32 v9, v7, v10 op_sel:[0,0,1]
	flat_store_dwordx2 v[4:5], v[8:9] offset:128
	v_or_b32_e32 v4, 32, v2
	v_add_u32_e32 v6, s18, v4
	v_ashrrev_i32_e32 v7, 31, v6
	v_lshl_add_u64 v[6:7], v[6:7], 2, s[12:13]
	flat_load_dword v3, v[6:7]
	v_ashrrev_i32_e32 v5, 31, v4
	v_lshlrev_b64 v[4:5], 11, v[4:5]
	v_lshl_add_u64 v[4:5], s[10:11], 0, v[4:5]
	v_lshl_add_u64 v[4:5], v[4:5], 0, v[0:1]
	s_waitcnt vmcnt(0) lgkmcnt(0)
	v_mul_f32_e32 v6, 0x3d800000, v3
	v_pk_mul_f32 v[8:9], v[126:127], v[6:7] op_sel_hi:[1,0]
	v_pk_mul_f32 v[10:11], v[124:125], v[6:7] op_sel_hi:[1,0]
	v_pk_mul_f32 v[12:13], v[122:123], v[6:7] op_sel_hi:[1,0]
	v_pk_mul_f32 v[14:15], v[120:121], v[6:7] op_sel_hi:[1,0]
	v_med3_f32 v3, v10, s69, v208
	v_med3_f32 v7, v11, s69, v208
	v_med3_f32 v10, v8, s69, v208
	v_mov_b32_e32 v8, v193
	v_cvt_pk_fp8_f32 v8, v3, v7
	v_med3_f32 v9, v9, s69, v208
	v_med3_f32 v3, v14, s69, v208
	v_med3_f32 v7, v15, s69, v208
	v_cvt_pk_fp8_f32 v8, v10, v9 op_sel:[0,0,1]
	v_mov_b32_e32 v9, v193
	v_cvt_pk_fp8_f32 v9, v3, v7
	v_med3_f32 v10, v12, s69, v208
	v_med3_f32 v11, v13, s69, v208
	v_pk_mul_f32 v[12:13], v[114:115], v[6:7] op_sel_hi:[1,0]
	v_cvt_pk_fp8_f32 v9, v10, v11 op_sel:[0,0,1]
	v_pk_mul_f32 v[10:11], v[116:117], v[6:7] op_sel_hi:[1,0]
	flat_store_dwordx2 v[4:5], v[8:9]
	v_pk_mul_f32 v[8:9], v[118:119], v[6:7] op_sel_hi:[1,0]
	v_med3_f32 v3, v10, s69, v208
	v_med3_f32 v10, v11, s69, v208
	v_med3_f32 v11, v8, s69, v208
	v_mov_b32_e32 v8, v193
	v_cvt_pk_fp8_f32 v8, v3, v10
	v_pk_mul_f32 v[6:7], v[112:113], v[6:7] op_sel_hi:[1,0]
	v_med3_f32 v9, v9, s69, v208
	v_med3_f32 v3, v6, s69, v208
	v_cvt_pk_fp8_f32 v8, v11, v9 op_sel:[0,0,1]
	v_med3_f32 v6, v7, s69, v208
	v_mov_b32_e32 v9, v193
	v_cvt_pk_fp8_f32 v9, v3, v6
	v_med3_f32 v7, v12, s69, v208
	v_med3_f32 v10, v13, s69, v208
	v_cvt_pk_fp8_f32 v9, v7, v10 op_sel:[0,0,1]
	flat_store_dwordx2 v[4:5], v[8:9] offset:128
	v_or_b32_e32 v4, 48, v2
	v_add_u32_e32 v6, s18, v4
	v_ashrrev_i32_e32 v7, 31, v6
	v_lshl_add_u64 v[6:7], v[6:7], 2, s[12:13]
	flat_load_dword v3, v[6:7]
	v_ashrrev_i32_e32 v5, 31, v4
	v_lshlrev_b64 v[4:5], 11, v[4:5]
	v_lshl_add_u64 v[4:5], s[10:11], 0, v[4:5]
	v_lshl_add_u64 v[4:5], v[4:5], 0, v[0:1]
	s_waitcnt vmcnt(0) lgkmcnt(0)
;     __device__ __forceinline__ void operator()(AccRef acc, const pg8::Unit& u, int wr, int wc, int fr, int fq) const {
;     ...
;         for (int ai = 0; ai < 2; ++ai)
; #pragma unroll
;             for (int m = 0; m < 4; ++m) { const int row = row0 + ai * 128 + m * 16; const float s = sw[u.lb + u.pb - u.pm * 256 + row] * (Y2_SCALE / (H_SCALE * W2_SCALE)); unsigned char* rowp = O + (size_t)row * DM + col0;
; #pragma unroll
;                 for (int bj = 0; bj < 2; ++bj) { const f32x4 v0 = acc[ai][bj][m][0] * s, v1 = acc[ai][bj][m][1] * s;
;                     u32x2 w; w.x = cvt4_fp8(v0[0], v0[1], v0[2], v0[3]); w.y = cvt4_fp8(v1[0], v1[1], v1[2], v1[3]);
;                     *(u32x2*)(rowp + bj * 128) = w; } }
	v_mul_f32_e32 v6, 0x3d800000, v3
	v_pk_mul_f32 v[8:9], v[110:111], v[6:7] op_sel_hi:[1,0]
	v_pk_mul_f32 v[10:11], v[108:109], v[6:7] op_sel_hi:[1,0]
	v_pk_mul_f32 v[12:13], v[106:107], v[6:7] op_sel_hi:[1,0]
	v_pk_mul_f32 v[14:15], v[104:105], v[6:7] op_sel_hi:[1,0]
	v_med3_f32 v3, v10, s69, v208
	v_med3_f32 v7, v11, s69, v208
	v_med3_f32 v10, v8, s69, v208
	v_mov_b32_e32 v8, v193
	v_cvt_pk_fp8_f32 v8, v3, v7
	v_med3_f32 v9, v9, s69, v208
	v_med3_f32 v3, v14, s69, v208
	v_med3_f32 v7, v15, s69, v208
	v_cvt_pk_fp8_f32 v8, v10, v9 op_sel:[0,0,1]
	v_mov_b32_e32 v9, v193
	v_cvt_pk_fp8_f32 v9, v3, v7
	v_med3_f32 v10, v12, s69, v208
	v_med3_f32 v11, v13, s69, v208
	v_pk_mul_f32 v[12:13], v[98:99], v[6:7] op_sel_hi:[1,0]
	v_cvt_pk_fp8_f32 v9, v10, v11 op_sel:[0,0,1]
	v_pk_mul_f32 v[10:11], v[100:101], v[6:7] op_sel_hi:[1,0]
	flat_store_dwordx2 v[4:5], v[8:9]
	v_pk_mul_f32 v[8:9], v[102:103], v[6:7] op_sel_hi:[1,0]
	v_med3_f32 v3, v10, s69, v208
	v_med3_f32 v10, v11, s69, v208
	v_med3_f32 v11, v8, s69, v208
	v_mov_b32_e32 v8, v193
	v_cvt_pk_fp8_f32 v8, v3, v10
	v_pk_mul_f32 v[6:7], v[96:97], v[6:7] op_sel_hi:[1,0]
	v_med3_f32 v9, v9, s69, v208
	v_med3_f32 v3, v6, s69, v208
	v_cvt_pk_fp8_f32 v8, v11, v9 op_sel:[0,0,1]
	v_med3_f32 v6, v7, s69, v208
	v_mov_b32_e32 v9, v193
	v_cvt_pk_fp8_f32 v9, v3, v6
	v_med3_f32 v7, v12, s69, v208
	v_med3_f32 v10, v13, s69, v208
	v_cvt_pk_fp8_f32 v9, v7, v10 op_sel:[0,0,1]
	flat_store_dwordx2 v[4:5], v[8:9] offset:128
	v_add_u32_e32 v4, 0x80, v2
	v_add_u32_e32 v6, s18, v4
	v_ashrrev_i32_e32 v7, 31, v6
	v_lshl_add_u64 v[6:7], v[6:7], 2, s[12:13]
	flat_load_dword v3, v[6:7]
	v_ashrrev_i32_e32 v5, 31, v4
	v_lshlrev_b64 v[4:5], 11, v[4:5]
	v_lshl_add_u64 v[4:5], s[10:11], 0, v[4:5]
	v_lshl_add_u64 v[4:5], v[4:5], 0, v[0:1]
	s_waitcnt vmcnt(0) lgkmcnt(0)
	v_mul_f32_e32 v6, 0x3d800000, v3
	v_pk_mul_f32 v[8:9], v[94:95], v[6:7] op_sel_hi:[1,0]
	v_pk_mul_f32 v[10:11], v[92:93], v[6:7] op_sel_hi:[1,0]
	v_pk_mul_f32 v[12:13], v[90:91], v[6:7] op_sel_hi:[1,0]
	v_pk_mul_f32 v[14:15], v[88:89], v[6:7] op_sel_hi:[1,0]
	v_med3_f32 v3, v10, s69, v208
	v_med3_f32 v7, v11, s69, v208
	v_med3_f32 v10, v8, s69, v208
	v_mov_b32_e32 v8, v193
	v_cvt_pk_fp8_f32 v8, v3, v7
	v_med3_f32 v9, v9, s69, v208
	v_med3_f32 v3, v14, s69, v208
	v_med3_f32 v7, v15, s69, v208
	v_cvt_pk_fp8_f32 v8, v10, v9 op_sel:[0,0,1]
	v_mov_b32_e32 v9, v193
	v_cvt_pk_fp8_f32 v9, v3, v7
	v_med3_f32 v10, v12, s69, v208
	v_med3_f32 v11, v13, s69, v208
	v_pk_mul_f32 v[12:13], v[82:83], v[6:7] op_sel_hi:[1,0]
	v_cvt_pk_fp8_f32 v9, v10, v11 op_sel:[0,0,1]
	v_pk_mul_f32 v[10:11], v[84:85], v[6:7] op_sel_hi:[1,0]
	flat_store_dwordx2 v[4:5], v[8:9]
	v_pk_mul_f32 v[8:9], v[86:87], v[6:7] op_sel_hi:[1,0]
	v_med3_f32 v3, v10, s69, v208
	v_med3_f32 v10, v11, s69, v208
	v_med3_f32 v11, v8, s69, v208
	v_mov_b32_e32 v8, v193
	v_cvt_pk_fp8_f32 v8, v3, v10
	v_pk_mul_f32 v[6:7], v[80:81], v[6:7] op_sel_hi:[1,0]
	v_med3_f32 v9, v9, s69, v208
	v_med3_f32 v3, v6, s69, v208
	v_cvt_pk_fp8_f32 v8, v11, v9 op_sel:[0,0,1]
	v_med3_f32 v6, v7, s69, v208
	v_mov_b32_e32 v9, v193
	v_cvt_pk_fp8_f32 v9, v3, v6
	v_med3_f32 v7, v12, s69, v208
	v_med3_f32 v10, v13, s69, v208
	v_cvt_pk_fp8_f32 v9, v7, v10 op_sel:[0,0,1]
	flat_store_dwordx2 v[4:5], v[8:9] offset:128
	v_add_u32_e32 v4, 0x90, v2
	v_add_u32_e32 v6, s18, v4
	v_ashrrev_i32_e32 v7, 31, v6
	v_lshl_add_u64 v[6:7], v[6:7], 2, s[12:13]
	flat_load_dword v3, v[6:7]
	v_ashrrev_i32_e32 v5, 31, v4
	v_lshlrev_b64 v[4:5], 11, v[4:5]
	v_lshl_add_u64 v[4:5], s[10:11], 0, v[4:5]
	v_lshl_add_u64 v[4:5], v[4:5], 0, v[0:1]
	s_waitcnt vmcnt(0) lgkmcnt(0)
;     __device__ __forceinline__ void operator()(AccRef acc, const pg8::Unit& u, int wr, int wc, int fr, int fq) const {
;     ...
;             for (int m = 0; m < 4; ++m) { const int row = row0 + ai * 128 + m * 16; const float s = sw[u.lb + u.pb - u.pm * 256 + row] * (Y2_SCALE / (H_SCALE * W2_SCALE)); unsigned char* rowp = O + (size_t)row * DM + col0;
; #pragma unroll
;                 for (int bj = 0; bj < 2; ++bj) { const f32x4 v0 = acc[ai][bj][m][0] * s, v1 = acc[ai][bj][m][1] * s;
;                     u32x2 w; w.x = cvt4_fp8(v0[0], v0[1], v0[2], v0[3]); w.y = cvt4_fp8(v1[0], v1[1], v1[2], v1[3]);
;                     *(u32x2*)(rowp + bj * 128) = w; } }
	v_mul_f32_e32 v6, 0x3d800000, v3
	v_pk_mul_f32 v[8:9], v[78:79], v[6:7] op_sel_hi:[1,0]
	v_pk_mul_f32 v[10:11], v[76:77], v[6:7] op_sel_hi:[1,0]
	v_pk_mul_f32 v[12:13], v[74:75], v[6:7] op_sel_hi:[1,0]
	v_pk_mul_f32 v[14:15], v[72:73], v[6:7] op_sel_hi:[1,0]
	v_med3_f32 v3, v10, s69, v208
	v_med3_f32 v7, v11, s69, v208
	v_med3_f32 v10, v8, s69, v208
	v_mov_b32_e32 v8, v193
	v_cvt_pk_fp8_f32 v8, v3, v7
	v_med3_f32 v9, v9, s69, v208
	v_med3_f32 v3, v14, s69, v208
	v_med3_f32 v7, v15, s69, v208
	v_cvt_pk_fp8_f32 v8, v10, v9 op_sel:[0,0,1]
	v_mov_b32_e32 v9, v193
	v_cvt_pk_fp8_f32 v9, v3, v7
	v_med3_f32 v10, v12, s69, v208
	v_med3_f32 v11, v13, s69, v208
	v_pk_mul_f32 v[12:13], v[66:67], v[6:7] op_sel_hi:[1,0]
	v_cvt_pk_fp8_f32 v9, v10, v11 op_sel:[0,0,1]
	v_pk_mul_f32 v[10:11], v[68:69], v[6:7] op_sel_hi:[1,0]
	flat_store_dwordx2 v[4:5], v[8:9]
	v_pk_mul_f32 v[8:9], v[70:71], v[6:7] op_sel_hi:[1,0]
	v_med3_f32 v3, v10, s69, v208
	v_med3_f32 v10, v11, s69, v208
	v_med3_f32 v11, v8, s69, v208
	v_mov_b32_e32 v8, v193
	v_cvt_pk_fp8_f32 v8, v3, v10
	v_pk_mul_f32 v[6:7], v[64:65], v[6:7] op_sel_hi:[1,0]
	v_med3_f32 v9, v9, s69, v208
	v_med3_f32 v3, v6, s69, v208
	v_cvt_pk_fp8_f32 v8, v11, v9 op_sel:[0,0,1]
	v_med3_f32 v6, v7, s69, v208
	v_mov_b32_e32 v9, v193
	v_cvt_pk_fp8_f32 v9, v3, v6
	v_med3_f32 v7, v12, s69, v208
	v_med3_f32 v10, v13, s69, v208
	v_cvt_pk_fp8_f32 v9, v7, v10 op_sel:[0,0,1]
	flat_store_dwordx2 v[4:5], v[8:9] offset:128
	v_add_u32_e32 v4, 0xa0, v2
	v_add_u32_e32 v6, s18, v4
	v_ashrrev_i32_e32 v7, 31, v6
	v_lshl_add_u64 v[6:7], v[6:7], 2, s[12:13]
	flat_load_dword v3, v[6:7]
	v_ashrrev_i32_e32 v5, 31, v4
	v_lshlrev_b64 v[4:5], 11, v[4:5]
	v_lshl_add_u64 v[4:5], s[10:11], 0, v[4:5]
	v_lshl_add_u64 v[4:5], v[4:5], 0, v[0:1]
	v_add_u32_e32 v2, 0xb0, v2
	s_waitcnt vmcnt(0) lgkmcnt(0)
	v_mul_f32_e32 v6, 0x3d800000, v3
	v_pk_mul_f32 v[8:9], v[62:63], v[6:7] op_sel_hi:[1,0]
	v_pk_mul_f32 v[10:11], v[60:61], v[6:7] op_sel_hi:[1,0]
	v_pk_mul_f32 v[12:13], v[58:59], v[6:7] op_sel_hi:[1,0]
	v_pk_mul_f32 v[14:15], v[56:57], v[6:7] op_sel_hi:[1,0]
	v_med3_f32 v3, v10, s69, v208
	v_med3_f32 v7, v11, s69, v208
	v_med3_f32 v10, v8, s69, v208
	v_mov_b32_e32 v8, v193
	v_cvt_pk_fp8_f32 v8, v3, v7
	v_med3_f32 v9, v9, s69, v208
	v_med3_f32 v3, v14, s69, v208
	v_med3_f32 v7, v15, s69, v208
	v_cvt_pk_fp8_f32 v8, v10, v9 op_sel:[0,0,1]
	v_mov_b32_e32 v9, v193
	v_cvt_pk_fp8_f32 v9, v3, v7
	v_med3_f32 v10, v12, s69, v208
	v_med3_f32 v11, v13, s69, v208
	v_pk_mul_f32 v[12:13], v[50:51], v[6:7] op_sel_hi:[1,0]
	v_cvt_pk_fp8_f32 v9, v10, v11 op_sel:[0,0,1]
	v_pk_mul_f32 v[10:11], v[52:53], v[6:7] op_sel_hi:[1,0]
	flat_store_dwordx2 v[4:5], v[8:9]
	v_pk_mul_f32 v[8:9], v[54:55], v[6:7] op_sel_hi:[1,0]
	v_med3_f32 v3, v10, s69, v208
	v_med3_f32 v10, v11, s69, v208
	v_med3_f32 v11, v8, s69, v208
	v_mov_b32_e32 v8, v193
	v_cvt_pk_fp8_f32 v8, v3, v10
	v_pk_mul_f32 v[6:7], v[48:49], v[6:7] op_sel_hi:[1,0]
	v_med3_f32 v9, v9, s69, v208
	v_med3_f32 v3, v6, s69, v208
	v_cvt_pk_fp8_f32 v8, v11, v9 op_sel:[0,0,1]
	v_med3_f32 v6, v7, s69, v208
	v_mov_b32_e32 v9, v193
	v_cvt_pk_fp8_f32 v9, v3, v6
	v_med3_f32 v7, v12, s69, v208
	v_med3_f32 v10, v13, s69, v208
	v_cvt_pk_fp8_f32 v9, v7, v10 op_sel:[0,0,1]
	flat_store_dwordx2 v[4:5], v[8:9] offset:128
	v_add_u32_e32 v4, s18, v2
	v_ashrrev_i32_e32 v5, 31, v4
	v_lshl_add_u64 v[4:5], v[4:5], 2, s[12:13]
	flat_load_dword v3, v[4:5]
	s_mov_b64 s[18:19], -1
	s_waitcnt vmcnt(0) lgkmcnt(0)
	v_mul_f32_e32 v4, 0x3d800000, v3
	v_ashrrev_i32_e32 v3, 31, v2
	v_lshlrev_b64 v[2:3], 11, v[2:3]
	v_lshl_add_u64 v[2:3], s[10:11], 0, v[2:3]
	v_lshl_add_u64 v[0:1], v[2:3], 0, v[0:1]
	v_pk_mul_f32 v[2:3], v[46:47], v[4:5] op_sel_hi:[1,0]
	v_pk_mul_f32 v[6:7], v[44:45], v[4:5] op_sel_hi:[1,0]
	v_pk_mul_f32 v[8:9], v[42:43], v[4:5] op_sel_hi:[1,0]
	v_pk_mul_f32 v[10:11], v[40:41], v[4:5] op_sel_hi:[1,0]
	v_med3_f32 v5, v6, s69, v208
	v_med3_f32 v6, v7, s69, v208
	v_med3_f32 v7, v2, s69, v208
	v_mov_b32_e32 v2, v193
	v_cvt_pk_fp8_f32 v2, v5, v6
	v_med3_f32 v3, v3, s69, v208
	v_med3_f32 v5, v10, s69, v208
	v_med3_f32 v6, v11, s69, v208
	v_cvt_pk_fp8_f32 v2, v7, v3 op_sel:[0,0,1]
	v_mov_b32_e32 v3, v193
	v_cvt_pk_fp8_f32 v3, v5, v6
	v_med3_f32 v7, v8, s69, v208
	v_med3_f32 v8, v9, s69, v208
	v_cvt_pk_fp8_f32 v3, v7, v8 op_sel:[0,0,1]
	v_pk_mul_f32 v[6:7], v[36:37], v[4:5] op_sel_hi:[1,0]
	v_pk_mul_f32 v[8:9], v[34:35], v[4:5] op_sel_hi:[1,0]
	v_med3_f32 v6, v6, s69, v208
	flat_store_dwordx2 v[0:1], v[2:3]
	v_pk_mul_f32 v[2:3], v[38:39], v[4:5] op_sel_hi:[1,0]
	v_med3_f32 v7, v7, s69, v208
	v_med3_f32 v10, v2, s69, v208
	v_mov_b32_e32 v2, v193
	v_cvt_pk_fp8_f32 v2, v6, v7
	v_pk_mul_f32 v[4:5], v[32:33], v[4:5] op_sel_hi:[1,0]
	v_med3_f32 v3, v3, s69, v208
	v_med3_f32 v4, v4, s69, v208
	v_cvt_pk_fp8_f32 v2, v10, v3 op_sel:[0,0,1]
	v_med3_f32 v5, v5, s69, v208
	v_mov_b32_e32 v3, v193
	v_cvt_pk_fp8_f32 v3, v4, v5
	v_med3_f32 v6, v8, s69, v208
	v_med3_f32 v7, v9, s69, v208
	v_cvt_pk_fp8_f32 v3, v6, v7 op_sel:[0,0,1]
	flat_store_dwordx2 v[0:1], v[2:3] offset:128
	s_cbranch_vccnz .LBB0_1201
	s_andn2_b64 vcc, exec, s[8:9]
	s_cbranch_vccnz .LBB0_1200
	s_barrier
	s_branch .LBB0_1200
